# wide global stores (dwordx4/x2) issued at agent scope sc1 (write-through) so the barrier release has little to write back
# speedup vs baseline: 1.0206x; 1.0130x over previous
.LBB0_27:
	s_add_u32 s16, s15, s86
	s_addc_u32 s17, s34, s87
	s_add_u32 s36, s16, 0xd0000
	s_addc_u32 s37, s17, 0
	global_load_dwordx4 v[18:21], v1, s[36:37] offset:16
	global_load_dwordx4 v[62:65], v228, s[16:17]
	v_lshl_add_u64 v[38:39], v[26:27], 0, s[86:87]
	global_load_dwordx2 v[68:69], v[38:39], off offset:-1024
	global_load_dwordx2 v[70:71], v[38:39], off offset:-512
	global_load_dwordx2 v[72:73], v[38:39], off
	global_load_dwordx2 v[74:75], v[38:39], off offset:512
	v_lshl_add_u64 v[38:39], v[36:37], 0, s[86:87]
	global_load_dwordx2 v[60:61], v[38:39], off offset:-1024
	global_load_dwordx2 v[58:59], v[38:39], off offset:-512
	global_load_dwordx2 v[56:57], v[38:39], off
	global_load_dwordx2 v[54:55], v[38:39], off offset:512
	v_lshl_add_u64 v[38:39], v[32:33], 0, s[86:87]
	global_load_dwordx2 v[52:53], v[38:39], off offset:-1024
	global_load_dwordx2 v[50:51], v[38:39], off offset:-512
	global_load_dwordx2 v[48:49], v[38:39], off
	global_load_dwordx2 v[46:47], v[38:39], off offset:512
	s_add_i32 s16, s14, 3
	s_ashr_i32 s17, s16, 31
	s_lshl_b64 s[36:37], s[16:17], 11
	v_lshl_add_u64 v[38:39], v[22:23], 0, s[36:37]
	global_load_dwordx2 v[44:45], v[38:39], off
	global_load_dwordx2 v[42:43], v[38:39], off offset:512
	global_load_dwordx2 v[40:41], v[38:39], off offset:1024
	s_nop 0
	global_load_dwordx2 v[38:39], v[38:39], off offset:1536
	s_lshl_b64 s[16:17], s[16:17], 12
	s_add_i32 s14, s14, 4
	s_add_u32 s15, s15, 32
	s_addc_u32 s34, s34, 0
	v_lshl_add_u64 v[26:27], v[26:27], 0, s[38:39]
	v_lshl_add_u64 v[32:33], v[32:33], 0, s[38:39]
	v_lshl_add_u64 v[36:37], v[36:37], 0, s[38:39]
	s_cmp_ge_i32 s14, s31
	s_waitcnt vmcnt(15)
	v_lshlrev_b32_e32 v66, 16, v68
	v_ffbh_u32_e32 v0, v63
	v_min_u32_e32 v0, 32, v0
	v_lshlrev_b64 v[62:63], v0, v[62:63]
	v_min_u32_e32 v62, 1, v62
	v_or_b32_e32 v62, v63, v62
	v_cvt_f32_u32_e32 v62, v62
	v_sub_u32_e32 v0, 32, v0
	v_and_b32_e32 v67, 0xffff0000, v68
	v_lshlrev_b32_e32 v68, 16, v69
	v_ldexp_f32 v0, v62, v0
	v_fmamk_f32 v0, v0, 0x32800000, v196
	v_cmp_gt_f32_e32 vcc, s96, v0
	v_mul_f32_e32 v62, 0x4b800000, v0
	v_and_b32_e32 v69, 0xffff0000, v69
	v_cndmask_b32_e32 v0, v0, v62, vcc
	v_rsq_f32_e32 v0, v0
	s_nop 0
	v_mul_f32_e32 v62, 0x45800000, v0
	v_cndmask_b32_e32 v0, v0, v62, vcc
	v_pk_mul_f32 v[66:67], v[0:1], v[66:67] op_sel_hi:[0,1]
	v_pk_mul_f32 v[68:69], v[0:1], v[68:69] op_sel_hi:[0,1]
	v_lshl_add_u64 v[62:63], v[30:31], 0, s[0:1]
	v_pk_mul_f32 v[66:67], v[14:15], v[66:67]
	v_pk_mul_f32 v[68:69], v[16:17], v[68:69]
	global_store_dwordx4 v[62:63], v[66:69], off sc1
	v_lshl_add_u64 v[30:31], v[30:31], 0, s[40:41]
	s_waitcnt vmcnt(15)
	v_lshlrev_b32_e32 v66, 16, v70
	v_and_b32_e32 v67, 0xffff0000, v70
	v_lshlrev_b32_e32 v68, 16, v71
	v_and_b32_e32 v69, 0xffff0000, v71
	v_pk_mul_f32 v[66:67], v[0:1], v[66:67] op_sel_hi:[0,1]
	v_pk_mul_f32 v[68:69], v[0:1], v[68:69] op_sel_hi:[0,1]
	v_pk_mul_f32 v[66:67], v[10:11], v[66:67]
	v_pk_mul_f32 v[68:69], v[12:13], v[68:69]
	global_store_dwordx4 v[62:63], v[66:69], off offset:1024 sc1
	s_waitcnt vmcnt(15)
	s_nop 0
	v_lshlrev_b32_e32 v66, 16, v72
	v_and_b32_e32 v67, 0xffff0000, v72
	v_lshlrev_b32_e32 v68, 16, v73
	v_and_b32_e32 v69, 0xffff0000, v73
	v_pk_mul_f32 v[66:67], v[0:1], v[66:67] op_sel_hi:[0,1]
	v_pk_mul_f32 v[68:69], v[0:1], v[68:69] op_sel_hi:[0,1]
	v_pk_mul_f32 v[66:67], v[6:7], v[66:67]
	v_pk_mul_f32 v[68:69], v[8:9], v[68:69]
	global_store_dwordx4 v[62:63], v[66:69], off offset:2048 sc1
	s_waitcnt vmcnt(15)
	s_nop 0
	v_lshlrev_b32_e32 v66, 16, v74
	v_and_b32_e32 v67, 0xffff0000, v74
	v_lshlrev_b32_e32 v68, 16, v75
	v_and_b32_e32 v69, 0xffff0000, v75
	v_pk_mul_f32 v[66:67], v[0:1], v[66:67] op_sel_hi:[0,1]
	v_pk_mul_f32 v[68:69], v[0:1], v[68:69] op_sel_hi:[0,1]
	v_ffbh_u32_e32 v0, v65
	v_pk_mul_f32 v[66:67], v[2:3], v[66:67]
	v_pk_mul_f32 v[68:69], v[4:5], v[68:69]
	v_min_u32_e32 v0, 32, v0
	global_store_dwordx4 v[62:63], v[66:69], off offset:3072 sc1
	v_lshlrev_b64 v[62:63], v0, v[64:65]
	v_min_u32_e32 v62, 1, v62
	v_or_b32_e32 v62, v63, v62
	v_cvt_f32_u32_e32 v62, v62
	v_sub_u32_e32 v0, 32, v0
	s_waitcnt vmcnt(15)
	v_and_b32_e32 v63, 0xffff0000, v60
	v_lshl_add_u64 v[66:67], v[34:35], 0, s[0:1]
	v_ldexp_f32 v0, v62, v0
	v_fmamk_f32 v0, v0, 0x32800000, v196
	v_cmp_gt_f32_e32 vcc, s96, v0
	v_mul_f32_e32 v62, 0x4b800000, v0
	v_lshl_add_u64 v[34:35], v[34:35], 0, s[40:41]
	v_cndmask_b32_e32 v0, v0, v62, vcc
	v_rsq_f32_e32 v0, v0
	s_nop 0
	v_mul_f32_e32 v62, 0x45800000, v0
	v_cndmask_b32_e32 v0, v0, v62, vcc
	v_lshlrev_b32_e32 v62, 16, v60
	v_lshlrev_b32_e32 v60, 16, v61
	v_and_b32_e32 v61, 0xffff0000, v61
	v_pk_mul_f32 v[60:61], v[0:1], v[60:61] op_sel_hi:[0,1]
	v_pk_mul_f32 v[62:63], v[0:1], v[62:63] op_sel_hi:[0,1]
	v_pk_mul_f32 v[64:65], v[16:17], v[60:61]
	s_waitcnt vmcnt(14)
	v_lshlrev_b32_e32 v60, 16, v58
	v_and_b32_e32 v61, 0xffff0000, v58
	v_lshlrev_b32_e32 v58, 16, v59
	v_and_b32_e32 v59, 0xffff0000, v59
	v_pk_mul_f32 v[62:63], v[14:15], v[62:63]
	v_pk_mul_f32 v[58:59], v[0:1], v[58:59] op_sel_hi:[0,1]
	global_store_dwordx4 v[66:67], v[62:65], off sc1
	v_pk_mul_f32 v[60:61], v[0:1], v[60:61] op_sel_hi:[0,1]
	v_pk_mul_f32 v[60:61], v[10:11], v[60:61]
	v_pk_mul_f32 v[62:63], v[12:13], v[58:59]
	s_waitcnt vmcnt(14)
	v_lshlrev_b32_e32 v58, 16, v56
	v_and_b32_e32 v59, 0xffff0000, v56
	v_lshlrev_b32_e32 v56, 16, v57
	v_and_b32_e32 v57, 0xffff0000, v57
	v_pk_mul_f32 v[56:57], v[0:1], v[56:57] op_sel_hi:[0,1]
	global_store_dwordx4 v[66:67], v[60:63], off offset:1024 sc1
	v_pk_mul_f32 v[58:59], v[0:1], v[58:59] op_sel_hi:[0,1]
	v_pk_mul_f32 v[58:59], v[6:7], v[58:59]
	v_pk_mul_f32 v[60:61], v[8:9], v[56:57]
	s_waitcnt vmcnt(14)
	v_lshlrev_b32_e32 v56, 16, v54
	v_and_b32_e32 v57, 0xffff0000, v54
	v_lshlrev_b32_e32 v54, 16, v55
	v_and_b32_e32 v55, 0xffff0000, v55
	v_pk_mul_f32 v[56:57], v[0:1], v[56:57] op_sel_hi:[0,1]
	v_pk_mul_f32 v[54:55], v[0:1], v[54:55] op_sel_hi:[0,1]
	v_ffbh_u32_e32 v0, v19
	v_min_u32_e32 v0, 32, v0
	v_lshlrev_b64 v[18:19], v0, v[18:19]
	v_min_u32_e32 v18, 1, v18
	v_or_b32_e32 v18, v19, v18
	v_cvt_f32_u32_e32 v18, v18
	v_sub_u32_e32 v0, 32, v0
	global_store_dwordx4 v[66:67], v[58:61], off offset:2048 sc1
	v_pk_mul_f32 v[56:57], v[2:3], v[56:57]
	v_ldexp_f32 v0, v18, v0
	v_fmamk_f32 v0, v0, 0x32800000, v196
	v_cmp_gt_f32_e32 vcc, s96, v0
	v_mul_f32_e32 v18, 0x4b800000, v0
	v_pk_mul_f32 v[58:59], v[4:5], v[54:55]
	v_cndmask_b32_e32 v0, v0, v18, vcc
	v_rsq_f32_e32 v0, v0
	s_waitcnt vmcnt(14)
	v_lshlrev_b32_e32 v54, 16, v52
	v_and_b32_e32 v55, 0xffff0000, v52
	v_lshlrev_b32_e32 v52, 16, v53
	v_mul_f32_e32 v18, 0x45800000, v0
	v_cndmask_b32_e32 v0, v0, v18, vcc
	v_and_b32_e32 v53, 0xffff0000, v53
	v_pk_mul_f32 v[52:53], v[0:1], v[52:53] op_sel_hi:[0,1]
	global_store_dwordx4 v[66:67], v[56:59], off offset:3072 sc1
	v_pk_mul_f32 v[54:55], v[0:1], v[54:55] op_sel_hi:[0,1]
	v_lshl_add_u64 v[18:19], v[28:29], 0, s[0:1]
	v_pk_mul_f32 v[56:57], v[16:17], v[52:53]
	s_waitcnt vmcnt(14)
	v_lshlrev_b32_e32 v52, 16, v50
	v_and_b32_e32 v53, 0xffff0000, v50
	v_lshlrev_b32_e32 v50, 16, v51
	v_and_b32_e32 v51, 0xffff0000, v51
	v_pk_mul_f32 v[54:55], v[14:15], v[54:55]
	v_pk_mul_f32 v[50:51], v[0:1], v[50:51] op_sel_hi:[0,1]
	global_store_dwordx4 v[18:19], v[54:57], off sc1
	v_pk_mul_f32 v[52:53], v[0:1], v[52:53] op_sel_hi:[0,1]
	v_pk_mul_f32 v[52:53], v[10:11], v[52:53]
	v_pk_mul_f32 v[54:55], v[12:13], v[50:51]
	s_waitcnt vmcnt(14)
	v_lshlrev_b32_e32 v50, 16, v48
	v_and_b32_e32 v51, 0xffff0000, v48
	v_lshlrev_b32_e32 v48, 16, v49
	v_and_b32_e32 v49, 0xffff0000, v49
	v_pk_mul_f32 v[48:49], v[0:1], v[48:49] op_sel_hi:[0,1]
	global_store_dwordx4 v[18:19], v[52:55], off offset:1024 sc1
	v_pk_mul_f32 v[50:51], v[0:1], v[50:51] op_sel_hi:[0,1]
	v_pk_mul_f32 v[50:51], v[6:7], v[50:51]
	v_pk_mul_f32 v[52:53], v[8:9], v[48:49]
	s_waitcnt vmcnt(14)
	v_lshlrev_b32_e32 v48, 16, v46
	v_and_b32_e32 v49, 0xffff0000, v46
	v_lshlrev_b32_e32 v46, 16, v47
	v_and_b32_e32 v47, 0xffff0000, v47
	v_pk_mul_f32 v[48:49], v[0:1], v[48:49] op_sel_hi:[0,1]
	v_pk_mul_f32 v[46:47], v[0:1], v[46:47] op_sel_hi:[0,1]
	v_ffbh_u32_e32 v0, v21
	global_store_dwordx4 v[18:19], v[50:53], off offset:2048 sc1
	v_pk_mul_f32 v[48:49], v[2:3], v[48:49]
	v_min_u32_e32 v0, 32, v0
	v_pk_mul_f32 v[50:51], v[4:5], v[46:47]
	global_store_dwordx4 v[18:19], v[48:51], off offset:3072 sc1
	v_lshlrev_b64 v[18:19], v0, v[20:21]
	v_min_u32_e32 v18, 1, v18
	v_or_b32_e32 v18, v19, v18
	v_cvt_f32_u32_e32 v18, v18
	v_sub_u32_e32 v0, 32, v0
	s_waitcnt vmcnt(15)
	v_and_b32_e32 v19, 0xffff0000, v44
	v_lshlrev_b32_e32 v20, 16, v45
	v_ldexp_f32 v0, v18, v0
	v_fmamk_f32 v0, v0, 0x32800000, v196
	v_cmp_gt_f32_e32 vcc, s96, v0
	v_mul_f32_e32 v18, 0x4b800000, v0
	v_and_b32_e32 v21, 0xffff0000, v45
	v_cndmask_b32_e32 v0, v0, v18, vcc
	v_rsq_f32_e32 v0, v0
	v_lshl_add_u64 v[46:47], v[24:25], 0, s[16:17]
	v_lshl_add_u64 v[28:29], v[28:29], 0, s[40:41]
	v_mul_f32_e32 v18, 0x45800000, v0
	v_cndmask_b32_e32 v0, v0, v18, vcc
	v_lshlrev_b32_e32 v18, 16, v44
	v_pk_mul_f32 v[18:19], v[0:1], v[18:19] op_sel_hi:[0,1]
	v_pk_mul_f32 v[20:21], v[0:1], v[20:21] op_sel_hi:[0,1]
	v_pk_mul_f32 v[18:19], v[14:15], v[18:19]
	v_pk_mul_f32 v[20:21], v[16:17], v[20:21]
	global_store_dwordx4 v[46:47], v[18:21], off sc1
	s_waitcnt vmcnt(15)
	s_nop 0
	v_lshlrev_b32_e32 v18, 16, v42
	v_and_b32_e32 v19, 0xffff0000, v42
	v_lshlrev_b32_e32 v20, 16, v43
	v_and_b32_e32 v21, 0xffff0000, v43
	v_pk_mul_f32 v[18:19], v[0:1], v[18:19] op_sel_hi:[0,1]
	v_pk_mul_f32 v[20:21], v[0:1], v[20:21] op_sel_hi:[0,1]
	v_pk_mul_f32 v[18:19], v[10:11], v[18:19]
	v_pk_mul_f32 v[20:21], v[12:13], v[20:21]
	global_store_dwordx4 v[46:47], v[18:21], off offset:1024 sc1
	s_waitcnt vmcnt(15)
	s_nop 0
	v_lshlrev_b32_e32 v18, 16, v40
	v_and_b32_e32 v19, 0xffff0000, v40
	v_lshlrev_b32_e32 v20, 16, v41
	v_and_b32_e32 v21, 0xffff0000, v41
	v_pk_mul_f32 v[18:19], v[0:1], v[18:19] op_sel_hi:[0,1]
	v_pk_mul_f32 v[20:21], v[0:1], v[20:21] op_sel_hi:[0,1]
	v_pk_mul_f32 v[18:19], v[6:7], v[18:19]
	v_pk_mul_f32 v[20:21], v[8:9], v[20:21]
	global_store_dwordx4 v[46:47], v[18:21], off offset:2048 sc1
	s_waitcnt vmcnt(15)
	s_nop 0
	v_lshlrev_b32_e32 v18, 16, v38
	v_and_b32_e32 v19, 0xffff0000, v38
	v_lshlrev_b32_e32 v20, 16, v39
	v_and_b32_e32 v21, 0xffff0000, v39
	v_pk_mul_f32 v[18:19], v[0:1], v[18:19] op_sel_hi:[0,1]
	v_pk_mul_f32 v[20:21], v[0:1], v[20:21] op_sel_hi:[0,1]
	v_pk_mul_f32 v[18:19], v[2:3], v[18:19]
	v_pk_mul_f32 v[20:21], v[4:5], v[20:21]
	global_store_dwordx4 v[46:47], v[18:21], off offset:3072 sc1
	s_cbranch_scc0 .LBB0_27

.LBB0_77:
	s_or_b64 exec, exec, s[64:65]
	v_lshlrev_b64 v[70:71], 2, v[74:75]
	v_lshl_add_u64 v[2:3], s[56:57], 0, v[70:71]
	v_lshl_or_b32 v0, v66, 6, v67
	global_load_dwordx4 v[66:69], v[2:3], off offset:16
	global_load_dwordx4 v[86:89], v[2:3], off
	v_lshl_add_u64 v[2:3], s[60:61], 0, v[70:71]
	v_lshl_add_u64 v[72:73], s[62:63], 0, v[70:71]
	v_lshl_add_u64 v[76:77], s[58:59], 0, v[70:71]
	global_load_dwordx4 v[62:65], v[2:3], off offset:16
	global_load_dwordx4 v[90:93], v[2:3], off
	s_nop 0
	global_load_dwordx4 v[2:5], v[72:73], off offset:16
	global_load_dwordx4 v[94:97], v[72:73], off
	s_nop 0
	global_load_dwordx4 v[70:73], v[76:77], off offset:16
	global_load_dwordx4 v[98:101], v[76:77], off
	v_lshlrev_b32_e32 v76, 16, v58
	v_and_b32_e32 v77, 0xffff0000, v58
	v_lshlrev_b32_e32 v58, 16, v59
	v_and_b32_e32 v59, 0xffff0000, v59
	s_waitcnt vmcnt(0)
	v_pk_fma_f32 v[76:77], v[86:87], v[76:77], v[98:99]
	v_lshlrev_b32_e32 v86, 16, v14
	v_and_b32_e32 v87, 0xffff0000, v14
	v_pk_fma_f32 v[76:77], v[90:91], v[86:87], v[76:77]
	v_lshlrev_b32_e32 v86, 16, v54
	v_and_b32_e32 v87, 0xffff0000, v54
	v_pk_fma_f32 v[76:77], v[94:95], v[86:87], v[76:77]
	v_pk_fma_f32 v[58:59], v[88:89], v[58:59], v[100:101]
	v_mul_f32_e32 v14, 0x3d372713, v76
	v_mul_f32_e32 v14, v76, v14
	v_fma_f32 v14, v76, v14, v76
	v_mul_f32_e32 v14, 0xc0135761, v14
	v_exp_f32_e32 v14, v14
	v_lshlrev_b32_e32 v54, 16, v55
	v_and_b32_e32 v55, 0xffff0000, v55
	v_add_f32_e32 v14, 1.0, v14
	v_rcp_f32_e32 v86, v14
	v_mul_f32_e32 v14, 0x3d372713, v77
	v_mul_f32_e32 v14, v77, v14
	v_fma_f32 v14, v77, v14, v77
	v_mul_f32_e32 v14, 0xc0135761, v14
	v_exp_f32_e32 v14, v14
	s_nop 0
	v_add_f32_e32 v14, 1.0, v14
	v_rcp_f32_e32 v87, v14
	v_lshlrev_b32_e32 v14, 16, v15
	v_and_b32_e32 v15, 0xffff0000, v15
	v_pk_fma_f32 v[14:15], v[92:93], v[14:15], v[58:59]
	v_pk_mul_f32 v[76:77], v[76:77], v[86:87]
	v_pk_fma_f32 v[14:15], v[96:97], v[54:55], v[14:15]
	v_lshlrev_b32_e32 v86, 16, v50
	v_and_b32_e32 v87, 0xffff0000, v50
	v_mul_f32_e32 v50, 0x3d372713, v14
	v_mul_f32_e32 v50, v14, v50
	v_fma_f32 v50, v14, v50, v14
	v_mul_f32_e32 v50, 0xc0135761, v50
	v_exp_f32_e32 v50, v50
	v_pk_mul_f32 v[76:77], v[76:77], v[86:87]
	v_add_f32_e32 v50, 1.0, v50
	v_rcp_f32_e32 v54, v50
	v_mul_f32_e32 v50, 0x3d372713, v15
	v_mul_f32_e32 v50, v15, v50
	v_fma_f32 v50, v15, v50, v15
	v_mul_f32_e32 v50, 0xc0135761, v50
	v_exp_f32_e32 v50, v50
	s_nop 0
	v_add_f32_e32 v50, 1.0, v50
	v_rcp_f32_e32 v55, v50
	v_lshlrev_b32_e32 v50, 16, v51
	v_and_b32_e32 v51, 0xffff0000, v51
	v_pk_mul_f32 v[14:15], v[14:15], v[54:55]
	s_nop 0
	v_pk_mul_f32 v[14:15], v[14:15], v[50:51]
	v_lshlrev_b32_e32 v50, 16, v60
	v_and_b32_e32 v51, 0xffff0000, v60
	v_pk_fma_f32 v[50:51], v[66:67], v[50:51], v[70:71]
	v_lshlrev_b32_e32 v54, 16, v16
	v_and_b32_e32 v55, 0xffff0000, v16
	v_pk_fma_f32 v[50:51], v[62:63], v[54:55], v[50:51]
	v_lshlrev_b32_e32 v54, 16, v56
	v_and_b32_e32 v55, 0xffff0000, v56
	v_pk_fma_f32 v[2:3], v[2:3], v[54:55], v[50:51]
	s_nop 0
	v_mul_f32_e32 v16, 0x3d372713, v2
	v_mul_f32_e32 v16, v2, v16
	v_fma_f32 v16, v2, v16, v2
	v_mul_f32_e32 v16, 0xc0135761, v16
	v_exp_f32_e32 v16, v16
	s_nop 0
	v_add_f32_e32 v16, 1.0, v16
	v_rcp_f32_e32 v50, v16
	v_mul_f32_e32 v16, 0x3d372713, v3
	v_mul_f32_e32 v16, v3, v16
	v_fma_f32 v16, v3, v16, v3
	v_mul_f32_e32 v16, 0xc0135761, v16
	v_exp_f32_e32 v16, v16
	s_nop 0
	v_add_f32_e32 v16, 1.0, v16
	v_rcp_f32_e32 v51, v16
	v_lshlrev_b32_e32 v16, 16, v17
	v_and_b32_e32 v17, 0xffff0000, v17
	v_pk_mul_f32 v[2:3], v[2:3], v[50:51]
	v_lshlrev_b32_e32 v50, 16, v52
	v_and_b32_e32 v51, 0xffff0000, v52
	v_pk_mul_f32 v[2:3], v[2:3], v[50:51]
	v_lshlrev_b32_e32 v50, 16, v61
	v_and_b32_e32 v51, 0xffff0000, v61
	v_pk_fma_f32 v[50:51], v[68:69], v[50:51], v[72:73]
	v_cvt_pk_bf16_f32 v52, v2, v3
	v_pk_fma_f32 v[16:17], v[64:65], v[16:17], v[50:51]
	v_lshlrev_b32_e32 v50, 16, v57
	v_and_b32_e32 v51, 0xffff0000, v57
	v_pk_fma_f32 v[4:5], v[4:5], v[50:51], v[16:17]
	v_mov_b64_e32 v[2:3], s[0:1]
	v_mul_f32_e32 v16, 0x3d372713, v4
	v_mul_f32_e32 v17, 0x3d372713, v5
	v_mul_f32_e32 v16, v4, v16
	v_mul_f32_e32 v17, v5, v17
	v_fma_f32 v16, v4, v16, v4
	v_fma_f32 v17, v5, v17, v5
	v_mul_f32_e32 v16, 0xc0135761, v16
	v_mul_f32_e32 v17, 0xc0135761, v17
	v_exp_f32_e32 v16, v16
	v_exp_f32_e32 v17, v17
	v_mad_i64_i32 v[2:3], s[42:43], v0, s2, v[2:3]
	v_add_f32_e32 v16, 1.0, v16
	v_add_f32_e32 v17, 1.0, v17
	v_rcp_f32_e32 v16, v16
	v_rcp_f32_e32 v17, v17
	v_cvt_pk_bf16_f32 v50, v76, v77
	v_cvt_pk_bf16_f32 v51, v14, v15
	v_lshl_add_u64 v[2:3], v[74:75], 1, v[2:3]
	v_pk_mul_f32 v[4:5], v[4:5], v[16:17]
	v_lshlrev_b32_e32 v16, 16, v53
	v_and_b32_e32 v17, 0xffff0000, v53
	v_pk_mul_f32 v[4:5], v[4:5], v[16:17]
	s_nop 0
	v_cvt_pk_bf16_f32 v53, v4, v5
	global_store_dwordx4 v[2:3], v[50:53], off sc1
	s_and_saveexec_b64 s[42:43], s[40:41]
	s_cbranch_execz .LBB0_79
	v_add_u32_e32 v0, v84, v83
	v_mad_i32_i24 v2, v0, s90, v80
	v_lshl_add_u32 v58, v2, 3, v234
	v_lshrrev_b32_e32 v2, 1, v0
	v_ashrrev_i32_e32 v59, 31, v58
	v_add_u32_e32 v2, s34, v2
	v_and_b32_e32 v0, 1, v0
	v_lshlrev_b64 v[54:55], 2, v[58:59]
	v_lshl_or_b32 v0, v2, 6, v0
	v_lshl_add_u64 v[2:3], s[56:57], 0, v[54:55]
	global_load_dwordx4 v[50:53], v[2:3], off offset:16
	global_load_dwordx4 v[60:63], v[2:3], off
	v_lshl_add_u64 v[2:3], s[60:61], 0, v[54:55]
	v_lshl_add_u64 v[56:57], s[62:63], 0, v[54:55]
	v_lshl_add_u64 v[72:73], s[58:59], 0, v[54:55]
	global_load_dwordx4 v[14:17], v[2:3], off offset:16
	global_load_dwordx4 v[64:67], v[2:3], off
	s_nop 0
	global_load_dwordx4 v[2:5], v[56:57], off offset:16
	global_load_dwordx4 v[68:71], v[56:57], off
	s_nop 0
	global_load_dwordx4 v[54:57], v[72:73], off offset:16
	s_nop 0
	global_load_dwordx4 v[72:75], v[72:73], off
	v_lshlrev_b32_e32 v76, 16, v38
	v_and_b32_e32 v77, 0xffff0000, v38
	s_waitcnt vmcnt(0)
	v_pk_fma_f32 v[60:61], v[60:61], v[76:77], v[72:73]
	v_lshlrev_b32_e32 v72, 16, v18
	v_and_b32_e32 v73, 0xffff0000, v18
	v_pk_fma_f32 v[60:61], v[64:65], v[72:73], v[60:61]
	v_lshlrev_b32_e32 v64, 16, v26
	v_and_b32_e32 v65, 0xffff0000, v26
	v_pk_fma_f32 v[60:61], v[68:69], v[64:65], v[60:61]
	s_nop 0
	v_mul_f32_e32 v18, 0x3d372713, v60
	v_mul_f32_e32 v18, v60, v18
	v_fma_f32 v18, v60, v18, v60
	v_mul_f32_e32 v18, 0xc0135761, v18
	v_exp_f32_e32 v18, v18
	s_nop 0
	v_add_f32_e32 v18, 1.0, v18
	v_rcp_f32_e32 v64, v18
	v_mul_f32_e32 v18, 0x3d372713, v61
	v_mul_f32_e32 v18, v61, v18
	v_fma_f32 v18, v61, v18, v61
	v_mul_f32_e32 v18, 0xc0135761, v18
	v_exp_f32_e32 v18, v18
	s_nop 0
	v_add_f32_e32 v18, 1.0, v18
	v_rcp_f32_e32 v65, v18
	v_lshlrev_b32_e32 v18, 16, v19
	v_and_b32_e32 v19, 0xffff0000, v19
	v_pk_mul_f32 v[60:61], v[60:61], v[64:65]
	v_lshlrev_b32_e32 v64, 16, v46
	v_and_b32_e32 v65, 0xffff0000, v46
	v_pk_mul_f32 v[60:61], v[60:61], v[64:65]
	v_lshlrev_b32_e32 v64, 16, v39
	v_and_b32_e32 v65, 0xffff0000, v39
	v_pk_fma_f32 v[62:63], v[62:63], v[64:65], v[74:75]
	s_nop 0
	v_pk_fma_f32 v[18:19], v[66:67], v[18:19], v[62:63]
	v_lshlrev_b32_e32 v62, 16, v27
	v_and_b32_e32 v63, 0xffff0000, v27
	v_pk_fma_f32 v[18:19], v[70:71], v[62:63], v[18:19]
	s_nop 0
	v_mul_f32_e32 v62, 0x3d372713, v18
	v_mul_f32_e32 v63, 0x3d372713, v19
	v_mul_f32_e32 v62, v18, v62
	v_mul_f32_e32 v63, v19, v63
	v_fma_f32 v62, v18, v62, v18
	v_fma_f32 v63, v19, v63, v19
	v_mul_f32_e32 v62, 0xc0135761, v62
	v_mul_f32_e32 v63, 0xc0135761, v63
	v_exp_f32_e32 v62, v62
	v_exp_f32_e32 v63, v63
	v_add_f32_e32 v62, 1.0, v62
	v_add_f32_e32 v63, 1.0, v63
	v_rcp_f32_e32 v62, v62
	v_rcp_f32_e32 v63, v63
	s_nop 0
	v_pk_mul_f32 v[18:19], v[18:19], v[62:63]
	v_lshlrev_b32_e32 v62, 16, v47
	v_and_b32_e32 v63, 0xffff0000, v47
	v_pk_mul_f32 v[18:19], v[18:19], v[62:63]
	v_lshlrev_b32_e32 v62, 16, v40
	v_and_b32_e32 v63, 0xffff0000, v40
	v_pk_fma_f32 v[50:51], v[50:51], v[62:63], v[54:55]
	v_lshlrev_b32_e32 v54, 16, v20
	v_and_b32_e32 v55, 0xffff0000, v20
	v_pk_fma_f32 v[14:15], v[14:15], v[54:55], v[50:51]
	v_lshlrev_b32_e32 v50, 16, v28
	v_and_b32_e32 v51, 0xffff0000, v28
	v_pk_fma_f32 v[2:3], v[2:3], v[50:51], v[14:15]
	v_lshlrev_b32_e32 v20, 16, v21
	v_mul_f32_e32 v14, 0x3d372713, v2
	v_mul_f32_e32 v15, 0x3d372713, v3
	v_mul_f32_e32 v14, v2, v14
	v_mul_f32_e32 v15, v3, v15
	v_fma_f32 v14, v2, v14, v2
	v_fma_f32 v15, v3, v15, v3
	v_mul_f32_e32 v14, 0xc0135761, v14
	v_mul_f32_e32 v15, 0xc0135761, v15
	v_exp_f32_e32 v14, v14
	v_exp_f32_e32 v15, v15
	v_and_b32_e32 v21, 0xffff0000, v21
	v_add_f32_e32 v14, 1.0, v14
	v_add_f32_e32 v15, 1.0, v15
	v_rcp_f32_e32 v14, v14
	v_rcp_f32_e32 v15, v15
	s_nop 0
	v_pk_mul_f32 v[2:3], v[2:3], v[14:15]
	v_lshlrev_b32_e32 v14, 16, v48
	v_and_b32_e32 v15, 0xffff0000, v48
	v_pk_mul_f32 v[2:3], v[2:3], v[14:15]
	v_lshlrev_b32_e32 v14, 16, v41
	v_and_b32_e32 v15, 0xffff0000, v41
	v_pk_fma_f32 v[14:15], v[52:53], v[14:15], v[56:57]
	s_nop 0
	v_pk_fma_f32 v[14:15], v[16:17], v[20:21], v[14:15]
	v_lshlrev_b32_e32 v16, 16, v29
	v_and_b32_e32 v17, 0xffff0000, v29
	v_pk_fma_f32 v[4:5], v[4:5], v[16:17], v[14:15]
	v_cvt_pk_bf16_f32 v16, v2, v3
	v_mul_f32_e32 v14, 0x3d372713, v4
	v_mul_f32_e32 v15, 0x3d372713, v5
	v_mul_f32_e32 v14, v4, v14
	v_mul_f32_e32 v15, v5, v15
	v_fma_f32 v14, v4, v14, v4
	v_fma_f32 v15, v5, v15, v5
	v_mul_f32_e32 v14, 0xc0135761, v14
	v_mul_f32_e32 v15, 0xc0135761, v15
	v_exp_f32_e32 v14, v14
	v_exp_f32_e32 v15, v15
	v_mov_b64_e32 v[2:3], s[0:1]
	v_mad_i64_i32 v[2:3], s[40:41], v0, s2, v[2:3]
	v_add_f32_e32 v14, 1.0, v14
	v_add_f32_e32 v15, 1.0, v15
	v_rcp_f32_e32 v14, v14
	v_rcp_f32_e32 v15, v15
	v_lshl_add_u64 v[2:3], v[58:59], 1, v[2:3]
	v_pk_mul_f32 v[4:5], v[4:5], v[14:15]
	v_lshlrev_b32_e32 v14, 16, v49
	v_and_b32_e32 v15, 0xffff0000, v49
	v_pk_mul_f32 v[4:5], v[4:5], v[14:15]
	v_cvt_pk_bf16_f32 v14, v60, v61
	v_cvt_pk_bf16_f32 v15, v18, v19
	v_cvt_pk_bf16_f32 v17, v4, v5
	global_store_dwordx4 v[2:3], v[14:17], off sc1
.LBB0_79:
	s_or_b64 exec, exec, s[42:43]
	s_and_saveexec_b64 s[40:41], s[38:39]
	s_cbranch_execz .LBB0_42
	v_add_u32_e32 v0, v82, v81
	v_mad_i32_i24 v2, v0, s90, v80
	v_lshl_add_u32 v54, v2, 3, v230
	v_lshrrev_b32_e32 v2, 1, v0
	v_ashrrev_i32_e32 v55, 31, v54
	v_add_u32_e32 v2, s34, v2
	v_and_b32_e32 v0, 1, v0
	v_lshlrev_b64 v[50:51], 2, v[54:55]
	v_lshl_or_b32 v0, v2, 6, v0
	v_lshl_add_u64 v[2:3], s[56:57], 0, v[50:51]
	global_load_dwordx4 v[18:21], v[2:3], off offset:16
	global_load_dwordx4 v[56:59], v[2:3], off
	v_lshl_add_u64 v[2:3], s[60:61], 0, v[50:51]
	v_lshl_add_u64 v[52:53], s[62:63], 0, v[50:51]
	v_lshl_add_u64 v[68:69], s[58:59], 0, v[50:51]
	global_load_dwordx4 v[14:17], v[2:3], off offset:16
	global_load_dwordx4 v[60:63], v[2:3], off
	s_nop 0
	global_load_dwordx4 v[2:5], v[52:53], off offset:16
	global_load_dwordx4 v[64:67], v[52:53], off
	s_nop 0
	global_load_dwordx4 v[50:53], v[68:69], off offset:16
	s_nop 0
	global_load_dwordx4 v[68:71], v[68:69], off
	v_lshlrev_b32_e32 v72, 16, v34
	v_and_b32_e32 v73, 0xffff0000, v34
	s_waitcnt vmcnt(0)
	v_pk_fma_f32 v[56:57], v[56:57], v[72:73], v[68:69]
	v_lshlrev_b32_e32 v68, 16, v22
	v_and_b32_e32 v69, 0xffff0000, v22
	v_pk_fma_f32 v[56:57], v[60:61], v[68:69], v[56:57]
	v_lshlrev_b32_e32 v60, 16, v30
	v_and_b32_e32 v61, 0xffff0000, v30
	v_pk_fma_f32 v[56:57], v[64:65], v[60:61], v[56:57]
	s_nop 0
	v_mul_f32_e32 v22, 0x3d372713, v56
	v_mul_f32_e32 v22, v56, v22
	v_fma_f32 v22, v56, v22, v56
	v_mul_f32_e32 v22, 0xc0135761, v22
	v_exp_f32_e32 v22, v22
	s_nop 0
	v_add_f32_e32 v22, 1.0, v22
	v_rcp_f32_e32 v60, v22
	v_mul_f32_e32 v22, 0x3d372713, v57
	v_mul_f32_e32 v22, v57, v22
	v_fma_f32 v22, v57, v22, v57
	v_mul_f32_e32 v22, 0xc0135761, v22
	v_exp_f32_e32 v22, v22
	s_nop 0
	v_add_f32_e32 v22, 1.0, v22
	v_rcp_f32_e32 v61, v22
	v_lshlrev_b32_e32 v22, 16, v23
	v_and_b32_e32 v23, 0xffff0000, v23
	v_pk_mul_f32 v[56:57], v[56:57], v[60:61]
	v_lshlrev_b32_e32 v60, 16, v42
	v_and_b32_e32 v61, 0xffff0000, v42
	v_pk_mul_f32 v[56:57], v[56:57], v[60:61]
	v_lshlrev_b32_e32 v60, 16, v35
	v_and_b32_e32 v61, 0xffff0000, v35
	v_pk_fma_f32 v[58:59], v[58:59], v[60:61], v[70:71]
	s_nop 0
	v_pk_fma_f32 v[22:23], v[62:63], v[22:23], v[58:59]
	v_lshlrev_b32_e32 v58, 16, v31
	v_and_b32_e32 v59, 0xffff0000, v31
	v_pk_fma_f32 v[22:23], v[66:67], v[58:59], v[22:23]
	s_nop 0
	v_mul_f32_e32 v58, 0x3d372713, v22
	v_mul_f32_e32 v59, 0x3d372713, v23
	v_mul_f32_e32 v58, v22, v58
	v_mul_f32_e32 v59, v23, v59
	v_fma_f32 v58, v22, v58, v22
	v_fma_f32 v59, v23, v59, v23
	v_mul_f32_e32 v58, 0xc0135761, v58
	v_mul_f32_e32 v59, 0xc0135761, v59
	v_exp_f32_e32 v58, v58
	v_exp_f32_e32 v59, v59
	v_add_f32_e32 v58, 1.0, v58
	v_add_f32_e32 v59, 1.0, v59
	v_rcp_f32_e32 v58, v58
	v_rcp_f32_e32 v59, v59
	s_nop 0
	v_pk_mul_f32 v[22:23], v[22:23], v[58:59]
	v_lshlrev_b32_e32 v58, 16, v43
	v_and_b32_e32 v59, 0xffff0000, v43
	v_pk_mul_f32 v[22:23], v[22:23], v[58:59]
	v_lshlrev_b32_e32 v58, 16, v36
	v_and_b32_e32 v59, 0xffff0000, v36
	v_pk_fma_f32 v[18:19], v[18:19], v[58:59], v[50:51]
	v_lshlrev_b32_e32 v50, 16, v24
	v_and_b32_e32 v51, 0xffff0000, v24
	v_pk_fma_f32 v[14:15], v[14:15], v[50:51], v[18:19]
	v_lshlrev_b32_e32 v18, 16, v32
	v_and_b32_e32 v19, 0xffff0000, v32
	v_pk_fma_f32 v[2:3], v[2:3], v[18:19], v[14:15]
	v_lshlrev_b32_e32 v18, 16, v25
	v_mul_f32_e32 v14, 0x3d372713, v2
	v_mul_f32_e32 v15, 0x3d372713, v3
	v_mul_f32_e32 v14, v2, v14
	v_mul_f32_e32 v15, v3, v15
	v_fma_f32 v14, v2, v14, v2
	v_fma_f32 v15, v3, v15, v3
	v_mul_f32_e32 v14, 0xc0135761, v14
	v_mul_f32_e32 v15, 0xc0135761, v15
	v_exp_f32_e32 v14, v14
	v_exp_f32_e32 v15, v15
	v_and_b32_e32 v19, 0xffff0000, v25
	v_add_f32_e32 v14, 1.0, v14
	v_add_f32_e32 v15, 1.0, v15
	v_rcp_f32_e32 v14, v14
	v_rcp_f32_e32 v15, v15
	s_nop 0
	v_pk_mul_f32 v[2:3], v[2:3], v[14:15]
	v_lshlrev_b32_e32 v14, 16, v44
	v_and_b32_e32 v15, 0xffff0000, v44
	v_pk_mul_f32 v[2:3], v[2:3], v[14:15]
	v_lshlrev_b32_e32 v14, 16, v37
	v_and_b32_e32 v15, 0xffff0000, v37
	v_pk_fma_f32 v[14:15], v[20:21], v[14:15], v[52:53]
	s_nop 0
	v_pk_fma_f32 v[14:15], v[16:17], v[18:19], v[14:15]
	v_lshlrev_b32_e32 v16, 16, v33
	v_and_b32_e32 v17, 0xffff0000, v33
	v_pk_fma_f32 v[4:5], v[4:5], v[16:17], v[14:15]
	v_cvt_pk_bf16_f32 v16, v2, v3
	v_mul_f32_e32 v14, 0x3d372713, v4
	v_mul_f32_e32 v15, 0x3d372713, v5
	v_mul_f32_e32 v14, v4, v14
	v_mul_f32_e32 v15, v5, v15
	v_fma_f32 v14, v4, v14, v4
	v_fma_f32 v15, v5, v15, v5
	v_mul_f32_e32 v14, 0xc0135761, v14
	v_mul_f32_e32 v15, 0xc0135761, v15
	v_exp_f32_e32 v14, v14
	v_exp_f32_e32 v15, v15
	v_mov_b64_e32 v[2:3], s[0:1]
	v_mad_i64_i32 v[2:3], s[38:39], v0, s2, v[2:3]
	v_add_f32_e32 v14, 1.0, v14
	v_add_f32_e32 v15, 1.0, v15
	v_rcp_f32_e32 v14, v14
	v_rcp_f32_e32 v15, v15
	v_lshl_add_u64 v[2:3], v[54:55], 1, v[2:3]
	v_pk_mul_f32 v[4:5], v[4:5], v[14:15]
	v_lshlrev_b32_e32 v14, 16, v45
	v_and_b32_e32 v15, 0xffff0000, v45
	v_pk_mul_f32 v[4:5], v[4:5], v[14:15]
	v_cvt_pk_bf16_f32 v14, v56, v57
	v_cvt_pk_bf16_f32 v15, v22, v23
	v_cvt_pk_bf16_f32 v17, v4, v5
	global_store_dwordx4 v[2:3], v[14:17], off sc1
	s_branch .LBB0_42

.LBB0_105:
	s_add_u32 s16, s74, 0x2200000
	v_readlane_b32 s0, v253, 39
	s_addc_u32 s17, s75, 0
	v_readlane_b32 s1, v253, 40
	s_and_b64 s[0:1], s[0:1], exec
	v_readlane_b32 s0, v253, 34
	s_cselect_b32 s14, s0, s16
	s_mov_b32 s0, -1
	v_readlane_b32 s1, v253, 35
	s_waitcnt vmcnt(0)
	s_barrier
	s_cselect_b32 s15, s1, s17
	v_mbcnt_lo_u32_b32 v0, s0, 0
	v_mbcnt_hi_u32_b32 v170, s0, v0
	s_ashr_i32 s39, s38, 31
	s_lshl_b32 s1, s62, 5
	s_lshl_b64 s[34:35], s[38:39], 8
	v_lshrrev_b32_e32 v0, 1, v170
	s_lshl_b32 s0, s91, 8
	s_or_b32 s34, s34, s1
	v_and_b32_e32 v0, 56, v0
	v_and_b32_e32 v131, 64, v231
	v_and_b32_e32 v130, 15, v170
	s_add_i32 s29, s0, s63
	v_lshl_add_u64 v[158:159], s[34:35], 0, v[0:1]
	v_xor_b32_e32 v0, 16, v231
	v_add_u32_e32 v131, 64, v131
	v_or_b32_e32 v160, s29, v130
	v_cmp_lt_i32_e32 vcc, v0, v131
	v_lshlrev_b64 v[176:177], 1, v[158:159]
	v_ashrrev_i32_e32 v161, 31, v160
	v_cndmask_b32_e32 v0, v231, v0, vcc
	v_lshlrev_b32_e32 v171, 2, v0
	v_xor_b32_e32 v0, 32, v231
	v_lshl_add_u64 v[162:163], s[16:17], 0, v[176:177]
	v_lshlrev_b64 v[178:179], 11, v[160:161]
	v_cmp_lt_i32_e32 vcc, v0, v131
	v_or_b32_e32 v182, s63, v130
	v_lshl_add_u64 v[130:131], v[162:163], 0, v[178:179]
	global_load_dwordx4 v[172:175], v[130:131], off
	global_load_dwordx4 v[154:157], v[130:131], off offset:256
	v_or_b32_e32 v130, 16, v160
	v_ashrrev_i32_e32 v131, 31, v130
	v_lshlrev_b64 v[168:169], 11, v[130:131]
	v_lshl_add_u64 v[130:131], v[162:163], 0, v[168:169]
	global_load_dwordx4 v[150:153], v[130:131], off
	global_load_dwordx4 v[146:149], v[130:131], off offset:256
	v_or_b32_e32 v130, 32, v160
	v_ashrrev_i32_e32 v131, 31, v130
	v_lshlrev_b64 v[166:167], 11, v[130:131]
	v_lshl_add_u64 v[130:131], v[162:163], 0, v[166:167]
	global_load_dwordx4 v[142:145], v[130:131], off
	global_load_dwordx4 v[138:141], v[130:131], off offset:256
	v_or_b32_e32 v130, 48, v160
	v_ashrrev_i32_e32 v131, 31, v130
	v_lshlrev_b64 v[164:165], 11, v[130:131]
	v_lshl_add_u64 v[130:131], v[162:163], 0, v[164:165]
	global_load_dwordx4 v[134:137], v[130:131], off
	s_nop 0
	global_load_dwordx4 v[130:133], v[130:131], off offset:256
	v_lshl_add_u64 v[178:179], s[14:15], 0, v[178:179]
	v_lshl_add_u64 v[176:177], v[178:179], 0, v[176:177]
	v_cndmask_b32_e32 v0, v231, v0, vcc
	v_lshlrev_b32_e32 v0, 2, v0
	s_lshl_b32 s1, s62, 2
	v_cmp_gt_u32_e32 vcc, 16, v170
	s_waitcnt vmcnt(0)
	v_lshlrev_b32_e32 v180, 16, v172
	v_and_b32_e32 v181, 0xffff0000, v172
	v_lshlrev_b32_e32 v172, 16, v173
	v_and_b32_e32 v173, 0xffff0000, v173
	v_pk_add_f32 v[128:129], v[128:129], v[172:173]
	v_lshlrev_b32_e32 v172, 16, v174
	v_and_b32_e32 v173, 0xffff0000, v174
	v_pk_add_f32 v[172:173], v[122:123], v[172:173]
	v_lshlrev_b32_e32 v122, 16, v175
	v_and_b32_e32 v123, 0xffff0000, v175
	v_pk_add_f32 v[126:127], v[126:127], v[180:181]
	v_pk_add_f32 v[174:175], v[124:125], v[122:123]
	v_cvt_pk_bf16_f32 v122, v126, v127
	v_cvt_pk_bf16_f32 v123, v128, v129
	v_cvt_pk_bf16_f32 v124, v172, v173
	v_cvt_pk_bf16_f32 v125, v174, v175
	global_store_dwordx4 v[176:177], v[122:125], off sc1
	s_nop 1
	v_pk_mul_f32 v[122:123], v[126:127], v[126:127]
	v_pk_mul_f32 v[126:127], v[172:173], v[172:173]
	v_lshlrev_b32_e32 v172, 16, v154
	v_and_b32_e32 v173, 0xffff0000, v154
	v_lshlrev_b32_e32 v154, 16, v155
	v_and_b32_e32 v155, 0xffff0000, v155
	v_pk_add_f32 v[120:121], v[120:121], v[154:155]
	v_lshlrev_b32_e32 v154, 16, v156
	v_and_b32_e32 v155, 0xffff0000, v156
	v_pk_add_f32 v[154:155], v[114:115], v[154:155]
	v_lshlrev_b32_e32 v114, 16, v157
	v_and_b32_e32 v115, 0xffff0000, v157
	v_pk_add_f32 v[118:119], v[118:119], v[172:173]
	v_pk_add_f32 v[156:157], v[116:117], v[114:115]
	v_cvt_pk_bf16_f32 v114, v118, v119
	v_cvt_pk_bf16_f32 v115, v120, v121
	v_cvt_pk_bf16_f32 v116, v154, v155
	v_cvt_pk_bf16_f32 v117, v156, v157
	global_store_dwordx4 v[176:177], v[114:117], off offset:256 sc1
	v_pk_mul_f32 v[124:125], v[128:129], v[128:129]
	v_pk_mul_f32 v[128:129], v[174:175], v[174:175]
	v_pk_mul_f32 v[114:115], v[118:119], v[118:119]
	v_pk_mul_f32 v[116:117], v[120:121], v[120:121]
	v_add_f32_e32 v114, v114, v115
	v_add_f32_e32 v116, v116, v117
	v_pk_mul_f32 v[118:119], v[154:155], v[154:155]
	v_pk_mul_f32 v[120:121], v[156:157], v[156:157]
	v_add_f32_e32 v114, v114, v116
	v_add_f32_e32 v115, v128, v129
	v_add_f32_e32 v116, v126, v127
	v_add_f32_e32 v120, v120, v121
	v_add_f32_e32 v118, v118, v119
	v_add_f32_e32 v115, v116, v115
	v_add_f32_e32 v116, v124, v125
	v_add_f32_e32 v117, v122, v123
	v_add_f32_e32 v118, v118, v120
	v_add_f32_e32 v116, v117, v116
	v_add_f32_e32 v114, v114, v118
	v_add_f32_e32 v115, v116, v115
	v_add_f32_e32 v114, v115, v114
	ds_bpermute_b32 v115, v171, v114
	s_waitcnt lgkmcnt(0)
	v_add_f32_e32 v115, v114, v115
	ds_bpermute_b32 v116, v0, v115
	v_lshl_or_b32 v114, v182, 4, s1
	s_and_saveexec_b64 s[16:17], vcc
	s_cbranch_execz .LBB0_107
	s_waitcnt lgkmcnt(0)
	v_add_f32_e32 v115, v115, v116
	ds_write_b32 v114, v115
.LBB0_107:
	s_or_b64 exec, exec, s[16:17]
	s_waitcnt lgkmcnt(0)
	v_lshlrev_b32_e32 v116, 16, v150
	v_and_b32_e32 v117, 0xffff0000, v150
	v_pk_add_f32 v[110:111], v[110:111], v[116:117]
	v_lshlrev_b32_e32 v116, 16, v151
	v_and_b32_e32 v117, 0xffff0000, v151
	v_pk_add_f32 v[112:113], v[112:113], v[116:117]
	v_lshlrev_b32_e32 v116, 16, v152
	v_and_b32_e32 v117, 0xffff0000, v152
	v_pk_add_f32 v[116:117], v[106:107], v[116:117]
	v_lshlrev_b32_e32 v106, 16, v153
	v_and_b32_e32 v107, 0xffff0000, v153
	v_pk_add_f32 v[118:119], v[108:109], v[106:107]
	v_lshl_add_u64 v[120:121], s[14:15], 0, v[168:169]
	v_cvt_pk_bf16_f32 v106, v110, v111
	v_cvt_pk_bf16_f32 v107, v112, v113
	v_cvt_pk_bf16_f32 v108, v116, v117
	v_cvt_pk_bf16_f32 v109, v118, v119
	v_lshl_add_u64 v[120:121], v[158:159], 1, v[120:121]
	global_store_dwordx4 v[120:121], v[106:109], off sc1
	s_nop 1
	v_pk_mul_f32 v[106:107], v[110:111], v[110:111]
	v_pk_mul_f32 v[110:111], v[116:117], v[116:117]
	v_lshlrev_b32_e32 v116, 16, v146
	v_and_b32_e32 v117, 0xffff0000, v146
	v_pk_add_f32 v[102:103], v[102:103], v[116:117]
	v_lshlrev_b32_e32 v116, 16, v147
	v_and_b32_e32 v117, 0xffff0000, v147
	v_pk_add_f32 v[104:105], v[104:105], v[116:117]
	v_lshlrev_b32_e32 v116, 16, v148
	v_and_b32_e32 v117, 0xffff0000, v148
	v_pk_add_f32 v[116:117], v[98:99], v[116:117]
	v_lshlrev_b32_e32 v98, 16, v149
	v_and_b32_e32 v99, 0xffff0000, v149
	v_pk_mul_f32 v[108:109], v[112:113], v[112:113]
	v_pk_mul_f32 v[112:113], v[118:119], v[118:119]
	v_pk_add_f32 v[118:119], v[100:101], v[98:99]
	v_cvt_pk_bf16_f32 v98, v102, v103
	v_cvt_pk_bf16_f32 v99, v104, v105
	v_cvt_pk_bf16_f32 v100, v116, v117
	v_cvt_pk_bf16_f32 v101, v118, v119
	global_store_dwordx4 v[120:121], v[98:101], off offset:256 sc1
	s_nop 1
	v_pk_mul_f32 v[98:99], v[102:103], v[102:103]
	v_pk_mul_f32 v[100:101], v[104:105], v[104:105]
	v_add_f32_e32 v98, v98, v99
	v_add_f32_e32 v100, v100, v101
	v_pk_mul_f32 v[102:103], v[116:117], v[116:117]
	v_pk_mul_f32 v[104:105], v[118:119], v[118:119]
	v_add_f32_e32 v98, v98, v100
	v_add_f32_e32 v99, v112, v113
	v_add_f32_e32 v100, v110, v111
	v_add_f32_e32 v104, v104, v105
	v_add_f32_e32 v102, v102, v103
	v_add_f32_e32 v99, v100, v99
	v_add_f32_e32 v100, v108, v109
	v_add_f32_e32 v101, v106, v107
	v_add_f32_e32 v102, v102, v104
	v_add_f32_e32 v100, v101, v100
	v_add_f32_e32 v98, v98, v102
	v_add_f32_e32 v99, v100, v99
	v_add_f32_e32 v98, v99, v98
	ds_bpermute_b32 v99, v171, v98
	s_waitcnt lgkmcnt(0)
	v_add_f32_e32 v98, v98, v99
	ds_bpermute_b32 v99, v0, v98
	s_and_saveexec_b64 s[16:17], vcc
	v_readlane_b32 s91, v253, 27
	v_readlane_b32 s92, v253, 28
	s_mov_b32 s89, 0x2e8ba2e9
	s_movk_i32 s90, 0xfea0
	s_movk_i32 s94, 0x2000
	v_readlane_b32 s93, v253, 29
	s_cbranch_execz .LBB0_109
	s_waitcnt lgkmcnt(0)
	v_add_f32_e32 v98, v98, v99
	ds_write_b32 v114, v98 offset:256
.LBB0_109:
	s_or_b64 exec, exec, s[16:17]
	v_lshlrev_b32_e32 v98, 16, v142
	s_waitcnt lgkmcnt(0)
	v_and_b32_e32 v99, 0xffff0000, v142
	v_pk_add_f32 v[94:95], v[94:95], v[98:99]
	v_lshlrev_b32_e32 v98, 16, v143
	v_and_b32_e32 v99, 0xffff0000, v143
	v_pk_add_f32 v[96:97], v[96:97], v[98:99]
	v_lshlrev_b32_e32 v98, 16, v144
	v_and_b32_e32 v99, 0xffff0000, v144
	v_pk_add_f32 v[98:99], v[90:91], v[98:99]
	v_lshlrev_b32_e32 v90, 16, v145
	v_and_b32_e32 v91, 0xffff0000, v145
	v_pk_add_f32 v[100:101], v[92:93], v[90:91]
	v_lshl_add_u64 v[102:103], s[14:15], 0, v[166:167]
	v_cvt_pk_bf16_f32 v90, v94, v95
	v_cvt_pk_bf16_f32 v91, v96, v97
	v_cvt_pk_bf16_f32 v92, v98, v99
	v_cvt_pk_bf16_f32 v93, v100, v101
	v_lshl_add_u64 v[102:103], v[158:159], 1, v[102:103]
	global_store_dwordx4 v[102:103], v[90:93], off sc1
	s_nop 1
	v_pk_mul_f32 v[90:91], v[94:95], v[94:95]
	v_pk_mul_f32 v[94:95], v[98:99], v[98:99]
	v_lshlrev_b32_e32 v98, 16, v138
	v_and_b32_e32 v99, 0xffff0000, v138
	v_pk_add_f32 v[86:87], v[86:87], v[98:99]
	v_lshlrev_b32_e32 v98, 16, v139
	v_and_b32_e32 v99, 0xffff0000, v139
	v_pk_add_f32 v[88:89], v[88:89], v[98:99]
	v_lshlrev_b32_e32 v98, 16, v140
	v_and_b32_e32 v99, 0xffff0000, v140
	v_pk_add_f32 v[98:99], v[82:83], v[98:99]
	v_lshlrev_b32_e32 v82, 16, v141
	v_and_b32_e32 v83, 0xffff0000, v141
	v_pk_mul_f32 v[92:93], v[96:97], v[96:97]
	v_pk_mul_f32 v[96:97], v[100:101], v[100:101]
	v_pk_add_f32 v[100:101], v[84:85], v[82:83]
	v_cvt_pk_bf16_f32 v82, v86, v87
	v_cvt_pk_bf16_f32 v83, v88, v89
	v_cvt_pk_bf16_f32 v84, v98, v99
	v_cvt_pk_bf16_f32 v85, v100, v101
	global_store_dwordx4 v[102:103], v[82:85], off offset:256 sc1
	s_nop 1
	v_pk_mul_f32 v[82:83], v[86:87], v[86:87]
	v_pk_mul_f32 v[84:85], v[88:89], v[88:89]
	v_add_f32_e32 v82, v82, v83
	v_add_f32_e32 v84, v84, v85
	v_pk_mul_f32 v[86:87], v[98:99], v[98:99]
	v_pk_mul_f32 v[88:89], v[100:101], v[100:101]
	v_add_f32_e32 v82, v82, v84
	v_add_f32_e32 v83, v96, v97
	v_add_f32_e32 v84, v94, v95
	v_add_f32_e32 v88, v88, v89
	v_add_f32_e32 v86, v86, v87
	v_add_f32_e32 v83, v84, v83
	v_add_f32_e32 v84, v92, v93
	v_add_f32_e32 v85, v90, v91
	v_add_f32_e32 v86, v86, v88
	v_add_f32_e32 v84, v85, v84
	v_add_f32_e32 v82, v82, v86
	v_add_f32_e32 v83, v84, v83
	v_add_f32_e32 v82, v83, v82
	ds_bpermute_b32 v83, v171, v82
	s_waitcnt lgkmcnt(0)
	v_add_f32_e32 v82, v82, v83
	ds_bpermute_b32 v83, v0, v82
	s_and_saveexec_b64 s[16:17], vcc
	s_cbranch_execz .LBB0_111
	s_waitcnt lgkmcnt(0)
	v_add_f32_e32 v82, v82, v83
	ds_write_b32 v114, v82 offset:512
.LBB0_111:
	s_or_b64 exec, exec, s[16:17]
	v_lshlrev_b32_e32 v82, 16, v134
	s_waitcnt lgkmcnt(0)
	v_and_b32_e32 v83, 0xffff0000, v134
	v_pk_add_f32 v[78:79], v[78:79], v[82:83]
	v_lshlrev_b32_e32 v82, 16, v135
	v_and_b32_e32 v83, 0xffff0000, v135
	v_pk_add_f32 v[80:81], v[80:81], v[82:83]
	v_lshlrev_b32_e32 v82, 16, v136
	v_and_b32_e32 v83, 0xffff0000, v136
	v_pk_add_f32 v[82:83], v[74:75], v[82:83]
	v_lshlrev_b32_e32 v74, 16, v137
	v_and_b32_e32 v75, 0xffff0000, v137
	v_pk_add_f32 v[84:85], v[76:77], v[74:75]
	v_lshl_add_u64 v[86:87], s[14:15], 0, v[164:165]
	v_cvt_pk_bf16_f32 v74, v78, v79
	v_cvt_pk_bf16_f32 v75, v80, v81
	v_cvt_pk_bf16_f32 v76, v82, v83
	v_cvt_pk_bf16_f32 v77, v84, v85
	v_lshl_add_u64 v[86:87], v[158:159], 1, v[86:87]
	global_store_dwordx4 v[86:87], v[74:77], off sc1
	s_nop 1
	v_pk_mul_f32 v[74:75], v[78:79], v[78:79]
	v_pk_mul_f32 v[78:79], v[82:83], v[82:83]
	v_lshlrev_b32_e32 v82, 16, v130
	v_and_b32_e32 v83, 0xffff0000, v130
	v_pk_add_f32 v[70:71], v[70:71], v[82:83]
	v_lshlrev_b32_e32 v82, 16, v131
	v_and_b32_e32 v83, 0xffff0000, v131
	v_pk_add_f32 v[72:73], v[72:73], v[82:83]
	v_lshlrev_b32_e32 v82, 16, v132
	v_and_b32_e32 v83, 0xffff0000, v132
	v_pk_add_f32 v[82:83], v[66:67], v[82:83]
	v_lshlrev_b32_e32 v66, 16, v133
	v_and_b32_e32 v67, 0xffff0000, v133
	v_pk_mul_f32 v[76:77], v[80:81], v[80:81]
	v_pk_mul_f32 v[80:81], v[84:85], v[84:85]
	v_pk_add_f32 v[84:85], v[68:69], v[66:67]
	v_cvt_pk_bf16_f32 v66, v70, v71
	v_cvt_pk_bf16_f32 v67, v72, v73
	v_cvt_pk_bf16_f32 v68, v82, v83
	v_cvt_pk_bf16_f32 v69, v84, v85
	global_store_dwordx4 v[86:87], v[66:69], off offset:256 sc1
	s_nop 1
	v_pk_mul_f32 v[66:67], v[70:71], v[70:71]
	v_pk_mul_f32 v[68:69], v[72:73], v[72:73]
	v_add_f32_e32 v66, v66, v67
	v_add_f32_e32 v68, v68, v69
	v_pk_mul_f32 v[70:71], v[82:83], v[82:83]
	v_pk_mul_f32 v[72:73], v[84:85], v[84:85]
	v_add_f32_e32 v66, v66, v68
	v_add_f32_e32 v67, v80, v81
	v_add_f32_e32 v68, v78, v79
	v_add_f32_e32 v72, v72, v73
	v_add_f32_e32 v70, v70, v71
	v_add_f32_e32 v67, v68, v67
	v_add_f32_e32 v68, v76, v77
	v_add_f32_e32 v69, v74, v75
	v_add_f32_e32 v70, v70, v72
	v_add_f32_e32 v68, v69, v68
	v_add_f32_e32 v66, v66, v70
	v_add_f32_e32 v67, v68, v67
	v_add_f32_e32 v66, v67, v66
	ds_bpermute_b32 v67, v171, v66
	s_waitcnt lgkmcnt(0)
	v_add_f32_e32 v66, v66, v67
	ds_bpermute_b32 v67, v0, v66
	s_and_saveexec_b64 s[16:17], vcc
	s_cbranch_execz .LBB0_113
	s_waitcnt lgkmcnt(0)
	v_add_f32_e32 v66, v66, v67
	ds_write_b32 v114, v66 offset:768
.LBB0_113:
	s_or_b64 exec, exec, s[16:17]
	s_waitcnt lgkmcnt(0)
	v_lshlrev_b64 v[66:67], 11, v[160:161]
	v_lshl_add_u64 v[104:105], v[66:67], 0, s[20:21]
	v_lshl_add_u64 v[68:69], v[162:163], 0, v[104:105]
	global_load_dwordx4 v[96:99], v[68:69], off
	global_load_dwordx4 v[100:103], v[68:69], off offset:256
	s_mov_b64 s[16:17], 0x48000
	v_lshl_add_u64 v[94:95], v[66:67], 0, s[16:17]
	s_mov_b64 s[16:17], 0x58000
	v_lshl_add_u64 v[68:69], v[162:163], 0, v[94:95]
	v_lshl_add_u64 v[92:93], v[66:67], 0, s[22:23]
	v_lshl_add_u64 v[90:91], v[66:67], 0, s[16:17]
	global_load_dwordx4 v[86:89], v[68:69], off
	global_load_dwordx4 v[82:85], v[68:69], off offset:256
	v_lshl_add_u64 v[68:69], v[162:163], 0, v[92:93]
	v_lshl_add_u64 v[66:67], v[162:163], 0, v[90:91]
	global_load_dwordx4 v[78:81], v[68:69], off
	global_load_dwordx4 v[74:77], v[68:69], off offset:256
	global_load_dwordx4 v[70:73], v[66:67], off
	s_nop 0
	global_load_dwordx4 v[66:69], v[66:67], off offset:256
	v_lshl_add_u64 v[104:105], s[14:15], 0, v[104:105]
	v_lshl_add_u64 v[104:105], v[158:159], 1, v[104:105]
	s_waitcnt vmcnt(7)
	v_lshlrev_b32_e32 v106, 16, v96
	v_and_b32_e32 v107, 0xffff0000, v96
	v_lshlrev_b32_e32 v96, 16, v97
	v_and_b32_e32 v97, 0xffff0000, v97
	v_pk_add_f32 v[64:65], v[64:65], v[96:97]
	v_lshlrev_b32_e32 v96, 16, v98
	v_and_b32_e32 v97, 0xffff0000, v98
	v_pk_add_f32 v[96:97], v[58:59], v[96:97]
	v_lshlrev_b32_e32 v58, 16, v99
	v_and_b32_e32 v59, 0xffff0000, v99
	v_pk_add_f32 v[62:63], v[62:63], v[106:107]
	v_pk_add_f32 v[98:99], v[60:61], v[58:59]
	v_cvt_pk_bf16_f32 v58, v62, v63
	v_cvt_pk_bf16_f32 v59, v64, v65
	v_cvt_pk_bf16_f32 v60, v96, v97
	v_cvt_pk_bf16_f32 v61, v98, v99
	global_store_dwordx4 v[104:105], v[58:61], off sc1
	s_nop 1
	v_pk_mul_f32 v[58:59], v[62:63], v[62:63]
	v_pk_mul_f32 v[62:63], v[96:97], v[96:97]
	s_waitcnt vmcnt(7)
	v_lshlrev_b32_e32 v96, 16, v100
	v_and_b32_e32 v97, 0xffff0000, v100
	v_pk_add_f32 v[54:55], v[54:55], v[96:97]
	v_lshlrev_b32_e32 v96, 16, v101
	v_and_b32_e32 v97, 0xffff0000, v101
	v_pk_add_f32 v[56:57], v[56:57], v[96:97]
	v_lshlrev_b32_e32 v96, 16, v102
	v_and_b32_e32 v97, 0xffff0000, v102
	v_pk_add_f32 v[96:97], v[50:51], v[96:97]
	v_lshlrev_b32_e32 v50, 16, v103
	v_and_b32_e32 v51, 0xffff0000, v103
	v_pk_mul_f32 v[60:61], v[64:65], v[64:65]
	v_pk_mul_f32 v[64:65], v[98:99], v[98:99]
	v_pk_add_f32 v[98:99], v[52:53], v[50:51]
	v_cvt_pk_bf16_f32 v50, v54, v55
	v_cvt_pk_bf16_f32 v51, v56, v57
	v_cvt_pk_bf16_f32 v52, v96, v97
	v_cvt_pk_bf16_f32 v53, v98, v99
	global_store_dwordx4 v[104:105], v[50:53], off offset:256 sc1
	s_nop 1
	v_pk_mul_f32 v[50:51], v[54:55], v[54:55]
	v_pk_mul_f32 v[52:53], v[56:57], v[56:57]
	v_add_f32_e32 v50, v50, v51
	v_add_f32_e32 v52, v52, v53
	v_pk_mul_f32 v[54:55], v[96:97], v[96:97]
	v_pk_mul_f32 v[56:57], v[98:99], v[98:99]
	v_add_f32_e32 v50, v50, v52
	v_add_f32_e32 v51, v64, v65
	v_add_f32_e32 v52, v62, v63
	v_add_f32_e32 v56, v56, v57
	v_add_f32_e32 v54, v54, v55
	v_add_f32_e32 v51, v52, v51
	v_add_f32_e32 v52, v60, v61
	v_add_f32_e32 v53, v58, v59
	v_add_f32_e32 v54, v54, v56
	v_add_f32_e32 v52, v53, v52
	v_add_f32_e32 v50, v50, v54
	v_add_f32_e32 v51, v52, v51
	v_add_f32_e32 v50, v51, v50
	ds_bpermute_b32 v51, v171, v50
	s_waitcnt lgkmcnt(0)
	v_add_f32_e32 v50, v50, v51
	ds_bpermute_b32 v51, v0, v50
	s_and_saveexec_b64 s[16:17], vcc
	s_cbranch_execz .LBB0_115
	s_waitcnt lgkmcnt(0)
	v_add_f32_e32 v50, v50, v51
	ds_write_b32 v114, v50 offset:2048
.LBB0_115:
	s_or_b64 exec, exec, s[16:17]
	s_waitcnt vmcnt(7)
	v_lshlrev_b32_e32 v50, 16, v86
	s_waitcnt lgkmcnt(0)
	v_and_b32_e32 v51, 0xffff0000, v86
	v_pk_add_f32 v[46:47], v[46:47], v[50:51]
	v_lshlrev_b32_e32 v50, 16, v87
	v_and_b32_e32 v51, 0xffff0000, v87
	v_pk_add_f32 v[48:49], v[48:49], v[50:51]
	v_lshlrev_b32_e32 v50, 16, v88
	v_and_b32_e32 v51, 0xffff0000, v88
	v_pk_add_f32 v[50:51], v[42:43], v[50:51]
	v_lshlrev_b32_e32 v42, 16, v89
	v_and_b32_e32 v43, 0xffff0000, v89
	v_pk_add_f32 v[52:53], v[44:45], v[42:43]
	v_lshl_add_u64 v[54:55], s[14:15], 0, v[94:95]
	v_cvt_pk_bf16_f32 v42, v46, v47
	v_cvt_pk_bf16_f32 v43, v48, v49
	v_cvt_pk_bf16_f32 v44, v50, v51
	v_cvt_pk_bf16_f32 v45, v52, v53
	v_lshl_add_u64 v[54:55], v[158:159], 1, v[54:55]
	global_store_dwordx4 v[54:55], v[42:45], off sc1
	s_nop 1
	v_pk_mul_f32 v[42:43], v[46:47], v[46:47]
	v_pk_mul_f32 v[46:47], v[50:51], v[50:51]
	s_waitcnt vmcnt(7)
	v_lshlrev_b32_e32 v50, 16, v82
	v_and_b32_e32 v51, 0xffff0000, v82
	v_pk_add_f32 v[38:39], v[38:39], v[50:51]
	v_lshlrev_b32_e32 v50, 16, v83
	v_and_b32_e32 v51, 0xffff0000, v83
	v_pk_add_f32 v[40:41], v[40:41], v[50:51]
	v_lshlrev_b32_e32 v50, 16, v84
	v_and_b32_e32 v51, 0xffff0000, v84
	v_pk_add_f32 v[50:51], v[34:35], v[50:51]
	v_lshlrev_b32_e32 v34, 16, v85
	v_and_b32_e32 v35, 0xffff0000, v85
	v_pk_mul_f32 v[44:45], v[48:49], v[48:49]
	v_pk_mul_f32 v[48:49], v[52:53], v[52:53]
	v_pk_add_f32 v[52:53], v[36:37], v[34:35]
	v_cvt_pk_bf16_f32 v34, v38, v39
	v_cvt_pk_bf16_f32 v35, v40, v41
	v_cvt_pk_bf16_f32 v36, v50, v51
	v_cvt_pk_bf16_f32 v37, v52, v53
	global_store_dwordx4 v[54:55], v[34:37], off offset:256 sc1
	s_nop 1
	v_pk_mul_f32 v[34:35], v[38:39], v[38:39]
	v_pk_mul_f32 v[36:37], v[40:41], v[40:41]
	v_add_f32_e32 v34, v34, v35
	v_add_f32_e32 v36, v36, v37
	v_pk_mul_f32 v[38:39], v[50:51], v[50:51]
	v_pk_mul_f32 v[40:41], v[52:53], v[52:53]
	v_add_f32_e32 v34, v34, v36
	v_add_f32_e32 v35, v48, v49
	v_add_f32_e32 v36, v46, v47
	v_add_f32_e32 v40, v40, v41
	v_add_f32_e32 v38, v38, v39
	v_add_f32_e32 v35, v36, v35
	v_add_f32_e32 v36, v44, v45
	v_add_f32_e32 v37, v42, v43
	v_add_f32_e32 v38, v38, v40
	v_add_f32_e32 v36, v37, v36
	v_add_f32_e32 v34, v34, v38
	v_add_f32_e32 v35, v36, v35
	v_add_f32_e32 v34, v35, v34
	ds_bpermute_b32 v35, v171, v34
	s_waitcnt lgkmcnt(0)
	v_add_f32_e32 v34, v34, v35
	ds_bpermute_b32 v35, v0, v34
	s_and_saveexec_b64 s[16:17], vcc
	s_cbranch_execz .LBB0_117
	s_waitcnt lgkmcnt(0)
	v_add_f32_e32 v34, v34, v35
	ds_write_b32 v114, v34 offset:2304
.LBB0_117:
	s_or_b64 exec, exec, s[16:17]
	s_waitcnt vmcnt(7)
	v_lshlrev_b32_e32 v34, 16, v78
	s_waitcnt lgkmcnt(0)
	v_and_b32_e32 v35, 0xffff0000, v78
	v_pk_add_f32 v[30:31], v[30:31], v[34:35]
	v_lshlrev_b32_e32 v34, 16, v79
	v_and_b32_e32 v35, 0xffff0000, v79
	v_pk_add_f32 v[32:33], v[32:33], v[34:35]
	v_lshlrev_b32_e32 v34, 16, v80
	v_and_b32_e32 v35, 0xffff0000, v80
	v_pk_add_f32 v[34:35], v[26:27], v[34:35]
	v_lshlrev_b32_e32 v26, 16, v81
	v_and_b32_e32 v27, 0xffff0000, v81
	v_pk_add_f32 v[36:37], v[28:29], v[26:27]
	v_lshl_add_u64 v[38:39], s[14:15], 0, v[92:93]
	v_cvt_pk_bf16_f32 v26, v30, v31
	v_cvt_pk_bf16_f32 v27, v32, v33
	v_cvt_pk_bf16_f32 v28, v34, v35
	v_cvt_pk_bf16_f32 v29, v36, v37
	v_lshl_add_u64 v[38:39], v[158:159], 1, v[38:39]
	global_store_dwordx4 v[38:39], v[26:29], off sc1
	s_nop 1
	v_pk_mul_f32 v[26:27], v[30:31], v[30:31]
	v_pk_mul_f32 v[30:31], v[34:35], v[34:35]
	s_waitcnt vmcnt(7)
	v_lshlrev_b32_e32 v34, 16, v74
	v_and_b32_e32 v35, 0xffff0000, v74
	v_pk_add_f32 v[22:23], v[22:23], v[34:35]
	v_lshlrev_b32_e32 v34, 16, v75
	v_and_b32_e32 v35, 0xffff0000, v75
	v_pk_add_f32 v[24:25], v[24:25], v[34:35]
	v_lshlrev_b32_e32 v34, 16, v76
	v_and_b32_e32 v35, 0xffff0000, v76
	v_pk_add_f32 v[34:35], v[18:19], v[34:35]
	v_lshlrev_b32_e32 v18, 16, v77
	v_and_b32_e32 v19, 0xffff0000, v77
	v_pk_mul_f32 v[28:29], v[32:33], v[32:33]
	v_pk_mul_f32 v[32:33], v[36:37], v[36:37]
	v_pk_add_f32 v[36:37], v[20:21], v[18:19]
	v_cvt_pk_bf16_f32 v18, v22, v23
	v_cvt_pk_bf16_f32 v19, v24, v25
	v_cvt_pk_bf16_f32 v20, v34, v35
	v_cvt_pk_bf16_f32 v21, v36, v37
	global_store_dwordx4 v[38:39], v[18:21], off offset:256 sc1
	s_nop 1
	v_pk_mul_f32 v[18:19], v[22:23], v[22:23]
	v_pk_mul_f32 v[20:21], v[24:25], v[24:25]
	v_add_f32_e32 v18, v18, v19
	v_add_f32_e32 v20, v20, v21
	v_pk_mul_f32 v[22:23], v[34:35], v[34:35]
	v_pk_mul_f32 v[24:25], v[36:37], v[36:37]
	v_add_f32_e32 v18, v18, v20
	v_add_f32_e32 v19, v32, v33
	v_add_f32_e32 v20, v30, v31
	v_add_f32_e32 v24, v24, v25
	v_add_f32_e32 v22, v22, v23
	v_add_f32_e32 v19, v20, v19
	v_add_f32_e32 v20, v28, v29
	v_add_f32_e32 v21, v26, v27
	v_add_f32_e32 v22, v22, v24
	v_add_f32_e32 v20, v21, v20
	v_add_f32_e32 v18, v18, v22
	v_add_f32_e32 v19, v20, v19
	v_add_f32_e32 v18, v19, v18
	ds_bpermute_b32 v19, v171, v18
	s_waitcnt lgkmcnt(0)
	v_add_f32_e32 v18, v18, v19
	ds_bpermute_b32 v19, v0, v18
	s_and_saveexec_b64 s[16:17], vcc
	s_cbranch_execz .LBB0_119
	s_waitcnt lgkmcnt(0)
	v_add_f32_e32 v18, v18, v19
	ds_write_b32 v114, v18 offset:2560
.LBB0_119:
	s_or_b64 exec, exec, s[16:17]
	s_waitcnt vmcnt(7)
	v_lshlrev_b32_e32 v18, 16, v70
	s_waitcnt lgkmcnt(0)
	v_and_b32_e32 v19, 0xffff0000, v70
	v_pk_add_f32 v[14:15], v[14:15], v[18:19]
	v_lshlrev_b32_e32 v18, 16, v71
	v_and_b32_e32 v19, 0xffff0000, v71
	v_pk_add_f32 v[16:17], v[16:17], v[18:19]
	v_lshlrev_b32_e32 v18, 16, v72
	v_and_b32_e32 v19, 0xffff0000, v72
	v_pk_add_f32 v[18:19], v[10:11], v[18:19]
	v_lshlrev_b32_e32 v10, 16, v73
	v_and_b32_e32 v11, 0xffff0000, v73
	v_pk_add_f32 v[20:21], v[12:13], v[10:11]
	v_lshl_add_u64 v[22:23], s[14:15], 0, v[90:91]
	v_cvt_pk_bf16_f32 v10, v14, v15
	v_cvt_pk_bf16_f32 v11, v16, v17
	v_cvt_pk_bf16_f32 v12, v18, v19
	v_cvt_pk_bf16_f32 v13, v20, v21
	v_lshl_add_u64 v[22:23], v[158:159], 1, v[22:23]
	global_store_dwordx4 v[22:23], v[10:13], off sc1
	s_nop 1
	v_pk_mul_f32 v[10:11], v[14:15], v[14:15]
	v_pk_mul_f32 v[14:15], v[18:19], v[18:19]
	s_waitcnt vmcnt(7)
	v_lshlrev_b32_e32 v18, 16, v66
	v_and_b32_e32 v19, 0xffff0000, v66
	v_pk_add_f32 v[6:7], v[6:7], v[18:19]
	v_lshlrev_b32_e32 v18, 16, v67
	v_and_b32_e32 v19, 0xffff0000, v67
	v_pk_add_f32 v[8:9], v[8:9], v[18:19]
	v_lshlrev_b32_e32 v18, 16, v68
	v_and_b32_e32 v19, 0xffff0000, v68
	v_pk_add_f32 v[18:19], v[2:3], v[18:19]
	v_lshlrev_b32_e32 v2, 16, v69
	v_and_b32_e32 v3, 0xffff0000, v69
	v_pk_mul_f32 v[12:13], v[16:17], v[16:17]
	v_pk_mul_f32 v[16:17], v[20:21], v[20:21]
	v_pk_add_f32 v[20:21], v[4:5], v[2:3]
	v_cvt_pk_bf16_f32 v2, v6, v7
	v_cvt_pk_bf16_f32 v3, v8, v9
	v_cvt_pk_bf16_f32 v4, v18, v19
	v_cvt_pk_bf16_f32 v5, v20, v21
	global_store_dwordx4 v[22:23], v[2:5], off offset:256 sc1
	s_nop 1
	v_pk_mul_f32 v[2:3], v[6:7], v[6:7]
	v_pk_mul_f32 v[4:5], v[8:9], v[8:9]
	v_add_f32_e32 v2, v2, v3
	v_add_f32_e32 v4, v4, v5
	v_pk_mul_f32 v[6:7], v[18:19], v[18:19]
	v_pk_mul_f32 v[8:9], v[20:21], v[20:21]
	v_add_f32_e32 v2, v2, v4
	v_add_f32_e32 v3, v16, v17
	v_add_f32_e32 v4, v14, v15
	v_add_f32_e32 v8, v8, v9
	v_add_f32_e32 v6, v6, v7
	v_add_f32_e32 v3, v4, v3
	v_add_f32_e32 v4, v12, v13
	v_add_f32_e32 v5, v10, v11
	v_add_f32_e32 v6, v6, v8
	v_add_f32_e32 v4, v5, v4
	v_add_f32_e32 v2, v2, v6
	v_add_f32_e32 v3, v4, v3
	v_add_f32_e32 v2, v3, v2
	ds_bpermute_b32 v3, v171, v2
	s_waitcnt lgkmcnt(0)
	v_add_f32_e32 v2, v2, v3
	ds_bpermute_b32 v0, v0, v2
	s_and_saveexec_b64 s[14:15], vcc
	s_cbranch_execz .LBB0_121
	s_waitcnt lgkmcnt(0)
	v_add_f32_e32 v0, v2, v0
	ds_write_b32 v114, v0 offset:2816

.LBB0_155:
	v_readlane_b32 s38, v253, 32
	s_andn2_b64 vcc, exec, s[48:49]
	s_lshl_b32 s52, s38, 14
	v_readlane_b32 s39, v253, 33
	s_cbranch_vccnz .LBB0_159
	s_and_b64 vcc, exec, s[36:37]
	s_cbranch_vccnz .LBB0_158
	v_lshrrev_b32_e32 v0, 3, v198
	v_and_b32_e32 v67, 7, v235
	v_lshlrev_b32_e32 v98, 4, v67
	v_mul_u32_u24_e32 v69, 0x84, v0
	v_add3_u32 v69, s52, v98, v69
	s_waitcnt vmcnt(7)
	v_pk_mul_f32 v[30:31], v[30:31], v[66:67] op_sel_hi:[1,0]
	ds_write2_b32 v69, v30, v31 offset1:1
	v_pk_mul_f32 v[30:31], v[32:33], v[66:67] op_sel_hi:[1,0]
	ds_write2_b32 v69, v30, v31 offset0:2 offset1:3
	v_add_u32_e32 v32, 0x420, v69
	s_waitcnt vmcnt(6)
	v_pk_mul_f32 v[30:31], v[38:39], v[68:69] op_sel_hi:[1,0]
	ds_write2_b32 v32, v30, v31 offset1:1
	v_add_u32_e32 v32, 0x428, v69
	v_pk_mul_f32 v[30:31], v[40:41], v[68:69] op_sel_hi:[1,0]
	ds_write2_b32 v32, v30, v31 offset1:1
	v_add_u32_e32 v32, 0x840, v69
	s_waitcnt vmcnt(5)
	v_pk_mul_f32 v[30:31], v[34:35], v[74:75] op_sel_hi:[1,0]
	ds_write2_b32 v32, v30, v31 offset1:1
	v_add_u32_e32 v32, 0x848, v69
	v_pk_mul_f32 v[30:31], v[36:37], v[74:75] op_sel_hi:[1,0]
	ds_write2_b32 v32, v30, v31 offset1:1
	v_add_u32_e32 v32, 0xc60, v69
	s_waitcnt vmcnt(4)
	v_pk_mul_f32 v[30:31], v[46:47], v[76:77] op_sel_hi:[1,0]
	ds_write2_b32 v32, v30, v31 offset1:1
	v_add_u32_e32 v32, 0xc68, v69
	v_pk_mul_f32 v[30:31], v[48:49], v[76:77] op_sel_hi:[1,0]
	ds_write2_b32 v32, v30, v31 offset1:1
	v_add_u32_e32 v32, 0x1080, v69
	s_waitcnt vmcnt(3)
	v_pk_mul_f32 v[30:31], v[42:43], v[82:83] op_sel_hi:[1,0]
	ds_write2_b32 v32, v30, v31 offset1:1
	v_add_u32_e32 v32, 0x1088, v69
	v_pk_mul_f32 v[30:31], v[44:45], v[82:83] op_sel_hi:[1,0]
	ds_write2_b32 v32, v30, v31 offset1:1
	v_add_u32_e32 v32, 0x14a0, v69
	s_waitcnt vmcnt(2)
	v_pk_mul_f32 v[30:31], v[54:55], v[84:85] op_sel_hi:[1,0]
	ds_write2_b32 v32, v30, v31 offset1:1
	v_add_u32_e32 v32, 0x14a8, v69
	v_pk_mul_f32 v[30:31], v[56:57], v[84:85] op_sel_hi:[1,0]
	ds_write2_b32 v32, v30, v31 offset1:1
	v_add_u32_e32 v32, 0x18c0, v69
	s_waitcnt vmcnt(1)
	v_pk_mul_f32 v[30:31], v[50:51], v[90:91] op_sel_hi:[1,0]
	ds_write2_b32 v32, v30, v31 offset1:1
	v_add_u32_e32 v32, 0x18c8, v69
	v_pk_mul_f32 v[30:31], v[52:53], v[90:91] op_sel_hi:[1,0]
	ds_write2_b32 v32, v30, v31 offset1:1
	v_add_u32_e32 v32, 0x1ce0, v69
	s_waitcnt vmcnt(0)
	v_pk_mul_f32 v[30:31], v[58:59], v[92:93] op_sel_hi:[1,0]
	ds_write2_b32 v32, v30, v31 offset1:1
	v_add_u32_e32 v32, 0x1ce8, v69
	v_pk_mul_f32 v[30:31], v[60:61], v[92:93] op_sel_hi:[1,0]
	ds_write2_b32 v32, v30, v31 offset1:1
	s_waitcnt lgkmcnt(0)
	v_mul_u32_u24_e32 v30, 0x420, v67
	v_lshlrev_b32_e32 v31, 2, v0
	v_add3_u32 v52, s52, v30, v31
	ds_read2_b32 v[34:35], v52 offset0:33 offset1:41
	ds_read2_b32 v[36:37], v52 offset1:8
	ds_read2_b32 v[38:39], v52 offset0:66 offset1:74
	ds_read2_b32 v[40:41], v52 offset0:99 offset1:107
	ds_read2_b32 v[42:43], v52 offset0:132 offset1:140
	ds_read2_b32 v[44:45], v52 offset0:165 offset1:173
	ds_read2_b32 v[46:47], v52 offset0:198 offset1:206
	ds_read2_b32 v[48:49], v52 offset0:231 offset1:239
	v_lshlrev_b32_e32 v0, 11, v0
	v_lshl_add_u64 v[50:51], s[16:17], 0, v[0:1]
	v_mov_b32_e32 v99, v1
	s_waitcnt lgkmcnt(6)
	v_cvt_pk_bf16_f32 v30, v36, v34
	s_waitcnt lgkmcnt(4)
	v_cvt_pk_bf16_f32 v31, v38, v40
	s_waitcnt lgkmcnt(2)
	v_cvt_pk_bf16_f32 v32, v42, v44
	s_waitcnt lgkmcnt(0)
	v_cvt_pk_bf16_f32 v33, v46, v48
	v_lshl_add_u64 v[50:51], v[50:51], 0, v[98:99]
	global_store_dwordx4 v[50:51], v[30:33], off sc1
	v_or_b32_e32 v34, 0x4000, v0
	s_nop 0
	v_cvt_pk_bf16_f32 v30, v37, v35
	v_cvt_pk_bf16_f32 v31, v39, v41
	v_cvt_pk_bf16_f32 v32, v43, v45
	v_cvt_pk_bf16_f32 v33, v47, v49
	v_mov_b32_e32 v35, v1
	ds_read2_b32 v[36:37], v52 offset0:49 offset1:57
	ds_read2_b32 v[38:39], v52 offset0:16 offset1:24
	ds_read2_b32 v[40:41], v52 offset0:82 offset1:90
	ds_read2_b32 v[42:43], v52 offset0:115 offset1:123
	ds_read2_b32 v[44:45], v52 offset0:148 offset1:156
	ds_read2_b32 v[46:47], v52 offset0:181 offset1:189
	ds_read2_b32 v[48:49], v52 offset0:214 offset1:222
	ds_read2_b32 v[50:51], v52 offset0:247 offset1:255
	v_lshl_add_u64 v[34:35], s[16:17], 0, v[34:35]
	v_lshl_add_u64 v[34:35], v[34:35], 0, v[98:99]
	global_store_dwordx4 v[34:35], v[30:33], off sc1
	v_or_b32_e32 v34, 0x8000, v0
	v_mov_b32_e32 v35, v1
	v_lshl_add_u64 v[34:35], s[16:17], 0, v[34:35]
	s_waitcnt lgkmcnt(6)
	v_cvt_pk_bf16_f32 v30, v38, v36
	s_waitcnt lgkmcnt(4)
	v_cvt_pk_bf16_f32 v31, v40, v42
	s_waitcnt lgkmcnt(2)
	v_cvt_pk_bf16_f32 v32, v44, v46
	s_waitcnt lgkmcnt(0)
	v_cvt_pk_bf16_f32 v33, v48, v50
	v_lshl_add_u64 v[34:35], v[34:35], 0, v[98:99]
	v_or_b32_e32 v0, 0xc000, v0
	global_store_dwordx4 v[34:35], v[30:33], off sc1
	v_lshl_add_u64 v[34:35], s[16:17], 0, v[0:1]
	v_lshl_add_u64 v[34:35], v[34:35], 0, v[98:99]
	v_cvt_pk_bf16_f32 v30, v39, v37
	v_cvt_pk_bf16_f32 v31, v41, v43
	v_cvt_pk_bf16_f32 v32, v45, v47
	v_cvt_pk_bf16_f32 v33, v49, v51
	global_store_dwordx4 v[34:35], v[30:33], off sc1
	s_waitcnt lgkmcnt(0)

.LBB0_174:
	s_andn2_b64 vcc, exec, s[38:39]
	s_cbranch_vccnz .LBB0_178
	s_cmp_eq_u32 s31, 0
	s_cbranch_scc1 .LBB0_177
	v_lshrrev_b32_e32 v0, 3, v198
	s_waitcnt vmcnt(7)
	v_and_b32_e32 v31, 7, v235
	v_lshlrev_b32_e32 v30, 4, v31
	v_mul_u32_u24_e32 v32, 0x84, v0
	v_add3_u32 v32, s52, v30, v32
	v_pk_mul_f32 v[2:3], v[2:3], v[70:71] op_sel_hi:[1,0]
	ds_write2_b32 v32, v2, v3 offset1:1
	v_pk_mul_f32 v[2:3], v[4:5], v[70:71] op_sel_hi:[1,0]
	ds_write2_b32 v32, v2, v3 offset0:2 offset1:3
	v_add_u32_e32 v4, 0x420, v32
	s_waitcnt vmcnt(6)
	v_pk_mul_f32 v[2:3], v[10:11], v[72:73] op_sel_hi:[1,0]
	ds_write2_b32 v4, v2, v3 offset1:1
	v_add_u32_e32 v4, 0x428, v32
	v_pk_mul_f32 v[2:3], v[12:13], v[72:73] op_sel_hi:[1,0]
	ds_write2_b32 v4, v2, v3 offset1:1
	v_add_u32_e32 v4, 0x840, v32
	s_waitcnt vmcnt(5)
	v_pk_mul_f32 v[2:3], v[6:7], v[78:79] op_sel_hi:[1,0]
	ds_write2_b32 v4, v2, v3 offset1:1
	v_add_u32_e32 v4, 0x848, v32
	v_pk_mul_f32 v[2:3], v[8:9], v[78:79] op_sel_hi:[1,0]
	ds_write2_b32 v4, v2, v3 offset1:1
	v_add_u32_e32 v4, 0xc60, v32
	s_waitcnt vmcnt(4)
	v_pk_mul_f32 v[2:3], v[18:19], v[80:81] op_sel_hi:[1,0]
	ds_write2_b32 v4, v2, v3 offset1:1
	v_add_u32_e32 v4, 0xc68, v32
	v_pk_mul_f32 v[2:3], v[20:21], v[80:81] op_sel_hi:[1,0]
	ds_write2_b32 v4, v2, v3 offset1:1
	v_add_u32_e32 v4, 0x1080, v32
	s_waitcnt vmcnt(3)
	v_pk_mul_f32 v[2:3], v[14:15], v[86:87] op_sel_hi:[1,0]
	ds_write2_b32 v4, v2, v3 offset1:1
	v_add_u32_e32 v4, 0x1088, v32
	v_pk_mul_f32 v[2:3], v[16:17], v[86:87] op_sel_hi:[1,0]
	ds_write2_b32 v4, v2, v3 offset1:1
	v_add_u32_e32 v4, 0x14a0, v32
	s_waitcnt vmcnt(2)
	v_pk_mul_f32 v[2:3], v[26:27], v[88:89] op_sel_hi:[1,0]
	ds_write2_b32 v4, v2, v3 offset1:1
	v_add_u32_e32 v4, 0x14a8, v32
	v_pk_mul_f32 v[2:3], v[28:29], v[88:89] op_sel_hi:[1,0]
	ds_write2_b32 v4, v2, v3 offset1:1
	v_add_u32_e32 v4, 0x18c0, v32
	s_waitcnt vmcnt(1)
	v_pk_mul_f32 v[2:3], v[22:23], v[94:95] op_sel_hi:[1,0]
	ds_write2_b32 v4, v2, v3 offset1:1
	v_add_u32_e32 v4, 0x18c8, v32
	v_pk_mul_f32 v[2:3], v[24:25], v[94:95] op_sel_hi:[1,0]
	ds_write2_b32 v4, v2, v3 offset1:1
	v_add_u32_e32 v4, 0x1ce0, v32
	s_waitcnt vmcnt(0)
	v_pk_mul_f32 v[2:3], v[62:63], v[96:97] op_sel_hi:[1,0]
	ds_write2_b32 v4, v2, v3 offset1:1
	v_add_u32_e32 v4, 0x1ce8, v32
	v_pk_mul_f32 v[2:3], v[64:65], v[96:97] op_sel_hi:[1,0]
	ds_write2_b32 v4, v2, v3 offset1:1
	s_waitcnt lgkmcnt(0)
	v_mul_u32_u24_e32 v2, 0x420, v31
	v_lshlrev_b32_e32 v3, 2, v0
	v_add3_u32 v24, s52, v2, v3
	ds_read2_b32 v[6:7], v24 offset0:33 offset1:41
	ds_read2_b32 v[8:9], v24 offset1:8
	ds_read2_b32 v[10:11], v24 offset0:66 offset1:74
	ds_read2_b32 v[12:13], v24 offset0:99 offset1:107
	ds_read2_b32 v[14:15], v24 offset0:132 offset1:140
	ds_read2_b32 v[16:17], v24 offset0:165 offset1:173
	ds_read2_b32 v[18:19], v24 offset0:198 offset1:206
	ds_read2_b32 v[20:21], v24 offset0:231 offset1:239
	v_lshlrev_b32_e32 v0, 11, v0
	v_lshl_add_u64 v[22:23], s[14:15], 0, v[0:1]
	v_mov_b32_e32 v31, v1
	s_waitcnt lgkmcnt(6)
	v_cvt_pk_bf16_f32 v2, v8, v6
	s_waitcnt lgkmcnt(4)
	v_cvt_pk_bf16_f32 v3, v10, v12
	s_waitcnt lgkmcnt(2)
	v_cvt_pk_bf16_f32 v4, v14, v16
	s_waitcnt lgkmcnt(0)
	v_cvt_pk_bf16_f32 v5, v18, v20
	v_lshl_add_u64 v[22:23], v[22:23], 0, v[30:31]
	global_store_dwordx4 v[22:23], v[2:5], off sc1
	v_or_b32_e32 v6, 0x4000, v0
	s_nop 0
	v_cvt_pk_bf16_f32 v2, v9, v7
	v_cvt_pk_bf16_f32 v3, v11, v13
	v_cvt_pk_bf16_f32 v4, v15, v17
	v_cvt_pk_bf16_f32 v5, v19, v21
	v_mov_b32_e32 v7, v1
	ds_read2_b32 v[8:9], v24 offset0:49 offset1:57
	ds_read2_b32 v[10:11], v24 offset0:16 offset1:24
	ds_read2_b32 v[12:13], v24 offset0:82 offset1:90
	ds_read2_b32 v[14:15], v24 offset0:115 offset1:123
	ds_read2_b32 v[16:17], v24 offset0:148 offset1:156
	ds_read2_b32 v[18:19], v24 offset0:181 offset1:189
	ds_read2_b32 v[20:21], v24 offset0:214 offset1:222
	ds_read2_b32 v[22:23], v24 offset0:247 offset1:255
	v_lshl_add_u64 v[6:7], s[14:15], 0, v[6:7]
	v_lshl_add_u64 v[6:7], v[6:7], 0, v[30:31]
	global_store_dwordx4 v[6:7], v[2:5], off sc1
	v_or_b32_e32 v6, 0x8000, v0
	v_mov_b32_e32 v7, v1
	v_lshl_add_u64 v[6:7], s[14:15], 0, v[6:7]
	s_waitcnt lgkmcnt(6)
	v_cvt_pk_bf16_f32 v2, v10, v8
	s_waitcnt lgkmcnt(4)
	v_cvt_pk_bf16_f32 v3, v12, v14
	s_waitcnt lgkmcnt(2)
	v_cvt_pk_bf16_f32 v4, v16, v18
	s_waitcnt lgkmcnt(0)
	v_cvt_pk_bf16_f32 v5, v20, v22
	v_lshl_add_u64 v[6:7], v[6:7], 0, v[30:31]
	v_or_b32_e32 v0, 0xc000, v0
	global_store_dwordx4 v[6:7], v[2:5], off sc1
	v_lshl_add_u64 v[6:7], s[14:15], 0, v[0:1]
	v_lshl_add_u64 v[6:7], v[6:7], 0, v[30:31]
	v_cvt_pk_bf16_f32 v2, v11, v9
	v_cvt_pk_bf16_f32 v3, v13, v15
	v_cvt_pk_bf16_f32 v4, v17, v19
	v_cvt_pk_bf16_f32 v5, v21, v23
	global_store_dwordx4 v[6:7], v[2:5], off sc1
	s_waitcnt lgkmcnt(0)

.LBB0_193:
	s_andn2_b64 vcc, exec, s[38:39]
	s_cbranch_vccnz .LBB0_197
	s_cmp_eq_u32 s31, 0
	s_cbranch_scc1 .LBB0_196
	v_lshrrev_b32_e32 v0, 3, v198
	s_waitcnt vmcnt(0)
	v_and_b32_e32 v63, 7, v235
	v_lshlrev_b32_e32 v62, 4, v63
	v_mul_u32_u24_e32 v64, 0x84, v0
	v_add3_u32 v64, s52, v62, v64
	v_pk_mul_f32 v[34:35], v[34:35], v[74:75] op_sel_hi:[1,0]
	ds_write2_b32 v64, v34, v35 offset1:1
	v_pk_mul_f32 v[34:35], v[36:37], v[74:75] op_sel_hi:[1,0]
	ds_write2_b32 v64, v34, v35 offset0:2 offset1:3
	v_add_u32_e32 v36, 0x420, v64
	v_pk_mul_f32 v[34:35], v[42:43], v[76:77] op_sel_hi:[1,0]
	ds_write2_b32 v36, v34, v35 offset1:1
	v_add_u32_e32 v36, 0x428, v64
	v_pk_mul_f32 v[34:35], v[44:45], v[76:77] op_sel_hi:[1,0]
	ds_write2_b32 v36, v34, v35 offset1:1
	v_add_u32_e32 v36, 0x840, v64
	v_pk_mul_f32 v[34:35], v[38:39], v[82:83] op_sel_hi:[1,0]
	ds_write2_b32 v36, v34, v35 offset1:1
	v_add_u32_e32 v36, 0x848, v64
	v_pk_mul_f32 v[34:35], v[40:41], v[82:83] op_sel_hi:[1,0]
	ds_write2_b32 v36, v34, v35 offset1:1
	v_add_u32_e32 v36, 0xc60, v64
	v_pk_mul_f32 v[34:35], v[50:51], v[84:85] op_sel_hi:[1,0]
	ds_write2_b32 v36, v34, v35 offset1:1
	v_add_u32_e32 v36, 0xc68, v64
	v_pk_mul_f32 v[34:35], v[52:53], v[84:85] op_sel_hi:[1,0]
	ds_write2_b32 v36, v34, v35 offset1:1
	v_add_u32_e32 v36, 0x1080, v64
	v_pk_mul_f32 v[34:35], v[46:47], v[90:91] op_sel_hi:[1,0]
	ds_write2_b32 v36, v34, v35 offset1:1
	v_add_u32_e32 v36, 0x1088, v64
	v_pk_mul_f32 v[34:35], v[48:49], v[90:91] op_sel_hi:[1,0]
	ds_write2_b32 v36, v34, v35 offset1:1
	v_add_u32_e32 v36, 0x14a0, v64
	v_pk_mul_f32 v[34:35], v[58:59], v[92:93] op_sel_hi:[1,0]
	ds_write2_b32 v36, v34, v35 offset1:1
	v_add_u32_e32 v36, 0x14a8, v64
	v_pk_mul_f32 v[34:35], v[60:61], v[92:93] op_sel_hi:[1,0]
	ds_write2_b32 v36, v34, v35 offset1:1
	v_add_u32_e32 v36, 0x18c0, v64
	v_pk_mul_f32 v[34:35], v[54:55], v[98:99] op_sel_hi:[1,0]
	ds_write2_b32 v36, v34, v35 offset1:1
	v_add_u32_e32 v36, 0x18c8, v64
	v_pk_mul_f32 v[34:35], v[56:57], v[98:99] op_sel_hi:[1,0]
	ds_write2_b32 v36, v34, v35 offset1:1
	v_add_u32_e32 v36, 0x1ce0, v64
	v_pk_mul_f32 v[34:35], v[66:67], v[100:101] op_sel_hi:[1,0]
	ds_write2_b32 v36, v34, v35 offset1:1
	v_add_u32_e32 v36, 0x1ce8, v64
	v_pk_mul_f32 v[34:35], v[68:69], v[100:101] op_sel_hi:[1,0]
	ds_write2_b32 v36, v34, v35 offset1:1
	s_waitcnt lgkmcnt(0)
	v_mul_u32_u24_e32 v34, 0x420, v63
	v_lshlrev_b32_e32 v35, 2, v0
	v_add3_u32 v56, s52, v34, v35
	ds_read2_b32 v[38:39], v56 offset0:33 offset1:41
	ds_read2_b32 v[40:41], v56 offset1:8
	ds_read2_b32 v[42:43], v56 offset0:66 offset1:74
	ds_read2_b32 v[44:45], v56 offset0:99 offset1:107
	ds_read2_b32 v[46:47], v56 offset0:132 offset1:140
	ds_read2_b32 v[48:49], v56 offset0:165 offset1:173
	ds_read2_b32 v[50:51], v56 offset0:198 offset1:206
	ds_read2_b32 v[52:53], v56 offset0:231 offset1:239
	v_lshlrev_b32_e32 v0, 11, v0
	v_lshl_add_u64 v[54:55], s[16:17], 0, v[0:1]
	v_mov_b32_e32 v63, v1
	s_waitcnt lgkmcnt(6)
	v_cvt_pk_bf16_f32 v34, v40, v38
	s_waitcnt lgkmcnt(4)
	v_cvt_pk_bf16_f32 v35, v42, v44
	s_waitcnt lgkmcnt(2)
	v_cvt_pk_bf16_f32 v36, v46, v48
	s_waitcnt lgkmcnt(0)
	v_cvt_pk_bf16_f32 v37, v50, v52
	v_lshl_add_u64 v[54:55], v[54:55], 0, v[62:63]
	global_store_dwordx4 v[54:55], v[34:37], off sc1
	v_or_b32_e32 v38, 0x4000, v0
	s_nop 0
	v_cvt_pk_bf16_f32 v34, v41, v39
	v_cvt_pk_bf16_f32 v35, v43, v45
	v_cvt_pk_bf16_f32 v36, v47, v49
	v_cvt_pk_bf16_f32 v37, v51, v53
	v_mov_b32_e32 v39, v1
	ds_read2_b32 v[40:41], v56 offset0:49 offset1:57
	ds_read2_b32 v[42:43], v56 offset0:16 offset1:24
	ds_read2_b32 v[44:45], v56 offset0:82 offset1:90
	ds_read2_b32 v[46:47], v56 offset0:115 offset1:123
	ds_read2_b32 v[48:49], v56 offset0:148 offset1:156
	ds_read2_b32 v[50:51], v56 offset0:181 offset1:189
	ds_read2_b32 v[52:53], v56 offset0:214 offset1:222
	ds_read2_b32 v[54:55], v56 offset0:247 offset1:255
	v_lshl_add_u64 v[38:39], s[16:17], 0, v[38:39]
	v_lshl_add_u64 v[38:39], v[38:39], 0, v[62:63]
	global_store_dwordx4 v[38:39], v[34:37], off sc1
	v_or_b32_e32 v38, 0x8000, v0
	v_mov_b32_e32 v39, v1
	v_lshl_add_u64 v[38:39], s[16:17], 0, v[38:39]
	s_waitcnt lgkmcnt(6)
	v_cvt_pk_bf16_f32 v34, v42, v40
	s_waitcnt lgkmcnt(4)
	v_cvt_pk_bf16_f32 v35, v44, v46
	s_waitcnt lgkmcnt(2)
	v_cvt_pk_bf16_f32 v36, v48, v50
	s_waitcnt lgkmcnt(0)
	v_cvt_pk_bf16_f32 v37, v52, v54
	v_lshl_add_u64 v[38:39], v[38:39], 0, v[62:63]
	v_or_b32_e32 v0, 0xc000, v0
	global_store_dwordx4 v[38:39], v[34:37], off sc1
	v_lshl_add_u64 v[38:39], s[16:17], 0, v[0:1]
	v_lshl_add_u64 v[38:39], v[38:39], 0, v[62:63]
	v_cvt_pk_bf16_f32 v34, v43, v41
	v_cvt_pk_bf16_f32 v35, v45, v47
	v_cvt_pk_bf16_f32 v36, v49, v51
	v_cvt_pk_bf16_f32 v37, v53, v55
	global_store_dwordx4 v[38:39], v[34:37], off sc1
	s_waitcnt lgkmcnt(0)

.LBB0_215:
	s_andn2_b64 vcc, exec, s[50:51]
	s_cbranch_vccnz .LBB0_219
	s_cmp_eq_u32 s31, 0
	s_cbranch_scc1 .LBB0_218
	s_waitcnt vmcnt(6)
	v_pk_mul_f32 v[2:3], v[120:121], v[2:3] op_sel_hi:[0,1]
	ds_write2_b32 v101, v2, v3 offset1:1
	v_pk_mul_f32 v[2:3], v[120:121], v[4:5] op_sel_hi:[0,1]
	ds_write2_b32 v101, v2, v3 offset0:2 offset1:3
	s_waitcnt vmcnt(7)
	v_pk_mul_f32 v[2:3], v[118:119], v[10:11] op_sel_hi:[0,1]
	v_add_u32_e32 v0, 0x420, v101
	ds_write2_b32 v0, v2, v3 offset1:1
	v_pk_mul_f32 v[2:3], v[118:119], v[12:13] op_sel_hi:[0,1]
	v_add_u32_e32 v0, 0x428, v101
	ds_write2_b32 v0, v2, v3 offset1:1
	s_waitcnt vmcnt(6)
	v_pk_mul_f32 v[2:3], v[124:125], v[6:7] op_sel_hi:[0,1]
	v_add_u32_e32 v0, 0x840, v101
	ds_write2_b32 v0, v2, v3 offset1:1
	v_pk_mul_f32 v[2:3], v[124:125], v[8:9] op_sel_hi:[0,1]
	v_add_u32_e32 v0, 0x848, v101
	ds_write2_b32 v0, v2, v3 offset1:1
	s_waitcnt vmcnt(5)
	v_pk_mul_f32 v[2:3], v[122:123], v[22:23] op_sel_hi:[0,1]
	v_add_u32_e32 v0, 0xc60, v101
	ds_write2_b32 v0, v2, v3 offset1:1
	v_pk_mul_f32 v[2:3], v[122:123], v[24:25] op_sel_hi:[0,1]
	v_add_u32_e32 v0, 0xc68, v101
	ds_write2_b32 v0, v2, v3 offset1:1
	s_waitcnt vmcnt(4)
	v_pk_mul_f32 v[2:3], v[128:129], v[14:15] op_sel_hi:[0,1]
	v_add_u32_e32 v0, 0x1080, v101
	ds_write2_b32 v0, v2, v3 offset1:1
	v_pk_mul_f32 v[2:3], v[128:129], v[16:17] op_sel_hi:[0,1]
	v_add_u32_e32 v0, 0x1088, v101
	ds_write2_b32 v0, v2, v3 offset1:1
	s_waitcnt vmcnt(5)
	v_pk_mul_f32 v[2:3], v[126:127], v[26:27] op_sel_hi:[0,1]
	v_add_u32_e32 v0, 0x14a0, v101
	ds_write2_b32 v0, v2, v3 offset1:1
	v_pk_mul_f32 v[2:3], v[126:127], v[28:29] op_sel_hi:[0,1]
	v_add_u32_e32 v0, 0x14a8, v101
	ds_write2_b32 v0, v2, v3 offset1:1
	s_waitcnt vmcnt(4)
	v_pk_mul_f32 v[2:3], v[132:133], v[18:19] op_sel_hi:[0,1]
	v_add_u32_e32 v0, 0x18c0, v101
	ds_write2_b32 v0, v2, v3 offset1:1
	v_pk_mul_f32 v[2:3], v[132:133], v[20:21] op_sel_hi:[0,1]
	v_add_u32_e32 v0, 0x18c8, v101
	ds_write2_b32 v0, v2, v3 offset1:1
	s_waitcnt vmcnt(0)
	v_pk_mul_f32 v[2:3], v[130:131], v[30:31] op_sel_hi:[0,1]
	v_add_u32_e32 v0, 0x1ce0, v101
	ds_write2_b32 v0, v2, v3 offset1:1
	v_pk_mul_f32 v[2:3], v[130:131], v[32:33] op_sel_hi:[0,1]
	v_add_u32_e32 v0, 0x1ce8, v101
	ds_write2_b32 v0, v2, v3 offset1:1
	s_waitcnt lgkmcnt(0)
	ds_read2_b32 v[6:7], v99 offset0:33 offset1:41
	ds_read2_b32 v[8:9], v99 offset1:8
	ds_read2_b32 v[10:11], v99 offset0:66 offset1:74
	ds_read2_b32 v[12:13], v99 offset0:99 offset1:107
	ds_read2_b32 v[14:15], v99 offset0:132 offset1:140
	ds_read2_b32 v[16:17], v99 offset0:165 offset1:173
	ds_read2_b32 v[18:19], v99 offset0:198 offset1:206
	ds_read2_b32 v[20:21], v99 offset0:231 offset1:239
	v_lshl_add_u64 v[22:23], s[14:15], 0, v[116:117]
	v_lshlrev_b32_e32 v0, 1, v106
	s_waitcnt lgkmcnt(6)
	v_cvt_pk_bf16_f32 v2, v8, v6
	s_waitcnt lgkmcnt(4)
	v_cvt_pk_bf16_f32 v3, v10, v12
	s_waitcnt lgkmcnt(2)
	v_cvt_pk_bf16_f32 v4, v14, v16
	s_waitcnt lgkmcnt(0)
	v_cvt_pk_bf16_f32 v5, v18, v20
	v_lshl_add_u64 v[22:23], v[22:23], 0, v[0:1]
	global_store_dwordx4 v[22:23], v[2:5], off sc1
	s_nop 1
	v_cvt_pk_bf16_f32 v2, v9, v7
	v_cvt_pk_bf16_f32 v3, v11, v13
	v_cvt_pk_bf16_f32 v4, v15, v17
	v_cvt_pk_bf16_f32 v5, v19, v21
	ds_read2_b32 v[8:9], v99 offset0:49 offset1:57
	ds_read2_b32 v[10:11], v99 offset0:16 offset1:24
	ds_read2_b32 v[12:13], v99 offset0:82 offset1:90
	ds_read2_b32 v[14:15], v99 offset0:115 offset1:123
	ds_read2_b32 v[16:17], v99 offset0:148 offset1:156
	ds_read2_b32 v[18:19], v99 offset0:181 offset1:189
	ds_read2_b32 v[20:21], v99 offset0:214 offset1:222
	ds_read2_b32 v[22:23], v99 offset0:247 offset1:255
	v_lshl_add_u64 v[6:7], s[14:15], 0, v[114:115]
	v_lshl_add_u64 v[6:7], v[6:7], 0, v[0:1]
	global_store_dwordx4 v[6:7], v[2:5], off sc1
	v_lshl_add_u64 v[6:7], s[14:15], 0, v[112:113]
	v_lshl_add_u64 v[6:7], v[6:7], 0, v[0:1]
	s_waitcnt lgkmcnt(6)
	v_cvt_pk_bf16_f32 v2, v10, v8
	s_waitcnt lgkmcnt(4)
	v_cvt_pk_bf16_f32 v3, v12, v14
	s_waitcnt lgkmcnt(2)
	v_cvt_pk_bf16_f32 v4, v16, v18
	s_waitcnt lgkmcnt(0)
	v_cvt_pk_bf16_f32 v5, v20, v22
	global_store_dwordx4 v[6:7], v[2:5], off sc1
	v_lshl_add_u64 v[6:7], s[14:15], 0, v[110:111]
	v_lshl_add_u64 v[6:7], v[6:7], 0, v[0:1]
	v_cvt_pk_bf16_f32 v2, v11, v9
	v_cvt_pk_bf16_f32 v3, v13, v15
	v_cvt_pk_bf16_f32 v4, v17, v19
	v_cvt_pk_bf16_f32 v5, v21, v23
	global_store_dwordx4 v[6:7], v[2:5], off sc1
	s_waitcnt lgkmcnt(0)

.LBB0_233:
	s_andn2_b64 vcc, exec, s[50:51]
	s_cbranch_vccnz .LBB0_200
	s_cmp_eq_u32 s31, 0
	s_cbranch_scc1 .LBB0_199
	s_waitcnt vmcnt(6)
	v_pk_mul_f32 v[2:3], v[2:3], v[120:121] op_sel_hi:[1,0]
	ds_write2_b32 v101, v2, v3 offset1:1
	v_pk_mul_f32 v[2:3], v[4:5], v[120:121] op_sel_hi:[1,0]
	ds_write2_b32 v101, v2, v3 offset0:2 offset1:3
	v_pk_mul_f32 v[2:3], v[10:11], v[118:119] op_sel_hi:[1,0]
	v_add_u32_e32 v0, 0x420, v101
	ds_write2_b32 v0, v2, v3 offset1:1
	v_pk_mul_f32 v[2:3], v[12:13], v[118:119] op_sel_hi:[1,0]
	v_add_u32_e32 v0, 0x428, v101
	ds_write2_b32 v0, v2, v3 offset1:1
	v_pk_mul_f32 v[2:3], v[6:7], v[124:125] op_sel_hi:[1,0]
	v_add_u32_e32 v0, 0x840, v101
	ds_write2_b32 v0, v2, v3 offset1:1
	v_pk_mul_f32 v[2:3], v[8:9], v[124:125] op_sel_hi:[1,0]
	v_add_u32_e32 v0, 0x848, v101
	ds_write2_b32 v0, v2, v3 offset1:1
	s_waitcnt vmcnt(5)
	v_pk_mul_f32 v[2:3], v[22:23], v[122:123] op_sel_hi:[1,0]
	v_add_u32_e32 v0, 0xc60, v101
	ds_write2_b32 v0, v2, v3 offset1:1
	v_pk_mul_f32 v[2:3], v[24:25], v[122:123] op_sel_hi:[1,0]
	v_add_u32_e32 v0, 0xc68, v101
	ds_write2_b32 v0, v2, v3 offset1:1
	s_waitcnt vmcnt(4)
	v_pk_mul_f32 v[2:3], v[14:15], v[128:129] op_sel_hi:[1,0]
	v_add_u32_e32 v0, 0x1080, v101
	ds_write2_b32 v0, v2, v3 offset1:1
	v_pk_mul_f32 v[2:3], v[16:17], v[128:129] op_sel_hi:[1,0]
	v_add_u32_e32 v0, 0x1088, v101
	ds_write2_b32 v0, v2, v3 offset1:1
	v_pk_mul_f32 v[2:3], v[26:27], v[126:127] op_sel_hi:[1,0]
	v_add_u32_e32 v0, 0x14a0, v101
	ds_write2_b32 v0, v2, v3 offset1:1
	v_pk_mul_f32 v[2:3], v[28:29], v[126:127] op_sel_hi:[1,0]
	v_add_u32_e32 v0, 0x14a8, v101
	ds_write2_b32 v0, v2, v3 offset1:1
	v_pk_mul_f32 v[2:3], v[18:19], v[132:133] op_sel_hi:[1,0]
	v_add_u32_e32 v0, 0x18c0, v101
	ds_write2_b32 v0, v2, v3 offset1:1
	v_pk_mul_f32 v[2:3], v[20:21], v[132:133] op_sel_hi:[1,0]
	v_add_u32_e32 v0, 0x18c8, v101
	ds_write2_b32 v0, v2, v3 offset1:1
	s_waitcnt vmcnt(0)
	v_pk_mul_f32 v[2:3], v[30:31], v[130:131] op_sel_hi:[1,0]
	v_add_u32_e32 v0, 0x1ce0, v101
	ds_write2_b32 v0, v2, v3 offset1:1
	v_pk_mul_f32 v[2:3], v[32:33], v[130:131] op_sel_hi:[1,0]
	v_add_u32_e32 v0, 0x1ce8, v101
	ds_write2_b32 v0, v2, v3 offset1:1
	s_waitcnt lgkmcnt(0)
	ds_read2_b32 v[6:7], v99 offset0:33 offset1:41
	ds_read2_b32 v[8:9], v99 offset1:8
	ds_read2_b32 v[10:11], v99 offset0:66 offset1:74
	ds_read2_b32 v[12:13], v99 offset0:99 offset1:107
	ds_read2_b32 v[14:15], v99 offset0:132 offset1:140
	ds_read2_b32 v[16:17], v99 offset0:165 offset1:173
	ds_read2_b32 v[18:19], v99 offset0:198 offset1:206
	ds_read2_b32 v[20:21], v99 offset0:231 offset1:239
	v_lshl_add_u64 v[22:23], s[14:15], 0, v[116:117]
	v_lshlrev_b32_e32 v0, 1, v106
	s_waitcnt lgkmcnt(6)
	v_cvt_pk_bf16_f32 v2, v8, v6
	s_waitcnt lgkmcnt(4)
	v_cvt_pk_bf16_f32 v3, v10, v12
	s_waitcnt lgkmcnt(2)
	v_cvt_pk_bf16_f32 v4, v14, v16
	s_waitcnt lgkmcnt(0)
	v_cvt_pk_bf16_f32 v5, v18, v20
	v_lshl_add_u64 v[22:23], v[22:23], 0, v[0:1]
	global_store_dwordx4 v[22:23], v[2:5], off sc1
	s_nop 1
	v_cvt_pk_bf16_f32 v2, v9, v7
	v_cvt_pk_bf16_f32 v3, v11, v13
	v_cvt_pk_bf16_f32 v4, v15, v17
	v_cvt_pk_bf16_f32 v5, v19, v21
	ds_read2_b32 v[8:9], v99 offset0:49 offset1:57
	ds_read2_b32 v[10:11], v99 offset0:16 offset1:24
	ds_read2_b32 v[12:13], v99 offset0:82 offset1:90
	ds_read2_b32 v[14:15], v99 offset0:115 offset1:123
	ds_read2_b32 v[16:17], v99 offset0:148 offset1:156
	ds_read2_b32 v[18:19], v99 offset0:181 offset1:189
	ds_read2_b32 v[20:21], v99 offset0:214 offset1:222
	ds_read2_b32 v[22:23], v99 offset0:247 offset1:255
	v_lshl_add_u64 v[6:7], s[14:15], 0, v[114:115]
	v_lshl_add_u64 v[6:7], v[6:7], 0, v[0:1]
	global_store_dwordx4 v[6:7], v[2:5], off sc1
	v_lshl_add_u64 v[6:7], s[14:15], 0, v[112:113]
	v_lshl_add_u64 v[6:7], v[6:7], 0, v[0:1]
	s_waitcnt lgkmcnt(6)
	v_cvt_pk_bf16_f32 v2, v10, v8
	s_waitcnt lgkmcnt(4)
	v_cvt_pk_bf16_f32 v3, v12, v14
	s_waitcnt lgkmcnt(2)
	v_cvt_pk_bf16_f32 v4, v16, v18
	s_waitcnt lgkmcnt(0)
	v_cvt_pk_bf16_f32 v5, v20, v22
	global_store_dwordx4 v[6:7], v[2:5], off sc1
	v_lshl_add_u64 v[6:7], s[14:15], 0, v[110:111]
	v_lshl_add_u64 v[6:7], v[6:7], 0, v[0:1]
	v_cvt_pk_bf16_f32 v2, v11, v9
	v_cvt_pk_bf16_f32 v3, v13, v15
	v_cvt_pk_bf16_f32 v4, v17, v19
	v_cvt_pk_bf16_f32 v5, v21, v23
	global_store_dwordx4 v[6:7], v[2:5], off sc1
	s_waitcnt lgkmcnt(0)
	s_branch .LBB0_199

.LBB0_258:
	s_and_b64 vcc, exec, s[38:39]
	s_cbranch_vccz .LBB0_262
	s_cmp_eq_u32 s31, 0
	s_cbranch_scc1 .LBB0_261
	s_waitcnt vmcnt(6)
	v_pk_mul_f32 v[2:3], v[2:3], v[120:121] op_sel_hi:[1,0]
	ds_write2_b32 v101, v2, v3 offset1:1
	v_pk_mul_f32 v[2:3], v[4:5], v[120:121] op_sel_hi:[1,0]
	ds_write2_b32 v101, v2, v3 offset0:2 offset1:3
	v_pk_mul_f32 v[2:3], v[10:11], v[118:119] op_sel_hi:[1,0]
	v_add_u32_e32 v4, 0x420, v101
	ds_write2_b32 v4, v2, v3 offset1:1
	v_pk_mul_f32 v[2:3], v[12:13], v[118:119] op_sel_hi:[1,0]
	v_add_u32_e32 v4, 0x428, v101
	ds_write2_b32 v4, v2, v3 offset1:1
	v_pk_mul_f32 v[2:3], v[6:7], v[124:125] op_sel_hi:[1,0]
	v_add_u32_e32 v4, 0x840, v101
	ds_write2_b32 v4, v2, v3 offset1:1
	v_pk_mul_f32 v[2:3], v[8:9], v[124:125] op_sel_hi:[1,0]
	v_add_u32_e32 v4, 0x848, v101
	ds_write2_b32 v4, v2, v3 offset1:1
	s_waitcnt vmcnt(5)
	v_pk_mul_f32 v[2:3], v[22:23], v[122:123] op_sel_hi:[1,0]
	v_add_u32_e32 v4, 0xc60, v101
	ds_write2_b32 v4, v2, v3 offset1:1
	v_pk_mul_f32 v[2:3], v[24:25], v[122:123] op_sel_hi:[1,0]
	v_add_u32_e32 v4, 0xc68, v101
	ds_write2_b32 v4, v2, v3 offset1:1
	s_waitcnt vmcnt(4)
	v_pk_mul_f32 v[2:3], v[14:15], v[128:129] op_sel_hi:[1,0]
	v_add_u32_e32 v4, 0x1080, v101
	ds_write2_b32 v4, v2, v3 offset1:1
	v_pk_mul_f32 v[2:3], v[16:17], v[128:129] op_sel_hi:[1,0]
	v_add_u32_e32 v4, 0x1088, v101
	ds_write2_b32 v4, v2, v3 offset1:1
	v_pk_mul_f32 v[2:3], v[26:27], v[126:127] op_sel_hi:[1,0]
	v_add_u32_e32 v4, 0x14a0, v101
	ds_write2_b32 v4, v2, v3 offset1:1
	v_pk_mul_f32 v[2:3], v[28:29], v[126:127] op_sel_hi:[1,0]
	v_add_u32_e32 v4, 0x14a8, v101
	ds_write2_b32 v4, v2, v3 offset1:1
	v_pk_mul_f32 v[2:3], v[18:19], v[132:133] op_sel_hi:[1,0]
	v_add_u32_e32 v4, 0x18c0, v101
	ds_write2_b32 v4, v2, v3 offset1:1
	v_pk_mul_f32 v[2:3], v[20:21], v[132:133] op_sel_hi:[1,0]
	v_add_u32_e32 v4, 0x18c8, v101
	ds_write2_b32 v4, v2, v3 offset1:1
	s_waitcnt vmcnt(0)
	v_pk_mul_f32 v[2:3], v[30:31], v[130:131] op_sel_hi:[1,0]
	v_add_u32_e32 v4, 0x1ce0, v101
	ds_write2_b32 v4, v2, v3 offset1:1
	v_pk_mul_f32 v[2:3], v[32:33], v[130:131] op_sel_hi:[1,0]
	v_add_u32_e32 v4, 0x1ce8, v101
	ds_write2_b32 v4, v2, v3 offset1:1
	s_waitcnt lgkmcnt(0)
	ds_read2_b32 v[6:7], v99 offset0:33 offset1:41
	ds_read2_b32 v[8:9], v99 offset1:8
	ds_read2_b32 v[10:11], v99 offset0:66 offset1:74
	ds_read2_b32 v[12:13], v99 offset0:99 offset1:107
	ds_read2_b32 v[14:15], v99 offset0:132 offset1:140
	ds_read2_b32 v[16:17], v99 offset0:165 offset1:173
	ds_read2_b32 v[18:19], v99 offset0:198 offset1:206
	ds_read2_b32 v[20:21], v99 offset0:231 offset1:239
	v_lshl_add_u64 v[22:23], s[14:15], 0, v[116:117]
	v_lshlrev_b32_e32 v24, 1, v106
	v_mov_b32_e32 v25, v1
	s_waitcnt lgkmcnt(6)
	v_cvt_pk_bf16_f32 v2, v8, v6
	s_waitcnt lgkmcnt(4)
	v_cvt_pk_bf16_f32 v3, v10, v12
	s_waitcnt lgkmcnt(2)
	v_cvt_pk_bf16_f32 v4, v14, v16
	s_waitcnt lgkmcnt(0)
	v_cvt_pk_bf16_f32 v5, v18, v20
	v_lshl_add_u64 v[22:23], v[22:23], 0, v[24:25]
	global_store_dwordx4 v[22:23], v[2:5], off sc1
	s_nop 1
	v_cvt_pk_bf16_f32 v2, v9, v7
	v_cvt_pk_bf16_f32 v3, v11, v13
	v_cvt_pk_bf16_f32 v4, v15, v17
	v_cvt_pk_bf16_f32 v5, v19, v21
	ds_read2_b32 v[8:9], v99 offset0:49 offset1:57
	ds_read2_b32 v[10:11], v99 offset0:16 offset1:24
	ds_read2_b32 v[12:13], v99 offset0:82 offset1:90
	ds_read2_b32 v[14:15], v99 offset0:115 offset1:123
	ds_read2_b32 v[16:17], v99 offset0:148 offset1:156
	ds_read2_b32 v[18:19], v99 offset0:181 offset1:189
	ds_read2_b32 v[20:21], v99 offset0:214 offset1:222
	ds_read2_b32 v[22:23], v99 offset0:247 offset1:255
	v_lshl_add_u64 v[6:7], s[14:15], 0, v[114:115]
	v_lshl_add_u64 v[6:7], v[6:7], 0, v[24:25]
	global_store_dwordx4 v[6:7], v[2:5], off sc1
	v_lshl_add_u64 v[6:7], s[14:15], 0, v[112:113]
	v_lshl_add_u64 v[6:7], v[6:7], 0, v[24:25]
	s_waitcnt lgkmcnt(6)
	v_cvt_pk_bf16_f32 v2, v10, v8
	s_waitcnt lgkmcnt(4)
	v_cvt_pk_bf16_f32 v3, v12, v14
	s_waitcnt lgkmcnt(2)
	v_cvt_pk_bf16_f32 v4, v16, v18
	s_waitcnt lgkmcnt(0)
	v_cvt_pk_bf16_f32 v5, v20, v22
	global_store_dwordx4 v[6:7], v[2:5], off sc1
	v_lshl_add_u64 v[6:7], s[14:15], 0, v[110:111]
	v_lshl_add_u64 v[6:7], v[6:7], 0, v[24:25]
	v_cvt_pk_bf16_f32 v2, v11, v9
	v_cvt_pk_bf16_f32 v3, v13, v15
	v_cvt_pk_bf16_f32 v4, v17, v19
	v_cvt_pk_bf16_f32 v5, v21, v23
	global_store_dwordx4 v[6:7], v[2:5], off sc1
	s_waitcnt lgkmcnt(0)

.LBB0_277:
	s_andn2_b64 vcc, exec, s[38:39]
	s_cbranch_vccnz .LBB0_281
	s_cmp_eq_u32 s31, 0
	s_cbranch_scc1 .LBB0_280
	s_waitcnt vmcnt(0)
	v_pk_mul_f32 v[2:3], v[58:59], v[134:135] op_sel_hi:[1,0]
	ds_write2_b32 v101, v2, v3 offset1:1
	v_pk_mul_f32 v[2:3], v[60:61], v[134:135] op_sel_hi:[1,0]
	ds_write2_b32 v101, v2, v3 offset0:2 offset1:3
	v_pk_mul_f32 v[2:3], v[74:75], v[136:137] op_sel_hi:[1,0]
	v_add_u32_e32 v4, 0x420, v101
	ds_write2_b32 v4, v2, v3 offset1:1
	v_pk_mul_f32 v[2:3], v[76:77], v[136:137] op_sel_hi:[1,0]
	v_add_u32_e32 v4, 0x428, v101
	ds_write2_b32 v4, v2, v3 offset1:1
	v_pk_mul_f32 v[2:3], v[70:71], v[138:139] op_sel_hi:[1,0]
	v_add_u32_e32 v4, 0x840, v101
	ds_write2_b32 v4, v2, v3 offset1:1
	v_pk_mul_f32 v[2:3], v[72:73], v[138:139] op_sel_hi:[1,0]
	v_add_u32_e32 v4, 0x848, v101
	ds_write2_b32 v4, v2, v3 offset1:1
	v_pk_mul_f32 v[2:3], v[82:83], v[140:141] op_sel_hi:[1,0]
	v_add_u32_e32 v4, 0xc60, v101
	ds_write2_b32 v4, v2, v3 offset1:1
	v_pk_mul_f32 v[2:3], v[84:85], v[140:141] op_sel_hi:[1,0]
	v_add_u32_e32 v4, 0xc68, v101
	ds_write2_b32 v4, v2, v3 offset1:1
	v_pk_mul_f32 v[2:3], v[78:79], v[142:143] op_sel_hi:[1,0]
	v_add_u32_e32 v4, 0x1080, v101
	ds_write2_b32 v4, v2, v3 offset1:1
	v_pk_mul_f32 v[2:3], v[80:81], v[142:143] op_sel_hi:[1,0]
	v_add_u32_e32 v4, 0x1088, v101
	ds_write2_b32 v4, v2, v3 offset1:1
	v_pk_mul_f32 v[2:3], v[90:91], v[144:145] op_sel_hi:[1,0]
	v_add_u32_e32 v4, 0x14a0, v101
	ds_write2_b32 v4, v2, v3 offset1:1
	v_pk_mul_f32 v[2:3], v[92:93], v[144:145] op_sel_hi:[1,0]
	v_add_u32_e32 v4, 0x14a8, v101
	ds_write2_b32 v4, v2, v3 offset1:1
	v_pk_mul_f32 v[2:3], v[86:87], v[146:147] op_sel_hi:[1,0]
	v_add_u32_e32 v4, 0x18c0, v101
	ds_write2_b32 v4, v2, v3 offset1:1
	v_pk_mul_f32 v[2:3], v[88:89], v[146:147] op_sel_hi:[1,0]
	v_add_u32_e32 v4, 0x18c8, v101
	ds_write2_b32 v4, v2, v3 offset1:1
	v_pk_mul_f32 v[2:3], v[94:95], v[148:149] op_sel_hi:[1,0]
	v_add_u32_e32 v4, 0x1ce0, v101
	ds_write2_b32 v4, v2, v3 offset1:1
	v_pk_mul_f32 v[2:3], v[96:97], v[148:149] op_sel_hi:[1,0]
	v_add_u32_e32 v4, 0x1ce8, v101
	ds_write2_b32 v4, v2, v3 offset1:1
	s_waitcnt lgkmcnt(0)
	ds_read2_b32 v[6:7], v99 offset0:33 offset1:41
	ds_read2_b32 v[8:9], v99 offset1:8
	ds_read2_b32 v[10:11], v99 offset0:66 offset1:74
	ds_read2_b32 v[12:13], v99 offset0:99 offset1:107
	ds_read2_b32 v[14:15], v99 offset0:132 offset1:140
	ds_read2_b32 v[16:17], v99 offset0:165 offset1:173
	ds_read2_b32 v[18:19], v99 offset0:198 offset1:206
	ds_read2_b32 v[20:21], v99 offset0:231 offset1:239
	v_lshl_add_u64 v[22:23], s[16:17], 0, v[116:117]
	v_lshlrev_b32_e32 v24, 1, v106
	v_mov_b32_e32 v25, v1
	s_waitcnt lgkmcnt(6)
	v_cvt_pk_bf16_f32 v2, v8, v6
	s_waitcnt lgkmcnt(4)
	v_cvt_pk_bf16_f32 v3, v10, v12
	s_waitcnt lgkmcnt(2)
	v_cvt_pk_bf16_f32 v4, v14, v16
	s_waitcnt lgkmcnt(0)
	v_cvt_pk_bf16_f32 v5, v18, v20
	v_lshl_add_u64 v[22:23], v[22:23], 0, v[24:25]
	global_store_dwordx4 v[22:23], v[2:5], off sc1
	s_nop 1
	v_cvt_pk_bf16_f32 v2, v9, v7
	v_cvt_pk_bf16_f32 v3, v11, v13
	v_cvt_pk_bf16_f32 v4, v15, v17
	v_cvt_pk_bf16_f32 v5, v19, v21
	ds_read2_b32 v[8:9], v99 offset0:49 offset1:57
	ds_read2_b32 v[10:11], v99 offset0:16 offset1:24
	ds_read2_b32 v[12:13], v99 offset0:82 offset1:90
	ds_read2_b32 v[14:15], v99 offset0:115 offset1:123
	ds_read2_b32 v[16:17], v99 offset0:148 offset1:156
	ds_read2_b32 v[18:19], v99 offset0:181 offset1:189
	ds_read2_b32 v[20:21], v99 offset0:214 offset1:222
	ds_read2_b32 v[22:23], v99 offset0:247 offset1:255
	v_lshl_add_u64 v[6:7], s[16:17], 0, v[114:115]
	v_lshl_add_u64 v[6:7], v[6:7], 0, v[24:25]
	global_store_dwordx4 v[6:7], v[2:5], off sc1
	v_lshl_add_u64 v[6:7], s[16:17], 0, v[112:113]
	v_lshl_add_u64 v[6:7], v[6:7], 0, v[24:25]
	s_waitcnt lgkmcnt(6)
	v_cvt_pk_bf16_f32 v2, v10, v8
	s_waitcnt lgkmcnt(4)
	v_cvt_pk_bf16_f32 v3, v12, v14
	s_waitcnt lgkmcnt(2)
	v_cvt_pk_bf16_f32 v4, v16, v18
	s_waitcnt lgkmcnt(0)
	v_cvt_pk_bf16_f32 v5, v20, v22
	global_store_dwordx4 v[6:7], v[2:5], off sc1
	v_lshl_add_u64 v[6:7], s[16:17], 0, v[110:111]
	v_lshl_add_u64 v[6:7], v[6:7], 0, v[24:25]
	v_cvt_pk_bf16_f32 v2, v11, v9
	v_cvt_pk_bf16_f32 v3, v13, v15
	v_cvt_pk_bf16_f32 v4, v17, v19
	v_cvt_pk_bf16_f32 v5, v21, v23
	global_store_dwordx4 v[6:7], v[2:5], off sc1
	s_waitcnt lgkmcnt(0)

.LBB0_287:
	s_andn2_b64 vcc, exec, s[36:37]
	s_cbranch_vccnz .LBB0_284
	s_cmp_eq_u32 s31, 0
	s_cbranch_scc1 .LBB0_283
	s_waitcnt vmcnt(6)
	v_pk_mul_f32 v[34:35], v[124:125], v[34:35] op_sel_hi:[0,1]
	ds_write2_b32 v101, v34, v35 offset1:1
	v_pk_mul_f32 v[34:35], v[124:125], v[36:37] op_sel_hi:[0,1]
	ds_write2_b32 v101, v34, v35 offset0:2 offset1:3
	s_waitcnt vmcnt(5)
	v_pk_mul_f32 v[34:35], v[126:127], v[42:43] op_sel_hi:[0,1]
	v_add_u32_e32 v36, 0x420, v101
	ds_write2_b32 v36, v34, v35 offset1:1
	v_pk_mul_f32 v[34:35], v[126:127], v[44:45] op_sel_hi:[0,1]
	v_add_u32_e32 v36, 0x428, v101
	ds_write2_b32 v36, v34, v35 offset1:1
	s_waitcnt vmcnt(4)
	v_pk_mul_f32 v[34:35], v[132:133], v[38:39] op_sel_hi:[0,1]
	v_add_u32_e32 v36, 0x840, v101
	ds_write2_b32 v36, v34, v35 offset1:1
	v_pk_mul_f32 v[34:35], v[132:133], v[40:41] op_sel_hi:[0,1]
	v_add_u32_e32 v36, 0x848, v101
	ds_write2_b32 v36, v34, v35 offset1:1
	v_pk_mul_f32 v[34:35], v[122:123], v[50:51] op_sel_hi:[0,1]
	v_add_u32_e32 v36, 0xc60, v101
	ds_write2_b32 v36, v34, v35 offset1:1
	v_pk_mul_f32 v[34:35], v[122:123], v[52:53] op_sel_hi:[0,1]
	v_add_u32_e32 v36, 0xc68, v101
	ds_write2_b32 v36, v34, v35 offset1:1
	s_waitcnt vmcnt(3)
	v_pk_mul_f32 v[34:35], v[130:131], v[46:47] op_sel_hi:[0,1]
	v_add_u32_e32 v36, 0x1080, v101
	ds_write2_b32 v36, v34, v35 offset1:1
	v_pk_mul_f32 v[34:35], v[130:131], v[48:49] op_sel_hi:[0,1]
	v_add_u32_e32 v36, 0x1088, v101
	ds_write2_b32 v36, v34, v35 offset1:1
	s_waitcnt vmcnt(0)
	v_pk_mul_f32 v[34:35], v[120:121], v[62:63] op_sel_hi:[0,1]
	v_add_u32_e32 v36, 0x14a0, v101
	ds_write2_b32 v36, v34, v35 offset1:1
	v_pk_mul_f32 v[34:35], v[120:121], v[64:65] op_sel_hi:[0,1]
	v_add_u32_e32 v36, 0x14a8, v101
	ds_write2_b32 v36, v34, v35 offset1:1
	v_pk_mul_f32 v[34:35], v[128:129], v[54:55] op_sel_hi:[0,1]
	v_add_u32_e32 v36, 0x18c0, v101
	ds_write2_b32 v36, v34, v35 offset1:1
	v_pk_mul_f32 v[34:35], v[128:129], v[56:57] op_sel_hi:[0,1]
	v_add_u32_e32 v36, 0x18c8, v101
	ds_write2_b32 v36, v34, v35 offset1:1
	v_pk_mul_f32 v[34:35], v[118:119], v[66:67] op_sel_hi:[0,1]
	v_add_u32_e32 v36, 0x1ce0, v101
	ds_write2_b32 v36, v34, v35 offset1:1
	v_pk_mul_f32 v[34:35], v[118:119], v[68:69] op_sel_hi:[0,1]
	v_add_u32_e32 v36, 0x1ce8, v101
	ds_write2_b32 v36, v34, v35 offset1:1
	s_waitcnt lgkmcnt(0)
	ds_read2_b32 v[38:39], v99 offset0:33 offset1:41
	ds_read2_b32 v[40:41], v99 offset1:8
	ds_read2_b32 v[42:43], v99 offset0:66 offset1:74
	ds_read2_b32 v[44:45], v99 offset0:99 offset1:107
	ds_read2_b32 v[46:47], v99 offset0:132 offset1:140
	ds_read2_b32 v[48:49], v99 offset0:165 offset1:173
	ds_read2_b32 v[50:51], v99 offset0:198 offset1:206
	ds_read2_b32 v[52:53], v99 offset0:231 offset1:239
	v_mad_u64_u32 v[54:55], s[36:37], s34, v104, 0
	v_lshl_add_u64 v[54:55], v[54:55], 1, s[14:15]
	v_lshlrev_b32_e32 v56, 1, v106
	v_mov_b32_e32 v57, v1
	s_waitcnt lgkmcnt(6)
	v_cvt_pk_bf16_f32 v34, v40, v38
	s_waitcnt lgkmcnt(4)
	v_cvt_pk_bf16_f32 v35, v42, v44
	s_waitcnt lgkmcnt(2)
	v_cvt_pk_bf16_f32 v36, v46, v48
	s_waitcnt lgkmcnt(0)
	v_cvt_pk_bf16_f32 v37, v50, v52
	v_lshl_add_u64 v[54:55], v[54:55], 0, v[56:57]
	global_store_dwordx4 v[54:55], v[34:37], off sc1
	s_nop 1
	v_cvt_pk_bf16_f32 v34, v41, v39
	v_cvt_pk_bf16_f32 v35, v43, v45
	v_cvt_pk_bf16_f32 v36, v47, v49
	v_cvt_pk_bf16_f32 v37, v51, v53
	v_mad_u64_u32 v[38:39], s[36:37], s34, v102, 0
	ds_read2_b32 v[40:41], v99 offset0:16 offset1:24
	ds_read2_b32 v[42:43], v99 offset0:49 offset1:57
	ds_read2_b32 v[44:45], v99 offset0:82 offset1:90
	ds_read2_b32 v[46:47], v99 offset0:115 offset1:123
	ds_read2_b32 v[48:49], v99 offset0:148 offset1:156
	ds_read2_b32 v[50:51], v99 offset0:181 offset1:189
	ds_read2_b32 v[52:53], v99 offset0:214 offset1:222
	ds_read2_b32 v[54:55], v99 offset0:247 offset1:255
	v_lshl_add_u64 v[38:39], v[38:39], 1, s[14:15]
	v_lshl_add_u64 v[38:39], v[38:39], 0, v[56:57]
	global_store_dwordx4 v[38:39], v[34:37], off sc1
	v_mad_u64_u32 v[38:39], s[36:37], s34, v100, 0
	v_lshl_add_u64 v[38:39], v[38:39], 1, s[14:15]
	s_waitcnt lgkmcnt(6)
	v_cvt_pk_bf16_f32 v34, v40, v42
	s_waitcnt lgkmcnt(4)
	v_cvt_pk_bf16_f32 v35, v44, v46
	s_waitcnt lgkmcnt(2)
	v_cvt_pk_bf16_f32 v36, v48, v50
	s_waitcnt lgkmcnt(0)
	v_cvt_pk_bf16_f32 v37, v52, v54
	v_lshl_add_u64 v[38:39], v[38:39], 0, v[56:57]
	global_store_dwordx4 v[38:39], v[34:37], off sc1
	v_mad_u64_u32 v[38:39], s[36:37], s34, v98, 0
	v_lshl_add_u64 v[38:39], v[38:39], 1, s[14:15]
	v_cvt_pk_bf16_f32 v34, v41, v43
	v_cvt_pk_bf16_f32 v35, v45, v47
	v_cvt_pk_bf16_f32 v36, v49, v51
	v_cvt_pk_bf16_f32 v37, v53, v55
	v_lshl_add_u64 v[38:39], v[38:39], 0, v[56:57]
	global_store_dwordx4 v[38:39], v[34:37], off sc1
	s_waitcnt lgkmcnt(0)
	s_branch .LBB0_283

.LBB0_292:
	s_and_b64 vcc, exec, s[16:17]
	s_cbranch_vccz .LBB0_296
	s_cmp_eq_u32 s31, 0
	s_cbranch_scc1 .LBB0_295
	s_waitcnt vmcnt(6)
	v_pk_mul_f32 v[34:35], v[34:35], v[124:125] op_sel_hi:[1,0]
	ds_write2_b32 v101, v34, v35 offset1:1
	v_pk_mul_f32 v[34:35], v[36:37], v[124:125] op_sel_hi:[1,0]
	ds_write2_b32 v101, v34, v35 offset0:2 offset1:3
	s_waitcnt vmcnt(5)
	v_pk_mul_f32 v[34:35], v[42:43], v[126:127] op_sel_hi:[1,0]
	v_add_u32_e32 v0, 0x420, v101
	ds_write2_b32 v0, v34, v35 offset1:1
	v_pk_mul_f32 v[34:35], v[44:45], v[126:127] op_sel_hi:[1,0]
	v_add_u32_e32 v0, 0x428, v101
	ds_write2_b32 v0, v34, v35 offset1:1
	s_waitcnt vmcnt(4)
	v_pk_mul_f32 v[34:35], v[38:39], v[132:133] op_sel_hi:[1,0]
	v_add_u32_e32 v0, 0x840, v101
	ds_write2_b32 v0, v34, v35 offset1:1
	v_pk_mul_f32 v[34:35], v[40:41], v[132:133] op_sel_hi:[1,0]
	v_add_u32_e32 v0, 0x848, v101
	ds_write2_b32 v0, v34, v35 offset1:1
	v_pk_mul_f32 v[34:35], v[50:51], v[122:123] op_sel_hi:[1,0]
	v_add_u32_e32 v0, 0xc60, v101
	ds_write2_b32 v0, v34, v35 offset1:1
	v_pk_mul_f32 v[34:35], v[52:53], v[122:123] op_sel_hi:[1,0]
	v_add_u32_e32 v0, 0xc68, v101
	ds_write2_b32 v0, v34, v35 offset1:1
	s_waitcnt vmcnt(3)
	v_pk_mul_f32 v[34:35], v[46:47], v[130:131] op_sel_hi:[1,0]
	v_add_u32_e32 v0, 0x1080, v101
	ds_write2_b32 v0, v34, v35 offset1:1
	v_pk_mul_f32 v[34:35], v[48:49], v[130:131] op_sel_hi:[1,0]
	v_add_u32_e32 v0, 0x1088, v101
	ds_write2_b32 v0, v34, v35 offset1:1
	s_waitcnt vmcnt(0)
	v_pk_mul_f32 v[34:35], v[62:63], v[120:121] op_sel_hi:[1,0]
	v_add_u32_e32 v0, 0x14a0, v101
	ds_write2_b32 v0, v34, v35 offset1:1
	v_pk_mul_f32 v[34:35], v[64:65], v[120:121] op_sel_hi:[1,0]
	v_add_u32_e32 v0, 0x14a8, v101
	ds_write2_b32 v0, v34, v35 offset1:1
	v_pk_mul_f32 v[34:35], v[54:55], v[128:129] op_sel_hi:[1,0]
	v_add_u32_e32 v0, 0x18c0, v101
	ds_write2_b32 v0, v34, v35 offset1:1
	v_pk_mul_f32 v[34:35], v[56:57], v[128:129] op_sel_hi:[1,0]
	v_add_u32_e32 v0, 0x18c8, v101
	ds_write2_b32 v0, v34, v35 offset1:1
	v_pk_mul_f32 v[34:35], v[66:67], v[118:119] op_sel_hi:[1,0]
	v_add_u32_e32 v0, 0x1ce0, v101
	ds_write2_b32 v0, v34, v35 offset1:1
	v_pk_mul_f32 v[34:35], v[68:69], v[118:119] op_sel_hi:[1,0]
	v_add_u32_e32 v0, 0x1ce8, v101
	ds_write2_b32 v0, v34, v35 offset1:1
	s_waitcnt lgkmcnt(0)
	ds_read2_b32 v[38:39], v99 offset0:33 offset1:41
	ds_read2_b32 v[40:41], v99 offset1:8
	ds_read2_b32 v[42:43], v99 offset0:66 offset1:74
	ds_read2_b32 v[44:45], v99 offset0:99 offset1:107
	ds_read2_b32 v[46:47], v99 offset0:132 offset1:140
	ds_read2_b32 v[48:49], v99 offset0:165 offset1:173
	ds_read2_b32 v[50:51], v99 offset0:198 offset1:206
	ds_read2_b32 v[52:53], v99 offset0:231 offset1:239
	v_mul_u32_u24_e32 v0, s34, v104
	v_lshlrev_b32_e32 v0, 1, v0
	v_lshl_add_u64 v[54:55], s[14:15], 0, v[0:1]
	v_lshlrev_b32_e32 v0, 1, v106
	s_lshl_b32 s14, s34, 3
	s_waitcnt lgkmcnt(6)
	v_cvt_pk_bf16_f32 v34, v40, v38
	s_waitcnt lgkmcnt(4)
	v_cvt_pk_bf16_f32 v35, v42, v44
	s_waitcnt lgkmcnt(2)
	v_cvt_pk_bf16_f32 v36, v46, v48
	s_waitcnt lgkmcnt(0)
	v_cvt_pk_bf16_f32 v37, v50, v52
	v_lshl_add_u64 v[56:57], v[54:55], 0, v[0:1]
	s_ashr_i32 s15, s14, 31
	global_store_dwordx4 v[56:57], v[34:37], off sc1
	s_lshl_b64 s[14:15], s[14:15], 1
	s_nop 0
	v_cvt_pk_bf16_f32 v34, v41, v39
	v_cvt_pk_bf16_f32 v35, v43, v45
	v_cvt_pk_bf16_f32 v36, v47, v49
	v_cvt_pk_bf16_f32 v37, v51, v53
	v_lshl_add_u64 v[38:39], v[54:55], 0, s[14:15]
	ds_read2_b32 v[42:43], v99 offset0:16 offset1:24
	ds_read2_b32 v[44:45], v99 offset0:49 offset1:57
	ds_read2_b32 v[46:47], v99 offset0:82 offset1:90
	ds_read2_b32 v[48:49], v99 offset0:115 offset1:123
	ds_read2_b32 v[50:51], v99 offset0:148 offset1:156
	ds_read2_b32 v[52:53], v99 offset0:181 offset1:189
	ds_read2_b32 v[54:55], v99 offset0:214 offset1:222
	ds_read2_b32 v[56:57], v99 offset0:247 offset1:255
	v_lshl_add_u64 v[40:41], v[38:39], 0, v[0:1]
	v_lshl_add_u64 v[38:39], v[38:39], 0, s[14:15]
	global_store_dwordx4 v[40:41], v[34:37], off sc1
	v_lshl_add_u64 v[40:41], v[38:39], 0, v[0:1]
	v_lshl_add_u64 v[38:39], v[38:39], 0, s[14:15]
	s_waitcnt lgkmcnt(6)
	v_cvt_pk_bf16_f32 v34, v42, v44
	s_waitcnt lgkmcnt(4)
	v_cvt_pk_bf16_f32 v35, v46, v48
	s_waitcnt lgkmcnt(2)
	v_cvt_pk_bf16_f32 v36, v50, v52
	s_waitcnt lgkmcnt(0)
	v_cvt_pk_bf16_f32 v37, v54, v56
	global_store_dwordx4 v[40:41], v[34:37], off sc1
	v_lshl_add_u64 v[38:39], v[38:39], 0, v[0:1]
	s_nop 0
	v_cvt_pk_bf16_f32 v34, v43, v45
	v_cvt_pk_bf16_f32 v35, v47, v49
	v_cvt_pk_bf16_f32 v36, v51, v53
	v_cvt_pk_bf16_f32 v37, v55, v57
	global_store_dwordx4 v[38:39], v[34:37], off sc1
	s_waitcnt lgkmcnt(0)

.LBB0_314:
	s_andn2_b64 vcc, exec, s[44:45]
	s_cbranch_vccnz .LBB0_318
	s_cmp_eq_u32 s31, 0
	s_cbranch_scc1 .LBB0_317
	s_waitcnt vmcnt(1)
	v_pk_mul_f32 v[26:27], v[126:127], v[26:27] op_sel_hi:[0,1]
	v_add_u32_e32 v0, 0x420, v101
	ds_write2_b32 v0, v26, v27 offset1:1
	v_pk_mul_f32 v[26:27], v[126:127], v[28:29] op_sel_hi:[0,1]
	v_add_u32_e32 v0, 0x428, v101
	ds_write2_b32 v0, v26, v27 offset1:1
	v_pk_mul_f32 v[22:23], v[132:133], v[22:23] op_sel_hi:[0,1]
	v_add_u32_e32 v0, 0x840, v101
	ds_write2_b32 v0, v22, v23 offset1:1
	v_pk_mul_f32 v[22:23], v[132:133], v[24:25] op_sel_hi:[0,1]
	v_add_u32_e32 v0, 0x848, v101
	ds_write2_b32 v0, v22, v23 offset1:1
	v_pk_mul_f32 v[18:19], v[122:123], v[18:19] op_sel_hi:[0,1]
	v_add_u32_e32 v0, 0xc60, v101
	ds_write2_b32 v0, v18, v19 offset1:1
	v_pk_mul_f32 v[18:19], v[122:123], v[20:21] op_sel_hi:[0,1]
	v_add_u32_e32 v0, 0xc68, v101
	ds_write2_b32 v0, v18, v19 offset1:1
	v_pk_mul_f32 v[14:15], v[130:131], v[14:15] op_sel_hi:[0,1]
	v_add_u32_e32 v0, 0x1080, v101
	ds_write2_b32 v0, v14, v15 offset1:1
	v_pk_mul_f32 v[14:15], v[130:131], v[16:17] op_sel_hi:[0,1]
	v_add_u32_e32 v0, 0x1088, v101
	ds_write2_b32 v0, v14, v15 offset1:1
	v_pk_mul_f32 v[10:11], v[120:121], v[10:11] op_sel_hi:[0,1]
	v_add_u32_e32 v0, 0x14a0, v101
	ds_write2_b32 v0, v10, v11 offset1:1
	v_pk_mul_f32 v[10:11], v[120:121], v[12:13] op_sel_hi:[0,1]
	v_add_u32_e32 v0, 0x14a8, v101
	ds_write2_b32 v0, v10, v11 offset1:1
	v_pk_mul_f32 v[6:7], v[128:129], v[6:7] op_sel_hi:[0,1]
	v_add_u32_e32 v0, 0x18c0, v101
	ds_write2_b32 v0, v6, v7 offset1:1
	v_pk_mul_f32 v[6:7], v[128:129], v[8:9] op_sel_hi:[0,1]
	v_add_u32_e32 v0, 0x18c8, v101
	s_waitcnt vmcnt(0)
	v_pk_mul_f32 v[30:31], v[124:125], v[30:31] op_sel_hi:[0,1]
	ds_write2_b32 v0, v6, v7 offset1:1
	v_pk_mul_f32 v[2:3], v[118:119], v[2:3] op_sel_hi:[0,1]
	v_add_u32_e32 v0, 0x1ce0, v101
	ds_write2_b32 v101, v30, v31 offset1:1
	v_pk_mul_f32 v[30:31], v[124:125], v[32:33] op_sel_hi:[0,1]
	ds_write2_b32 v0, v2, v3 offset1:1
	v_pk_mul_f32 v[2:3], v[118:119], v[4:5] op_sel_hi:[0,1]
	v_add_u32_e32 v0, 0x1ce8, v101
	ds_write2_b32 v101, v30, v31 offset0:2 offset1:3
	ds_write2_b32 v0, v2, v3 offset1:1
	s_waitcnt lgkmcnt(0)
	ds_read2_b32 v[6:7], v99 offset0:33 offset1:41
	ds_read2_b32 v[8:9], v99 offset1:8
	ds_read2_b32 v[10:11], v99 offset0:66 offset1:74
	ds_read2_b32 v[12:13], v99 offset0:99 offset1:107
	ds_read2_b32 v[14:15], v99 offset0:132 offset1:140
	ds_read2_b32 v[16:17], v99 offset0:165 offset1:173
	ds_read2_b32 v[18:19], v99 offset0:198 offset1:206
	ds_read2_b32 v[20:21], v99 offset0:231 offset1:239
	v_mad_u64_u32 v[22:23], s[44:45], s34, v104, 0
	v_lshl_add_u64 v[22:23], v[22:23], 1, s[0:1]
	v_lshlrev_b32_e32 v0, 1, v106
	s_waitcnt lgkmcnt(6)
	v_cvt_pk_bf16_f32 v2, v8, v6
	s_waitcnt lgkmcnt(4)
	v_cvt_pk_bf16_f32 v3, v10, v12
	s_waitcnt lgkmcnt(2)
	v_cvt_pk_bf16_f32 v4, v14, v16
	s_waitcnt lgkmcnt(0)
	v_cvt_pk_bf16_f32 v5, v18, v20
	v_lshl_add_u64 v[22:23], v[22:23], 0, v[0:1]
	global_store_dwordx4 v[22:23], v[2:5], off sc1
	s_nop 1
	v_cvt_pk_bf16_f32 v2, v9, v7
	v_cvt_pk_bf16_f32 v3, v11, v13
	v_cvt_pk_bf16_f32 v4, v15, v17
	v_cvt_pk_bf16_f32 v5, v19, v21
	v_mad_u64_u32 v[6:7], s[44:45], s34, v102, 0
	ds_read2_b32 v[8:9], v99 offset0:16 offset1:24
	ds_read2_b32 v[10:11], v99 offset0:49 offset1:57
	ds_read2_b32 v[12:13], v99 offset0:82 offset1:90
	ds_read2_b32 v[14:15], v99 offset0:115 offset1:123
	ds_read2_b32 v[16:17], v99 offset0:148 offset1:156
	ds_read2_b32 v[18:19], v99 offset0:181 offset1:189
	ds_read2_b32 v[20:21], v99 offset0:214 offset1:222
	ds_read2_b32 v[22:23], v99 offset0:247 offset1:255
	v_lshl_add_u64 v[6:7], v[6:7], 1, s[0:1]
	v_lshl_add_u64 v[6:7], v[6:7], 0, v[0:1]
	global_store_dwordx4 v[6:7], v[2:5], off sc1
	v_mad_u64_u32 v[6:7], s[44:45], s34, v100, 0
	v_lshl_add_u64 v[6:7], v[6:7], 1, s[0:1]
	s_waitcnt lgkmcnt(6)
	v_cvt_pk_bf16_f32 v2, v8, v10
	s_waitcnt lgkmcnt(4)
	v_cvt_pk_bf16_f32 v3, v12, v14
	s_waitcnt lgkmcnt(2)
	v_cvt_pk_bf16_f32 v4, v16, v18
	s_waitcnt lgkmcnt(0)
	v_cvt_pk_bf16_f32 v5, v20, v22
	v_lshl_add_u64 v[6:7], v[6:7], 0, v[0:1]
	global_store_dwordx4 v[6:7], v[2:5], off sc1
	v_mad_u64_u32 v[6:7], s[44:45], s34, v98, 0
	v_lshl_add_u64 v[6:7], v[6:7], 1, s[0:1]
	v_cvt_pk_bf16_f32 v2, v9, v11
	v_cvt_pk_bf16_f32 v3, v13, v15
	v_cvt_pk_bf16_f32 v4, v17, v19
	v_cvt_pk_bf16_f32 v5, v21, v23
	v_lshl_add_u64 v[6:7], v[6:7], 0, v[0:1]
	global_store_dwordx4 v[6:7], v[2:5], off sc1
	s_waitcnt lgkmcnt(0)

.LBB0_332:
	s_andn2_b64 vcc, exec, s[44:45]
	s_cbranch_vccnz .LBB0_299
	s_cmp_eq_u32 s31, 0
	s_cbranch_scc1 .LBB0_298
	s_waitcnt vmcnt(1)
	v_pk_mul_f32 v[26:27], v[26:27], v[126:127] op_sel_hi:[1,0]
	v_add_u32_e32 v0, 0x420, v101
	ds_write2_b32 v0, v26, v27 offset1:1
	v_pk_mul_f32 v[26:27], v[28:29], v[126:127] op_sel_hi:[1,0]
	v_add_u32_e32 v0, 0x428, v101
	ds_write2_b32 v0, v26, v27 offset1:1
	v_pk_mul_f32 v[22:23], v[22:23], v[132:133] op_sel_hi:[1,0]
	v_add_u32_e32 v0, 0x840, v101
	ds_write2_b32 v0, v22, v23 offset1:1
	v_pk_mul_f32 v[22:23], v[24:25], v[132:133] op_sel_hi:[1,0]
	v_add_u32_e32 v0, 0x848, v101
	ds_write2_b32 v0, v22, v23 offset1:1
	v_pk_mul_f32 v[18:19], v[18:19], v[122:123] op_sel_hi:[1,0]
	v_add_u32_e32 v0, 0xc60, v101
	ds_write2_b32 v0, v18, v19 offset1:1
	v_pk_mul_f32 v[18:19], v[20:21], v[122:123] op_sel_hi:[1,0]
	v_add_u32_e32 v0, 0xc68, v101
	ds_write2_b32 v0, v18, v19 offset1:1
	v_pk_mul_f32 v[14:15], v[14:15], v[130:131] op_sel_hi:[1,0]
	v_add_u32_e32 v0, 0x1080, v101
	ds_write2_b32 v0, v14, v15 offset1:1
	v_pk_mul_f32 v[14:15], v[16:17], v[130:131] op_sel_hi:[1,0]
	v_add_u32_e32 v0, 0x1088, v101
	ds_write2_b32 v0, v14, v15 offset1:1
	v_pk_mul_f32 v[10:11], v[10:11], v[120:121] op_sel_hi:[1,0]
	v_add_u32_e32 v0, 0x14a0, v101
	ds_write2_b32 v0, v10, v11 offset1:1
	v_pk_mul_f32 v[10:11], v[12:13], v[120:121] op_sel_hi:[1,0]
	v_add_u32_e32 v0, 0x14a8, v101
	ds_write2_b32 v0, v10, v11 offset1:1
	v_pk_mul_f32 v[6:7], v[6:7], v[128:129] op_sel_hi:[1,0]
	v_add_u32_e32 v0, 0x18c0, v101
	ds_write2_b32 v0, v6, v7 offset1:1
	v_pk_mul_f32 v[6:7], v[8:9], v[128:129] op_sel_hi:[1,0]
	v_add_u32_e32 v0, 0x18c8, v101
	s_waitcnt vmcnt(0)
	v_pk_mul_f32 v[30:31], v[30:31], v[124:125] op_sel_hi:[1,0]
	ds_write2_b32 v0, v6, v7 offset1:1
	v_pk_mul_f32 v[2:3], v[2:3], v[118:119] op_sel_hi:[1,0]
	v_add_u32_e32 v0, 0x1ce0, v101
	ds_write2_b32 v101, v30, v31 offset1:1
	v_pk_mul_f32 v[30:31], v[32:33], v[124:125] op_sel_hi:[1,0]
	ds_write2_b32 v0, v2, v3 offset1:1
	v_pk_mul_f32 v[2:3], v[4:5], v[118:119] op_sel_hi:[1,0]
	v_add_u32_e32 v0, 0x1ce8, v101
	ds_write2_b32 v101, v30, v31 offset0:2 offset1:3
	ds_write2_b32 v0, v2, v3 offset1:1
	s_waitcnt lgkmcnt(0)
	ds_read2_b32 v[6:7], v99 offset0:33 offset1:41
	ds_read2_b32 v[8:9], v99 offset1:8
	ds_read2_b32 v[10:11], v99 offset0:66 offset1:74
	ds_read2_b32 v[12:13], v99 offset0:99 offset1:107
	ds_read2_b32 v[14:15], v99 offset0:132 offset1:140
	ds_read2_b32 v[16:17], v99 offset0:165 offset1:173
	ds_read2_b32 v[18:19], v99 offset0:198 offset1:206
	ds_read2_b32 v[20:21], v99 offset0:231 offset1:239
	v_mad_u64_u32 v[22:23], s[36:37], s34, v104, 0
	v_lshl_add_u64 v[22:23], v[22:23], 1, s[0:1]
	v_lshlrev_b32_e32 v0, 1, v106
	s_waitcnt lgkmcnt(6)
	v_cvt_pk_bf16_f32 v2, v8, v6
	s_waitcnt lgkmcnt(4)
	v_cvt_pk_bf16_f32 v3, v10, v12
	s_waitcnt lgkmcnt(2)
	v_cvt_pk_bf16_f32 v4, v14, v16
	s_waitcnt lgkmcnt(0)
	v_cvt_pk_bf16_f32 v5, v18, v20
	v_lshl_add_u64 v[22:23], v[22:23], 0, v[0:1]
	global_store_dwordx4 v[22:23], v[2:5], off sc1
	s_nop 1
	v_cvt_pk_bf16_f32 v2, v9, v7
	v_cvt_pk_bf16_f32 v3, v11, v13
	v_cvt_pk_bf16_f32 v4, v15, v17
	v_cvt_pk_bf16_f32 v5, v19, v21
	v_mad_u64_u32 v[6:7], s[36:37], s34, v102, 0
	ds_read2_b32 v[8:9], v99 offset0:16 offset1:24
	ds_read2_b32 v[10:11], v99 offset0:49 offset1:57
	ds_read2_b32 v[12:13], v99 offset0:82 offset1:90
	ds_read2_b32 v[14:15], v99 offset0:115 offset1:123
	ds_read2_b32 v[16:17], v99 offset0:148 offset1:156
	ds_read2_b32 v[18:19], v99 offset0:181 offset1:189
	ds_read2_b32 v[20:21], v99 offset0:214 offset1:222
	ds_read2_b32 v[22:23], v99 offset0:247 offset1:255
	v_lshl_add_u64 v[6:7], v[6:7], 1, s[0:1]
	v_lshl_add_u64 v[6:7], v[6:7], 0, v[0:1]
	global_store_dwordx4 v[6:7], v[2:5], off sc1
	v_mad_u64_u32 v[6:7], s[36:37], s34, v100, 0
	v_lshl_add_u64 v[6:7], v[6:7], 1, s[0:1]
	s_waitcnt lgkmcnt(6)
	v_cvt_pk_bf16_f32 v2, v8, v10
	s_waitcnt lgkmcnt(4)
	v_cvt_pk_bf16_f32 v3, v12, v14
	s_waitcnt lgkmcnt(2)
	v_cvt_pk_bf16_f32 v4, v16, v18
	s_waitcnt lgkmcnt(0)
	v_cvt_pk_bf16_f32 v5, v20, v22
	v_lshl_add_u64 v[6:7], v[6:7], 0, v[0:1]
	global_store_dwordx4 v[6:7], v[2:5], off sc1
	v_mad_u64_u32 v[6:7], s[36:37], s34, v98, 0
	v_lshl_add_u64 v[6:7], v[6:7], 1, s[0:1]
	v_cvt_pk_bf16_f32 v2, v9, v11
	v_cvt_pk_bf16_f32 v3, v13, v15
	v_cvt_pk_bf16_f32 v4, v17, v19
	v_cvt_pk_bf16_f32 v5, v21, v23
	v_lshl_add_u64 v[6:7], v[6:7], 0, v[0:1]
	global_store_dwordx4 v[6:7], v[2:5], off sc1
	s_waitcnt lgkmcnt(0)
	s_branch .LBB0_298

.LBB0_343:
	s_cmp_eq_u32 s31, 0
	s_cbranch_scc1 .LBB0_345
	s_waitcnt vmcnt(1)
	v_pk_mul_f32 v[26:27], v[26:27], v[126:127] op_sel_hi:[1,0]
	v_add_u32_e32 v0, 0x420, v101
	ds_write2_b32 v0, v26, v27 offset1:1
	v_pk_mul_f32 v[26:27], v[28:29], v[126:127] op_sel_hi:[1,0]
	v_add_u32_e32 v0, 0x428, v101
	ds_write2_b32 v0, v26, v27 offset1:1
	v_pk_mul_f32 v[22:23], v[22:23], v[132:133] op_sel_hi:[1,0]
	v_add_u32_e32 v0, 0x840, v101
	ds_write2_b32 v0, v22, v23 offset1:1
	v_pk_mul_f32 v[22:23], v[24:25], v[132:133] op_sel_hi:[1,0]
	v_add_u32_e32 v0, 0x848, v101
	ds_write2_b32 v0, v22, v23 offset1:1
	v_pk_mul_f32 v[18:19], v[18:19], v[122:123] op_sel_hi:[1,0]
	v_add_u32_e32 v0, 0xc60, v101
	ds_write2_b32 v0, v18, v19 offset1:1
	v_pk_mul_f32 v[18:19], v[20:21], v[122:123] op_sel_hi:[1,0]
	v_add_u32_e32 v0, 0xc68, v101
	ds_write2_b32 v0, v18, v19 offset1:1
	v_pk_mul_f32 v[14:15], v[14:15], v[130:131] op_sel_hi:[1,0]
	v_add_u32_e32 v0, 0x1080, v101
	ds_write2_b32 v0, v14, v15 offset1:1
	v_pk_mul_f32 v[14:15], v[16:17], v[130:131] op_sel_hi:[1,0]
	v_add_u32_e32 v0, 0x1088, v101
	ds_write2_b32 v0, v14, v15 offset1:1
	v_pk_mul_f32 v[10:11], v[10:11], v[120:121] op_sel_hi:[1,0]
	v_add_u32_e32 v0, 0x14a0, v101
	ds_write2_b32 v0, v10, v11 offset1:1
	v_pk_mul_f32 v[10:11], v[12:13], v[120:121] op_sel_hi:[1,0]
	v_add_u32_e32 v0, 0x14a8, v101
	ds_write2_b32 v0, v10, v11 offset1:1
	v_pk_mul_f32 v[6:7], v[6:7], v[128:129] op_sel_hi:[1,0]
	v_add_u32_e32 v0, 0x18c0, v101
	ds_write2_b32 v0, v6, v7 offset1:1
	v_pk_mul_f32 v[6:7], v[8:9], v[128:129] op_sel_hi:[1,0]
	v_add_u32_e32 v0, 0x18c8, v101
	s_waitcnt vmcnt(0)
	v_pk_mul_f32 v[30:31], v[30:31], v[124:125] op_sel_hi:[1,0]
	ds_write2_b32 v0, v6, v7 offset1:1
	v_pk_mul_f32 v[2:3], v[2:3], v[118:119] op_sel_hi:[1,0]
	v_add_u32_e32 v0, 0x1ce0, v101
	ds_write2_b32 v101, v30, v31 offset1:1
	v_pk_mul_f32 v[30:31], v[32:33], v[124:125] op_sel_hi:[1,0]
	ds_write2_b32 v0, v2, v3 offset1:1
	v_pk_mul_f32 v[2:3], v[4:5], v[118:119] op_sel_hi:[1,0]
	v_add_u32_e32 v0, 0x1ce8, v101
	ds_write2_b32 v101, v30, v31 offset0:2 offset1:3
	ds_write2_b32 v0, v2, v3 offset1:1
	s_waitcnt lgkmcnt(0)
	ds_read2_b32 v[6:7], v99 offset0:33 offset1:41
	ds_read2_b32 v[8:9], v99 offset1:8
	ds_read2_b32 v[10:11], v99 offset0:66 offset1:74
	ds_read2_b32 v[12:13], v99 offset0:99 offset1:107
	ds_read2_b32 v[14:15], v99 offset0:132 offset1:140
	ds_read2_b32 v[16:17], v99 offset0:165 offset1:173
	ds_read2_b32 v[18:19], v99 offset0:198 offset1:206
	ds_read2_b32 v[20:21], v99 offset0:231 offset1:239
	v_mad_u64_u32 v[22:23], s[14:15], s34, v104, 0
	v_lshl_add_u64 v[22:23], v[22:23], 1, s[0:1]
	v_lshlrev_b32_e32 v0, 1, v106
	s_waitcnt lgkmcnt(6)
	v_cvt_pk_bf16_f32 v2, v8, v6
	s_waitcnt lgkmcnt(4)
	v_cvt_pk_bf16_f32 v3, v10, v12
	s_waitcnt lgkmcnt(2)
	v_cvt_pk_bf16_f32 v4, v14, v16
	s_waitcnt lgkmcnt(0)
	v_cvt_pk_bf16_f32 v5, v18, v20
	v_lshl_add_u64 v[22:23], v[22:23], 0, v[0:1]
	global_store_dwordx4 v[22:23], v[2:5], off sc1
	s_nop 1
	v_cvt_pk_bf16_f32 v2, v9, v7
	v_cvt_pk_bf16_f32 v3, v11, v13
	v_cvt_pk_bf16_f32 v4, v15, v17
	v_cvt_pk_bf16_f32 v5, v19, v21
	v_mad_u64_u32 v[6:7], s[14:15], s34, v102, 0
	ds_read2_b32 v[8:9], v99 offset0:16 offset1:24
	ds_read2_b32 v[10:11], v99 offset0:49 offset1:57
	ds_read2_b32 v[12:13], v99 offset0:82 offset1:90
	ds_read2_b32 v[14:15], v99 offset0:115 offset1:123
	ds_read2_b32 v[16:17], v99 offset0:148 offset1:156
	ds_read2_b32 v[18:19], v99 offset0:181 offset1:189
	ds_read2_b32 v[20:21], v99 offset0:214 offset1:222
	ds_read2_b32 v[22:23], v99 offset0:247 offset1:255
	v_lshl_add_u64 v[6:7], v[6:7], 1, s[0:1]
	v_lshl_add_u64 v[6:7], v[6:7], 0, v[0:1]
	global_store_dwordx4 v[6:7], v[2:5], off sc1
	v_mad_u64_u32 v[6:7], s[14:15], s34, v100, 0
	v_lshl_add_u64 v[6:7], v[6:7], 1, s[0:1]
	s_waitcnt lgkmcnt(6)
	v_cvt_pk_bf16_f32 v2, v8, v10
	s_waitcnt lgkmcnt(4)
	v_cvt_pk_bf16_f32 v3, v12, v14
	s_waitcnt lgkmcnt(2)
	v_cvt_pk_bf16_f32 v4, v16, v18
	s_waitcnt lgkmcnt(0)
	v_cvt_pk_bf16_f32 v5, v20, v22
	v_lshl_add_u64 v[6:7], v[6:7], 0, v[0:1]
	global_store_dwordx4 v[6:7], v[2:5], off sc1
	v_mad_u64_u32 v[6:7], s[14:15], s34, v98, 0
	v_lshl_add_u64 v[6:7], v[6:7], 1, s[0:1]
	v_cvt_pk_bf16_f32 v2, v9, v11
	v_cvt_pk_bf16_f32 v3, v13, v15
	v_cvt_pk_bf16_f32 v4, v17, v19
	v_cvt_pk_bf16_f32 v5, v21, v23
	v_lshl_add_u64 v[6:7], v[6:7], 0, v[0:1]
	global_store_dwordx4 v[6:7], v[2:5], off sc1
	s_waitcnt lgkmcnt(0)

.LBB0_362:
	s_or_saveexec_b64 s[38:39], s[38:39]
	s_lshl_b64 s[40:41], s[66:67], 2
	s_xor_b64 exec, exec, s[38:39]
	s_cbranch_execz .LBB0_364
	v_or_b32_e32 v203, s40, v0
	v_mov_b64_e32 v[200:201], s[42:43]
	v_mad_u64_u32 v[200:201], s[82:83], v203, s2, v[200:201]
	v_mov_b32_e32 v195, v194
	v_mad_i32_i24 v201, s41, v232, v201
	s_lshl_b64 s[50:51], s[66:67], 1
	v_cvt_pk_bf16_f32 v154, v190, v191
	v_cvt_pk_bf16_f32 v155, v188, v189
	v_cvt_pk_bf16_f32 v156, v160, v161
	v_cvt_pk_bf16_f32 v157, v158, v159
	v_lshl_add_u64 v[200:201], v[182:183], 1, v[200:201]
	v_pk_mul_f32 v[146:147], v[194:195], v[146:147]
	v_or_b32_e32 v202, s50, v0
	global_store_dwordx4 v[200:201], v[154:157], off sc1
	v_pk_mul_f32 v[150:151], v[194:195], v[150:151]
	s_nop 0
	v_mov_b32_e32 v154, v194
	v_mov_b32_e32 v155, v194
	v_cvt_pk_bf16_f32 v156, v146, v147
	v_mov_b64_e32 v[146:147], s[44:45]
	v_pk_mul_f32 v[152:153], v[154:155], v[152:153]
	v_pk_mul_f32 v[148:149], v[154:155], v[148:149]
	v_mad_u64_u32 v[200:201], s[82:83], v202, s2, v[146:147]
	v_cvt_pk_bf16_f32 v154, v150, v151
	v_cvt_pk_bf16_f32 v155, v152, v153
	v_cvt_pk_bf16_f32 v157, v148, v149
	v_mad_i32_i24 v201, s51, v232, v201
.LBB0_364:
	s_or_b64 exec, exec, s[38:39]
	v_mul_f32_e32 v146, 0x4b800000, v192
	v_cndmask_b32_e32 v146, v192, v146, vcc
	v_rsq_f32_e32 v146, v146
	s_mov_b32 s38, 0x32800000
	v_mul_f32_e32 v147, 0x45800000, v146
	v_cndmask_b32_e32 v192, v146, v147, vcc
	v_ffbh_u32_e32 v146, v187
	v_min_u32_e32 v148, 32, v146
	v_lshlrev_b64 v[146:147], v148, v[186:187]
	v_min_u32_e32 v146, 1, v146
	v_or_b32_e32 v146, v147, v146
	v_cvt_f32_u32_e32 v146, v146
	v_sub_u32_e32 v147, 32, v148
	v_pk_mul_f32 v[142:143], v[192:193], v[142:143] op_sel_hi:[0,1]
	v_pk_mul_f32 v[134:135], v[192:193], v[134:135] op_sel_hi:[0,1]
	v_ldexp_f32 v147, v146, v147
	v_ffbh_u32_e32 v146, v185
	v_min_u32_e32 v146, 32, v146
	v_lshlrev_b64 v[148:149], v146, v[184:185]
	v_min_u32_e32 v148, 1, v148
	v_or_b32_e32 v148, v149, v148
	v_cvt_f32_u32_e32 v148, v148
	v_sub_u32_e32 v146, 32, v146
	v_pk_mul_f32 v[144:145], v[192:193], v[144:145] op_sel_hi:[0,1]
	v_pk_mul_f32 v[136:137], v[192:193], v[136:137] op_sel_hi:[0,1]
	v_ldexp_f32 v146, v148, v146
	v_pk_fma_f32 v[146:147], v[146:147], s[38:39], v[196:197] op_sel_hi:[1,0,0]
	v_pk_mul_f32 v[130:131], v[192:193], v[130:131] op_sel_hi:[0,1]
	v_mul_f32_e32 v148, 0x4b800000, v147
	v_cmp_gt_f32_e64 s[38:39], s96, v147
	v_pk_mul_f32 v[132:133], v[192:193], v[132:133] op_sel_hi:[0,1]
	v_cmp_gt_f32_e32 vcc, s96, v146
	v_cndmask_b32_e64 v147, v147, v148, s[38:39]
	v_rsq_f32_e32 v147, v147
	s_nop 0
	v_mul_f32_e32 v148, 0x45800000, v147
	v_cndmask_b32_e64 v152, v147, v148, s[38:39]
	v_lshlrev_b64 v[148:149], 1, v[182:183]
	v_lshl_add_u64 v[184:185], v[200:201], 0, v[148:149]
	global_store_dwordx4 v[184:185], v[154:157], off sc1
	v_pk_mul_f32 v[126:127], v[152:153], v[126:127] op_sel_hi:[0,1]
	v_pk_mul_f32 v[118:119], v[152:153], v[118:119] op_sel_hi:[0,1]
	v_mov_b32_e32 v156, v1
	v_mov_b32_e32 v157, v1
	v_mov_b32_e32 v154, v1
	v_mov_b32_dpp v156, v190 row_ror:2 row_mask:0xf bank_mask:0xf
	v_mov_b32_e32 v155, v1
	v_mov_b32_dpp v157, v191 row_ror:2 row_mask:0xf bank_mask:0xf
	v_mov_b32_dpp v154, v190 row_ror:1 row_mask:0xf bank_mask:0xf
	v_mov_b32_dpp v156, v142 row_shr:2 row_mask:0xf bank_mask:0xf
	v_mov_b32_dpp v155, v191 row_ror:1 row_mask:0xf bank_mask:0xf
	v_mov_b32_dpp v157, v143 row_shr:2 row_mask:0xf bank_mask:0xf
	v_mov_b32_dpp v154, v142 row_shr:1 row_mask:0xf bank_mask:0xf
	v_mov_b32_dpp v155, v143 row_shr:1 row_mask:0xf bank_mask:0xf
	v_pk_fma_f32 v[156:157], v[74:75], v[156:157], v[86:87]
	v_pk_mul_f32 v[128:129], v[152:153], v[128:129] op_sel_hi:[0,1]
	v_pk_fma_f32 v[154:155], v[78:79], v[154:155], v[156:157]
	v_pk_mul_f32 v[120:121], v[152:153], v[120:121] op_sel_hi:[0,1]
	v_pk_fma_f32 v[154:155], v[142:143], v[82:83], v[154:155]
	v_pk_mul_f32 v[114:115], v[152:153], v[114:115] op_sel_hi:[0,1]
	v_mul_f32_e32 v151, 0x3d372713, v154
	v_mul_f32_e32 v151, v154, v151
	v_fma_f32 v151, v154, v151, v154
	v_mul_f32_e32 v151, 0xc0135761, v151
	v_exp_f32_e32 v151, v151
	v_mul_f32_e32 v147, 0x4b800000, v146
	v_cndmask_b32_e32 v146, v146, v147, vcc
	v_rsq_f32_e32 v146, v146
	v_add_f32_e32 v151, 1.0, v151
	v_rcp_f32_e32 v156, v151
	v_mul_f32_e32 v151, 0x3d372713, v155
	v_mul_f32_e32 v151, v155, v151
	v_fma_f32 v151, v155, v151, v155
	v_mul_f32_e32 v151, 0xc0135761, v151
	v_exp_f32_e32 v151, v151
	v_pk_mul_f32 v[116:117], v[152:153], v[116:117] op_sel_hi:[0,1]
	v_mul_f32_e32 v147, 0x45800000, v146
	v_cndmask_b32_e32 v150, v146, v147, vcc
	v_add_f32_e32 v151, 1.0, v151
	v_rcp_f32_e32 v157, v151
	v_cmp_lt_u32_e32 vcc, 13, v0
	v_lshl_add_u64 v[146:147], v[0:1], 0, -12
	v_pk_mul_f32 v[154:155], v[154:155], v[156:157]
	v_mov_b32_e32 v156, v1
	v_mov_b32_e32 v157, v1
	v_pk_mul_f32 v[154:155], v[134:135], v[154:155]
	v_mov_b32_e32 v134, v1
	v_mov_b32_dpp v156, v188 row_ror:2 row_mask:0xf bank_mask:0xf
	v_mov_b32_e32 v135, v1
	v_mov_b32_dpp v157, v189 row_ror:2 row_mask:0xf bank_mask:0xf
	v_mov_b32_dpp v134, v188 row_ror:1 row_mask:0xf bank_mask:0xf
	v_mov_b32_dpp v156, v144 row_shr:2 row_mask:0xf bank_mask:0xf
	v_mov_b32_dpp v135, v189 row_ror:1 row_mask:0xf bank_mask:0xf
	v_mov_b32_dpp v157, v145 row_shr:2 row_mask:0xf bank_mask:0xf
	v_mov_b32_dpp v134, v144 row_shr:1 row_mask:0xf bank_mask:0xf
	v_mov_b32_dpp v135, v145 row_shr:1 row_mask:0xf bank_mask:0xf
	v_pk_fma_f32 v[156:157], v[76:77], v[156:157], v[88:89]
	s_nop 0
	v_pk_fma_f32 v[134:135], v[80:81], v[134:135], v[156:157]
	s_nop 0
	v_pk_fma_f32 v[134:135], v[144:145], v[84:85], v[134:135]
	s_nop 0
	v_mul_f32_e32 v151, 0x3d372713, v134
	v_mul_f32_e32 v151, v134, v151
	v_fma_f32 v151, v134, v151, v134
	v_mul_f32_e32 v151, 0xc0135761, v151
	v_exp_f32_e32 v151, v151
	s_nop 0
	v_add_f32_e32 v151, 1.0, v151
	v_rcp_f32_e32 v156, v151
	v_mul_f32_e32 v151, 0x3d372713, v135
	v_mul_f32_e32 v151, v135, v151
	v_fma_f32 v151, v135, v151, v135
	v_mul_f32_e32 v151, 0xc0135761, v151
	v_exp_f32_e32 v151, v151
	s_nop 0
	v_add_f32_e32 v151, 1.0, v151
	v_rcp_f32_e32 v157, v151
	v_pk_mul_f32 v[110:111], v[150:151], v[110:111] op_sel_hi:[0,1]
	v_pk_mul_f32 v[102:103], v[150:151], v[102:103] op_sel_hi:[0,1]
	v_pk_mul_f32 v[112:113], v[150:151], v[112:113] op_sel_hi:[0,1]
	v_pk_mul_f32 v[134:135], v[134:135], v[156:157]
	v_pk_mul_f32 v[104:105], v[150:151], v[104:105] op_sel_hi:[0,1]
	v_pk_mul_f32 v[156:157], v[136:137], v[134:135]
	v_pk_mul_f32 v[134:135], v[192:193], v[140:141] op_sel_hi:[0,1]
	v_mov_b32_e32 v140, v1
	v_mov_b32_e32 v141, v1
	v_pk_mul_f32 v[136:137], v[192:193], v[138:139] op_sel_hi:[0,1]
	v_mov_b32_e32 v138, v1
	v_mov_b32_dpp v140, v160 row_ror:2 row_mask:0xf bank_mask:0xf
	v_mov_b32_e32 v139, v1
	v_mov_b32_dpp v141, v161 row_ror:2 row_mask:0xf bank_mask:0xf
	v_mov_b32_dpp v138, v160 row_ror:1 row_mask:0xf bank_mask:0xf
	v_mov_b32_dpp v140, v136 row_shr:2 row_mask:0xf bank_mask:0xf
	v_mov_b32_dpp v139, v161 row_ror:1 row_mask:0xf bank_mask:0xf
	v_mov_b32_dpp v141, v137 row_shr:2 row_mask:0xf bank_mask:0xf
	v_mov_b32_dpp v138, v136 row_shr:1 row_mask:0xf bank_mask:0xf
	v_mov_b32_dpp v139, v137 row_shr:1 row_mask:0xf bank_mask:0xf
	v_pk_fma_f32 v[140:141], v[46:47], v[140:141], v[62:63]
	v_pk_mul_f32 v[98:99], v[150:151], v[98:99] op_sel_hi:[0,1]
	v_pk_fma_f32 v[138:139], v[50:51], v[138:139], v[140:141]
	v_pk_mul_f32 v[100:101], v[150:151], v[100:101] op_sel_hi:[0,1]
	v_pk_fma_f32 v[138:139], v[136:137], v[58:59], v[138:139]
	s_nop 0
	v_mul_f32_e32 v140, 0x3d372713, v138
	v_mul_f32_e32 v141, 0x3d372713, v139
	v_mul_f32_e32 v140, v138, v140
	v_mul_f32_e32 v141, v139, v141
	v_fma_f32 v140, v138, v140, v138
	v_fma_f32 v141, v139, v141, v139
	v_mul_f32_e32 v140, 0xc0135761, v140
	v_mul_f32_e32 v141, 0xc0135761, v141
	v_exp_f32_e32 v140, v140
	v_exp_f32_e32 v141, v141
	v_add_f32_e32 v140, 1.0, v140
	v_add_f32_e32 v141, 1.0, v141
	v_rcp_f32_e32 v140, v140
	v_rcp_f32_e32 v141, v141
	s_nop 0
	v_pk_mul_f32 v[138:139], v[138:139], v[140:141]
	v_mov_b32_e32 v140, v1
	v_mov_b32_e32 v141, v1
	v_pk_mul_f32 v[130:131], v[130:131], v[138:139]
	v_mov_b32_e32 v138, v1
	v_mov_b32_dpp v140, v158 row_ror:2 row_mask:0xf bank_mask:0xf
	v_mov_b32_e32 v139, v1
	v_mov_b32_dpp v141, v159 row_ror:2 row_mask:0xf bank_mask:0xf
	v_mov_b32_dpp v138, v158 row_ror:1 row_mask:0xf bank_mask:0xf
	v_mov_b32_dpp v140, v134 row_shr:2 row_mask:0xf bank_mask:0xf
	v_mov_b32_dpp v139, v159 row_ror:1 row_mask:0xf bank_mask:0xf
	v_mov_b32_dpp v141, v135 row_shr:2 row_mask:0xf bank_mask:0xf
	v_mov_b32_dpp v138, v134 row_shr:1 row_mask:0xf bank_mask:0xf
	v_mov_b32_dpp v139, v135 row_shr:1 row_mask:0xf bank_mask:0xf
	v_pk_fma_f32 v[140:141], v[48:49], v[140:141], v[64:65]
	s_nop 0
	v_pk_fma_f32 v[138:139], v[52:53], v[138:139], v[140:141]
	s_nop 0
	v_pk_fma_f32 v[138:139], v[134:135], v[60:61], v[138:139]
	s_nop 0
	v_mul_f32_e32 v140, 0x3d372713, v138
	v_mul_f32_e32 v141, 0x3d372713, v139
	v_mul_f32_e32 v140, v138, v140
	v_mul_f32_e32 v141, v139, v141
	v_fma_f32 v140, v138, v140, v138
	v_fma_f32 v141, v139, v141, v139
	v_mul_f32_e32 v140, 0xc0135761, v140
	v_mul_f32_e32 v141, 0xc0135761, v141
	v_exp_f32_e32 v140, v140
	v_exp_f32_e32 v141, v141
	v_add_f32_e32 v140, 1.0, v140
	v_add_f32_e32 v141, 1.0, v141
	v_rcp_f32_e32 v140, v140
	v_rcp_f32_e32 v141, v141
	s_nop 0
	v_pk_mul_f32 v[138:139], v[138:139], v[140:141]
	s_nop 0
	v_pk_mul_f32 v[132:133], v[132:133], v[138:139]
	v_cvt_pk_bf16_f32 v140, v130, v131
	v_cvt_pk_bf16_f32 v141, v132, v133
	v_or_b32_e32 v132, 16, v193
	v_mov_b64_e32 v[130:131], s[16:17]
	v_mad_i64_i32 v[132:133], s[38:39], v132, s2, v[130:131]
	v_cvt_pk_bf16_f32 v138, v154, v155
	v_cvt_pk_bf16_f32 v139, v156, v157
	v_lshl_add_u64 v[132:133], v[132:133], 0, v[148:149]
	global_store_dwordx4 v[132:133], v[138:141], off sc1
	v_mov_b32_e32 v132, v1
	v_mov_b32_e32 v133, v1
	v_mov_b32_e32 v138, v1
	v_mov_b32_e32 v139, v1
	v_mov_b32_dpp v132, v142 row_ror:1 row_mask:0xf bank_mask:0xf
	v_mov_b32_dpp v138, v142 row_ror:2 row_mask:0xf bank_mask:0xf
	v_mov_b32_dpp v139, v143 row_ror:2 row_mask:0xf bank_mask:0xf
	v_mov_b32_dpp v133, v143 row_ror:1 row_mask:0xf bank_mask:0xf
	v_mov_b32_dpp v138, v126 row_shr:2 row_mask:0xf bank_mask:0xf
	v_mov_b32_dpp v139, v127 row_shr:2 row_mask:0xf bank_mask:0xf
	v_mov_b32_dpp v132, v126 row_shr:1 row_mask:0xf bank_mask:0xf
	v_mov_b32_dpp v133, v127 row_shr:1 row_mask:0xf bank_mask:0xf
	v_pk_fma_f32 v[138:139], v[74:75], v[138:139], v[86:87]
	s_nop 0
	v_pk_fma_f32 v[132:133], v[78:79], v[132:133], v[138:139]
	s_nop 0
	v_pk_fma_f32 v[132:133], v[126:127], v[82:83], v[132:133]
	s_nop 0
	v_mul_f32_e32 v138, 0x3d372713, v132
	v_mul_f32_e32 v139, 0x3d372713, v133
	v_mul_f32_e32 v138, v132, v138
	v_mul_f32_e32 v139, v133, v139
	v_fma_f32 v138, v132, v138, v132
	v_fma_f32 v139, v133, v139, v133
	v_mul_f32_e32 v138, 0xc0135761, v138
	v_mul_f32_e32 v139, 0xc0135761, v139
	v_exp_f32_e32 v138, v138
	v_exp_f32_e32 v139, v139
	v_add_f32_e32 v138, 1.0, v138
	v_add_f32_e32 v139, 1.0, v139
	v_rcp_f32_e32 v138, v138
	v_rcp_f32_e32 v139, v139
	s_nop 0
	v_pk_mul_f32 v[132:133], v[132:133], v[138:139]
	v_mov_b32_e32 v138, v1
	v_mov_b32_e32 v139, v1
	v_pk_mul_f32 v[132:133], v[118:119], v[132:133]
	v_mov_b32_e32 v118, v1
	v_mov_b32_dpp v138, v144 row_ror:2 row_mask:0xf bank_mask:0xf
	v_mov_b32_e32 v119, v1
	v_mov_b32_dpp v139, v145 row_ror:2 row_mask:0xf bank_mask:0xf
	v_mov_b32_dpp v118, v144 row_ror:1 row_mask:0xf bank_mask:0xf
	v_mov_b32_dpp v138, v128 row_shr:2 row_mask:0xf bank_mask:0xf
	v_mov_b32_dpp v119, v145 row_ror:1 row_mask:0xf bank_mask:0xf
	v_mov_b32_dpp v139, v129 row_shr:2 row_mask:0xf bank_mask:0xf
	v_mov_b32_dpp v118, v128 row_shr:1 row_mask:0xf bank_mask:0xf
	v_mov_b32_dpp v119, v129 row_shr:1 row_mask:0xf bank_mask:0xf
	v_pk_fma_f32 v[138:139], v[76:77], v[138:139], v[88:89]
	s_nop 0
	v_pk_fma_f32 v[118:119], v[80:81], v[118:119], v[138:139]
	s_nop 0
	v_pk_fma_f32 v[118:119], v[128:129], v[84:85], v[118:119]
	s_nop 0
	v_mul_f32_e32 v138, 0x3d372713, v118
	v_mul_f32_e32 v139, 0x3d372713, v119
	v_mul_f32_e32 v138, v118, v138
	v_mul_f32_e32 v139, v119, v139
	v_fma_f32 v138, v118, v138, v118
	v_fma_f32 v139, v119, v139, v119
	v_mul_f32_e32 v138, 0xc0135761, v138
	v_mul_f32_e32 v139, 0xc0135761, v139
	v_exp_f32_e32 v138, v138
	v_exp_f32_e32 v139, v139
	v_add_f32_e32 v138, 1.0, v138
	v_add_f32_e32 v139, 1.0, v139
	v_rcp_f32_e32 v138, v138
	v_rcp_f32_e32 v139, v139
	s_nop 0
	v_pk_mul_f32 v[118:119], v[118:119], v[138:139]
	s_nop 0
	v_pk_mul_f32 v[138:139], v[120:121], v[118:119]
	v_pk_mul_f32 v[118:119], v[152:153], v[124:125] op_sel_hi:[0,1]
	v_mov_b32_e32 v124, v1
	v_mov_b32_e32 v125, v1
	v_pk_mul_f32 v[120:121], v[152:153], v[122:123] op_sel_hi:[0,1]
	v_mov_b32_e32 v122, v1
	v_mov_b32_dpp v124, v136 row_ror:2 row_mask:0xf bank_mask:0xf
	v_mov_b32_e32 v123, v1
	v_mov_b32_dpp v125, v137 row_ror:2 row_mask:0xf bank_mask:0xf
	v_mov_b32_dpp v122, v136 row_ror:1 row_mask:0xf bank_mask:0xf
	v_mov_b32_dpp v124, v120 row_shr:2 row_mask:0xf bank_mask:0xf
	v_mov_b32_dpp v123, v137 row_ror:1 row_mask:0xf bank_mask:0xf
	v_mov_b32_dpp v125, v121 row_shr:2 row_mask:0xf bank_mask:0xf
	v_mov_b32_dpp v122, v120 row_shr:1 row_mask:0xf bank_mask:0xf
	v_mov_b32_dpp v123, v121 row_shr:1 row_mask:0xf bank_mask:0xf
	v_pk_fma_f32 v[124:125], v[46:47], v[124:125], v[62:63]
	s_nop 0
	v_pk_fma_f32 v[122:123], v[50:51], v[122:123], v[124:125]
	s_nop 0
	v_pk_fma_f32 v[122:123], v[120:121], v[58:59], v[122:123]
	s_nop 0
	v_mul_f32_e32 v124, 0x3d372713, v122
	v_mul_f32_e32 v125, 0x3d372713, v123
	v_mul_f32_e32 v124, v122, v124
	v_mul_f32_e32 v125, v123, v125
	v_fma_f32 v124, v122, v124, v122
	v_fma_f32 v125, v123, v125, v123
	v_mul_f32_e32 v124, 0xc0135761, v124
	v_mul_f32_e32 v125, 0xc0135761, v125
	v_exp_f32_e32 v124, v124
	v_exp_f32_e32 v125, v125
	v_add_f32_e32 v124, 1.0, v124
	v_add_f32_e32 v125, 1.0, v125
	v_rcp_f32_e32 v124, v124
	v_rcp_f32_e32 v125, v125
	s_nop 0
	v_pk_mul_f32 v[122:123], v[122:123], v[124:125]
	v_mov_b32_e32 v124, v1
	v_mov_b32_e32 v125, v1
	v_pk_mul_f32 v[122:123], v[114:115], v[122:123]
	v_mov_b32_e32 v114, v1
	v_mov_b32_dpp v124, v134 row_ror:2 row_mask:0xf bank_mask:0xf
	v_mov_b32_e32 v115, v1
	v_mov_b32_dpp v125, v135 row_ror:2 row_mask:0xf bank_mask:0xf
	v_mov_b32_dpp v114, v134 row_ror:1 row_mask:0xf bank_mask:0xf
	v_mov_b32_dpp v124, v118 row_shr:2 row_mask:0xf bank_mask:0xf
	v_mov_b32_dpp v115, v135 row_ror:1 row_mask:0xf bank_mask:0xf
	v_mov_b32_dpp v125, v119 row_shr:2 row_mask:0xf bank_mask:0xf
	v_mov_b32_dpp v114, v118 row_shr:1 row_mask:0xf bank_mask:0xf
	v_mov_b32_dpp v115, v119 row_shr:1 row_mask:0xf bank_mask:0xf
	v_pk_fma_f32 v[124:125], v[48:49], v[124:125], v[64:65]
	s_nop 0
	v_pk_fma_f32 v[114:115], v[52:53], v[114:115], v[124:125]
	s_nop 0
	v_pk_fma_f32 v[114:115], v[118:119], v[60:61], v[114:115]
	s_nop 0
	v_mul_f32_e32 v124, 0x3d372713, v114
	v_mul_f32_e32 v125, 0x3d372713, v115
	v_mul_f32_e32 v124, v114, v124
	v_mul_f32_e32 v125, v115, v125
	v_fma_f32 v124, v114, v124, v114
	v_fma_f32 v125, v115, v125, v115
	v_mul_f32_e32 v124, 0xc0135761, v124
	v_mul_f32_e32 v125, 0xc0135761, v125
	v_exp_f32_e32 v124, v124
	v_exp_f32_e32 v125, v125
	v_add_f32_e32 v124, 1.0, v124
	v_add_f32_e32 v125, 1.0, v125
	v_rcp_f32_e32 v124, v124
	v_rcp_f32_e32 v125, v125
	s_nop 0
	v_pk_mul_f32 v[114:115], v[114:115], v[124:125]
	s_nop 0
	v_pk_mul_f32 v[124:125], v[116:117], v[114:115]
	v_cvt_pk_bf16_f32 v116, v122, v123
	v_or_b32_e32 v122, 32, v193
	v_mad_i64_i32 v[122:123], s[38:39], v122, s2, v[130:131]
	v_cvt_pk_bf16_f32 v114, v132, v133
	v_cvt_pk_bf16_f32 v115, v138, v139
	v_cvt_pk_bf16_f32 v117, v124, v125
	v_lshl_add_u64 v[122:123], v[122:123], 0, v[148:149]
	global_store_dwordx4 v[122:123], v[114:117], off sc1
	s_nop 1
	v_mov_b32_e32 v116, v1
	v_mov_b32_e32 v117, v1
	v_mov_b32_e32 v114, v1
	v_mov_b32_dpp v116, v126 row_ror:2 row_mask:0xf bank_mask:0xf
	v_mov_b32_e32 v115, v1
	v_mov_b32_dpp v117, v127 row_ror:2 row_mask:0xf bank_mask:0xf
	v_mov_b32_dpp v114, v126 row_ror:1 row_mask:0xf bank_mask:0xf
	v_mov_b32_dpp v116, v110 row_shr:2 row_mask:0xf bank_mask:0xf
	v_mov_b32_dpp v115, v127 row_ror:1 row_mask:0xf bank_mask:0xf
	v_mov_b32_dpp v117, v111 row_shr:2 row_mask:0xf bank_mask:0xf
	v_mov_b32_dpp v114, v110 row_shr:1 row_mask:0xf bank_mask:0xf
	v_mov_b32_dpp v115, v111 row_shr:1 row_mask:0xf bank_mask:0xf
	v_pk_fma_f32 v[116:117], v[74:75], v[116:117], v[86:87]
	s_nop 0
	v_pk_fma_f32 v[114:115], v[78:79], v[114:115], v[116:117]
	s_nop 0
	v_pk_fma_f32 v[114:115], v[110:111], v[82:83], v[114:115]
	s_nop 0
	v_mul_f32_e32 v116, 0x3d372713, v114
	v_mul_f32_e32 v117, 0x3d372713, v115
	v_mul_f32_e32 v116, v114, v116
	v_mul_f32_e32 v117, v115, v117
	v_fma_f32 v116, v114, v116, v114
	v_fma_f32 v117, v115, v117, v115
	v_mul_f32_e32 v116, 0xc0135761, v116
	v_mul_f32_e32 v117, 0xc0135761, v117
	v_exp_f32_e32 v116, v116
	v_exp_f32_e32 v117, v117
	v_add_f32_e32 v116, 1.0, v116
	v_add_f32_e32 v117, 1.0, v117
	v_rcp_f32_e32 v116, v116
	v_rcp_f32_e32 v117, v117
	s_nop 0
	v_pk_mul_f32 v[114:115], v[114:115], v[116:117]
	v_mov_b32_e32 v116, v1
	v_mov_b32_e32 v117, v1
	v_pk_mul_f32 v[114:115], v[102:103], v[114:115]
	v_mov_b32_e32 v102, v1
	v_mov_b32_dpp v116, v128 row_ror:2 row_mask:0xf bank_mask:0xf
	v_mov_b32_e32 v103, v1
	v_mov_b32_dpp v117, v129 row_ror:2 row_mask:0xf bank_mask:0xf
	v_mov_b32_dpp v102, v128 row_ror:1 row_mask:0xf bank_mask:0xf
	v_mov_b32_dpp v116, v112 row_shr:2 row_mask:0xf bank_mask:0xf
	v_mov_b32_dpp v103, v129 row_ror:1 row_mask:0xf bank_mask:0xf
	v_mov_b32_dpp v117, v113 row_shr:2 row_mask:0xf bank_mask:0xf
	v_mov_b32_dpp v102, v112 row_shr:1 row_mask:0xf bank_mask:0xf
	v_mov_b32_dpp v103, v113 row_shr:1 row_mask:0xf bank_mask:0xf
	v_pk_fma_f32 v[116:117], v[76:77], v[116:117], v[88:89]
	s_nop 0
	v_pk_fma_f32 v[102:103], v[80:81], v[102:103], v[116:117]
	s_nop 0
	v_pk_fma_f32 v[102:103], v[112:113], v[84:85], v[102:103]
	s_nop 0
	v_mul_f32_e32 v116, 0x3d372713, v102
	v_mul_f32_e32 v117, 0x3d372713, v103
	v_mul_f32_e32 v116, v102, v116
	v_mul_f32_e32 v117, v103, v117
	v_fma_f32 v116, v102, v116, v102
	v_fma_f32 v117, v103, v117, v103
	v_mul_f32_e32 v116, 0xc0135761, v116
	v_mul_f32_e32 v117, 0xc0135761, v117
	v_exp_f32_e32 v116, v116
	v_exp_f32_e32 v117, v117
	v_add_f32_e32 v116, 1.0, v116
	v_add_f32_e32 v117, 1.0, v117
	v_rcp_f32_e32 v116, v116
	v_rcp_f32_e32 v117, v117
	s_nop 0
	v_pk_mul_f32 v[102:103], v[102:103], v[116:117]
	s_nop 0
	v_pk_mul_f32 v[116:117], v[104:105], v[102:103]
	v_pk_mul_f32 v[102:103], v[150:151], v[108:109] op_sel_hi:[0,1]
	v_mov_b32_e32 v108, v1
	v_mov_b32_e32 v109, v1
	v_pk_mul_f32 v[104:105], v[150:151], v[106:107] op_sel_hi:[0,1]
	v_mov_b32_e32 v106, v1
	v_mov_b32_dpp v108, v120 row_ror:2 row_mask:0xf bank_mask:0xf
	v_mov_b32_e32 v107, v1
	v_mov_b32_dpp v109, v121 row_ror:2 row_mask:0xf bank_mask:0xf
	v_mov_b32_dpp v106, v120 row_ror:1 row_mask:0xf bank_mask:0xf
	v_mov_b32_dpp v108, v104 row_shr:2 row_mask:0xf bank_mask:0xf
	v_mov_b32_dpp v107, v121 row_ror:1 row_mask:0xf bank_mask:0xf
	v_mov_b32_dpp v109, v105 row_shr:2 row_mask:0xf bank_mask:0xf
	v_mov_b32_dpp v106, v104 row_shr:1 row_mask:0xf bank_mask:0xf
	v_mov_b32_dpp v107, v105 row_shr:1 row_mask:0xf bank_mask:0xf
	v_pk_fma_f32 v[108:109], v[46:47], v[108:109], v[62:63]
	s_nop 0
	v_pk_fma_f32 v[106:107], v[50:51], v[106:107], v[108:109]
	s_nop 0
	v_pk_fma_f32 v[106:107], v[104:105], v[58:59], v[106:107]
	s_nop 0
	v_mul_f32_e32 v108, 0x3d372713, v106
	v_mul_f32_e32 v109, 0x3d372713, v107
	v_mul_f32_e32 v108, v106, v108
	v_mul_f32_e32 v109, v107, v109
	v_fma_f32 v108, v106, v108, v106
	v_fma_f32 v109, v107, v109, v107
	v_mul_f32_e32 v108, 0xc0135761, v108
	v_mul_f32_e32 v109, 0xc0135761, v109
	v_exp_f32_e32 v108, v108
	v_exp_f32_e32 v109, v109
	v_add_f32_e32 v108, 1.0, v108
	v_add_f32_e32 v109, 1.0, v109
	v_rcp_f32_e32 v108, v108
	v_rcp_f32_e32 v109, v109
	s_nop 0
	v_pk_mul_f32 v[106:107], v[106:107], v[108:109]
	v_mov_b32_e32 v108, v1
	v_mov_b32_e32 v109, v1
	v_pk_mul_f32 v[106:107], v[98:99], v[106:107]
	v_mov_b32_e32 v98, v1
	v_mov_b32_dpp v108, v118 row_ror:2 row_mask:0xf bank_mask:0xf
	v_mov_b32_e32 v99, v1
	v_mov_b32_dpp v109, v119 row_ror:2 row_mask:0xf bank_mask:0xf
	v_mov_b32_dpp v98, v118 row_ror:1 row_mask:0xf bank_mask:0xf
	v_mov_b32_dpp v108, v102 row_shr:2 row_mask:0xf bank_mask:0xf
	v_mov_b32_dpp v99, v119 row_ror:1 row_mask:0xf bank_mask:0xf
	v_mov_b32_dpp v109, v103 row_shr:2 row_mask:0xf bank_mask:0xf
	v_mov_b32_dpp v98, v102 row_shr:1 row_mask:0xf bank_mask:0xf
	v_mov_b32_dpp v99, v103 row_shr:1 row_mask:0xf bank_mask:0xf
	v_pk_fma_f32 v[108:109], v[48:49], v[108:109], v[64:65]
	s_nop 0
	v_pk_fma_f32 v[98:99], v[52:53], v[98:99], v[108:109]
	s_nop 0
	v_pk_fma_f32 v[98:99], v[102:103], v[60:61], v[98:99]
	s_nop 0
	v_mul_f32_e32 v108, 0x3d372713, v98
	v_mul_f32_e32 v109, 0x3d372713, v99
	v_mul_f32_e32 v108, v98, v108
	v_mul_f32_e32 v109, v99, v109
	v_fma_f32 v108, v98, v108, v98
	v_fma_f32 v109, v99, v109, v99
	v_mul_f32_e32 v108, 0xc0135761, v108
	v_mul_f32_e32 v109, 0xc0135761, v109
	v_exp_f32_e32 v108, v108
	v_exp_f32_e32 v109, v109
	v_add_f32_e32 v108, 1.0, v108
	v_add_f32_e32 v109, 1.0, v109
	v_rcp_f32_e32 v108, v108
	v_rcp_f32_e32 v109, v109
	s_nop 0
	v_pk_mul_f32 v[98:99], v[98:99], v[108:109]
	s_nop 0
	v_pk_mul_f32 v[108:109], v[100:101], v[98:99]
	v_cvt_pk_bf16_f32 v100, v106, v107
	v_or_b32_e32 v106, 48, v193
	v_mad_i64_i32 v[106:107], s[38:39], v106, s2, v[130:131]
	v_cvt_pk_bf16_f32 v98, v114, v115
	v_cvt_pk_bf16_f32 v99, v116, v117
	v_cvt_pk_bf16_f32 v101, v108, v109
	v_lshl_add_u64 v[106:107], v[106:107], 0, v[148:149]
	global_store_dwordx4 v[106:107], v[98:101], off sc1
	s_mov_b64 s[38:39], exec
	s_and_b64 s[50:51], s[38:39], vcc
	v_mov_b32_e32 v228, v221
	s_mov_b64 exec, s[50:51]
	s_cbranch_execz .LBB0_366
	v_lshl_add_u64 v[106:107], v[146:147], 0, s[40:41]
	v_cvt_pk_bf16_f32 v101, v102, v103
	v_mov_b64_e32 v[102:103], s[42:43]
	v_mad_u64_u32 v[102:103], s[40:41], v106, s2, v[102:103]
	v_mad_i32_i24 v103, v107, s2, v103
	v_cvt_pk_bf16_f32 v98, v110, v111
	v_cvt_pk_bf16_f32 v99, v112, v113
	v_cvt_pk_bf16_f32 v100, v104, v105
	v_lshl_add_u64 v[102:103], v[182:183], 1, v[102:103]
	global_store_dwordx4 v[102:103], v[98:101], off sc1

.LBB0_368:
	s_or_saveexec_b64 s[36:37], s[36:37]
	s_lshl_b64 s[40:41], s[66:67], 2
	s_xor_b64 exec, exec, s[36:37]
	s_cbranch_execz .LBB0_370
	s_lshl_b64 s[50:51], s[66:67], 1
	v_or_b32_e32 v103, s50, v0
	v_or_b32_e32 v0, s40, v0
	v_mov_b64_e32 v[106:107], s[42:43]
	v_mad_u64_u32 v[106:107], s[66:67], v0, s2, v[106:107]
	v_mov_b32_e32 v105, v104
	v_mad_i32_i24 v107, s41, v232, v107
	v_cvt_pk_bf16_f32 v90, v100, v101
	v_cvt_pk_bf16_f32 v91, v98, v99
	v_cvt_pk_bf16_f32 v92, v96, v97
	v_cvt_pk_bf16_f32 v93, v94, v95
	v_lshl_add_u64 v[106:107], v[182:183], 1, v[106:107]
	v_pk_mul_f32 v[66:67], v[104:105], v[66:67]
	global_store_dwordx4 v[106:107], v[90:93], off sc1
	v_pk_mul_f32 v[70:71], v[104:105], v[70:71]
	s_nop 0
	v_mov_b32_e32 v90, v104
	v_mov_b32_e32 v91, v104
	v_cvt_pk_bf16_f32 v92, v66, v67
	v_mov_b64_e32 v[66:67], s[44:45]
	v_pk_mul_f32 v[72:73], v[90:91], v[72:73]
	v_pk_mul_f32 v[68:69], v[90:91], v[68:69]
	v_mad_u64_u32 v[110:111], s[66:67], v103, s2, v[66:67]
	v_cvt_pk_bf16_f32 v90, v70, v71
	v_cvt_pk_bf16_f32 v91, v72, v73
	v_cvt_pk_bf16_f32 v93, v68, v69
	v_mad_i32_i24 v111, s51, v232, v111
.LBB0_370:
	s_or_b64 exec, exec, s[36:37]
	v_mul_f32_e32 v0, 0x4b800000, v102
	v_cndmask_b32_e64 v0, v102, v0, s[38:39]
	v_rsq_f32_e32 v0, v0
	s_mov_b32 s36, 0x32800000
	v_mov_b32_e32 v72, v1
	v_mov_b32_e32 v73, v1
	v_mul_f32_e32 v66, 0x45800000, v0
	v_cndmask_b32_e64 v68, v0, v66, s[38:39]
	v_ffbh_u32_e32 v0, v177
	v_min_u32_e32 v0, 32, v0
	v_lshlrev_b64 v[66:67], v0, v[176:177]
	v_min_u32_e32 v66, 1, v66
	v_or_b32_e32 v66, v67, v66
	v_cvt_f32_u32_e32 v66, v66
	v_sub_u32_e32 v0, 32, v0
	v_pk_mul_f32 v[54:55], v[68:69], v[54:55] op_sel_hi:[0,1]
	v_mov_b32_dpp v72, v100 row_ror:2 row_mask:0xf bank_mask:0xf
	v_ldexp_f32 v67, v66, v0
	v_ffbh_u32_e32 v0, v175
	v_min_u32_e32 v0, 32, v0
	v_lshlrev_b64 v[70:71], v0, v[174:175]
	v_min_u32_e32 v66, 1, v70
	v_or_b32_e32 v66, v71, v66
	v_cvt_f32_u32_e32 v66, v66
	v_sub_u32_e32 v0, 32, v0
	v_mov_b32_dpp v73, v101 row_ror:2 row_mask:0xf bank_mask:0xf
	v_mov_b32_dpp v72, v54 row_shr:2 row_mask:0xf bank_mask:0xf
	v_ldexp_f32 v66, v66, v0
	v_pk_fma_f32 v[70:71], v[66:67], s[36:37], v[196:197] op_sel_hi:[1,0,0]
	v_mov_b32_dpp v73, v55 row_shr:2 row_mask:0xf bank_mask:0xf
	v_mul_f32_e32 v0, 0x4b800000, v71
	v_cmp_gt_f32_e64 s[38:39], s96, v71
	v_cmp_gt_f32_e64 s[36:37], s96, v70
	v_pk_fma_f32 v[72:73], v[74:75], v[72:73], v[86:87]
	v_cndmask_b32_e64 v0, v71, v0, s[38:39]
	v_rsq_f32_e32 v0, v0
	v_pk_mul_f32 v[38:39], v[68:69], v[38:39] op_sel_hi:[0,1]
	v_pk_mul_f32 v[56:57], v[68:69], v[56:57] op_sel_hi:[0,1]
	v_pk_mul_f32 v[40:41], v[68:69], v[40:41] op_sel_hi:[0,1]
	v_mul_f32_e32 v66, 0x45800000, v0
	v_cndmask_b32_e64 v66, v0, v66, s[38:39]
	v_mul_f32_e32 v0, 0x4b800000, v70
	v_cndmask_b32_e64 v0, v70, v0, s[36:37]
	v_lshl_add_u64 v[70:71], v[110:111], 0, v[148:149]
	v_rsq_f32_e32 v0, v0
	global_store_dwordx4 v[70:71], v[90:93], off sc1
	v_mov_b32_e32 v70, v1
	v_mov_b32_e32 v71, v1
	v_mul_f32_e32 v67, 0x45800000, v0
	v_mov_b32_dpp v70, v100 row_ror:1 row_mask:0xf bank_mask:0xf
	v_mov_b32_dpp v71, v101 row_ror:1 row_mask:0xf bank_mask:0xf
	v_cndmask_b32_e64 v0, v0, v67, s[36:37]
	v_mov_b32_dpp v70, v54 row_shr:1 row_mask:0xf bank_mask:0xf
	v_mov_b32_dpp v71, v55 row_shr:1 row_mask:0xf bank_mask:0xf
	v_pk_fma_f32 v[70:71], v[78:79], v[70:71], v[72:73]
	v_pk_mul_f32 v[34:35], v[68:69], v[34:35] op_sel_hi:[0,1]
	v_pk_fma_f32 v[70:71], v[54:55], v[82:83], v[70:71]
	v_pk_mul_f32 v[36:37], v[68:69], v[36:37] op_sel_hi:[0,1]
	v_mul_f32_e32 v67, 0x3d372713, v70
	v_mul_f32_e32 v67, v70, v67
	v_fma_f32 v67, v70, v67, v70
	v_mul_f32_e32 v67, 0xc0135761, v67
	v_exp_f32_e32 v67, v67
	v_pk_mul_f32 v[14:15], v[0:1], v[14:15] op_sel_hi:[0,1]
	v_pk_mul_f32 v[6:7], v[0:1], v[6:7] op_sel_hi:[0,1]
	v_pk_mul_f32 v[16:17], v[0:1], v[16:17] op_sel_hi:[0,1]
	v_add_f32_e32 v67, 1.0, v67
	v_rcp_f32_e32 v72, v67
	v_mul_f32_e32 v67, 0x3d372713, v71
	v_mul_f32_e32 v67, v71, v67
	v_fma_f32 v67, v71, v67, v71
	v_mul_f32_e32 v67, 0xc0135761, v67
	v_exp_f32_e32 v67, v67
	v_pk_mul_f32 v[8:9], v[0:1], v[8:9] op_sel_hi:[0,1]
	v_pk_mul_f32 v[2:3], v[0:1], v[2:3] op_sel_hi:[0,1]
	v_pk_mul_f32 v[4:5], v[0:1], v[4:5] op_sel_hi:[0,1]
	v_add_f32_e32 v67, 1.0, v67
	v_rcp_f32_e32 v73, v67
	s_nop 0
	v_pk_mul_f32 v[70:71], v[70:71], v[72:73]
	v_mov_b32_e32 v72, v1
	v_mov_b32_e32 v73, v1
	v_pk_mul_f32 v[70:71], v[38:39], v[70:71]
	v_mov_b32_e32 v38, v1
	v_mov_b32_dpp v72, v98 row_ror:2 row_mask:0xf bank_mask:0xf
	v_mov_b32_e32 v39, v1
	v_mov_b32_dpp v73, v99 row_ror:2 row_mask:0xf bank_mask:0xf
	v_mov_b32_dpp v38, v98 row_ror:1 row_mask:0xf bank_mask:0xf
	v_mov_b32_dpp v72, v56 row_shr:2 row_mask:0xf bank_mask:0xf
	v_mov_b32_dpp v39, v99 row_ror:1 row_mask:0xf bank_mask:0xf
	v_mov_b32_dpp v73, v57 row_shr:2 row_mask:0xf bank_mask:0xf
	v_mov_b32_dpp v38, v56 row_shr:1 row_mask:0xf bank_mask:0xf
	v_mov_b32_dpp v39, v57 row_shr:1 row_mask:0xf bank_mask:0xf
	v_pk_fma_f32 v[72:73], v[76:77], v[72:73], v[88:89]
	s_nop 0
	v_pk_fma_f32 v[38:39], v[80:81], v[38:39], v[72:73]
	s_nop 0
	v_pk_fma_f32 v[38:39], v[56:57], v[84:85], v[38:39]
	s_nop 0
	v_mul_f32_e32 v67, 0x3d372713, v38
	v_mul_f32_e32 v67, v38, v67
	v_fma_f32 v67, v38, v67, v38
	v_mul_f32_e32 v67, 0xc0135761, v67
	v_exp_f32_e32 v67, v67
	s_nop 0
	v_add_f32_e32 v67, 1.0, v67
	v_rcp_f32_e32 v72, v67
	v_mul_f32_e32 v67, 0x3d372713, v39
	v_mul_f32_e32 v67, v39, v67
	v_fma_f32 v67, v39, v67, v39
	v_mul_f32_e32 v67, 0xc0135761, v67
	v_exp_f32_e32 v67, v67
	s_nop 0
	v_add_f32_e32 v67, 1.0, v67
	v_rcp_f32_e32 v73, v67
	v_pk_mul_f32 v[30:31], v[66:67], v[30:31] op_sel_hi:[0,1]
	v_pk_mul_f32 v[22:23], v[66:67], v[22:23] op_sel_hi:[0,1]
	v_pk_mul_f32 v[32:33], v[66:67], v[32:33] op_sel_hi:[0,1]
	v_pk_mul_f32 v[38:39], v[38:39], v[72:73]
	v_pk_mul_f32 v[24:25], v[66:67], v[24:25] op_sel_hi:[0,1]
	v_pk_mul_f32 v[72:73], v[40:41], v[38:39]
	v_pk_mul_f32 v[38:39], v[68:69], v[44:45] op_sel_hi:[0,1]
	v_mov_b32_e32 v44, v1
	v_mov_b32_e32 v45, v1
	v_pk_mul_f32 v[40:41], v[68:69], v[42:43] op_sel_hi:[0,1]
	v_mov_b32_e32 v42, v1
	v_mov_b32_dpp v44, v96 row_ror:2 row_mask:0xf bank_mask:0xf
	v_mov_b32_e32 v43, v1
	v_mov_b32_dpp v45, v97 row_ror:2 row_mask:0xf bank_mask:0xf
	v_mov_b32_dpp v42, v96 row_ror:1 row_mask:0xf bank_mask:0xf
	v_mov_b32_dpp v44, v40 row_shr:2 row_mask:0xf bank_mask:0xf
	v_mov_b32_dpp v43, v97 row_ror:1 row_mask:0xf bank_mask:0xf
	v_mov_b32_dpp v45, v41 row_shr:2 row_mask:0xf bank_mask:0xf
	v_mov_b32_dpp v42, v40 row_shr:1 row_mask:0xf bank_mask:0xf
	v_mov_b32_dpp v43, v41 row_shr:1 row_mask:0xf bank_mask:0xf
	v_pk_fma_f32 v[44:45], v[46:47], v[44:45], v[62:63]
	v_pk_mul_f32 v[18:19], v[66:67], v[18:19] op_sel_hi:[0,1]
	v_pk_fma_f32 v[42:43], v[50:51], v[42:43], v[44:45]
	v_pk_mul_f32 v[20:21], v[66:67], v[20:21] op_sel_hi:[0,1]
	v_pk_fma_f32 v[42:43], v[40:41], v[58:59], v[42:43]
	s_nop 0
	v_mul_f32_e32 v44, 0x3d372713, v42
	v_mul_f32_e32 v45, 0x3d372713, v43
	v_mul_f32_e32 v44, v42, v44
	v_mul_f32_e32 v45, v43, v45
	v_fma_f32 v44, v42, v44, v42
	v_fma_f32 v45, v43, v45, v43
	v_mul_f32_e32 v44, 0xc0135761, v44
	v_mul_f32_e32 v45, 0xc0135761, v45
	v_exp_f32_e32 v44, v44
	v_exp_f32_e32 v45, v45
	v_add_f32_e32 v44, 1.0, v44
	v_add_f32_e32 v45, 1.0, v45
	v_rcp_f32_e32 v44, v44
	v_rcp_f32_e32 v45, v45
	s_nop 0
	v_pk_mul_f32 v[42:43], v[42:43], v[44:45]
	v_mov_b32_e32 v44, v1
	v_mov_b32_e32 v45, v1
	v_pk_mul_f32 v[34:35], v[34:35], v[42:43]
	v_mov_b32_e32 v42, v1
	v_mov_b32_dpp v44, v94 row_ror:2 row_mask:0xf bank_mask:0xf
	v_mov_b32_e32 v43, v1
	v_mov_b32_dpp v45, v95 row_ror:2 row_mask:0xf bank_mask:0xf
	v_mov_b32_dpp v42, v94 row_ror:1 row_mask:0xf bank_mask:0xf
	v_mov_b32_dpp v44, v38 row_shr:2 row_mask:0xf bank_mask:0xf
	v_mov_b32_dpp v43, v95 row_ror:1 row_mask:0xf bank_mask:0xf
	v_mov_b32_dpp v45, v39 row_shr:2 row_mask:0xf bank_mask:0xf
	v_mov_b32_dpp v42, v38 row_shr:1 row_mask:0xf bank_mask:0xf
	v_mov_b32_dpp v43, v39 row_shr:1 row_mask:0xf bank_mask:0xf
	v_pk_fma_f32 v[44:45], v[48:49], v[44:45], v[64:65]
	s_nop 0
	v_pk_fma_f32 v[42:43], v[52:53], v[42:43], v[44:45]
	s_nop 0
	v_pk_fma_f32 v[42:43], v[38:39], v[60:61], v[42:43]
	s_nop 0
	v_mul_f32_e32 v44, 0x3d372713, v42
	v_mul_f32_e32 v45, 0x3d372713, v43
	v_mul_f32_e32 v44, v42, v44
	v_mul_f32_e32 v45, v43, v45
	v_fma_f32 v44, v42, v44, v42
	v_fma_f32 v45, v43, v45, v43
	v_mul_f32_e32 v44, 0xc0135761, v44
	v_mul_f32_e32 v45, 0xc0135761, v45
	v_exp_f32_e32 v44, v44
	v_exp_f32_e32 v45, v45
	v_add_f32_e32 v44, 1.0, v44
	v_add_f32_e32 v45, 1.0, v45
	v_rcp_f32_e32 v44, v44
	v_rcp_f32_e32 v45, v45
	s_nop 0
	v_pk_mul_f32 v[42:43], v[42:43], v[44:45]
	s_nop 0
	v_pk_mul_f32 v[36:37], v[36:37], v[42:43]
	v_cvt_pk_bf16_f32 v44, v34, v35
	v_cvt_pk_bf16_f32 v45, v36, v37
	v_add_u32_e32 v36, 0x90, v193
	v_mov_b64_e32 v[34:35], s[16:17]
	v_mad_i64_i32 v[36:37], s[36:37], v36, s2, v[34:35]
	v_cvt_pk_bf16_f32 v42, v70, v71
	v_cvt_pk_bf16_f32 v43, v72, v73
	v_lshl_add_u64 v[36:37], v[36:37], 0, v[148:149]
	global_store_dwordx4 v[36:37], v[42:45], off sc1
	v_mov_b32_e32 v36, v1
	v_mov_b32_e32 v37, v1
	v_mov_b32_e32 v42, v1
	v_mov_b32_e32 v43, v1
	v_mov_b32_dpp v36, v54 row_ror:1 row_mask:0xf bank_mask:0xf
	v_mov_b32_dpp v42, v54 row_ror:2 row_mask:0xf bank_mask:0xf
	v_mov_b32_dpp v43, v55 row_ror:2 row_mask:0xf bank_mask:0xf
	v_mov_b32_dpp v37, v55 row_ror:1 row_mask:0xf bank_mask:0xf
	v_mov_b32_dpp v42, v30 row_shr:2 row_mask:0xf bank_mask:0xf
	v_mov_b32_dpp v43, v31 row_shr:2 row_mask:0xf bank_mask:0xf
	v_mov_b32_dpp v36, v30 row_shr:1 row_mask:0xf bank_mask:0xf
	v_mov_b32_dpp v37, v31 row_shr:1 row_mask:0xf bank_mask:0xf
	v_pk_fma_f32 v[42:43], v[74:75], v[42:43], v[86:87]
	s_nop 0
	v_pk_fma_f32 v[36:37], v[78:79], v[36:37], v[42:43]
	s_nop 0
	v_pk_fma_f32 v[36:37], v[30:31], v[82:83], v[36:37]
	s_nop 0
	v_mul_f32_e32 v42, 0x3d372713, v36
	v_mul_f32_e32 v43, 0x3d372713, v37
	v_mul_f32_e32 v42, v36, v42
	v_mul_f32_e32 v43, v37, v43
	v_fma_f32 v42, v36, v42, v36
	v_fma_f32 v43, v37, v43, v37
	v_mul_f32_e32 v42, 0xc0135761, v42
	v_mul_f32_e32 v43, 0xc0135761, v43
	v_exp_f32_e32 v42, v42
	v_exp_f32_e32 v43, v43
	v_add_f32_e32 v42, 1.0, v42
	v_add_f32_e32 v43, 1.0, v43
	v_rcp_f32_e32 v42, v42
	v_rcp_f32_e32 v43, v43
	s_nop 0
	v_pk_mul_f32 v[36:37], v[36:37], v[42:43]
	v_mov_b32_e32 v42, v1
	v_mov_b32_e32 v43, v1
	v_pk_mul_f32 v[36:37], v[22:23], v[36:37]
	v_mov_b32_e32 v22, v1
	v_mov_b32_dpp v42, v56 row_ror:2 row_mask:0xf bank_mask:0xf
	v_mov_b32_e32 v23, v1
	v_mov_b32_dpp v43, v57 row_ror:2 row_mask:0xf bank_mask:0xf
	v_mov_b32_dpp v22, v56 row_ror:1 row_mask:0xf bank_mask:0xf
	v_mov_b32_dpp v42, v32 row_shr:2 row_mask:0xf bank_mask:0xf
	v_mov_b32_dpp v23, v57 row_ror:1 row_mask:0xf bank_mask:0xf
	v_mov_b32_dpp v43, v33 row_shr:2 row_mask:0xf bank_mask:0xf
	v_mov_b32_dpp v22, v32 row_shr:1 row_mask:0xf bank_mask:0xf
	v_mov_b32_dpp v23, v33 row_shr:1 row_mask:0xf bank_mask:0xf
	v_pk_fma_f32 v[42:43], v[76:77], v[42:43], v[88:89]
	s_nop 0
	v_pk_fma_f32 v[22:23], v[80:81], v[22:23], v[42:43]
	s_nop 0
	v_pk_fma_f32 v[22:23], v[32:33], v[84:85], v[22:23]
	s_nop 0
	v_mul_f32_e32 v42, 0x3d372713, v22
	v_mul_f32_e32 v43, 0x3d372713, v23
	v_mul_f32_e32 v42, v22, v42
	v_mul_f32_e32 v43, v23, v43
	v_fma_f32 v42, v22, v42, v22
	v_fma_f32 v43, v23, v43, v23
	v_mul_f32_e32 v42, 0xc0135761, v42
	v_mul_f32_e32 v43, 0xc0135761, v43
	v_exp_f32_e32 v42, v42
	v_exp_f32_e32 v43, v43
	v_add_f32_e32 v42, 1.0, v42
	v_add_f32_e32 v43, 1.0, v43
	v_rcp_f32_e32 v42, v42
	v_rcp_f32_e32 v43, v43
	s_nop 0
	v_pk_mul_f32 v[22:23], v[22:23], v[42:43]
	s_nop 0
	v_pk_mul_f32 v[42:43], v[24:25], v[22:23]
	v_pk_mul_f32 v[22:23], v[66:67], v[28:29] op_sel_hi:[0,1]
	v_mov_b32_e32 v28, v1
	v_mov_b32_e32 v29, v1
	v_pk_mul_f32 v[24:25], v[66:67], v[26:27] op_sel_hi:[0,1]
	v_mov_b32_e32 v26, v1
	v_mov_b32_dpp v28, v40 row_ror:2 row_mask:0xf bank_mask:0xf
	v_mov_b32_e32 v27, v1
	v_mov_b32_dpp v29, v41 row_ror:2 row_mask:0xf bank_mask:0xf
	v_mov_b32_dpp v26, v40 row_ror:1 row_mask:0xf bank_mask:0xf
	v_mov_b32_dpp v28, v24 row_shr:2 row_mask:0xf bank_mask:0xf
	v_mov_b32_dpp v27, v41 row_ror:1 row_mask:0xf bank_mask:0xf
	v_mov_b32_dpp v29, v25 row_shr:2 row_mask:0xf bank_mask:0xf
	v_mov_b32_dpp v26, v24 row_shr:1 row_mask:0xf bank_mask:0xf
	v_mov_b32_dpp v27, v25 row_shr:1 row_mask:0xf bank_mask:0xf
	v_pk_fma_f32 v[28:29], v[46:47], v[28:29], v[62:63]
	s_nop 0
	v_pk_fma_f32 v[26:27], v[50:51], v[26:27], v[28:29]
	s_nop 0
	v_pk_fma_f32 v[26:27], v[24:25], v[58:59], v[26:27]
	s_nop 0
	v_mul_f32_e32 v28, 0x3d372713, v26
	v_mul_f32_e32 v29, 0x3d372713, v27
	v_mul_f32_e32 v28, v26, v28
	v_mul_f32_e32 v29, v27, v29
	v_fma_f32 v28, v26, v28, v26
	v_fma_f32 v29, v27, v29, v27
	v_mul_f32_e32 v28, 0xc0135761, v28
	v_mul_f32_e32 v29, 0xc0135761, v29
	v_exp_f32_e32 v28, v28
	v_exp_f32_e32 v29, v29
	v_add_f32_e32 v28, 1.0, v28
	v_add_f32_e32 v29, 1.0, v29
	v_rcp_f32_e32 v28, v28
	v_rcp_f32_e32 v29, v29
	s_nop 0
	v_pk_mul_f32 v[26:27], v[26:27], v[28:29]
	v_mov_b32_e32 v28, v1
	v_mov_b32_e32 v29, v1
	v_pk_mul_f32 v[26:27], v[18:19], v[26:27]
	v_mov_b32_e32 v18, v1
	v_mov_b32_dpp v28, v38 row_ror:2 row_mask:0xf bank_mask:0xf
	v_mov_b32_e32 v19, v1
	v_mov_b32_dpp v29, v39 row_ror:2 row_mask:0xf bank_mask:0xf
	v_mov_b32_dpp v18, v38 row_ror:1 row_mask:0xf bank_mask:0xf
	v_mov_b32_dpp v28, v22 row_shr:2 row_mask:0xf bank_mask:0xf
	v_mov_b32_dpp v19, v39 row_ror:1 row_mask:0xf bank_mask:0xf
	v_mov_b32_dpp v29, v23 row_shr:2 row_mask:0xf bank_mask:0xf
	v_mov_b32_dpp v18, v22 row_shr:1 row_mask:0xf bank_mask:0xf
	v_mov_b32_dpp v19, v23 row_shr:1 row_mask:0xf bank_mask:0xf
	v_pk_fma_f32 v[28:29], v[48:49], v[28:29], v[64:65]
	s_nop 0
	v_pk_fma_f32 v[18:19], v[52:53], v[18:19], v[28:29]
	s_nop 0
	v_pk_fma_f32 v[18:19], v[22:23], v[60:61], v[18:19]
	s_nop 0
	v_mul_f32_e32 v28, 0x3d372713, v18
	v_mul_f32_e32 v29, 0x3d372713, v19
	v_mul_f32_e32 v28, v18, v28
	v_mul_f32_e32 v29, v19, v29
	v_fma_f32 v28, v18, v28, v18
	v_fma_f32 v29, v19, v29, v19
	v_mul_f32_e32 v28, 0xc0135761, v28
	v_mul_f32_e32 v29, 0xc0135761, v29
	v_exp_f32_e32 v28, v28
	v_exp_f32_e32 v29, v29
	v_add_f32_e32 v28, 1.0, v28
	v_add_f32_e32 v29, 1.0, v29
	v_rcp_f32_e32 v28, v28
	v_rcp_f32_e32 v29, v29
	s_nop 0
	v_pk_mul_f32 v[18:19], v[18:19], v[28:29]
	s_nop 0
	v_pk_mul_f32 v[28:29], v[20:21], v[18:19]
	v_cvt_pk_bf16_f32 v20, v26, v27
	v_add_u32_e32 v26, 0xa0, v193
	v_mad_i64_i32 v[26:27], s[36:37], v26, s2, v[34:35]
	v_cvt_pk_bf16_f32 v18, v36, v37
	v_cvt_pk_bf16_f32 v19, v42, v43
	v_cvt_pk_bf16_f32 v21, v28, v29
	v_lshl_add_u64 v[26:27], v[26:27], 0, v[148:149]
	global_store_dwordx4 v[26:27], v[18:21], off sc1
	s_nop 1
	v_mov_b32_e32 v20, v1
	v_mov_b32_e32 v21, v1
	v_mov_b32_e32 v18, v1
	v_mov_b32_dpp v20, v30 row_ror:2 row_mask:0xf bank_mask:0xf
	v_mov_b32_e32 v19, v1
	v_mov_b32_dpp v21, v31 row_ror:2 row_mask:0xf bank_mask:0xf
	v_mov_b32_dpp v18, v30 row_ror:1 row_mask:0xf bank_mask:0xf
	v_mov_b32_dpp v20, v14 row_shr:2 row_mask:0xf bank_mask:0xf
	v_mov_b32_dpp v19, v31 row_ror:1 row_mask:0xf bank_mask:0xf
	v_mov_b32_dpp v21, v15 row_shr:2 row_mask:0xf bank_mask:0xf
	v_mov_b32_dpp v18, v14 row_shr:1 row_mask:0xf bank_mask:0xf
	v_mov_b32_dpp v19, v15 row_shr:1 row_mask:0xf bank_mask:0xf
	v_pk_fma_f32 v[20:21], v[74:75], v[20:21], v[86:87]
	s_nop 0
	v_pk_fma_f32 v[18:19], v[78:79], v[18:19], v[20:21]
	s_nop 0
	v_pk_fma_f32 v[18:19], v[14:15], v[82:83], v[18:19]
	s_nop 0
	v_mul_f32_e32 v20, 0x3d372713, v18
	v_mul_f32_e32 v21, 0x3d372713, v19
	v_mul_f32_e32 v20, v18, v20
	v_mul_f32_e32 v21, v19, v21
	v_fma_f32 v20, v18, v20, v18
	v_fma_f32 v21, v19, v21, v19
	v_mul_f32_e32 v20, 0xc0135761, v20
	v_mul_f32_e32 v21, 0xc0135761, v21
	v_exp_f32_e32 v20, v20
	v_exp_f32_e32 v21, v21
	v_add_f32_e32 v20, 1.0, v20
	v_add_f32_e32 v21, 1.0, v21
	v_rcp_f32_e32 v20, v20
	v_rcp_f32_e32 v21, v21
	s_nop 0
	v_pk_mul_f32 v[18:19], v[18:19], v[20:21]
	v_mov_b32_e32 v20, v1
	v_mov_b32_e32 v21, v1
	v_pk_mul_f32 v[18:19], v[6:7], v[18:19]
	v_mov_b32_e32 v6, v1
	v_mov_b32_dpp v20, v32 row_ror:2 row_mask:0xf bank_mask:0xf
	v_mov_b32_e32 v7, v1
	v_mov_b32_dpp v21, v33 row_ror:2 row_mask:0xf bank_mask:0xf
	v_mov_b32_dpp v6, v32 row_ror:1 row_mask:0xf bank_mask:0xf
	v_mov_b32_dpp v20, v16 row_shr:2 row_mask:0xf bank_mask:0xf
	v_mov_b32_dpp v7, v33 row_ror:1 row_mask:0xf bank_mask:0xf
	v_mov_b32_dpp v21, v17 row_shr:2 row_mask:0xf bank_mask:0xf
	v_mov_b32_dpp v6, v16 row_shr:1 row_mask:0xf bank_mask:0xf
	v_mov_b32_dpp v7, v17 row_shr:1 row_mask:0xf bank_mask:0xf
	v_pk_fma_f32 v[20:21], v[76:77], v[20:21], v[88:89]
	s_nop 0
	v_pk_fma_f32 v[6:7], v[80:81], v[6:7], v[20:21]
	s_nop 0
	v_pk_fma_f32 v[6:7], v[16:17], v[84:85], v[6:7]
	s_nop 0
	v_mul_f32_e32 v20, 0x3d372713, v6
	v_mul_f32_e32 v21, 0x3d372713, v7
	v_mul_f32_e32 v20, v6, v20
	v_mul_f32_e32 v21, v7, v21
	v_fma_f32 v20, v6, v20, v6
	v_fma_f32 v21, v7, v21, v7
	v_mul_f32_e32 v20, 0xc0135761, v20
	v_mul_f32_e32 v21, 0xc0135761, v21
	v_exp_f32_e32 v20, v20
	v_exp_f32_e32 v21, v21
	v_add_f32_e32 v20, 1.0, v20
	v_add_f32_e32 v21, 1.0, v21
	v_rcp_f32_e32 v20, v20
	v_rcp_f32_e32 v21, v21
	s_nop 0
	v_pk_mul_f32 v[6:7], v[6:7], v[20:21]
	s_nop 0
	v_pk_mul_f32 v[20:21], v[8:9], v[6:7]
	v_pk_mul_f32 v[6:7], v[0:1], v[12:13] op_sel_hi:[0,1]
	v_mov_b32_e32 v12, v1
	v_mov_b32_e32 v13, v1
	v_pk_mul_f32 v[8:9], v[0:1], v[10:11] op_sel_hi:[0,1]
	v_mov_b32_e32 v10, v1
	v_mov_b32_dpp v12, v24 row_ror:2 row_mask:0xf bank_mask:0xf
	v_mov_b32_e32 v11, v1
	v_mov_b32_dpp v13, v25 row_ror:2 row_mask:0xf bank_mask:0xf
	v_mov_b32_dpp v10, v24 row_ror:1 row_mask:0xf bank_mask:0xf
	v_mov_b32_dpp v12, v8 row_shr:2 row_mask:0xf bank_mask:0xf
	v_mov_b32_dpp v11, v25 row_ror:1 row_mask:0xf bank_mask:0xf
	v_mov_b32_dpp v13, v9 row_shr:2 row_mask:0xf bank_mask:0xf
	v_mov_b32_dpp v10, v8 row_shr:1 row_mask:0xf bank_mask:0xf
	v_mov_b32_dpp v11, v9 row_shr:1 row_mask:0xf bank_mask:0xf
	v_pk_fma_f32 v[12:13], v[46:47], v[12:13], v[62:63]
	s_nop 0
	v_pk_fma_f32 v[10:11], v[50:51], v[10:11], v[12:13]
	s_nop 0
	v_pk_fma_f32 v[10:11], v[8:9], v[58:59], v[10:11]
	s_nop 0
	v_mul_f32_e32 v12, 0x3d372713, v10
	v_mul_f32_e32 v13, 0x3d372713, v11
	v_mul_f32_e32 v12, v10, v12
	v_mul_f32_e32 v13, v11, v13
	v_fma_f32 v12, v10, v12, v10
	v_fma_f32 v13, v11, v13, v11
	v_mul_f32_e32 v12, 0xc0135761, v12
	v_mul_f32_e32 v13, 0xc0135761, v13
	v_exp_f32_e32 v12, v12
	v_exp_f32_e32 v13, v13
	v_add_f32_e32 v12, 1.0, v12
	v_add_f32_e32 v13, 1.0, v13
	v_rcp_f32_e32 v12, v12
	v_rcp_f32_e32 v13, v13
	s_nop 0
	v_pk_mul_f32 v[10:11], v[10:11], v[12:13]
	v_mov_b32_e32 v12, v1
	v_mov_b32_e32 v13, v1
	v_pk_mul_f32 v[10:11], v[2:3], v[10:11]
	v_mov_b32_e32 v2, v1
	v_mov_b32_dpp v12, v22 row_ror:2 row_mask:0xf bank_mask:0xf
	v_mov_b32_e32 v3, v1
	v_mov_b32_dpp v13, v23 row_ror:2 row_mask:0xf bank_mask:0xf
	v_mov_b32_dpp v2, v22 row_ror:1 row_mask:0xf bank_mask:0xf
	v_mov_b32_dpp v12, v6 row_shr:2 row_mask:0xf bank_mask:0xf
	v_mov_b32_dpp v3, v23 row_ror:1 row_mask:0xf bank_mask:0xf
	v_mov_b32_dpp v13, v7 row_shr:2 row_mask:0xf bank_mask:0xf
	v_mov_b32_dpp v2, v6 row_shr:1 row_mask:0xf bank_mask:0xf
	v_mov_b32_dpp v3, v7 row_shr:1 row_mask:0xf bank_mask:0xf
	v_pk_fma_f32 v[12:13], v[48:49], v[12:13], v[64:65]
	s_nop 0
	v_pk_fma_f32 v[2:3], v[52:53], v[2:3], v[12:13]
	s_nop 0
	v_pk_fma_f32 v[2:3], v[6:7], v[60:61], v[2:3]
	s_nop 0
	v_mul_f32_e32 v12, 0x3d372713, v2
	v_mul_f32_e32 v0, 0x3d372713, v3
	v_mul_f32_e32 v12, v2, v12
	v_mul_f32_e32 v0, v3, v0
	v_fma_f32 v12, v2, v12, v2
	v_fma_f32 v0, v3, v0, v3
	v_mul_f32_e32 v12, 0xc0135761, v12
	v_mul_f32_e32 v0, 0xc0135761, v0
	v_exp_f32_e32 v12, v12
	v_exp_f32_e32 v0, v0
	v_add_f32_e32 v12, 1.0, v12
	v_add_f32_e32 v0, 1.0, v0
	v_rcp_f32_e32 v12, v12
	v_rcp_f32_e32 v13, v0
	v_add_u32_e32 v0, 0xb0, v193
	v_pk_mul_f32 v[2:3], v[2:3], v[12:13]
	s_nop 0
	v_pk_mul_f32 v[12:13], v[4:5], v[2:3]
	v_cvt_pk_bf16_f32 v4, v10, v11
	v_mad_i64_i32 v[10:11], s[36:37], v0, s2, v[34:35]
	v_cvt_pk_bf16_f32 v2, v18, v19
	v_cvt_pk_bf16_f32 v3, v20, v21
	v_cvt_pk_bf16_f32 v5, v12, v13
	v_lshl_add_u64 v[10:11], v[10:11], 0, v[148:149]
	global_store_dwordx4 v[10:11], v[2:5], off sc1
	s_and_saveexec_b64 s[36:37], vcc
	s_cbranch_execz .LBB0_372
	v_lshl_add_u64 v[10:11], v[146:147], 0, s[40:41]
	v_cvt_pk_bf16_f32 v5, v6, v7
	v_mov_b64_e32 v[6:7], s[42:43]
	v_mad_u64_u32 v[6:7], s[38:39], v10, s2, v[6:7]
	v_mad_i32_i24 v7, v11, s2, v7
	v_cvt_pk_bf16_f32 v2, v14, v15
	v_cvt_pk_bf16_f32 v3, v16, v17
	v_cvt_pk_bf16_f32 v4, v8, v9
	v_lshl_add_u64 v[6:7], v[182:183], 1, v[6:7]
	global_store_dwordx4 v[6:7], v[2:5], off sc1

.LBB0_404:
	s_mov_b32 s0, -1
	s_add_u32 s14, s74, 0x2200000
	s_waitcnt vmcnt(0)
	s_barrier
	s_addc_u32 s15, s75, 0
	v_mbcnt_lo_u32_b32 v0, s0, 0
	v_mbcnt_hi_u32_b32 v166, s0, v0
	s_lshl_b32 s0, s88, 8
	v_and_b32_e32 v130, 15, v166
	s_add_i32 s17, s0, s63
	v_or_b32_e32 v156, s17, v130
	s_ashr_i32 s17, s16, 31
	s_lshl_b32 s1, s62, 5
	s_lshl_b64 s[16:17], s[16:17], 8
	v_lshrrev_b32_e32 v0, 1, v166
	s_or_b32 s16, s16, s1
	v_and_b32_e32 v0, 56, v0
	v_and_b32_e32 v131, 64, v231
	v_lshl_add_u64 v[154:155], s[16:17], 0, v[0:1]
	v_xor_b32_e32 v0, 16, v231
	v_add_u32_e32 v131, 64, v131
	v_cmp_lt_i32_e32 vcc, v0, v131
	v_lshlrev_b64 v[178:179], 1, v[154:155]
	s_mov_b64 s[16:17], 0x8800000
	v_cndmask_b32_e32 v0, v231, v0, vcc
	v_lshlrev_b32_e32 v168, 2, v0
	v_xor_b32_e32 v0, 32, v231
	v_cmp_lt_i32_e32 vcc, v0, v131
	v_ashrrev_i32_e32 v157, 31, v156
	v_lshlrev_b64 v[180:181], 11, v[156:157]
	v_cndmask_b32_e32 v0, v231, v0, vcc
	v_lshlrev_b32_e32 v167, 2, v0
	v_or_b32_e32 v0, s63, v130
	v_lshl_add_u64 v[130:131], s[74:75], 0, v[178:179]
	v_lshl_add_u64 v[158:159], v[130:131], 0, s[16:17]
	v_lshl_add_u64 v[130:131], v[158:159], 0, v[180:181]
	global_load_dwordx4 v[170:173], v[130:131], off
	global_load_dwordx4 v[174:177], v[130:131], off offset:256
	v_or_b32_e32 v130, 16, v156
	v_ashrrev_i32_e32 v131, 31, v130
	v_lshlrev_b64 v[164:165], 11, v[130:131]
	v_lshl_add_u64 v[130:131], v[158:159], 0, v[164:165]
	global_load_dwordx4 v[150:153], v[130:131], off
	global_load_dwordx4 v[146:149], v[130:131], off offset:256
	v_or_b32_e32 v130, 32, v156
	v_ashrrev_i32_e32 v131, 31, v130
	v_lshlrev_b64 v[162:163], 11, v[130:131]
	v_lshl_add_u64 v[130:131], v[158:159], 0, v[162:163]
	global_load_dwordx4 v[142:145], v[130:131], off
	global_load_dwordx4 v[138:141], v[130:131], off offset:256
	v_or_b32_e32 v130, 48, v156
	v_ashrrev_i32_e32 v131, 31, v130
	v_lshlrev_b64 v[160:161], 11, v[130:131]
	v_lshl_add_u64 v[130:131], v[158:159], 0, v[160:161]
	global_load_dwordx4 v[134:137], v[130:131], off
	s_nop 0
	global_load_dwordx4 v[130:133], v[130:131], off offset:256
	v_lshl_add_u64 v[180:181], s[14:15], 0, v[180:181]
	v_lshl_add_u64 v[178:179], v[180:181], 0, v[178:179]
	v_cmp_gt_u32_e32 vcc, 16, v166
	s_lshl_b32 s1, s62, 2
	s_waitcnt vmcnt(0)
	v_lshlrev_b32_e32 v182, 16, v170
	v_and_b32_e32 v183, 0xffff0000, v170
	v_lshlrev_b32_e32 v170, 16, v171
	v_and_b32_e32 v171, 0xffff0000, v171
	v_pk_add_f32 v[128:129], v[128:129], v[170:171]
	v_lshlrev_b32_e32 v170, 16, v172
	v_and_b32_e32 v171, 0xffff0000, v172
	v_pk_add_f32 v[170:171], v[122:123], v[170:171]
	v_lshlrev_b32_e32 v122, 16, v173
	v_and_b32_e32 v123, 0xffff0000, v173
	v_pk_add_f32 v[126:127], v[126:127], v[182:183]
	v_pk_add_f32 v[172:173], v[124:125], v[122:123]
	v_cvt_pk_bf16_f32 v122, v126, v127
	v_cvt_pk_bf16_f32 v123, v128, v129
	v_cvt_pk_bf16_f32 v124, v170, v171
	v_cvt_pk_bf16_f32 v125, v172, v173
	global_store_dwordx4 v[178:179], v[122:125], off sc1
	s_nop 1
	v_pk_mul_f32 v[122:123], v[126:127], v[126:127]
	v_pk_mul_f32 v[126:127], v[170:171], v[170:171]
	v_lshlrev_b32_e32 v170, 16, v174
	v_and_b32_e32 v171, 0xffff0000, v174
	v_pk_add_f32 v[118:119], v[118:119], v[170:171]
	v_lshlrev_b32_e32 v170, 16, v175
	v_and_b32_e32 v171, 0xffff0000, v175
	v_pk_add_f32 v[120:121], v[120:121], v[170:171]
	v_lshlrev_b32_e32 v170, 16, v176
	v_and_b32_e32 v171, 0xffff0000, v176
	v_pk_add_f32 v[170:171], v[114:115], v[170:171]
	v_lshlrev_b32_e32 v114, 16, v177
	v_and_b32_e32 v115, 0xffff0000, v177
	v_pk_mul_f32 v[124:125], v[128:129], v[128:129]
	v_pk_mul_f32 v[128:129], v[172:173], v[172:173]
	v_pk_add_f32 v[172:173], v[116:117], v[114:115]
	v_cvt_pk_bf16_f32 v114, v118, v119
	v_cvt_pk_bf16_f32 v115, v120, v121
	v_cvt_pk_bf16_f32 v116, v170, v171
	v_cvt_pk_bf16_f32 v117, v172, v173
	global_store_dwordx4 v[178:179], v[114:117], off offset:256 sc1
	s_nop 1
	v_pk_mul_f32 v[114:115], v[118:119], v[118:119]
	v_pk_mul_f32 v[116:117], v[120:121], v[120:121]
	v_add_f32_e32 v114, v114, v115
	v_add_f32_e32 v116, v116, v117
	v_pk_mul_f32 v[118:119], v[170:171], v[170:171]
	v_pk_mul_f32 v[120:121], v[172:173], v[172:173]
	v_add_f32_e32 v114, v114, v116
	v_add_f32_e32 v115, v128, v129
	v_add_f32_e32 v116, v126, v127
	v_add_f32_e32 v120, v120, v121
	v_add_f32_e32 v118, v118, v119
	v_add_f32_e32 v115, v116, v115
	v_add_f32_e32 v116, v124, v125
	v_add_f32_e32 v117, v122, v123
	v_add_f32_e32 v118, v118, v120
	v_add_f32_e32 v116, v117, v116
	v_add_f32_e32 v114, v114, v118
	v_add_f32_e32 v115, v116, v115
	v_add_f32_e32 v114, v115, v114
	ds_bpermute_b32 v115, v168, v114
	s_waitcnt lgkmcnt(0)
	v_add_f32_e32 v114, v114, v115
	ds_bpermute_b32 v115, v167, v114
	s_and_saveexec_b64 s[16:17], vcc
	s_cbranch_execz .LBB0_406
	v_lshl_or_b32 v116, v0, 4, s1
	s_waitcnt lgkmcnt(0)
	v_add_f32_e32 v114, v114, v115
	ds_write_b32 v116, v114
.LBB0_406:
	s_or_b64 exec, exec, s[16:17]
	v_lshlrev_b32_e32 v114, 16, v150
	s_waitcnt lgkmcnt(0)
	v_and_b32_e32 v115, 0xffff0000, v150
	v_pk_add_f32 v[110:111], v[110:111], v[114:115]
	v_lshlrev_b32_e32 v114, 16, v151
	v_and_b32_e32 v115, 0xffff0000, v151
	v_pk_add_f32 v[112:113], v[112:113], v[114:115]
	v_lshlrev_b32_e32 v114, 16, v152
	v_and_b32_e32 v115, 0xffff0000, v152
	v_pk_add_f32 v[114:115], v[106:107], v[114:115]
	v_lshlrev_b32_e32 v106, 16, v153
	v_and_b32_e32 v107, 0xffff0000, v153
	v_pk_add_f32 v[116:117], v[108:109], v[106:107]
	v_lshl_add_u64 v[118:119], s[14:15], 0, v[164:165]
	v_cvt_pk_bf16_f32 v106, v110, v111
	v_cvt_pk_bf16_f32 v107, v112, v113
	v_cvt_pk_bf16_f32 v108, v114, v115
	v_cvt_pk_bf16_f32 v109, v116, v117
	v_lshl_add_u64 v[118:119], v[154:155], 1, v[118:119]
	global_store_dwordx4 v[118:119], v[106:109], off sc1
	s_nop 1
	v_pk_mul_f32 v[106:107], v[110:111], v[110:111]
	v_pk_mul_f32 v[110:111], v[114:115], v[114:115]
	v_lshlrev_b32_e32 v114, 16, v146
	v_and_b32_e32 v115, 0xffff0000, v146
	v_pk_add_f32 v[102:103], v[102:103], v[114:115]
	v_lshlrev_b32_e32 v114, 16, v147
	v_and_b32_e32 v115, 0xffff0000, v147
	v_pk_add_f32 v[104:105], v[104:105], v[114:115]
	v_lshlrev_b32_e32 v114, 16, v148
	v_and_b32_e32 v115, 0xffff0000, v148
	v_pk_add_f32 v[114:115], v[98:99], v[114:115]
	v_lshlrev_b32_e32 v98, 16, v149
	v_and_b32_e32 v99, 0xffff0000, v149
	v_pk_mul_f32 v[108:109], v[112:113], v[112:113]
	v_pk_mul_f32 v[112:113], v[116:117], v[116:117]
	v_pk_add_f32 v[116:117], v[100:101], v[98:99]
	v_cvt_pk_bf16_f32 v98, v102, v103
	v_cvt_pk_bf16_f32 v99, v104, v105
	v_cvt_pk_bf16_f32 v100, v114, v115
	v_cvt_pk_bf16_f32 v101, v116, v117
	global_store_dwordx4 v[118:119], v[98:101], off offset:256 sc1
	s_nop 1
	v_pk_mul_f32 v[98:99], v[102:103], v[102:103]
	v_pk_mul_f32 v[100:101], v[104:105], v[104:105]
	v_add_f32_e32 v98, v98, v99
	v_add_f32_e32 v100, v100, v101
	v_pk_mul_f32 v[102:103], v[114:115], v[114:115]
	v_pk_mul_f32 v[104:105], v[116:117], v[116:117]
	v_add_f32_e32 v98, v98, v100
	v_add_f32_e32 v99, v112, v113
	v_add_f32_e32 v100, v110, v111
	v_add_f32_e32 v104, v104, v105
	v_add_f32_e32 v102, v102, v103
	v_add_f32_e32 v99, v100, v99
	v_add_f32_e32 v100, v108, v109
	v_add_f32_e32 v101, v106, v107
	v_add_f32_e32 v102, v102, v104
	v_add_f32_e32 v100, v101, v100
	v_add_f32_e32 v98, v98, v102
	v_add_f32_e32 v99, v100, v99
	v_add_f32_e32 v98, v99, v98
	ds_bpermute_b32 v99, v168, v98
	s_waitcnt lgkmcnt(0)
	v_add_f32_e32 v98, v98, v99
	ds_bpermute_b32 v99, v167, v98
	s_and_saveexec_b64 s[16:17], vcc
	s_mov_b32 s89, 0x2e8ba2e9
	s_mov_b32 s29, 0x47800000
	s_cbranch_execz .LBB0_408
	v_lshl_or_b32 v100, v0, 4, s1
	s_waitcnt lgkmcnt(0)
	v_add_f32_e32 v98, v98, v99
	ds_write_b32 v100, v98 offset:256
.LBB0_408:
	s_or_b64 exec, exec, s[16:17]
	v_lshlrev_b32_e32 v98, 16, v142
	s_waitcnt lgkmcnt(0)
	v_and_b32_e32 v99, 0xffff0000, v142
	v_pk_add_f32 v[94:95], v[94:95], v[98:99]
	v_lshlrev_b32_e32 v98, 16, v143
	v_and_b32_e32 v99, 0xffff0000, v143
	v_pk_add_f32 v[96:97], v[96:97], v[98:99]
	v_lshlrev_b32_e32 v98, 16, v144
	v_and_b32_e32 v99, 0xffff0000, v144
	v_pk_add_f32 v[98:99], v[90:91], v[98:99]
	v_lshlrev_b32_e32 v90, 16, v145
	v_and_b32_e32 v91, 0xffff0000, v145
	v_pk_add_f32 v[100:101], v[92:93], v[90:91]
	v_lshl_add_u64 v[102:103], s[14:15], 0, v[162:163]
	v_cvt_pk_bf16_f32 v90, v94, v95
	v_cvt_pk_bf16_f32 v91, v96, v97
	v_cvt_pk_bf16_f32 v92, v98, v99
	v_cvt_pk_bf16_f32 v93, v100, v101
	v_lshl_add_u64 v[102:103], v[154:155], 1, v[102:103]
	global_store_dwordx4 v[102:103], v[90:93], off sc1
	s_nop 1
	v_pk_mul_f32 v[90:91], v[94:95], v[94:95]
	v_pk_mul_f32 v[94:95], v[98:99], v[98:99]
	v_lshlrev_b32_e32 v98, 16, v138
	v_and_b32_e32 v99, 0xffff0000, v138
	v_pk_add_f32 v[86:87], v[86:87], v[98:99]
	v_lshlrev_b32_e32 v98, 16, v139
	v_and_b32_e32 v99, 0xffff0000, v139
	v_pk_add_f32 v[88:89], v[88:89], v[98:99]
	v_lshlrev_b32_e32 v98, 16, v140
	v_and_b32_e32 v99, 0xffff0000, v140
	v_pk_add_f32 v[98:99], v[82:83], v[98:99]
	v_lshlrev_b32_e32 v82, 16, v141
	v_and_b32_e32 v83, 0xffff0000, v141
	v_pk_mul_f32 v[92:93], v[96:97], v[96:97]
	v_pk_mul_f32 v[96:97], v[100:101], v[100:101]
	v_pk_add_f32 v[100:101], v[84:85], v[82:83]
	v_cvt_pk_bf16_f32 v82, v86, v87
	v_cvt_pk_bf16_f32 v83, v88, v89
	v_cvt_pk_bf16_f32 v84, v98, v99
	v_cvt_pk_bf16_f32 v85, v100, v101
	global_store_dwordx4 v[102:103], v[82:85], off offset:256 sc1
	s_nop 1
	v_pk_mul_f32 v[82:83], v[86:87], v[86:87]
	v_pk_mul_f32 v[84:85], v[88:89], v[88:89]
	v_add_f32_e32 v82, v82, v83
	v_add_f32_e32 v84, v84, v85
	v_pk_mul_f32 v[86:87], v[98:99], v[98:99]
	v_pk_mul_f32 v[88:89], v[100:101], v[100:101]
	v_add_f32_e32 v82, v82, v84
	v_add_f32_e32 v83, v96, v97
	v_add_f32_e32 v84, v94, v95
	v_add_f32_e32 v88, v88, v89
	v_add_f32_e32 v86, v86, v87
	v_add_f32_e32 v83, v84, v83
	v_add_f32_e32 v84, v92, v93
	v_add_f32_e32 v85, v90, v91
	v_add_f32_e32 v86, v86, v88
	v_add_f32_e32 v84, v85, v84
	v_add_f32_e32 v82, v82, v86
	v_add_f32_e32 v83, v84, v83
	v_add_f32_e32 v82, v83, v82
	ds_bpermute_b32 v83, v168, v82
	s_waitcnt lgkmcnt(0)
	v_add_f32_e32 v82, v82, v83
	ds_bpermute_b32 v83, v167, v82
	s_and_saveexec_b64 s[16:17], vcc
	s_cbranch_execz .LBB0_410
	v_lshl_or_b32 v84, v0, 4, s1
	s_waitcnt lgkmcnt(0)
	v_add_f32_e32 v82, v82, v83
	ds_write_b32 v84, v82 offset:512
.LBB0_410:
	s_or_b64 exec, exec, s[16:17]
	v_lshlrev_b32_e32 v82, 16, v134
	s_waitcnt lgkmcnt(0)
	v_and_b32_e32 v83, 0xffff0000, v134
	v_pk_add_f32 v[78:79], v[78:79], v[82:83]
	v_lshlrev_b32_e32 v82, 16, v135
	v_and_b32_e32 v83, 0xffff0000, v135
	v_pk_add_f32 v[80:81], v[80:81], v[82:83]
	v_lshlrev_b32_e32 v82, 16, v136
	v_and_b32_e32 v83, 0xffff0000, v136
	v_pk_add_f32 v[82:83], v[74:75], v[82:83]
	v_lshlrev_b32_e32 v74, 16, v137
	v_and_b32_e32 v75, 0xffff0000, v137
	v_pk_add_f32 v[84:85], v[76:77], v[74:75]
	v_lshl_add_u64 v[86:87], s[14:15], 0, v[160:161]
	v_cvt_pk_bf16_f32 v74, v78, v79
	v_cvt_pk_bf16_f32 v75, v80, v81
	v_cvt_pk_bf16_f32 v76, v82, v83
	v_cvt_pk_bf16_f32 v77, v84, v85
	v_lshl_add_u64 v[86:87], v[154:155], 1, v[86:87]
	global_store_dwordx4 v[86:87], v[74:77], off sc1
	s_nop 1
	v_pk_mul_f32 v[74:75], v[78:79], v[78:79]
	v_pk_mul_f32 v[78:79], v[82:83], v[82:83]
	v_lshlrev_b32_e32 v82, 16, v130
	v_and_b32_e32 v83, 0xffff0000, v130
	v_pk_add_f32 v[70:71], v[70:71], v[82:83]
	v_lshlrev_b32_e32 v82, 16, v131
	v_and_b32_e32 v83, 0xffff0000, v131
	v_pk_add_f32 v[72:73], v[72:73], v[82:83]
	v_lshlrev_b32_e32 v82, 16, v132
	v_and_b32_e32 v83, 0xffff0000, v132
	v_pk_add_f32 v[82:83], v[66:67], v[82:83]
	v_lshlrev_b32_e32 v66, 16, v133
	v_and_b32_e32 v67, 0xffff0000, v133
	v_pk_mul_f32 v[76:77], v[80:81], v[80:81]
	v_pk_mul_f32 v[80:81], v[84:85], v[84:85]
	v_pk_add_f32 v[84:85], v[68:69], v[66:67]
	v_cvt_pk_bf16_f32 v66, v70, v71
	v_cvt_pk_bf16_f32 v67, v72, v73
	v_cvt_pk_bf16_f32 v68, v82, v83
	v_cvt_pk_bf16_f32 v69, v84, v85
	global_store_dwordx4 v[86:87], v[66:69], off offset:256 sc1
	s_nop 1
	v_pk_mul_f32 v[66:67], v[70:71], v[70:71]
	v_pk_mul_f32 v[68:69], v[72:73], v[72:73]
	v_add_f32_e32 v66, v66, v67
	v_add_f32_e32 v68, v68, v69
	v_pk_mul_f32 v[70:71], v[82:83], v[82:83]
	v_pk_mul_f32 v[72:73], v[84:85], v[84:85]
	v_add_f32_e32 v66, v66, v68
	v_add_f32_e32 v67, v80, v81
	v_add_f32_e32 v68, v78, v79
	v_add_f32_e32 v72, v72, v73
	v_add_f32_e32 v70, v70, v71
	v_add_f32_e32 v67, v68, v67
	v_add_f32_e32 v68, v76, v77
	v_add_f32_e32 v69, v74, v75
	v_add_f32_e32 v70, v70, v72
	v_add_f32_e32 v68, v69, v68
	v_add_f32_e32 v66, v66, v70
	v_add_f32_e32 v67, v68, v67
	v_add_f32_e32 v66, v67, v66
	ds_bpermute_b32 v67, v168, v66
	s_waitcnt lgkmcnt(0)
	v_add_f32_e32 v66, v66, v67
	ds_bpermute_b32 v67, v167, v66
	s_and_saveexec_b64 s[16:17], vcc
	s_cbranch_execz .LBB0_412
	v_lshl_or_b32 v68, v0, 4, s1
	s_waitcnt lgkmcnt(0)
	v_add_f32_e32 v66, v66, v67
	ds_write_b32 v68, v66 offset:768
.LBB0_412:
	s_or_b64 exec, exec, s[16:17]
	s_waitcnt lgkmcnt(0)
	v_lshlrev_b64 v[66:67], 11, v[156:157]
	v_lshl_add_u64 v[104:105], v[66:67], 0, s[20:21]
	v_lshl_add_u64 v[68:69], v[158:159], 0, v[104:105]
	global_load_dwordx4 v[96:99], v[68:69], off
	global_load_dwordx4 v[100:103], v[68:69], off offset:256
	s_mov_b64 s[16:17], 0x48000
	v_lshl_add_u64 v[94:95], v[66:67], 0, s[16:17]
	s_mov_b64 s[16:17], 0x58000
	v_lshl_add_u64 v[68:69], v[158:159], 0, v[94:95]
	v_lshl_add_u64 v[92:93], v[66:67], 0, s[22:23]
	v_lshl_add_u64 v[90:91], v[66:67], 0, s[16:17]
	global_load_dwordx4 v[86:89], v[68:69], off
	global_load_dwordx4 v[82:85], v[68:69], off offset:256
	v_lshl_add_u64 v[68:69], v[158:159], 0, v[92:93]
	v_lshl_add_u64 v[66:67], v[158:159], 0, v[90:91]
	global_load_dwordx4 v[78:81], v[68:69], off
	global_load_dwordx4 v[74:77], v[68:69], off offset:256
	global_load_dwordx4 v[70:73], v[66:67], off
	s_nop 0
	global_load_dwordx4 v[66:69], v[66:67], off offset:256
	v_lshl_add_u64 v[104:105], s[14:15], 0, v[104:105]
	v_lshl_add_u64 v[104:105], v[154:155], 1, v[104:105]
	s_waitcnt vmcnt(7)
	v_lshlrev_b32_e32 v106, 16, v96
	v_and_b32_e32 v107, 0xffff0000, v96
	v_lshlrev_b32_e32 v96, 16, v97
	v_and_b32_e32 v97, 0xffff0000, v97
	v_pk_add_f32 v[64:65], v[64:65], v[96:97]
	v_lshlrev_b32_e32 v96, 16, v98
	v_and_b32_e32 v97, 0xffff0000, v98
	v_pk_add_f32 v[96:97], v[58:59], v[96:97]
	v_lshlrev_b32_e32 v58, 16, v99
	v_and_b32_e32 v59, 0xffff0000, v99
	v_pk_add_f32 v[62:63], v[62:63], v[106:107]
	v_pk_add_f32 v[98:99], v[60:61], v[58:59]
	v_cvt_pk_bf16_f32 v58, v62, v63
	v_cvt_pk_bf16_f32 v59, v64, v65
	v_cvt_pk_bf16_f32 v60, v96, v97
	v_cvt_pk_bf16_f32 v61, v98, v99
	global_store_dwordx4 v[104:105], v[58:61], off sc1
	s_nop 1
	v_pk_mul_f32 v[58:59], v[62:63], v[62:63]
	v_pk_mul_f32 v[62:63], v[96:97], v[96:97]
	s_waitcnt vmcnt(7)
	v_lshlrev_b32_e32 v96, 16, v100
	v_and_b32_e32 v97, 0xffff0000, v100
	v_pk_add_f32 v[54:55], v[54:55], v[96:97]
	v_lshlrev_b32_e32 v96, 16, v101
	v_and_b32_e32 v97, 0xffff0000, v101
	v_pk_add_f32 v[56:57], v[56:57], v[96:97]
	v_lshlrev_b32_e32 v96, 16, v102
	v_and_b32_e32 v97, 0xffff0000, v102
	v_pk_add_f32 v[96:97], v[50:51], v[96:97]
	v_lshlrev_b32_e32 v50, 16, v103
	v_and_b32_e32 v51, 0xffff0000, v103
	v_pk_mul_f32 v[60:61], v[64:65], v[64:65]
	v_pk_mul_f32 v[64:65], v[98:99], v[98:99]
	v_pk_add_f32 v[98:99], v[52:53], v[50:51]
	v_cvt_pk_bf16_f32 v50, v54, v55
	v_cvt_pk_bf16_f32 v51, v56, v57
	v_cvt_pk_bf16_f32 v52, v96, v97
	v_cvt_pk_bf16_f32 v53, v98, v99
	global_store_dwordx4 v[104:105], v[50:53], off offset:256 sc1
	s_nop 1
	v_pk_mul_f32 v[50:51], v[54:55], v[54:55]
	v_pk_mul_f32 v[52:53], v[56:57], v[56:57]
	v_add_f32_e32 v50, v50, v51
	v_add_f32_e32 v52, v52, v53
	v_pk_mul_f32 v[54:55], v[96:97], v[96:97]
	v_pk_mul_f32 v[56:57], v[98:99], v[98:99]
	v_add_f32_e32 v50, v50, v52
	v_add_f32_e32 v51, v64, v65
	v_add_f32_e32 v52, v62, v63
	v_add_f32_e32 v56, v56, v57
	v_add_f32_e32 v54, v54, v55
	v_add_f32_e32 v51, v52, v51
	v_add_f32_e32 v52, v60, v61
	v_add_f32_e32 v53, v58, v59
	v_add_f32_e32 v54, v54, v56
	v_add_f32_e32 v52, v53, v52
	v_add_f32_e32 v50, v50, v54
	v_add_f32_e32 v51, v52, v51
	v_add_f32_e32 v50, v51, v50
	ds_bpermute_b32 v51, v168, v50
	s_waitcnt lgkmcnt(0)
	v_add_f32_e32 v50, v50, v51
	ds_bpermute_b32 v51, v167, v50
	s_and_saveexec_b64 s[16:17], vcc
	s_cbranch_execz .LBB0_414
	v_lshl_or_b32 v52, v0, 4, s1
	s_waitcnt lgkmcnt(0)
	v_add_f32_e32 v50, v50, v51
	ds_write_b32 v52, v50 offset:2048
.LBB0_414:
	s_or_b64 exec, exec, s[16:17]
	s_waitcnt vmcnt(7)
	v_lshlrev_b32_e32 v50, 16, v86
	s_waitcnt lgkmcnt(0)
	v_and_b32_e32 v51, 0xffff0000, v86
	v_pk_add_f32 v[46:47], v[46:47], v[50:51]
	v_lshlrev_b32_e32 v50, 16, v87
	v_and_b32_e32 v51, 0xffff0000, v87
	v_pk_add_f32 v[48:49], v[48:49], v[50:51]
	v_lshlrev_b32_e32 v50, 16, v88
	v_and_b32_e32 v51, 0xffff0000, v88
	v_pk_add_f32 v[50:51], v[42:43], v[50:51]
	v_lshlrev_b32_e32 v42, 16, v89
	v_and_b32_e32 v43, 0xffff0000, v89
	v_pk_add_f32 v[52:53], v[44:45], v[42:43]
	v_lshl_add_u64 v[54:55], s[14:15], 0, v[94:95]
	v_cvt_pk_bf16_f32 v42, v46, v47
	v_cvt_pk_bf16_f32 v43, v48, v49
	v_cvt_pk_bf16_f32 v44, v50, v51
	v_cvt_pk_bf16_f32 v45, v52, v53
	v_lshl_add_u64 v[54:55], v[154:155], 1, v[54:55]
	global_store_dwordx4 v[54:55], v[42:45], off sc1
	s_nop 1
	v_pk_mul_f32 v[42:43], v[46:47], v[46:47]
	v_pk_mul_f32 v[46:47], v[50:51], v[50:51]
	s_waitcnt vmcnt(7)
	v_lshlrev_b32_e32 v50, 16, v82
	v_and_b32_e32 v51, 0xffff0000, v82
	v_pk_add_f32 v[38:39], v[38:39], v[50:51]
	v_lshlrev_b32_e32 v50, 16, v83
	v_and_b32_e32 v51, 0xffff0000, v83
	v_pk_add_f32 v[40:41], v[40:41], v[50:51]
	v_lshlrev_b32_e32 v50, 16, v84
	v_and_b32_e32 v51, 0xffff0000, v84
	v_pk_add_f32 v[50:51], v[34:35], v[50:51]
	v_lshlrev_b32_e32 v34, 16, v85
	v_and_b32_e32 v35, 0xffff0000, v85
	v_pk_mul_f32 v[44:45], v[48:49], v[48:49]
	v_pk_mul_f32 v[48:49], v[52:53], v[52:53]
	v_pk_add_f32 v[52:53], v[36:37], v[34:35]
	v_cvt_pk_bf16_f32 v34, v38, v39
	v_cvt_pk_bf16_f32 v35, v40, v41
	v_cvt_pk_bf16_f32 v36, v50, v51
	v_cvt_pk_bf16_f32 v37, v52, v53
	global_store_dwordx4 v[54:55], v[34:37], off offset:256 sc1
	s_nop 1
	v_pk_mul_f32 v[34:35], v[38:39], v[38:39]
	v_pk_mul_f32 v[36:37], v[40:41], v[40:41]
	v_add_f32_e32 v34, v34, v35
	v_add_f32_e32 v36, v36, v37
	v_pk_mul_f32 v[38:39], v[50:51], v[50:51]
	v_pk_mul_f32 v[40:41], v[52:53], v[52:53]
	v_add_f32_e32 v34, v34, v36
	v_add_f32_e32 v35, v48, v49
	v_add_f32_e32 v36, v46, v47
	v_add_f32_e32 v40, v40, v41
	v_add_f32_e32 v38, v38, v39
	v_add_f32_e32 v35, v36, v35
	v_add_f32_e32 v36, v44, v45
	v_add_f32_e32 v37, v42, v43
	v_add_f32_e32 v38, v38, v40
	v_add_f32_e32 v36, v37, v36
	v_add_f32_e32 v34, v34, v38
	v_add_f32_e32 v35, v36, v35
	v_add_f32_e32 v34, v35, v34
	ds_bpermute_b32 v35, v168, v34
	s_waitcnt lgkmcnt(0)
	v_add_f32_e32 v34, v34, v35
	ds_bpermute_b32 v35, v167, v34
	s_and_saveexec_b64 s[16:17], vcc
	s_cbranch_execz .LBB0_416
	v_lshl_or_b32 v36, v0, 4, s1
	s_waitcnt lgkmcnt(0)
	v_add_f32_e32 v34, v34, v35
	ds_write_b32 v36, v34 offset:2304
.LBB0_416:
	s_or_b64 exec, exec, s[16:17]
	s_waitcnt vmcnt(7)
	v_lshlrev_b32_e32 v34, 16, v78
	s_waitcnt lgkmcnt(0)
	v_and_b32_e32 v35, 0xffff0000, v78
	v_pk_add_f32 v[30:31], v[30:31], v[34:35]
	v_lshlrev_b32_e32 v34, 16, v79
	v_and_b32_e32 v35, 0xffff0000, v79
	v_pk_add_f32 v[32:33], v[32:33], v[34:35]
	v_lshlrev_b32_e32 v34, 16, v80
	v_and_b32_e32 v35, 0xffff0000, v80
	v_pk_add_f32 v[34:35], v[26:27], v[34:35]
	v_lshlrev_b32_e32 v26, 16, v81
	v_and_b32_e32 v27, 0xffff0000, v81
	v_pk_add_f32 v[36:37], v[28:29], v[26:27]
	v_lshl_add_u64 v[38:39], s[14:15], 0, v[92:93]
	v_cvt_pk_bf16_f32 v26, v30, v31
	v_cvt_pk_bf16_f32 v27, v32, v33
	v_cvt_pk_bf16_f32 v28, v34, v35
	v_cvt_pk_bf16_f32 v29, v36, v37
	v_lshl_add_u64 v[38:39], v[154:155], 1, v[38:39]
	global_store_dwordx4 v[38:39], v[26:29], off sc1
	s_nop 1
	v_pk_mul_f32 v[26:27], v[30:31], v[30:31]
	v_pk_mul_f32 v[30:31], v[34:35], v[34:35]
	s_waitcnt vmcnt(7)
	v_lshlrev_b32_e32 v34, 16, v74
	v_and_b32_e32 v35, 0xffff0000, v74
	v_pk_add_f32 v[22:23], v[22:23], v[34:35]
	v_lshlrev_b32_e32 v34, 16, v75
	v_and_b32_e32 v35, 0xffff0000, v75
	v_pk_add_f32 v[24:25], v[24:25], v[34:35]
	v_lshlrev_b32_e32 v34, 16, v76
	v_and_b32_e32 v35, 0xffff0000, v76
	v_pk_add_f32 v[34:35], v[18:19], v[34:35]
	v_lshlrev_b32_e32 v18, 16, v77
	v_and_b32_e32 v19, 0xffff0000, v77
	v_pk_mul_f32 v[28:29], v[32:33], v[32:33]
	v_pk_mul_f32 v[32:33], v[36:37], v[36:37]
	v_pk_add_f32 v[36:37], v[20:21], v[18:19]
	v_cvt_pk_bf16_f32 v18, v22, v23
	v_cvt_pk_bf16_f32 v19, v24, v25
	v_cvt_pk_bf16_f32 v20, v34, v35
	v_cvt_pk_bf16_f32 v21, v36, v37
	global_store_dwordx4 v[38:39], v[18:21], off offset:256 sc1
	s_nop 1
	v_pk_mul_f32 v[18:19], v[22:23], v[22:23]
	v_pk_mul_f32 v[20:21], v[24:25], v[24:25]
	v_add_f32_e32 v18, v18, v19
	v_add_f32_e32 v20, v20, v21
	v_pk_mul_f32 v[22:23], v[34:35], v[34:35]
	v_pk_mul_f32 v[24:25], v[36:37], v[36:37]
	v_add_f32_e32 v18, v18, v20
	v_add_f32_e32 v19, v32, v33
	v_add_f32_e32 v20, v30, v31
	v_add_f32_e32 v24, v24, v25
	v_add_f32_e32 v22, v22, v23
	v_add_f32_e32 v19, v20, v19
	v_add_f32_e32 v20, v28, v29
	v_add_f32_e32 v21, v26, v27
	v_add_f32_e32 v22, v22, v24
	v_add_f32_e32 v20, v21, v20
	v_add_f32_e32 v18, v18, v22
	v_add_f32_e32 v19, v20, v19
	v_add_f32_e32 v18, v19, v18
	ds_bpermute_b32 v19, v168, v18
	s_waitcnt lgkmcnt(0)
	v_add_f32_e32 v18, v18, v19
	ds_bpermute_b32 v19, v167, v18
	s_and_saveexec_b64 s[16:17], vcc
	s_cbranch_execz .LBB0_418
	v_lshl_or_b32 v20, v0, 4, s1
	s_waitcnt lgkmcnt(0)
	v_add_f32_e32 v18, v18, v19
	ds_write_b32 v20, v18 offset:2560
.LBB0_418:
	s_or_b64 exec, exec, s[16:17]
	s_waitcnt vmcnt(7)
	v_lshlrev_b32_e32 v18, 16, v70
	s_waitcnt lgkmcnt(0)
	v_and_b32_e32 v19, 0xffff0000, v70
	v_pk_add_f32 v[14:15], v[14:15], v[18:19]
	v_lshlrev_b32_e32 v18, 16, v71
	v_and_b32_e32 v19, 0xffff0000, v71
	v_pk_add_f32 v[16:17], v[16:17], v[18:19]
	v_lshlrev_b32_e32 v18, 16, v72
	v_and_b32_e32 v19, 0xffff0000, v72
	v_pk_add_f32 v[18:19], v[10:11], v[18:19]
	v_lshlrev_b32_e32 v10, 16, v73
	v_and_b32_e32 v11, 0xffff0000, v73
	v_pk_add_f32 v[20:21], v[12:13], v[10:11]
	v_lshl_add_u64 v[22:23], s[14:15], 0, v[90:91]
	v_cvt_pk_bf16_f32 v10, v14, v15
	v_cvt_pk_bf16_f32 v11, v16, v17
	v_cvt_pk_bf16_f32 v12, v18, v19
	v_cvt_pk_bf16_f32 v13, v20, v21
	v_lshl_add_u64 v[22:23], v[154:155], 1, v[22:23]
	global_store_dwordx4 v[22:23], v[10:13], off sc1
	s_nop 1
	v_pk_mul_f32 v[10:11], v[14:15], v[14:15]
	v_pk_mul_f32 v[14:15], v[18:19], v[18:19]
	s_waitcnt vmcnt(7)
	v_lshlrev_b32_e32 v18, 16, v66
	v_and_b32_e32 v19, 0xffff0000, v66
	v_pk_add_f32 v[6:7], v[6:7], v[18:19]
	v_lshlrev_b32_e32 v18, 16, v67
	v_and_b32_e32 v19, 0xffff0000, v67
	v_pk_add_f32 v[8:9], v[8:9], v[18:19]
	v_lshlrev_b32_e32 v18, 16, v68
	v_and_b32_e32 v19, 0xffff0000, v68
	v_pk_add_f32 v[18:19], v[2:3], v[18:19]
	v_lshlrev_b32_e32 v2, 16, v69
	v_and_b32_e32 v3, 0xffff0000, v69
	v_pk_mul_f32 v[12:13], v[16:17], v[16:17]
	v_pk_mul_f32 v[16:17], v[20:21], v[20:21]
	v_pk_add_f32 v[20:21], v[4:5], v[2:3]
	v_cvt_pk_bf16_f32 v2, v6, v7
	v_cvt_pk_bf16_f32 v3, v8, v9
	v_cvt_pk_bf16_f32 v4, v18, v19
	v_cvt_pk_bf16_f32 v5, v20, v21
	global_store_dwordx4 v[22:23], v[2:5], off offset:256 sc1
	s_nop 1
	v_pk_mul_f32 v[2:3], v[6:7], v[6:7]
	v_pk_mul_f32 v[4:5], v[8:9], v[8:9]
	v_add_f32_e32 v2, v2, v3
	v_add_f32_e32 v4, v4, v5
	v_pk_mul_f32 v[6:7], v[18:19], v[18:19]
	v_pk_mul_f32 v[8:9], v[20:21], v[20:21]
	v_add_f32_e32 v2, v2, v4
	v_add_f32_e32 v3, v16, v17
	v_add_f32_e32 v4, v14, v15
	v_add_f32_e32 v8, v8, v9
	v_add_f32_e32 v6, v6, v7
	v_add_f32_e32 v3, v4, v3
	v_add_f32_e32 v4, v12, v13
	v_add_f32_e32 v5, v10, v11
	v_add_f32_e32 v6, v6, v8
	v_add_f32_e32 v4, v5, v4
	v_add_f32_e32 v2, v2, v6
	v_add_f32_e32 v3, v4, v3
	v_add_f32_e32 v2, v3, v2
	ds_bpermute_b32 v3, v168, v2
	s_waitcnt lgkmcnt(0)
	v_add_f32_e32 v2, v2, v3
	ds_bpermute_b32 v3, v167, v2
	s_and_saveexec_b64 s[14:15], vcc
	s_cbranch_execz .LBB0_420
	v_lshl_or_b32 v0, v0, 4, s1
	s_waitcnt lgkmcnt(0)
	v_add_f32_e32 v2, v2, v3
	ds_write_b32 v0, v2 offset:2816

.LBB0_478:
	s_or_b64 exec, exec, s[14:15]
	s_lshl_b32 s14, s34, 8
	s_add_i32 s14, s14, s1
	s_ashr_i32 s1, s0, 31
	s_waitcnt lgkmcnt(0)
	s_barrier
	s_lshl_b64 s[0:1], s[0:1], 9
	s_add_u32 s0, s74, s0
	ds_read_b128 v[136:139], v192 offset:4096
	v_or_b32_e32 v130, s14, v193
	s_addc_u32 s1, s75, s1
	s_lshl_b32 s14, s31, 6
	s_add_u32 s0, s0, s14
	s_addc_u32 s1, s1, 0
	v_and_b32_e32 v0, 0x70, v0
	s_waitcnt lgkmcnt(1)
	v_lshl_add_u64 v[18:19], s[0:1], 0, v[0:1]
	s_mov_b64 s[0:1], 0xa800000
	v_lshl_add_u64 v[134:135], v[18:19], 0, s[0:1]
	s_waitcnt lgkmcnt(0)
	v_mov_b32_e32 v18, v137
	v_mov_b32_e32 v19, v138
	v_mov_b32_e32 v137, v139
	v_pk_add_f32 v[18:19], v[18:19], v[136:137]
	s_nop 0
	v_add_f32_e32 v0, v18, v19
	v_div_scale_f32 v18, s[0:1], v0, v0, 1.0
	v_rcp_f32_e32 v19, v18
	s_nop 0
	v_fma_f32 v131, -v18, v19, 1.0
	v_fmac_f32_e32 v19, v131, v19
	v_div_scale_f32 v131, vcc, 1.0, v0, 1.0
	v_mul_f32_e32 v136, v131, v19
	v_fma_f32 v137, -v18, v136, v131
	v_fmac_f32_e32 v136, v137, v19
	v_fma_f32 v18, -v18, v136, v131
	v_div_fmas_f32 v18, v18, v19, v136
	v_div_fixup_f32 v0, v18, v0, 1.0
	v_ashrrev_i32_e32 v131, 31, v130
	v_lshlrev_b64 v[18:19], 11, v[130:131]
	v_pk_mul_f32 v[118:119], v[118:119], v[0:1] op_sel_hi:[1,0]
	v_pk_mul_f32 v[116:117], v[116:117], v[0:1] op_sel_hi:[1,0]
	v_pk_mul_f32 v[122:123], v[122:123], v[0:1] op_sel_hi:[1,0]
	v_pk_mul_f32 v[120:121], v[120:121], v[0:1] op_sel_hi:[1,0]
	v_lshl_add_u64 v[18:19], v[134:135], 0, v[18:19]
	v_cvt_pk_bf16_f32 v116, v116, v117
	v_cvt_pk_bf16_f32 v117, v118, v119
	v_cvt_pk_bf16_f32 v118, v120, v121
	v_cvt_pk_bf16_f32 v119, v122, v123
	global_store_dwordx4 v[18:19], v[116:119], off sc1
	v_pk_mul_f32 v[120:121], v[132:133], v[0:1] op_sel_hi:[1,0]
	v_pk_mul_f32 v[122:123], v[128:129], v[0:1] op_sel_hi:[1,0]
	v_pk_mul_f32 v[118:119], v[126:127], v[0:1] op_sel_hi:[1,0]
	v_pk_mul_f32 v[116:117], v[124:125], v[0:1] op_sel_hi:[1,0]
	s_nop 0
	v_cvt_pk_bf16_f32 v116, v116, v117
	v_cvt_pk_bf16_f32 v117, v118, v119
	v_cvt_pk_bf16_f32 v118, v122, v123
	v_cvt_pk_bf16_f32 v119, v120, v121
	global_store_dwordx4 v[18:19], v[116:119], off offset:256 sc1
	ds_read_b128 v[116:119], v192 offset:4352
	s_waitcnt lgkmcnt(0)
	v_mov_b32_e32 v120, v117
	v_mov_b32_e32 v121, v118
	v_mov_b32_e32 v117, v119
	v_pk_add_f32 v[116:117], v[120:121], v[116:117]
	s_nop 0
	v_add_f32_e32 v0, v116, v117
	v_div_scale_f32 v116, s[0:1], v0, v0, 1.0
	v_rcp_f32_e32 v117, v116
	s_nop 0
	v_fma_f32 v118, -v116, v117, 1.0
	v_fmac_f32_e32 v117, v118, v117
	v_div_scale_f32 v118, vcc, 1.0, v0, 1.0
	v_mul_f32_e32 v119, v118, v117
	v_fma_f32 v120, -v116, v119, v118
	v_fmac_f32_e32 v119, v120, v117
	v_fma_f32 v116, -v116, v119, v118
	v_div_fmas_f32 v116, v116, v117, v119
	v_div_fixup_f32 v0, v116, v0, 1.0
	v_or_b32_e32 v116, 16, v130
	v_ashrrev_i32_e32 v117, 31, v116
	v_lshlrev_b64 v[116:117], 11, v[116:117]
	v_pk_mul_f32 v[94:95], v[94:95], v[0:1] op_sel_hi:[1,0]
	v_pk_mul_f32 v[84:85], v[84:85], v[0:1] op_sel_hi:[1,0]
	v_pk_mul_f32 v[90:91], v[90:91], v[0:1] op_sel_hi:[1,0]
	v_lshl_add_u64 v[120:121], v[134:135], 0, v[116:117]
	v_cvt_pk_bf16_f32 v116, v84, v85
	v_cvt_pk_bf16_f32 v117, v94, v95
	v_cvt_pk_bf16_f32 v118, v90, v91
	v_pk_mul_f32 v[84:85], v[98:99], v[0:1] op_sel_hi:[1,0]
	v_pk_mul_f32 v[88:89], v[88:89], v[0:1] op_sel_hi:[1,0]
	v_pk_mul_f32 v[94:95], v[108:109], v[0:1] op_sel_hi:[1,0]
	v_pk_mul_f32 v[90:91], v[104:105], v[0:1] op_sel_hi:[1,0]
	v_cvt_pk_bf16_f32 v88, v88, v89
	v_cvt_pk_bf16_f32 v89, v84, v85
	v_cvt_pk_bf16_f32 v90, v90, v91
	v_cvt_pk_bf16_f32 v91, v94, v95
	global_store_dwordx4 v[120:121], v[88:91], off offset:256 sc1
	ds_read_b128 v[88:91], v192 offset:4608
	v_pk_mul_f32 v[100:101], v[100:101], v[0:1] op_sel_hi:[1,0]
	s_waitcnt lgkmcnt(0)
	v_mov_b32_e32 v84, v89
	v_mov_b32_e32 v85, v90
	v_mov_b32_e32 v89, v91
	v_pk_add_f32 v[84:85], v[84:85], v[88:89]
	v_cvt_pk_bf16_f32 v119, v100, v101
	v_add_f32_e32 v0, v84, v85
	v_div_scale_f32 v84, s[0:1], v0, v0, 1.0
	v_rcp_f32_e32 v85, v84
	global_store_dwordx4 v[120:121], v[116:119], off sc1
	v_fma_f32 v88, -v84, v85, 1.0
	v_fmac_f32_e32 v85, v88, v85
	v_div_scale_f32 v88, vcc, 1.0, v0, 1.0
	v_mul_f32_e32 v89, v88, v85
	v_fma_f32 v90, -v84, v89, v88
	v_fmac_f32_e32 v89, v90, v85
	v_fma_f32 v84, -v84, v89, v88
	v_div_fmas_f32 v84, v84, v85, v89
	v_div_fixup_f32 v0, v84, v0, 1.0
	v_or_b32_e32 v84, 32, v130
	v_ashrrev_i32_e32 v85, 31, v84
	v_lshlrev_b64 v[84:85], 11, v[84:85]
	v_lshl_add_u64 v[88:89], v[134:135], 0, v[84:85]
	v_pk_mul_f32 v[90:91], v[92:93], v[0:1] op_sel_hi:[1,0]
	v_pk_mul_f32 v[84:85], v[86:87], v[0:1] op_sel_hi:[1,0]
	v_pk_mul_f32 v[92:93], v[102:103], v[0:1] op_sel_hi:[1,0]
	v_pk_mul_f32 v[86:87], v[96:97], v[0:1] op_sel_hi:[1,0]
	v_cvt_pk_bf16_f32 v84, v84, v85
	v_cvt_pk_bf16_f32 v85, v90, v91
	v_cvt_pk_bf16_f32 v86, v86, v87
	v_cvt_pk_bf16_f32 v87, v92, v93
	global_store_dwordx4 v[88:89], v[84:87], off sc1
	v_pk_mul_f32 v[90:91], v[114:115], v[0:1] op_sel_hi:[1,0]
	v_pk_mul_f32 v[92:93], v[112:113], v[0:1] op_sel_hi:[1,0]
	v_pk_mul_f32 v[86:87], v[110:111], v[0:1] op_sel_hi:[1,0]
	v_pk_mul_f32 v[84:85], v[106:107], v[0:1] op_sel_hi:[1,0]
	s_nop 0
	v_cvt_pk_bf16_f32 v84, v84, v85
	v_cvt_pk_bf16_f32 v85, v86, v87
	v_cvt_pk_bf16_f32 v86, v92, v93
	v_cvt_pk_bf16_f32 v87, v90, v91
	global_store_dwordx4 v[88:89], v[84:87], off offset:256 sc1
	ds_read_b128 v[84:87], v192 offset:4864
	s_waitcnt lgkmcnt(0)
	v_mov_b32_e32 v88, v85
	v_mov_b32_e32 v89, v86
	v_mov_b32_e32 v85, v87
	v_pk_add_f32 v[84:85], v[88:89], v[84:85]
	s_nop 0
	v_add_f32_e32 v0, v84, v85
	v_div_scale_f32 v84, s[0:1], v0, v0, 1.0
	v_rcp_f32_e32 v85, v84
	s_nop 0
	v_fma_f32 v86, -v84, v85, 1.0
	v_fmac_f32_e32 v85, v86, v85
	v_div_scale_f32 v86, vcc, 1.0, v0, 1.0
	v_mul_f32_e32 v87, v86, v85
	v_fma_f32 v88, -v84, v87, v86
	v_fmac_f32_e32 v87, v88, v85
	v_fma_f32 v84, -v84, v87, v86
	v_div_fmas_f32 v84, v84, v85, v87
	v_div_fixup_f32 v0, v84, v0, 1.0
	v_or_b32_e32 v84, 48, v130
	v_ashrrev_i32_e32 v85, 31, v84
	v_lshlrev_b64 v[84:85], 11, v[84:85]
	v_pk_mul_f32 v[60:61], v[60:61], v[0:1] op_sel_hi:[1,0]
	v_pk_mul_f32 v[52:53], v[52:53], v[0:1] op_sel_hi:[1,0]
	v_pk_mul_f32 v[56:57], v[56:57], v[0:1] op_sel_hi:[1,0]
	v_lshl_add_u64 v[88:89], v[134:135], 0, v[84:85]
	v_cvt_pk_bf16_f32 v84, v52, v53
	v_cvt_pk_bf16_f32 v85, v60, v61
	v_cvt_pk_bf16_f32 v86, v56, v57
	v_pk_mul_f32 v[56:57], v[66:67], v[0:1] op_sel_hi:[1,0]
	v_pk_mul_f32 v[52:53], v[54:55], v[0:1] op_sel_hi:[1,0]
	v_pk_mul_f32 v[60:61], v[76:77], v[0:1] op_sel_hi:[1,0]
	v_pk_mul_f32 v[54:55], v[70:71], v[0:1] op_sel_hi:[1,0]
	v_cvt_pk_bf16_f32 v52, v52, v53
	v_cvt_pk_bf16_f32 v53, v56, v57
	v_cvt_pk_bf16_f32 v54, v54, v55
	v_cvt_pk_bf16_f32 v55, v60, v61
	global_store_dwordx4 v[88:89], v[52:55], off offset:256 sc1
	ds_read_b128 v[52:55], v192 offset:6144
	v_pk_mul_f32 v[68:69], v[68:69], v[0:1] op_sel_hi:[1,0]
	s_waitcnt lgkmcnt(0)
	v_mov_b32_e32 v56, v53
	v_mov_b32_e32 v57, v54
	v_mov_b32_e32 v53, v55
	v_pk_add_f32 v[52:53], v[56:57], v[52:53]
	v_cvt_pk_bf16_f32 v87, v68, v69
	v_add_f32_e32 v0, v52, v53
	v_div_scale_f32 v52, s[0:1], v0, v0, 1.0
	v_rcp_f32_e32 v53, v52
	s_mov_b32 s0, 0x40000
	global_store_dwordx4 v[88:89], v[84:87], off sc1
	v_fma_f32 v54, -v52, v53, 1.0
	v_fmac_f32_e32 v53, v54, v53
	v_div_scale_f32 v54, vcc, 1.0, v0, 1.0
	v_mul_f32_e32 v55, v54, v53
	v_fma_f32 v56, -v52, v55, v54
	v_fmac_f32_e32 v55, v56, v53
	v_fma_f32 v52, -v52, v55, v54
	v_div_fmas_f32 v52, v52, v53, v55
	v_div_fixup_f32 v0, v52, v0, 1.0
	v_pk_mul_f32 v[54:55], v[62:63], v[0:1] op_sel_hi:[1,0]
	v_pk_mul_f32 v[52:53], v[58:59], v[0:1] op_sel_hi:[1,0]
	v_pk_mul_f32 v[58:59], v[74:75], v[0:1] op_sel_hi:[1,0]
	v_pk_mul_f32 v[60:61], v[64:65], v[0:1] op_sel_hi:[1,0]
	v_cvt_pk_bf16_f32 v52, v52, v53
	v_cvt_pk_bf16_f32 v53, v54, v55
	v_cvt_pk_bf16_f32 v55, v58, v59
	v_add_co_u32_e32 v58, vcc, s0, v18
	v_cvt_pk_bf16_f32 v54, v60, v61
	s_nop 0
	v_addc_co_u32_e32 v59, vcc, 0, v19, vcc
	global_store_dwordx4 v[58:59], v[52:55], off sc1
	v_pk_mul_f32 v[58:59], v[82:83], v[0:1] op_sel_hi:[1,0]
	v_pk_mul_f32 v[60:61], v[80:81], v[0:1] op_sel_hi:[1,0]
	v_pk_mul_f32 v[54:55], v[78:79], v[0:1] op_sel_hi:[1,0]
	v_pk_mul_f32 v[52:53], v[72:73], v[0:1] op_sel_hi:[1,0]
	v_lshl_add_u64 v[56:57], v[18:19], 0, s[20:21]
	v_cvt_pk_bf16_f32 v52, v52, v53
	v_cvt_pk_bf16_f32 v53, v54, v55
	v_cvt_pk_bf16_f32 v54, v60, v61
	v_cvt_pk_bf16_f32 v55, v58, v59
	global_store_dwordx4 v[56:57], v[52:55], off offset:256 sc1
	ds_read_b128 v[52:55], v192 offset:6400
	s_waitcnt lgkmcnt(0)
	v_mov_b32_e32 v56, v53
	v_mov_b32_e32 v57, v54
	v_mov_b32_e32 v53, v55
	v_pk_add_f32 v[52:53], v[56:57], v[52:53]
	s_nop 0
	v_add_f32_e32 v0, v52, v53
	v_div_scale_f32 v52, s[0:1], v0, v0, 1.0
	v_rcp_f32_e32 v53, v52
	s_mov_b64 s[0:1], 0x48000
	v_fma_f32 v54, -v52, v53, 1.0
	v_fmac_f32_e32 v53, v54, v53
	v_div_scale_f32 v54, vcc, 1.0, v0, 1.0
	v_mul_f32_e32 v55, v54, v53
	v_fma_f32 v56, -v52, v55, v54
	v_fmac_f32_e32 v55, v56, v53
	v_fma_f32 v52, -v52, v55, v54
	v_div_fmas_f32 v52, v52, v53, v55
	v_div_fixup_f32 v0, v52, v0, 1.0
	v_lshl_add_u64 v[52:53], v[18:19], 0, s[0:1]
	v_pk_mul_f32 v[24:25], v[24:25], v[0:1] op_sel_hi:[1,0]
	s_mov_b32 s0, 0x48000
	v_pk_mul_f32 v[30:31], v[30:31], v[0:1] op_sel_hi:[1,0]
	v_pk_mul_f32 v[40:41], v[40:41], v[0:1] op_sel_hi:[1,0]
	v_pk_mul_f32 v[54:55], v[28:29], v[0:1] op_sel_hi:[1,0]
	v_cvt_pk_bf16_f32 v28, v24, v25
	v_add_co_u32_e32 v24, vcc, s0, v18
	v_cvt_pk_bf16_f32 v29, v30, v31
	v_cvt_pk_bf16_f32 v30, v54, v55
	v_cvt_pk_bf16_f32 v31, v40, v41
	v_addc_co_u32_e32 v25, vcc, 0, v19, vcc
	global_store_dwordx4 v[24:25], v[28:31], off sc1
	v_pk_mul_f32 v[24:25], v[34:35], v[0:1] op_sel_hi:[1,0]
	v_pk_mul_f32 v[20:21], v[20:21], v[0:1] op_sel_hi:[1,0]
	v_pk_mul_f32 v[34:35], v[44:45], v[0:1] op_sel_hi:[1,0]
	v_pk_mul_f32 v[30:31], v[36:37], v[0:1] op_sel_hi:[1,0]
	v_cvt_pk_bf16_f32 v28, v20, v21
	v_cvt_pk_bf16_f32 v29, v24, v25
	v_cvt_pk_bf16_f32 v30, v30, v31
	v_cvt_pk_bf16_f32 v31, v34, v35
	global_store_dwordx4 v[52:53], v[28:31], off offset:256 sc1
	ds_read_b128 v[28:31], v192 offset:6656
	s_waitcnt lgkmcnt(0)
	v_mov_b32_e32 v20, v29
	v_mov_b32_e32 v21, v30
	v_mov_b32_e32 v29, v31
	v_pk_add_f32 v[20:21], v[20:21], v[28:29]
	s_nop 0
	v_add_f32_e32 v0, v20, v21
	v_div_scale_f32 v20, s[0:1], v0, v0, 1.0
	v_rcp_f32_e32 v21, v20
	s_mov_b32 s0, 0x50000
	v_fma_f32 v24, -v20, v21, 1.0
	v_fmac_f32_e32 v21, v24, v21
	v_div_scale_f32 v24, vcc, 1.0, v0, 1.0
	v_mul_f32_e32 v25, v24, v21
	v_fma_f32 v28, -v20, v25, v24
	v_fmac_f32_e32 v25, v28, v21
	v_fma_f32 v20, -v20, v25, v24
	v_div_fmas_f32 v20, v20, v21, v25
	v_div_fixup_f32 v0, v20, v0, 1.0
	v_pk_mul_f32 v[26:27], v[26:27], v[0:1] op_sel_hi:[1,0]
	v_pk_mul_f32 v[20:21], v[22:23], v[0:1] op_sel_hi:[1,0]
	v_pk_mul_f32 v[28:29], v[42:43], v[0:1] op_sel_hi:[1,0]
	v_pk_mul_f32 v[22:23], v[32:33], v[0:1] op_sel_hi:[1,0]
	v_cvt_pk_bf16_f32 v20, v20, v21
	v_cvt_pk_bf16_f32 v21, v26, v27
	v_add_co_u32_e32 v26, vcc, s0, v18
	v_cvt_pk_bf16_f32 v22, v22, v23
	v_cvt_pk_bf16_f32 v23, v28, v29
	v_addc_co_u32_e32 v27, vcc, 0, v19, vcc
	global_store_dwordx4 v[26:27], v[20:23], off sc1
	v_pk_mul_f32 v[26:27], v[50:51], v[0:1] op_sel_hi:[1,0]
	v_pk_mul_f32 v[28:29], v[48:49], v[0:1] op_sel_hi:[1,0]
	v_pk_mul_f32 v[22:23], v[46:47], v[0:1] op_sel_hi:[1,0]
	v_pk_mul_f32 v[20:21], v[38:39], v[0:1] op_sel_hi:[1,0]
	v_lshl_add_u64 v[24:25], v[18:19], 0, s[22:23]
	v_cvt_pk_bf16_f32 v20, v20, v21
	v_cvt_pk_bf16_f32 v21, v22, v23
	v_cvt_pk_bf16_f32 v22, v28, v29
	v_cvt_pk_bf16_f32 v23, v26, v27
	global_store_dwordx4 v[24:25], v[20:23], off offset:256 sc1
	ds_read_b128 v[20:23], v192 offset:6912
	s_waitcnt lgkmcnt(0)
	v_mov_b32_e32 v24, v21
	v_mov_b32_e32 v25, v22
	v_mov_b32_e32 v21, v23
	v_pk_add_f32 v[20:21], v[24:25], v[20:21]
	s_nop 0
	v_add_f32_e32 v0, v20, v21
	v_div_scale_f32 v20, s[0:1], v0, v0, 1.0
	v_rcp_f32_e32 v21, v20
	s_mov_b64 s[0:1], 0x58000
	v_fma_f32 v22, -v20, v21, 1.0
	v_fmac_f32_e32 v21, v22, v21
	v_div_scale_f32 v22, vcc, 1.0, v0, 1.0
	v_mul_f32_e32 v23, v22, v21
	v_fma_f32 v24, -v20, v23, v22
	v_fmac_f32_e32 v23, v24, v21
	v_fma_f32 v20, -v20, v23, v22
	v_div_fmas_f32 v20, v20, v21, v23
	v_div_fixup_f32 v0, v20, v0, 1.0
	v_lshl_add_u64 v[20:21], v[18:19], 0, s[0:1]
	v_pk_mul_f32 v[8:9], v[8:9], v[0:1] op_sel_hi:[1,0]
	v_pk_mul_f32 v[4:5], v[4:5], v[0:1] op_sel_hi:[1,0]
	s_mov_b32 s0, 0x58000
	v_pk_mul_f32 v[14:15], v[14:15], v[0:1] op_sel_hi:[1,0]
	v_pk_mul_f32 v[6:7], v[6:7], v[0:1] op_sel_hi:[1,0]
	v_cvt_pk_bf16_f32 v4, v4, v5
	v_cvt_pk_bf16_f32 v5, v8, v9
	v_add_co_u32_e32 v8, vcc, s0, v18
	v_cvt_pk_bf16_f32 v6, v6, v7
	v_cvt_pk_bf16_f32 v7, v14, v15
	v_addc_co_u32_e32 v9, vcc, 0, v19, vcc
	global_store_dwordx4 v[8:9], v[4:7], off sc1
	v_pk_mul_f32 v[2:3], v[2:3], v[0:1] op_sel_hi:[1,0]
	v_pk_mul_f32 v[8:9], v[10:11], v[0:1] op_sel_hi:[1,0]
	v_pk_mul_f32 v[4:5], v[12:13], v[0:1] op_sel_hi:[1,0]
	v_pk_mul_f32 v[6:7], v[16:17], v[0:1] op_sel_hi:[1,0]
	v_cvt_pk_bf16_f32 v2, v2, v3
	v_cvt_pk_bf16_f32 v3, v4, v5
	v_cvt_pk_bf16_f32 v4, v8, v9
	v_cvt_pk_bf16_f32 v5, v6, v7
	global_store_dwordx4 v[20:21], v[2:5], off offset:256 sc1
	s_waitcnt lgkmcnt(0)
	s_barrier

.LBB0_503:
	s_mov_b32 s0, -1
	s_add_u32 s14, s74, 0x8800000
	s_waitcnt vmcnt(0)
	s_barrier
	s_addc_u32 s15, s75, 0
	v_mbcnt_lo_u32_b32 v0, s0, 0
	v_mbcnt_hi_u32_b32 v166, s0, v0
	s_lshl_b32 s0, s90, 8
	v_and_b32_e32 v130, 15, v166
	s_add_i32 s17, s0, s65
	v_or_b32_e32 v156, s17, v130
	s_ashr_i32 s17, s16, 31
	s_lshl_b32 s1, s64, 5
	s_lshl_b64 s[16:17], s[16:17], 8
	v_lshrrev_b32_e32 v0, 1, v166
	s_or_b32 s16, s16, s1
	v_and_b32_e32 v0, 56, v0
	v_and_b32_e32 v131, 64, v231
	v_lshl_add_u64 v[154:155], s[16:17], 0, v[0:1]
	v_xor_b32_e32 v0, 16, v231
	v_add_u32_e32 v131, 64, v131
	v_cmp_lt_i32_e32 vcc, v0, v131
	v_readlane_b32 s16, v253, 34
	v_lshlrev_b64 v[178:179], 1, v[154:155]
	v_cndmask_b32_e32 v0, v231, v0, vcc
	v_lshlrev_b32_e32 v168, 2, v0
	v_xor_b32_e32 v0, 32, v231
	v_cmp_lt_i32_e32 vcc, v0, v131
	v_readlane_b32 s17, v253, 35
	v_ashrrev_i32_e32 v157, 31, v156
	v_cndmask_b32_e32 v0, v231, v0, vcc
	v_lshl_add_u64 v[158:159], s[16:17], 0, v[178:179]
	v_lshlrev_b64 v[180:181], 11, v[156:157]
	v_lshlrev_b32_e32 v167, 2, v0
	v_or_b32_e32 v0, s65, v130
	v_lshl_add_u64 v[130:131], v[158:159], 0, v[180:181]
	global_load_dwordx4 v[170:173], v[130:131], off
	global_load_dwordx4 v[174:177], v[130:131], off offset:256
	v_or_b32_e32 v130, 16, v156
	v_ashrrev_i32_e32 v131, 31, v130
	v_lshlrev_b64 v[164:165], 11, v[130:131]
	v_lshl_add_u64 v[130:131], v[158:159], 0, v[164:165]
	global_load_dwordx4 v[150:153], v[130:131], off
	global_load_dwordx4 v[146:149], v[130:131], off offset:256
	v_or_b32_e32 v130, 32, v156
	v_ashrrev_i32_e32 v131, 31, v130
	v_lshlrev_b64 v[162:163], 11, v[130:131]
	v_lshl_add_u64 v[130:131], v[158:159], 0, v[162:163]
	global_load_dwordx4 v[142:145], v[130:131], off
	global_load_dwordx4 v[138:141], v[130:131], off offset:256
	v_or_b32_e32 v130, 48, v156
	v_ashrrev_i32_e32 v131, 31, v130
	v_lshlrev_b64 v[160:161], 11, v[130:131]
	v_lshl_add_u64 v[130:131], v[158:159], 0, v[160:161]
	global_load_dwordx4 v[134:137], v[130:131], off
	s_nop 0
	global_load_dwordx4 v[130:133], v[130:131], off offset:256
	v_lshl_add_u64 v[180:181], s[14:15], 0, v[180:181]
	v_lshl_add_u64 v[178:179], v[180:181], 0, v[178:179]
	v_cmp_gt_u32_e32 vcc, 16, v166
	s_lshl_b32 s1, s64, 2
	s_waitcnt vmcnt(0)
	v_lshlrev_b32_e32 v182, 16, v170
	v_and_b32_e32 v183, 0xffff0000, v170
	v_lshlrev_b32_e32 v170, 16, v171
	v_and_b32_e32 v171, 0xffff0000, v171
	v_pk_add_f32 v[128:129], v[128:129], v[170:171]
	v_lshlrev_b32_e32 v170, 16, v172
	v_and_b32_e32 v171, 0xffff0000, v172
	v_pk_add_f32 v[170:171], v[122:123], v[170:171]
	v_lshlrev_b32_e32 v122, 16, v173
	v_and_b32_e32 v123, 0xffff0000, v173
	v_pk_add_f32 v[126:127], v[126:127], v[182:183]
	v_pk_add_f32 v[172:173], v[124:125], v[122:123]
	v_cvt_pk_bf16_f32 v122, v126, v127
	v_cvt_pk_bf16_f32 v123, v128, v129
	v_cvt_pk_bf16_f32 v124, v170, v171
	v_cvt_pk_bf16_f32 v125, v172, v173
	global_store_dwordx4 v[178:179], v[122:125], off sc1
	s_nop 1
	v_pk_mul_f32 v[122:123], v[126:127], v[126:127]
	v_pk_mul_f32 v[126:127], v[170:171], v[170:171]
	v_lshlrev_b32_e32 v170, 16, v174
	v_and_b32_e32 v171, 0xffff0000, v174
	v_pk_add_f32 v[118:119], v[118:119], v[170:171]
	v_lshlrev_b32_e32 v170, 16, v175
	v_and_b32_e32 v171, 0xffff0000, v175
	v_pk_add_f32 v[120:121], v[120:121], v[170:171]
	v_lshlrev_b32_e32 v170, 16, v176
	v_and_b32_e32 v171, 0xffff0000, v176
	v_pk_add_f32 v[170:171], v[114:115], v[170:171]
	v_lshlrev_b32_e32 v114, 16, v177
	v_and_b32_e32 v115, 0xffff0000, v177
	v_pk_mul_f32 v[124:125], v[128:129], v[128:129]
	v_pk_mul_f32 v[128:129], v[172:173], v[172:173]
	v_pk_add_f32 v[172:173], v[116:117], v[114:115]
	v_cvt_pk_bf16_f32 v114, v118, v119
	v_cvt_pk_bf16_f32 v115, v120, v121
	v_cvt_pk_bf16_f32 v116, v170, v171
	v_cvt_pk_bf16_f32 v117, v172, v173
	global_store_dwordx4 v[178:179], v[114:117], off offset:256 sc1
	s_nop 1
	v_pk_mul_f32 v[114:115], v[118:119], v[118:119]
	v_pk_mul_f32 v[116:117], v[120:121], v[120:121]
	v_add_f32_e32 v114, v114, v115
	v_add_f32_e32 v116, v116, v117
	v_pk_mul_f32 v[118:119], v[170:171], v[170:171]
	v_pk_mul_f32 v[120:121], v[172:173], v[172:173]
	v_add_f32_e32 v114, v114, v116
	v_add_f32_e32 v115, v128, v129
	v_add_f32_e32 v116, v126, v127
	v_add_f32_e32 v120, v120, v121
	v_add_f32_e32 v118, v118, v119
	v_add_f32_e32 v115, v116, v115
	v_add_f32_e32 v116, v124, v125
	v_add_f32_e32 v117, v122, v123
	v_add_f32_e32 v118, v118, v120
	v_add_f32_e32 v116, v117, v116
	v_add_f32_e32 v114, v114, v118
	v_add_f32_e32 v115, v116, v115
	v_add_f32_e32 v114, v115, v114
	ds_bpermute_b32 v115, v168, v114
	s_waitcnt lgkmcnt(0)
	v_add_f32_e32 v114, v114, v115
	ds_bpermute_b32 v115, v167, v114
	s_and_saveexec_b64 s[16:17], vcc
	s_cbranch_execz .LBB0_505
	v_lshl_or_b32 v116, v0, 4, s1
	s_waitcnt lgkmcnt(0)
	v_add_f32_e32 v114, v114, v115
	ds_write_b32 v116, v114
.LBB0_505:
	s_or_b64 exec, exec, s[16:17]
	v_lshlrev_b32_e32 v114, 16, v150
	s_waitcnt lgkmcnt(0)
	v_and_b32_e32 v115, 0xffff0000, v150
	v_pk_add_f32 v[110:111], v[110:111], v[114:115]
	v_lshlrev_b32_e32 v114, 16, v151
	v_and_b32_e32 v115, 0xffff0000, v151
	v_pk_add_f32 v[112:113], v[112:113], v[114:115]
	v_lshlrev_b32_e32 v114, 16, v152
	v_and_b32_e32 v115, 0xffff0000, v152
	v_pk_add_f32 v[114:115], v[106:107], v[114:115]
	v_lshlrev_b32_e32 v106, 16, v153
	v_and_b32_e32 v107, 0xffff0000, v153
	v_pk_add_f32 v[116:117], v[108:109], v[106:107]
	v_lshl_add_u64 v[118:119], s[14:15], 0, v[164:165]
	v_cvt_pk_bf16_f32 v106, v110, v111
	v_cvt_pk_bf16_f32 v107, v112, v113
	v_cvt_pk_bf16_f32 v108, v114, v115
	v_cvt_pk_bf16_f32 v109, v116, v117
	v_lshl_add_u64 v[118:119], v[154:155], 1, v[118:119]
	global_store_dwordx4 v[118:119], v[106:109], off sc1
	s_nop 1
	v_pk_mul_f32 v[106:107], v[110:111], v[110:111]
	v_pk_mul_f32 v[110:111], v[114:115], v[114:115]
	v_lshlrev_b32_e32 v114, 16, v146
	v_and_b32_e32 v115, 0xffff0000, v146
	v_pk_add_f32 v[102:103], v[102:103], v[114:115]
	v_lshlrev_b32_e32 v114, 16, v147
	v_and_b32_e32 v115, 0xffff0000, v147
	v_pk_add_f32 v[104:105], v[104:105], v[114:115]
	v_lshlrev_b32_e32 v114, 16, v148
	v_and_b32_e32 v115, 0xffff0000, v148
	v_pk_add_f32 v[114:115], v[98:99], v[114:115]
	v_lshlrev_b32_e32 v98, 16, v149
	v_and_b32_e32 v99, 0xffff0000, v149
	v_pk_mul_f32 v[108:109], v[112:113], v[112:113]
	v_pk_mul_f32 v[112:113], v[116:117], v[116:117]
	v_pk_add_f32 v[116:117], v[100:101], v[98:99]
	v_cvt_pk_bf16_f32 v98, v102, v103
	v_cvt_pk_bf16_f32 v99, v104, v105
	v_cvt_pk_bf16_f32 v100, v114, v115
	v_cvt_pk_bf16_f32 v101, v116, v117
	global_store_dwordx4 v[118:119], v[98:101], off offset:256 sc1
	s_nop 1
	v_pk_mul_f32 v[98:99], v[102:103], v[102:103]
	v_pk_mul_f32 v[100:101], v[104:105], v[104:105]
	v_add_f32_e32 v98, v98, v99
	v_add_f32_e32 v100, v100, v101
	v_pk_mul_f32 v[102:103], v[114:115], v[114:115]
	v_pk_mul_f32 v[104:105], v[116:117], v[116:117]
	v_add_f32_e32 v98, v98, v100
	v_add_f32_e32 v99, v112, v113
	v_add_f32_e32 v100, v110, v111
	v_add_f32_e32 v104, v104, v105
	v_add_f32_e32 v102, v102, v103
	v_add_f32_e32 v99, v100, v99
	v_add_f32_e32 v100, v108, v109
	v_add_f32_e32 v101, v106, v107
	v_add_f32_e32 v102, v102, v104
	v_add_f32_e32 v100, v101, v100
	v_add_f32_e32 v98, v98, v102
	v_add_f32_e32 v99, v100, v99
	v_add_f32_e32 v98, v99, v98
	ds_bpermute_b32 v99, v168, v98
	s_waitcnt lgkmcnt(0)
	v_add_f32_e32 v98, v98, v99
	ds_bpermute_b32 v99, v167, v98
	s_and_saveexec_b64 s[16:17], vcc
	v_readlane_b32 s38, v253, 47
	v_readlane_b32 s91, v253, 27
	s_mov_b32 s89, 0x2e8ba2e9
	s_movk_i32 s90, 0xfea0
	s_mov_b32 s29, 0x47800000
	v_readlane_b32 s39, v253, 48
	s_cbranch_execz .LBB0_507
	v_lshl_or_b32 v100, v0, 4, s1
	s_waitcnt lgkmcnt(0)
	v_add_f32_e32 v98, v98, v99
	ds_write_b32 v100, v98 offset:256

.LBB0_545:
	s_mov_b32 s0, -1
	s_add_u32 s16, s74, 0x8800000
	s_waitcnt vmcnt(0)
	s_barrier
	s_addc_u32 s17, s75, 0
	v_mbcnt_lo_u32_b32 v0, s0, 0
	v_mbcnt_hi_u32_b32 v190, s0, v0
	s_lshl_b32 s14, s90, 8
	v_and_b32_e32 v193, 15, v190
	s_add_i32 s0, s14, s60
	s_ashr_i32 s37, s36, 31
	s_lshl_b32 s15, s61, 5
	v_or_b32_e32 v180, s0, v193
	s_lshl_b64 s[0:1], s[36:37], 8
	v_lshrrev_b32_e32 v0, 1, v190
	s_or_b32 s0, s0, s15
	v_and_b32_e32 v0, 56, v0
	v_lshl_add_u64 v[178:179], s[0:1], 0, v[0:1]
	v_readlane_b32 s0, v253, 47
	v_readlane_b32 s1, v253, 48
	v_ashrrev_i32_e32 v181, 31, v180
	v_lshlrev_b64 v[130:131], 12, v[180:181]
	v_lshl_add_u64 v[182:183], v[178:179], 2, s[0:1]
	v_lshl_add_u64 v[130:131], v[182:183], 0, v[130:131]
	global_load_dwordx4 v[200:203], v[130:131], off
	global_load_dwordx4 v[204:207], v[130:131], off offset:16
	global_load_dwordx4 v[208:211], v[130:131], off offset:512
	global_load_dwordx4 v[212:215], v[130:131], off offset:528
	v_or_b32_e32 v188, 16, v180
	v_or_b32_e32 v186, 32, v180
	v_or_b32_e32 v184, 48, v180
	v_ashrrev_i32_e32 v189, 31, v188
	v_ashrrev_i32_e32 v187, 31, v186
	v_ashrrev_i32_e32 v185, 31, v184
	v_lshlrev_b64 v[130:131], 12, v[188:189]
	v_lshlrev_b64 v[132:133], 12, v[186:187]
	v_lshlrev_b64 v[134:135], 12, v[184:185]
	v_lshl_add_u64 v[130:131], v[182:183], 0, v[130:131]
	v_lshl_add_u64 v[132:133], v[182:183], 0, v[132:133]
	v_lshl_add_u64 v[134:135], v[182:183], 0, v[134:135]
	global_load_dwordx4 v[170:173], v[130:131], off offset:16
	global_load_dwordx4 v[174:177], v[130:131], off
	global_load_dwordx4 v[162:165], v[130:131], off offset:528
	global_load_dwordx4 v[166:169], v[130:131], off offset:512
	global_load_dwordx4 v[154:157], v[132:133], off offset:16
	global_load_dwordx4 v[158:161], v[132:133], off
	global_load_dwordx4 v[146:149], v[132:133], off offset:528
	global_load_dwordx4 v[150:153], v[132:133], off offset:512
	global_load_dwordx4 v[138:141], v[134:135], off offset:16
	global_load_dwordx4 v[142:145], v[134:135], off
	s_nop 0
	global_load_dwordx4 v[130:133], v[134:135], off offset:528
	s_nop 0
	global_load_dwordx4 v[134:137], v[134:135], off offset:512
	v_and_b32_e32 v191, 64, v231
	v_xor_b32_e32 v0, 16, v231
	v_add_u32_e32 v191, 64, v191
	v_xor_b32_e32 v192, 32, v231
	v_cmp_lt_i32_e32 vcc, v0, v191
	v_lshlrev_b64 v[194:195], 11, v[180:181]
	s_lshl_b32 s15, s61, 2
	v_cndmask_b32_e32 v0, v231, v0, vcc
	v_cmp_lt_i32_e32 vcc, v192, v191
	s_waitcnt vmcnt(0)
	v_pk_add_f32 v[128:129], v[128:129], v[202:203]
	v_pk_add_f32 v[126:127], v[126:127], v[200:201]
	v_pk_add_f32 v[124:125], v[124:125], v[206:207]
	v_pk_add_f32 v[122:123], v[122:123], v[204:205]
	v_pk_add_f32 v[200:201], v[116:117], v[214:215]
	v_pk_add_f32 v[202:203], v[114:115], v[212:213]
	v_cvt_pk_bf16_f32 v114, v126, v127
	v_cvt_pk_bf16_f32 v115, v128, v129
	v_cvt_pk_bf16_f32 v116, v122, v123
	v_cvt_pk_bf16_f32 v117, v124, v125
	v_mul_f32_e32 v127, v127, v127
	v_mul_f32_e32 v129, v129, v129
	v_mul_f32_e32 v123, v123, v123
	v_mul_f32_e32 v125, v125, v125
	v_fmac_f32_e32 v127, v126, v126
	v_fmac_f32_e32 v129, v128, v128
	v_fmac_f32_e32 v123, v122, v122
	v_fmac_f32_e32 v125, v124, v124
	v_pk_add_f32 v[120:121], v[120:121], v[210:211]
	v_pk_add_f32 v[118:119], v[118:119], v[208:209]
	v_add_f32_e32 v122, v127, v129
	v_add_f32_e32 v123, v123, v125
	v_cndmask_b32_e32 v191, v231, v192, vcc
	v_lshlrev_b32_e32 v192, 2, v0
	v_or_b32_e32 v0, s60, v193
	v_mul_f32_e32 v181, v119, v119
	v_mul_f32_e32 v193, v121, v121
	v_mul_f32_e32 v204, v203, v203
	v_add_f32_e32 v122, v122, v123
	v_mul_f32_e32 v123, v201, v201
	v_fmac_f32_e32 v181, v118, v118
	v_fmac_f32_e32 v193, v120, v120
	v_fmac_f32_e32 v204, v202, v202
	v_fmac_f32_e32 v123, v200, v200
	v_add_f32_e32 v124, v181, v193
	v_add_f32_e32 v123, v204, v123
	v_add_f32_e32 v123, v124, v123
	v_add_f32_e32 v124, v122, v123
	ds_bpermute_b32 v125, v192, v124
	v_lshl_add_u64 v[122:123], s[16:17], 0, v[194:195]
	v_lshl_add_u64 v[122:123], v[178:179], 1, v[122:123]
	v_lshlrev_b32_e32 v191, 2, v191
	global_store_dwordx4 v[122:123], v[114:117], off sc1
	v_cmp_gt_u32_e32 vcc, 16, v190
	s_waitcnt lgkmcnt(0)
	v_add_f32_e32 v114, v124, v125
	ds_bpermute_b32 v115, v191, v114
	v_cvt_pk_bf16_f32 v116, v118, v119
	v_cvt_pk_bf16_f32 v117, v120, v121
	v_cvt_pk_bf16_f32 v118, v202, v203
	v_cvt_pk_bf16_f32 v119, v200, v201
	global_store_dwordx4 v[122:123], v[116:119], off offset:256 sc1
	s_and_saveexec_b64 s[0:1], vcc
	s_cbranch_execz .LBB0_547
	v_lshl_or_b32 v116, v0, 4, s15
	s_waitcnt lgkmcnt(0)
	v_add_f32_e32 v114, v114, v115
	ds_write_b32 v116, v114
.LBB0_547:
	s_or_b64 exec, exec, s[0:1]
	v_pk_add_f32 v[110:111], v[110:111], v[174:175]
	v_pk_add_f32 v[112:113], v[112:113], v[176:177]
	v_pk_add_f32 v[118:119], v[106:107], v[170:171]
	v_cvt_pk_bf16_f32 v106, v110, v111
	v_mul_f32_e32 v111, v111, v111
	v_fmac_f32_e32 v111, v110, v110
	v_mul_f32_e32 v110, v113, v113
	v_pk_add_f32 v[116:117], v[108:109], v[172:173]
	v_fmac_f32_e32 v110, v112, v112
	v_cvt_pk_bf16_f32 v107, v112, v113
	v_add_f32_e32 v110, v111, v110
	v_mul_f32_e32 v111, v119, v119
	v_mul_f32_e32 v112, v117, v117
	v_fmac_f32_e32 v111, v118, v118
	v_fmac_f32_e32 v112, v116, v116
	v_pk_add_f32 v[104:105], v[104:105], v[168:169]
	v_pk_add_f32 v[102:103], v[102:103], v[166:167]
	v_add_f32_e32 v111, v111, v112
	v_pk_add_f32 v[112:113], v[98:99], v[162:163]
	v_mul_f32_e32 v98, v103, v103
	v_mul_f32_e32 v99, v105, v105
	v_cvt_pk_bf16_f32 v109, v116, v117
	v_add_f32_e32 v116, v110, v111
	v_pk_add_f32 v[110:111], v[100:101], v[164:165]
	v_fmac_f32_e32 v98, v102, v102
	v_fmac_f32_e32 v99, v104, v104
	v_add_f32_e32 v98, v98, v99
	v_mul_f32_e32 v99, v113, v113
	v_mul_f32_e32 v100, v111, v111
	v_fmac_f32_e32 v99, v112, v112
	v_fmac_f32_e32 v100, v110, v110
	v_add_f32_e32 v99, v99, v100
	v_add_f32_e32 v98, v98, v99
	v_add_f32_e32 v101, v116, v98
	ds_bpermute_b32 v116, v192, v101
	s_waitcnt lgkmcnt(1)
	v_lshlrev_b64 v[114:115], 11, v[188:189]
	v_lshl_add_u64 v[98:99], s[16:17], 0, v[114:115]
	v_lshl_add_u64 v[114:115], v[178:179], 1, v[98:99]
	v_cvt_pk_bf16_f32 v108, v118, v119
	s_waitcnt lgkmcnt(0)
	v_add_f32_e32 v98, v101, v116
	ds_bpermute_b32 v99, v191, v98
	v_cvt_pk_bf16_f32 v100, v102, v103
	v_cvt_pk_bf16_f32 v101, v104, v105
	v_cvt_pk_bf16_f32 v102, v112, v113
	v_cvt_pk_bf16_f32 v103, v110, v111
	global_store_dwordx4 v[114:115], v[106:109], off sc1
	global_store_dwordx4 v[114:115], v[100:103], off offset:256 sc1
	s_and_saveexec_b64 s[0:1], vcc
	v_readlane_b32 s91, v253, 27
	s_mov_b32 s89, 0x2e8ba2e9
	s_movk_i32 s90, 0xfea0
	s_mov_b32 s29, 0x47800000
	s_cbranch_execz .LBB0_549
	v_lshl_or_b32 v100, v0, 4, s15
	s_waitcnt lgkmcnt(0)
	v_add_f32_e32 v98, v98, v99
	ds_write_b32 v100, v98 offset:256
.LBB0_549:
	s_or_b64 exec, exec, s[0:1]
	v_pk_add_f32 v[94:95], v[94:95], v[158:159]
	v_pk_add_f32 v[96:97], v[96:97], v[160:161]
	v_pk_add_f32 v[102:103], v[90:91], v[154:155]
	v_cvt_pk_bf16_f32 v90, v94, v95
	v_mul_f32_e32 v95, v95, v95
	v_fmac_f32_e32 v95, v94, v94
	v_mul_f32_e32 v94, v97, v97
	v_pk_add_f32 v[100:101], v[92:93], v[156:157]
	v_fmac_f32_e32 v94, v96, v96
	v_cvt_pk_bf16_f32 v91, v96, v97
	v_add_f32_e32 v94, v95, v94
	v_mul_f32_e32 v95, v103, v103
	v_mul_f32_e32 v96, v101, v101
	v_fmac_f32_e32 v95, v102, v102
	v_fmac_f32_e32 v96, v100, v100
	v_pk_add_f32 v[88:89], v[88:89], v[152:153]
	v_pk_add_f32 v[86:87], v[86:87], v[150:151]
	v_add_f32_e32 v95, v95, v96
	v_pk_add_f32 v[96:97], v[82:83], v[146:147]
	v_mul_f32_e32 v82, v87, v87
	v_mul_f32_e32 v83, v89, v89
	v_cvt_pk_bf16_f32 v93, v100, v101
	v_add_f32_e32 v100, v94, v95
	v_pk_add_f32 v[94:95], v[84:85], v[148:149]
	v_fmac_f32_e32 v82, v86, v86
	v_fmac_f32_e32 v83, v88, v88
	v_add_f32_e32 v82, v82, v83
	v_mul_f32_e32 v83, v97, v97
	v_mul_f32_e32 v84, v95, v95
	v_fmac_f32_e32 v83, v96, v96
	v_fmac_f32_e32 v84, v94, v94
	v_add_f32_e32 v83, v83, v84
	v_add_f32_e32 v82, v82, v83
	v_add_f32_e32 v85, v100, v82
	ds_bpermute_b32 v100, v192, v85
	s_waitcnt lgkmcnt(1)
	v_lshlrev_b64 v[98:99], 11, v[186:187]
	v_lshl_add_u64 v[82:83], s[16:17], 0, v[98:99]
	v_lshl_add_u64 v[98:99], v[178:179], 1, v[82:83]
	v_cvt_pk_bf16_f32 v92, v102, v103
	s_waitcnt lgkmcnt(0)
	v_add_f32_e32 v82, v85, v100
	ds_bpermute_b32 v83, v191, v82
	v_cvt_pk_bf16_f32 v84, v86, v87
	v_cvt_pk_bf16_f32 v85, v88, v89
	v_cvt_pk_bf16_f32 v86, v96, v97
	v_cvt_pk_bf16_f32 v87, v94, v95
	global_store_dwordx4 v[98:99], v[90:93], off sc1
	global_store_dwordx4 v[98:99], v[84:87], off offset:256 sc1
	s_and_saveexec_b64 s[0:1], vcc
	s_cbranch_execz .LBB0_551
	v_lshl_or_b32 v84, v0, 4, s15
	s_waitcnt lgkmcnt(0)
	v_add_f32_e32 v82, v82, v83
	ds_write_b32 v84, v82 offset:512
.LBB0_551:
	s_or_b64 exec, exec, s[0:1]
	v_pk_add_f32 v[78:79], v[78:79], v[142:143]
	v_pk_add_f32 v[80:81], v[80:81], v[144:145]
	v_pk_add_f32 v[86:87], v[74:75], v[138:139]
	v_cvt_pk_bf16_f32 v74, v78, v79
	v_mul_f32_e32 v79, v79, v79
	v_fmac_f32_e32 v79, v78, v78
	v_mul_f32_e32 v78, v81, v81
	v_pk_add_f32 v[84:85], v[76:77], v[140:141]
	v_fmac_f32_e32 v78, v80, v80
	v_cvt_pk_bf16_f32 v75, v80, v81
	v_add_f32_e32 v78, v79, v78
	v_mul_f32_e32 v79, v87, v87
	v_mul_f32_e32 v80, v85, v85
	v_fmac_f32_e32 v79, v86, v86
	v_fmac_f32_e32 v80, v84, v84
	v_pk_add_f32 v[72:73], v[72:73], v[136:137]
	v_pk_add_f32 v[70:71], v[70:71], v[134:135]
	v_add_f32_e32 v79, v79, v80
	v_pk_add_f32 v[80:81], v[66:67], v[130:131]
	v_mul_f32_e32 v66, v71, v71
	v_mul_f32_e32 v67, v73, v73
	v_cvt_pk_bf16_f32 v77, v84, v85
	v_add_f32_e32 v84, v78, v79
	v_pk_add_f32 v[78:79], v[68:69], v[132:133]
	v_fmac_f32_e32 v66, v70, v70
	v_fmac_f32_e32 v67, v72, v72
	v_add_f32_e32 v66, v66, v67
	v_mul_f32_e32 v67, v81, v81
	v_mul_f32_e32 v68, v79, v79
	v_fmac_f32_e32 v67, v80, v80
	v_fmac_f32_e32 v68, v78, v78
	v_add_f32_e32 v67, v67, v68
	v_add_f32_e32 v66, v66, v67
	v_add_f32_e32 v69, v84, v66
	ds_bpermute_b32 v84, v192, v69
	s_waitcnt lgkmcnt(1)
	v_lshlrev_b64 v[82:83], 11, v[184:185]
	v_lshl_add_u64 v[66:67], s[16:17], 0, v[82:83]
	v_lshl_add_u64 v[82:83], v[178:179], 1, v[66:67]
	v_cvt_pk_bf16_f32 v76, v86, v87
	s_waitcnt lgkmcnt(0)
	v_add_f32_e32 v66, v69, v84
	ds_bpermute_b32 v67, v191, v66
	v_cvt_pk_bf16_f32 v68, v70, v71
	v_cvt_pk_bf16_f32 v69, v72, v73
	v_cvt_pk_bf16_f32 v70, v80, v81
	v_cvt_pk_bf16_f32 v71, v78, v79
	global_store_dwordx4 v[82:83], v[74:77], off sc1
	global_store_dwordx4 v[82:83], v[68:71], off offset:256 sc1
	s_and_saveexec_b64 s[0:1], vcc
	s_cbranch_execz .LBB0_553
	v_lshl_or_b32 v68, v0, 4, s15
	s_waitcnt lgkmcnt(0)
	v_add_f32_e32 v66, v66, v67
	ds_write_b32 v68, v66 offset:768
.LBB0_553:
	s_or_b64 exec, exec, s[0:1]
	v_add_u32_e32 v136, 0x80, v180
	v_ashrrev_i32_e32 v137, 31, v136
	s_waitcnt lgkmcnt(0)
	v_lshlrev_b64 v[66:67], 12, v[136:137]
	v_lshl_add_u64 v[66:67], v[182:183], 0, v[66:67]
	global_load_dwordx4 v[120:123], v[66:67], off
	global_load_dwordx4 v[124:127], v[66:67], off offset:16
	global_load_dwordx4 v[128:131], v[66:67], off offset:512
	global_load_dwordx4 v[132:135], v[66:67], off offset:528
	v_add_u32_e32 v118, 0x90, v180
	v_add_u32_e32 v116, 0xa0, v180
	v_add_u32_e32 v114, 0xb0, v180
	v_ashrrev_i32_e32 v119, 31, v118
	v_ashrrev_i32_e32 v117, 31, v116
	v_ashrrev_i32_e32 v115, 31, v114
	v_lshlrev_b64 v[66:67], 12, v[118:119]
	v_lshlrev_b64 v[68:69], 12, v[116:117]
	v_lshlrev_b64 v[70:71], 12, v[114:115]
	v_lshl_add_u64 v[66:67], v[182:183], 0, v[66:67]
	v_lshl_add_u64 v[68:69], v[182:183], 0, v[68:69]
	v_lshl_add_u64 v[70:71], v[182:183], 0, v[70:71]
	global_load_dwordx4 v[106:109], v[66:67], off offset:16
	global_load_dwordx4 v[110:113], v[66:67], off
	global_load_dwordx4 v[98:101], v[66:67], off offset:528
	global_load_dwordx4 v[102:105], v[66:67], off offset:512
	global_load_dwordx4 v[90:93], v[68:69], off offset:16
	global_load_dwordx4 v[94:97], v[68:69], off
	global_load_dwordx4 v[82:85], v[68:69], off offset:528
	global_load_dwordx4 v[86:89], v[68:69], off offset:512
	global_load_dwordx4 v[74:77], v[70:71], off offset:16
	global_load_dwordx4 v[78:81], v[70:71], off
	s_nop 0
	global_load_dwordx4 v[66:69], v[70:71], off offset:528
	s_nop 0
	global_load_dwordx4 v[70:73], v[70:71], off offset:512
	v_lshlrev_b64 v[136:137], 11, v[136:137]
	s_waitcnt vmcnt(15)
	v_pk_add_f32 v[64:65], v[64:65], v[122:123]
	v_pk_add_f32 v[62:63], v[62:63], v[120:121]
	s_waitcnt vmcnt(14)
	v_pk_add_f32 v[60:61], v[60:61], v[126:127]
	v_pk_add_f32 v[58:59], v[58:59], v[124:125]
	s_waitcnt vmcnt(13)
	v_pk_add_f32 v[56:57], v[56:57], v[130:131]
	v_pk_add_f32 v[54:55], v[54:55], v[128:129]
	s_waitcnt vmcnt(12)
	v_pk_add_f32 v[120:121], v[52:53], v[134:135]
	v_pk_add_f32 v[122:123], v[50:51], v[132:133]
	v_cvt_pk_bf16_f32 v50, v62, v63
	v_cvt_pk_bf16_f32 v51, v64, v65
	v_cvt_pk_bf16_f32 v52, v58, v59
	v_cvt_pk_bf16_f32 v53, v60, v61
	v_mul_f32_e32 v63, v63, v63
	v_mul_f32_e32 v65, v65, v65
	v_mul_f32_e32 v59, v59, v59
	v_mul_f32_e32 v61, v61, v61
	v_mul_f32_e32 v124, v55, v55
	v_mul_f32_e32 v125, v57, v57
	v_mul_f32_e32 v126, v123, v123
	v_mul_f32_e32 v127, v121, v121
	v_fmac_f32_e32 v63, v62, v62
	v_fmac_f32_e32 v65, v64, v64
	v_fmac_f32_e32 v59, v58, v58
	v_fmac_f32_e32 v61, v60, v60
	v_fmac_f32_e32 v124, v54, v54
	v_fmac_f32_e32 v125, v56, v56
	v_fmac_f32_e32 v126, v122, v122
	v_fmac_f32_e32 v127, v120, v120
	v_add_f32_e32 v58, v63, v65
	v_add_f32_e32 v59, v59, v61
	v_add_f32_e32 v60, v124, v125
	v_add_f32_e32 v61, v126, v127
	v_add_f32_e32 v58, v58, v59
	v_add_f32_e32 v59, v60, v61
	v_add_f32_e32 v60, v58, v59
	ds_bpermute_b32 v61, v192, v60
	v_lshl_add_u64 v[58:59], s[16:17], 0, v[136:137]
	v_lshl_add_u64 v[58:59], v[178:179], 1, v[58:59]
	global_store_dwordx4 v[58:59], v[50:53], off sc1
	s_waitcnt lgkmcnt(0)
	s_nop 0
	v_add_f32_e32 v50, v60, v61
	ds_bpermute_b32 v51, v191, v50
	v_cvt_pk_bf16_f32 v52, v54, v55
	v_cvt_pk_bf16_f32 v53, v56, v57
	v_cvt_pk_bf16_f32 v54, v122, v123
	v_cvt_pk_bf16_f32 v55, v120, v121
	global_store_dwordx4 v[58:59], v[52:55], off offset:256 sc1
	s_and_saveexec_b64 s[0:1], vcc
	s_cbranch_execz .LBB0_555
	v_lshl_or_b32 v52, v0, 4, s15
	s_waitcnt lgkmcnt(0)
	v_add_f32_e32 v50, v50, v51
	ds_write_b32 v52, v50 offset:2048
.LBB0_555:
	s_or_b64 exec, exec, s[0:1]
	s_waitcnt vmcnt(12)
	v_pk_add_f32 v[46:47], v[46:47], v[110:111]
	v_pk_add_f32 v[48:49], v[48:49], v[112:113]
	v_pk_add_f32 v[54:55], v[42:43], v[106:107]
	v_cvt_pk_bf16_f32 v42, v46, v47
	v_mul_f32_e32 v47, v47, v47
	v_fmac_f32_e32 v47, v46, v46
	v_mul_f32_e32 v46, v49, v49
	v_pk_add_f32 v[52:53], v[44:45], v[108:109]
	v_fmac_f32_e32 v46, v48, v48
	v_cvt_pk_bf16_f32 v43, v48, v49
	v_add_f32_e32 v46, v47, v46
	v_mul_f32_e32 v47, v55, v55
	v_mul_f32_e32 v48, v53, v53
	v_fmac_f32_e32 v47, v54, v54
	v_fmac_f32_e32 v48, v52, v52
	s_waitcnt vmcnt(10)
	v_pk_add_f32 v[40:41], v[40:41], v[104:105]
	v_pk_add_f32 v[38:39], v[38:39], v[102:103]
	v_add_f32_e32 v47, v47, v48
	v_pk_add_f32 v[48:49], v[34:35], v[98:99]
	v_mul_f32_e32 v34, v39, v39
	v_mul_f32_e32 v35, v41, v41
	v_cvt_pk_bf16_f32 v45, v52, v53
	v_add_f32_e32 v52, v46, v47
	v_pk_add_f32 v[46:47], v[36:37], v[100:101]
	v_fmac_f32_e32 v34, v38, v38
	v_fmac_f32_e32 v35, v40, v40
	v_add_f32_e32 v34, v34, v35
	v_mul_f32_e32 v35, v49, v49
	v_mul_f32_e32 v36, v47, v47
	v_fmac_f32_e32 v35, v48, v48
	v_fmac_f32_e32 v36, v46, v46
	v_add_f32_e32 v35, v35, v36
	v_add_f32_e32 v34, v34, v35
	v_add_f32_e32 v37, v52, v34
	ds_bpermute_b32 v52, v192, v37
	s_waitcnt lgkmcnt(1)
	v_lshlrev_b64 v[50:51], 11, v[118:119]
	v_lshl_add_u64 v[34:35], s[16:17], 0, v[50:51]
	v_lshl_add_u64 v[50:51], v[178:179], 1, v[34:35]
	v_cvt_pk_bf16_f32 v44, v54, v55
	s_waitcnt lgkmcnt(0)
	v_add_f32_e32 v34, v37, v52
	ds_bpermute_b32 v35, v191, v34
	v_cvt_pk_bf16_f32 v36, v38, v39
	v_cvt_pk_bf16_f32 v37, v40, v41
	v_cvt_pk_bf16_f32 v38, v48, v49
	v_cvt_pk_bf16_f32 v39, v46, v47
	global_store_dwordx4 v[50:51], v[42:45], off sc1
	global_store_dwordx4 v[50:51], v[36:39], off offset:256 sc1
	s_and_saveexec_b64 s[0:1], vcc
	s_cbranch_execz .LBB0_557
	v_lshl_or_b32 v36, v0, 4, s15
	s_waitcnt lgkmcnt(0)
	v_add_f32_e32 v34, v34, v35
	ds_write_b32 v36, v34 offset:2304
.LBB0_557:
	s_or_b64 exec, exec, s[0:1]
	s_waitcnt vmcnt(10)
	v_pk_add_f32 v[30:31], v[30:31], v[94:95]
	v_pk_add_f32 v[32:33], v[32:33], v[96:97]
	v_pk_add_f32 v[38:39], v[26:27], v[90:91]
	v_cvt_pk_bf16_f32 v26, v30, v31
	v_mul_f32_e32 v31, v31, v31
	v_fmac_f32_e32 v31, v30, v30
	v_mul_f32_e32 v30, v33, v33
	v_pk_add_f32 v[36:37], v[28:29], v[92:93]
	v_fmac_f32_e32 v30, v32, v32
	v_cvt_pk_bf16_f32 v27, v32, v33
	v_add_f32_e32 v30, v31, v30
	v_mul_f32_e32 v31, v39, v39
	v_mul_f32_e32 v32, v37, v37
	v_fmac_f32_e32 v31, v38, v38
	v_fmac_f32_e32 v32, v36, v36
	s_waitcnt vmcnt(8)
	v_pk_add_f32 v[24:25], v[24:25], v[88:89]
	v_pk_add_f32 v[22:23], v[22:23], v[86:87]
	v_add_f32_e32 v31, v31, v32
	v_pk_add_f32 v[32:33], v[18:19], v[82:83]
	v_mul_f32_e32 v18, v23, v23
	v_mul_f32_e32 v19, v25, v25
	v_cvt_pk_bf16_f32 v29, v36, v37
	v_add_f32_e32 v36, v30, v31
	v_pk_add_f32 v[30:31], v[20:21], v[84:85]
	v_fmac_f32_e32 v18, v22, v22
	v_fmac_f32_e32 v19, v24, v24
	v_add_f32_e32 v18, v18, v19
	v_mul_f32_e32 v19, v33, v33
	v_mul_f32_e32 v20, v31, v31
	v_fmac_f32_e32 v19, v32, v32
	v_fmac_f32_e32 v20, v30, v30
	v_add_f32_e32 v19, v19, v20
	v_add_f32_e32 v18, v18, v19
	v_add_f32_e32 v21, v36, v18
	ds_bpermute_b32 v36, v192, v21
	s_waitcnt lgkmcnt(1)
	v_lshlrev_b64 v[34:35], 11, v[116:117]
	v_lshl_add_u64 v[18:19], s[16:17], 0, v[34:35]
	v_lshl_add_u64 v[34:35], v[178:179], 1, v[18:19]
	v_cvt_pk_bf16_f32 v28, v38, v39
	s_waitcnt lgkmcnt(0)
	v_add_f32_e32 v18, v21, v36
	ds_bpermute_b32 v19, v191, v18
	v_cvt_pk_bf16_f32 v20, v22, v23
	v_cvt_pk_bf16_f32 v21, v24, v25
	v_cvt_pk_bf16_f32 v22, v32, v33
	v_cvt_pk_bf16_f32 v23, v30, v31
	global_store_dwordx4 v[34:35], v[26:29], off sc1
	global_store_dwordx4 v[34:35], v[20:23], off offset:256 sc1
	s_and_saveexec_b64 s[0:1], vcc
	s_cbranch_execz .LBB0_559
	v_lshl_or_b32 v20, v0, 4, s15
	s_waitcnt lgkmcnt(0)
	v_add_f32_e32 v18, v18, v19
	ds_write_b32 v20, v18 offset:2560
.LBB0_559:
	s_or_b64 exec, exec, s[0:1]
	s_waitcnt vmcnt(8)
	v_pk_add_f32 v[14:15], v[14:15], v[78:79]
	v_pk_add_f32 v[16:17], v[16:17], v[80:81]
	v_pk_add_f32 v[22:23], v[10:11], v[74:75]
	v_cvt_pk_bf16_f32 v10, v14, v15
	v_mul_f32_e32 v15, v15, v15
	v_fmac_f32_e32 v15, v14, v14
	v_mul_f32_e32 v14, v17, v17
	v_pk_add_f32 v[20:21], v[12:13], v[76:77]
	v_fmac_f32_e32 v14, v16, v16
	v_cvt_pk_bf16_f32 v11, v16, v17
	v_add_f32_e32 v14, v15, v14
	v_mul_f32_e32 v15, v23, v23
	v_mul_f32_e32 v16, v21, v21
	v_fmac_f32_e32 v15, v22, v22
	v_fmac_f32_e32 v16, v20, v20
	s_waitcnt vmcnt(6)
	v_pk_add_f32 v[8:9], v[8:9], v[72:73]
	v_pk_add_f32 v[6:7], v[6:7], v[70:71]
	v_add_f32_e32 v15, v15, v16
	v_pk_add_f32 v[16:17], v[2:3], v[66:67]
	v_mul_f32_e32 v2, v7, v7
	v_mul_f32_e32 v3, v9, v9
	v_cvt_pk_bf16_f32 v13, v20, v21
	v_add_f32_e32 v20, v14, v15
	v_pk_add_f32 v[14:15], v[4:5], v[68:69]
	v_fmac_f32_e32 v2, v6, v6
	v_fmac_f32_e32 v3, v8, v8
	v_add_f32_e32 v2, v2, v3
	v_mul_f32_e32 v3, v17, v17
	v_mul_f32_e32 v4, v15, v15
	v_fmac_f32_e32 v3, v16, v16
	v_fmac_f32_e32 v4, v14, v14
	v_add_f32_e32 v3, v3, v4
	v_add_f32_e32 v2, v2, v3
	v_add_f32_e32 v5, v20, v2
	ds_bpermute_b32 v20, v192, v5
	s_waitcnt lgkmcnt(1)
	v_lshlrev_b64 v[18:19], 11, v[114:115]
	v_lshl_add_u64 v[2:3], s[16:17], 0, v[18:19]
	v_lshl_add_u64 v[18:19], v[178:179], 1, v[2:3]
	v_cvt_pk_bf16_f32 v12, v22, v23
	s_waitcnt lgkmcnt(0)
	v_add_f32_e32 v2, v5, v20
	ds_bpermute_b32 v3, v191, v2
	v_cvt_pk_bf16_f32 v4, v6, v7
	v_cvt_pk_bf16_f32 v5, v8, v9
	v_cvt_pk_bf16_f32 v6, v16, v17
	v_cvt_pk_bf16_f32 v7, v14, v15
	global_store_dwordx4 v[18:19], v[10:13], off sc1
	global_store_dwordx4 v[18:19], v[4:7], off offset:256 sc1
	s_and_saveexec_b64 s[0:1], vcc
	s_cbranch_execz .LBB0_561
	v_lshl_or_b32 v0, v0, 4, s15
	s_waitcnt lgkmcnt(0)
	v_add_f32_e32 v2, v2, v3
	ds_write_b32 v0, v2 offset:2816

.LBB0_582:
	v_lshrrev_b64 v[8:9], 8, v[6:7]
	v_and_b32_e32 v8, -4, v8
	v_lshl_add_u64 v[8:9], s[48:49], 0, v[8:9]
	global_load_dword v0, v[8:9], off
	s_nop 0
	global_load_dwordx4 v[8:11], v[2:3], off
	v_lshl_add_u64 v[6:7], v[6:7], 0, s[4:5]
	s_mov_b64 s[54:55], 0xfffff
	v_cmp_lt_u64_e32 vcc, s[54:55], v[6:7]
	v_lshl_add_u64 v[2:3], v[2:3], 0, s[68:69]
	s_or_b64 s[50:51], vcc, s[50:51]
	s_waitcnt vmcnt(0)
	v_pk_mul_f32 v[8:9], v[0:1], v[8:9] op_sel_hi:[0,1]
	v_pk_mul_f32 v[10:11], v[0:1], v[10:11] op_sel_hi:[0,1]
	v_cvt_pk_bf16_f32 v8, v8, v9
	v_cvt_pk_bf16_f32 v9, v10, v11
	global_store_dwordx2 v[4:5], v[8:9], off sc1
	v_lshl_add_u64 v[4:5], v[4:5], 0, s[8:9]
	s_andn2_b64 exec, exec, s[50:51]
	s_cbranch_execnz .LBB0_582

.LBB0_585:
	s_ashr_i32 s35, s29, 31
	s_lshr_b32 s35, s35, 27
	s_add_i32 s35, s29, s35
	s_ashr_i32 s35, s35, 5
	s_lshl_b32 s48, s35, 6
	s_lshl_b32 s35, s35, 10
	s_sub_i32 s46, s31, s35
	v_or_b32_e32 v38, s48, v102
	s_ashr_i32 s47, s46, 31
	v_ashrrev_i32_e32 v39, 31, v38
	v_or_b32_e32 v10, 8, v38
	v_lshl_add_u64 v[54:55], s[46:47], 2, v[2:3]
	v_lshlrev_b64 v[6:7], 12, v[38:39]
	v_ashrrev_i32_e32 v11, 31, v10
	v_lshl_add_u64 v[6:7], v[54:55], 0, v[6:7]
	v_lshlrev_b64 v[10:11], 12, v[10:11]
	v_or_b32_e32 v14, 16, v38
	global_load_dwordx4 v[6:9], v[6:7], off
	v_lshl_add_u64 v[10:11], v[54:55], 0, v[10:11]
	v_ashrrev_i32_e32 v15, 31, v14
	global_load_dwordx4 v[10:13], v[10:11], off
	v_lshlrev_b64 v[14:15], 12, v[14:15]
	v_or_b32_e32 v34, 24, v38
	v_lshl_add_u64 v[14:15], v[54:55], 0, v[14:15]
	v_ashrrev_i32_e32 v35, 31, v34
	global_load_dwordx4 v[14:17], v[14:15], off
	v_lshlrev_b64 v[34:35], 12, v[34:35]
	v_or_b32_e32 v42, 32, v38
	v_lshl_add_u64 v[34:35], v[54:55], 0, v[34:35]
	v_ashrrev_i32_e32 v43, 31, v42
	global_load_dwordx4 v[34:37], v[34:35], off
	v_lshlrev_b64 v[42:43], 12, v[42:43]
	v_or_b32_e32 v46, 40, v38
	v_lshl_add_u64 v[42:43], v[54:55], 0, v[42:43]
	v_ashrrev_i32_e32 v47, 31, v46
	global_load_dwordx4 v[42:45], v[42:43], off
	v_lshlrev_b64 v[46:47], 12, v[46:47]
	v_or_b32_e32 v50, 48, v38
	v_lshl_add_u64 v[46:47], v[54:55], 0, v[46:47]
	v_ashrrev_i32_e32 v51, 31, v50
	global_load_dwordx4 v[46:49], v[46:47], off
	v_lshlrev_b64 v[50:51], 12, v[50:51]
	v_or_b32_e32 v38, 56, v38
	v_lshl_add_u64 v[50:51], v[54:55], 0, v[50:51]
	v_ashrrev_i32_e32 v39, 31, v38
	global_load_dwordx4 v[50:53], v[50:51], off
	v_lshlrev_b64 v[38:39], 12, v[38:39]
	v_lshl_add_u64 v[38:39], v[54:55], 0, v[38:39]
	global_load_dwordx4 v[54:57], v[38:39], off
	v_add_u32_e32 v0, v40, v71
	s_ashr_i32 s49, s48, 31
	s_add_i32 s29, s29, s72
	s_add_i32 s31, s31, s28
	s_cmpk_lt_i32 s29, 0x200
	s_waitcnt vmcnt(7)
	ds_write2_b32 v0, v6, v7 offset1:1
	ds_write2_b32 v0, v8, v9 offset0:2 offset1:3
	v_add_u32_e32 v6, 0x420, v0
	s_waitcnt vmcnt(6)
	ds_write2_b32 v6, v10, v11 offset1:1
	v_add_u32_e32 v6, 0x428, v0
	ds_write2_b32 v6, v12, v13 offset1:1
	v_add_u32_e32 v6, 0x840, v0
	v_lshl_add_u64 v[10:11], s[48:49], 1, v[4:5]
	s_waitcnt vmcnt(5)
	ds_write2_b32 v6, v14, v15 offset1:1
	v_add_u32_e32 v6, 0x848, v0
	ds_write2_b32 v6, v16, v17 offset1:1
	v_add_u32_e32 v6, 0xc60, v0
	s_waitcnt vmcnt(4)
	ds_write2_b32 v6, v34, v35 offset1:1
	v_add_u32_e32 v6, 0xc68, v0
	ds_write2_b32 v6, v36, v37 offset1:1
	v_add_u32_e32 v6, 0x1080, v0
	s_waitcnt vmcnt(3)
	ds_write2_b32 v6, v42, v43 offset1:1
	v_add_u32_e32 v6, 0x1088, v0
	ds_write2_b32 v6, v44, v45 offset1:1
	v_add_u32_e32 v6, 0x14a0, v0
	s_waitcnt vmcnt(2)
	ds_write2_b32 v6, v46, v47 offset1:1
	v_add_u32_e32 v6, 0x14a8, v0
	ds_write2_b32 v6, v48, v49 offset1:1
	v_add_u32_e32 v6, 0x18c0, v0
	v_add_u32_e32 v46, s46, v102
	s_waitcnt vmcnt(1)
	ds_write2_b32 v6, v50, v51 offset1:1
	v_add_u32_e32 v6, 0x18c8, v0
	ds_write2_b32 v6, v52, v53 offset1:1
	v_add_u32_e32 v6, 0x1ce0, v0
	v_add_u32_e32 v0, 0x1ce8, v0
	s_waitcnt vmcnt(0)
	ds_write2_b32 v6, v54, v55 offset1:1
	ds_write2_b32 v0, v56, v57 offset1:1
	s_waitcnt lgkmcnt(0)
	ds_read2_b32 v[12:13], v41 offset0:33 offset1:41
	ds_read2_b32 v[14:15], v41 offset1:8
	ds_read2_b32 v[16:17], v41 offset0:66 offset1:74
	ds_read2_b32 v[34:35], v41 offset0:99 offset1:107
	ds_read2_b32 v[36:37], v41 offset0:132 offset1:140
	ds_read2_b32 v[38:39], v41 offset0:165 offset1:173
	ds_read2_b32 v[42:43], v41 offset0:198 offset1:206
	ds_read2_b32 v[44:45], v41 offset0:231 offset1:239
	v_ashrrev_i32_e32 v47, 31, v46
	v_lshlrev_b64 v[48:49], 11, v[46:47]
	s_waitcnt lgkmcnt(6)
	v_cvt_pk_bf16_f32 v6, v14, v12
	s_waitcnt lgkmcnt(4)
	v_cvt_pk_bf16_f32 v7, v16, v34
	s_waitcnt lgkmcnt(2)
	v_cvt_pk_bf16_f32 v8, v36, v38
	s_waitcnt lgkmcnt(0)
	v_cvt_pk_bf16_f32 v9, v42, v44
	v_lshl_add_u64 v[48:49], v[10:11], 0, v[48:49]
	v_add_u32_e32 v12, 8, v46
	global_store_dwordx4 v[48:49], v[6:9], off sc1
	v_add_u32_e32 v48, 16, v46
	v_ashrrev_i32_e32 v49, 31, v48
	v_cvt_pk_bf16_f32 v6, v15, v13
	v_ashrrev_i32_e32 v13, 31, v12
	v_lshlrev_b64 v[12:13], 11, v[12:13]
	v_cvt_pk_bf16_f32 v7, v17, v35
	v_cvt_pk_bf16_f32 v8, v37, v39
	v_cvt_pk_bf16_f32 v9, v43, v45
	v_lshl_add_u64 v[12:13], v[10:11], 0, v[12:13]
	global_store_dwordx4 v[12:13], v[6:9], off sc1
	ds_read2_b32 v[12:13], v41 offset0:49 offset1:57
	ds_read2_b32 v[14:15], v41 offset0:16 offset1:24
	ds_read2_b32 v[16:17], v41 offset0:82 offset1:90
	ds_read2_b32 v[34:35], v41 offset0:115 offset1:123
	ds_read2_b32 v[36:37], v41 offset0:148 offset1:156
	ds_read2_b32 v[38:39], v41 offset0:181 offset1:189
	ds_read2_b32 v[42:43], v41 offset0:214 offset1:222
	ds_read2_b32 v[44:45], v41 offset0:247 offset1:255
	v_lshlrev_b64 v[48:49], 11, v[48:49]
	s_waitcnt lgkmcnt(6)
	v_cvt_pk_bf16_f32 v6, v14, v12
	s_waitcnt lgkmcnt(4)
	v_cvt_pk_bf16_f32 v7, v16, v34
	s_waitcnt lgkmcnt(2)
	v_cvt_pk_bf16_f32 v8, v36, v38
	s_waitcnt lgkmcnt(0)
	v_cvt_pk_bf16_f32 v9, v42, v44
	v_lshl_add_u64 v[48:49], v[10:11], 0, v[48:49]
	v_add_u32_e32 v12, 24, v46
	global_store_dwordx4 v[48:49], v[6:9], off sc1
	s_nop 1
	v_cvt_pk_bf16_f32 v6, v15, v13
	v_ashrrev_i32_e32 v13, 31, v12
	v_lshlrev_b64 v[12:13], 11, v[12:13]
	v_cvt_pk_bf16_f32 v7, v17, v35
	v_cvt_pk_bf16_f32 v8, v37, v39
	v_cvt_pk_bf16_f32 v9, v43, v45
	v_lshl_add_u64 v[10:11], v[10:11], 0, v[12:13]
	global_store_dwordx4 v[10:11], v[6:9], off sc1
	s_waitcnt lgkmcnt(0)
	s_cbranch_scc1 .LBB0_585

.LBB0_588:
	s_ashr_i32 s46, s29, 31
	s_lshr_b32 s46, s46, 26
	s_add_i32 s46, s29, s46
	s_and_b32 s48, s46, 0xffffffc0
	s_lshl_b32 s46, s46, 5
	s_and_b32 s46, s46, 0xfffff800
	s_sub_i32 s46, s35, s46
	v_or_b32_e32 v38, s48, v102
	s_ashr_i32 s47, s46, 31
	v_ashrrev_i32_e32 v39, 31, v38
	v_or_b32_e32 v10, 8, v38
	v_lshl_add_u64 v[54:55], s[46:47], 2, v[4:5]
	v_lshlrev_b64 v[6:7], 13, v[38:39]
	v_ashrrev_i32_e32 v11, 31, v10
	v_lshl_add_u64 v[6:7], v[54:55], 0, v[6:7]
	v_lshlrev_b64 v[10:11], 13, v[10:11]
	v_or_b32_e32 v14, 16, v38
	global_load_dwordx4 v[6:9], v[6:7], off
	v_lshl_add_u64 v[10:11], v[54:55], 0, v[10:11]
	v_ashrrev_i32_e32 v15, 31, v14
	global_load_dwordx4 v[10:13], v[10:11], off
	v_lshlrev_b64 v[14:15], 13, v[14:15]
	v_or_b32_e32 v34, 24, v38
	v_lshl_add_u64 v[14:15], v[54:55], 0, v[14:15]
	v_ashrrev_i32_e32 v35, 31, v34
	global_load_dwordx4 v[14:17], v[14:15], off
	v_lshlrev_b64 v[34:35], 13, v[34:35]
	v_or_b32_e32 v42, 32, v38
	v_lshl_add_u64 v[34:35], v[54:55], 0, v[34:35]
	v_ashrrev_i32_e32 v43, 31, v42
	global_load_dwordx4 v[34:37], v[34:35], off
	v_lshlrev_b64 v[42:43], 13, v[42:43]
	v_or_b32_e32 v46, 40, v38
	v_lshl_add_u64 v[42:43], v[54:55], 0, v[42:43]
	v_ashrrev_i32_e32 v47, 31, v46
	global_load_dwordx4 v[42:45], v[42:43], off
	v_lshlrev_b64 v[46:47], 13, v[46:47]
	v_or_b32_e32 v50, 48, v38
	v_lshl_add_u64 v[46:47], v[54:55], 0, v[46:47]
	v_ashrrev_i32_e32 v51, 31, v50
	global_load_dwordx4 v[46:49], v[46:47], off
	v_lshlrev_b64 v[50:51], 13, v[50:51]
	v_or_b32_e32 v38, 56, v38
	v_lshl_add_u64 v[50:51], v[54:55], 0, v[50:51]
	v_ashrrev_i32_e32 v39, 31, v38
	global_load_dwordx4 v[50:53], v[50:51], off
	v_lshlrev_b64 v[38:39], 13, v[38:39]
	v_lshl_add_u64 v[38:39], v[54:55], 0, v[38:39]
	global_load_dwordx4 v[54:57], v[38:39], off
	v_add_u32_e32 v0, v40, v71
	s_ashr_i32 s49, s48, 31
	s_add_i32 s29, s29, s72
	s_add_i32 s35, s35, s28
	s_cmpk_lt_i32 s29, 0x400
	s_waitcnt vmcnt(7)
	ds_write2_b32 v0, v6, v7 offset1:1
	ds_write2_b32 v0, v8, v9 offset0:2 offset1:3
	v_add_u32_e32 v6, 0x420, v0
	s_waitcnt vmcnt(6)
	ds_write2_b32 v6, v10, v11 offset1:1
	v_add_u32_e32 v6, 0x428, v0
	ds_write2_b32 v6, v12, v13 offset1:1
	v_add_u32_e32 v6, 0x840, v0
	v_lshl_add_u64 v[10:11], s[48:49], 1, v[2:3]
	s_waitcnt vmcnt(5)
	ds_write2_b32 v6, v14, v15 offset1:1
	v_add_u32_e32 v6, 0x848, v0
	ds_write2_b32 v6, v16, v17 offset1:1
	v_add_u32_e32 v6, 0xc60, v0
	s_waitcnt vmcnt(4)
	ds_write2_b32 v6, v34, v35 offset1:1
	v_add_u32_e32 v6, 0xc68, v0
	ds_write2_b32 v6, v36, v37 offset1:1
	v_add_u32_e32 v6, 0x1080, v0
	s_waitcnt vmcnt(3)
	ds_write2_b32 v6, v42, v43 offset1:1
	v_add_u32_e32 v6, 0x1088, v0
	ds_write2_b32 v6, v44, v45 offset1:1
	v_add_u32_e32 v6, 0x14a0, v0
	s_waitcnt vmcnt(2)
	ds_write2_b32 v6, v46, v47 offset1:1
	v_add_u32_e32 v6, 0x14a8, v0
	ds_write2_b32 v6, v48, v49 offset1:1
	v_add_u32_e32 v6, 0x18c0, v0
	v_add_u32_e32 v46, s46, v102
	s_waitcnt vmcnt(1)
	ds_write2_b32 v6, v50, v51 offset1:1
	v_add_u32_e32 v6, 0x18c8, v0
	ds_write2_b32 v6, v52, v53 offset1:1
	v_add_u32_e32 v6, 0x1ce0, v0
	v_add_u32_e32 v0, 0x1ce8, v0
	s_waitcnt vmcnt(0)
	ds_write2_b32 v6, v54, v55 offset1:1
	ds_write2_b32 v0, v56, v57 offset1:1
	s_waitcnt lgkmcnt(0)
	ds_read2_b32 v[12:13], v41 offset0:33 offset1:41
	ds_read2_b32 v[14:15], v41 offset1:8
	ds_read2_b32 v[16:17], v41 offset0:66 offset1:74
	ds_read2_b32 v[34:35], v41 offset0:99 offset1:107
	ds_read2_b32 v[36:37], v41 offset0:132 offset1:140
	ds_read2_b32 v[38:39], v41 offset0:165 offset1:173
	ds_read2_b32 v[42:43], v41 offset0:198 offset1:206
	ds_read2_b32 v[44:45], v41 offset0:231 offset1:239
	v_ashrrev_i32_e32 v47, 31, v46
	v_lshlrev_b64 v[48:49], 11, v[46:47]
	s_waitcnt lgkmcnt(6)
	v_cvt_pk_bf16_f32 v6, v14, v12
	s_waitcnt lgkmcnt(4)
	v_cvt_pk_bf16_f32 v7, v16, v34
	s_waitcnt lgkmcnt(2)
	v_cvt_pk_bf16_f32 v8, v36, v38
	s_waitcnt lgkmcnt(0)
	v_cvt_pk_bf16_f32 v9, v42, v44
	v_lshl_add_u64 v[48:49], v[10:11], 0, v[48:49]
	v_add_u32_e32 v12, 8, v46
	global_store_dwordx4 v[48:49], v[6:9], off sc1
	v_add_u32_e32 v48, 16, v46
	v_ashrrev_i32_e32 v49, 31, v48
	v_cvt_pk_bf16_f32 v6, v15, v13
	v_ashrrev_i32_e32 v13, 31, v12
	v_lshlrev_b64 v[12:13], 11, v[12:13]
	v_cvt_pk_bf16_f32 v7, v17, v35
	v_cvt_pk_bf16_f32 v8, v37, v39
	v_cvt_pk_bf16_f32 v9, v43, v45
	v_lshl_add_u64 v[12:13], v[10:11], 0, v[12:13]
	global_store_dwordx4 v[12:13], v[6:9], off sc1
	ds_read2_b32 v[12:13], v41 offset0:49 offset1:57
	ds_read2_b32 v[14:15], v41 offset0:16 offset1:24
	ds_read2_b32 v[16:17], v41 offset0:82 offset1:90
	ds_read2_b32 v[34:35], v41 offset0:115 offset1:123
	ds_read2_b32 v[36:37], v41 offset0:148 offset1:156
	ds_read2_b32 v[38:39], v41 offset0:181 offset1:189
	ds_read2_b32 v[42:43], v41 offset0:214 offset1:222
	ds_read2_b32 v[44:45], v41 offset0:247 offset1:255
	v_lshlrev_b64 v[48:49], 11, v[48:49]
	s_waitcnt lgkmcnt(6)
	v_cvt_pk_bf16_f32 v6, v14, v12
	s_waitcnt lgkmcnt(4)
	v_cvt_pk_bf16_f32 v7, v16, v34
	s_waitcnt lgkmcnt(2)
	v_cvt_pk_bf16_f32 v8, v36, v38
	s_waitcnt lgkmcnt(0)
	v_cvt_pk_bf16_f32 v9, v42, v44
	v_lshl_add_u64 v[48:49], v[10:11], 0, v[48:49]
	v_add_u32_e32 v12, 24, v46
	global_store_dwordx4 v[48:49], v[6:9], off sc1
	s_nop 1
	v_cvt_pk_bf16_f32 v6, v15, v13
	v_ashrrev_i32_e32 v13, 31, v12
	v_lshlrev_b64 v[12:13], 11, v[12:13]
	v_cvt_pk_bf16_f32 v7, v17, v35
	v_cvt_pk_bf16_f32 v8, v37, v39
	v_cvt_pk_bf16_f32 v9, v43, v45
	v_lshl_add_u64 v[10:11], v[10:11], 0, v[12:13]
	global_store_dwordx4 v[10:11], v[6:9], off sc1
	s_waitcnt lgkmcnt(0)
	s_cbranch_scc1 .LBB0_588

.LBB0_591:
	global_load_dwordx4 v[2:5], v[36:37], off offset:-2048
	s_add_i32 s29, s29, s72
	s_cmpk_lt_i32 s29, 0x200
	s_waitcnt vmcnt(0)
	v_pk_mul_f32 v[6:7], v[4:5], v[4:5]
	v_pk_mul_f32 v[8:9], v[2:3], v[2:3]
	s_nop 0
	v_pk_mov_b32 v[10:11], v[8:9], v[6:7] op_sel:[1,0]
	v_mov_b32_e32 v9, v7
	v_pk_add_f32 v[48:49], v[10:11], v[8:9]
	global_load_dwordx4 v[10:13], v[36:37], off offset:-1024
	v_pk_add_f32 v[48:49], v[48:49], v[48:49] op_sel:[0,1] op_sel_hi:[1,0]
	s_waitcnt vmcnt(0)
	v_pk_mul_f32 v[6:7], v[12:13], v[12:13]
	v_pk_mul_f32 v[8:9], v[10:11], v[10:11]
	s_nop 0
	v_pk_mov_b32 v[14:15], v[8:9], v[6:7] op_sel:[1,0]
	v_mov_b32_e32 v9, v7
	v_pk_add_f32 v[50:51], v[14:15], v[8:9]
	global_load_dwordx4 v[14:17], v[36:37], off
	global_load_dwordx4 v[6:9], v[36:37], off offset:1024
	v_pk_add_f32 v[50:51], v[50:51], v[50:51] op_sel:[0,1] op_sel_hi:[1,0]
	v_lshl_add_u64 v[36:37], v[36:37], 0, s[76:77]
	s_waitcnt vmcnt(0)
	v_mul_f32_e32 v0, v6, v6
	v_mul_f32_e32 v52, v7, v7
	v_mov_b32_e32 v49, v0
	v_mov_b32_e32 v51, v52
	v_mul_f32_e32 v0, v15, v15
	v_mul_f32_e32 v53, v8, v8
	v_pk_add_f32 v[48:49], v[48:49], v[50:51]
	v_pk_fma_f32 v[50:51], v[14:15], v[14:15], v[0:1] op_sel_hi:[1,1,0]
	v_mul_f32_e32 v0, v17, v17
	v_mul_f32_e32 v54, v9, v9
	v_mov_b32_e32 v51, v53
	v_pk_fma_f32 v[52:53], v[16:17], v[16:17], v[0:1] op_sel_hi:[1,1,0]
	s_nop 0
	v_mov_b32_e32 v53, v54
	v_pk_add_f32 v[50:51], v[50:51], v[52:53]
	s_nop 0
	v_pk_add_f32 v[48:49], v[48:49], v[50:51]
	s_nop 0
	v_add_f32_e32 v0, v48, v49
	ds_bpermute_b32 v48, v42, v0
	s_waitcnt lgkmcnt(0)
	v_add_f32_e32 v0, v0, v48
	ds_bpermute_b32 v48, v43, v0
	s_waitcnt lgkmcnt(0)
	v_add_f32_e32 v0, v0, v48
	ds_bpermute_b32 v48, v44, v0
	s_waitcnt lgkmcnt(0)
	v_add_f32_e32 v0, v0, v48
	ds_bpermute_b32 v48, v45, v0
	s_waitcnt lgkmcnt(0)
	v_add_f32_e32 v0, v0, v48
	ds_bpermute_b32 v48, v46, v0
	s_waitcnt lgkmcnt(0)
	v_add_f32_e32 v0, v0, v48
	ds_bpermute_b32 v48, v47, v0
	s_waitcnt lgkmcnt(0)
	v_add_f32_e32 v0, v0, v48
	v_fmamk_f32 v0, v0, 0x3a800000, v196
	v_cmp_gt_f32_e32 vcc, s96, v0
	v_mul_f32_e32 v48, 0x4b800000, v0
	s_nop 0
	v_cndmask_b32_e32 v0, v0, v48, vcc
	v_rsq_f32_e32 v0, v0
	s_nop 0
	v_mul_f32_e32 v48, 0x45800000, v0
	v_cndmask_b32_e32 v0, v0, v48, vcc
	global_load_dwordx4 v[48:51], v[34:35], off
	v_pk_mul_f32 v[2:3], v[2:3], v[0:1] op_sel_hi:[1,0]
	v_pk_mul_f32 v[4:5], v[4:5], v[0:1] op_sel_hi:[1,0]
	v_pk_mul_f32 v[10:11], v[10:11], v[0:1] op_sel_hi:[1,0]
	v_pk_mul_f32 v[6:7], v[6:7], v[0:1] op_sel_hi:[1,0]
	s_waitcnt vmcnt(0)
	v_pk_mul_f32 v[2:3], v[48:49], v[2:3]
	v_pk_mul_f32 v[4:5], v[50:51], v[4:5]
	v_cvt_pk_bf16_f32 v2, v2, v3
	v_cvt_pk_bf16_f32 v3, v4, v5
	global_store_dwordx2 v[38:39], v[2:3], off offset:-1024 sc1
	global_load_dwordx4 v[2:5], v[34:35], off offset:1024
	s_waitcnt vmcnt(0)
	v_pk_mul_f32 v[2:3], v[2:3], v[10:11]
	v_pk_mul_f32 v[10:11], v[12:13], v[0:1] op_sel_hi:[1,0]
	v_cvt_pk_bf16_f32 v2, v2, v3
	v_pk_mul_f32 v[4:5], v[4:5], v[10:11]
	v_pk_mul_f32 v[10:11], v[14:15], v[0:1] op_sel_hi:[1,0]
	v_cvt_pk_bf16_f32 v3, v4, v5
	global_store_dwordx2 v[38:39], v[2:3], off offset:-512 sc1
	global_load_dwordx4 v[2:5], v[34:35], off offset:2048
	s_waitcnt vmcnt(0)
	v_pk_mul_f32 v[2:3], v[2:3], v[10:11]
	v_pk_mul_f32 v[10:11], v[16:17], v[0:1] op_sel_hi:[1,0]
	v_cvt_pk_bf16_f32 v2, v2, v3
	v_pk_mul_f32 v[4:5], v[4:5], v[10:11]
	s_nop 0
	v_cvt_pk_bf16_f32 v3, v4, v5
	global_store_dwordx2 v[38:39], v[2:3], off sc1
	global_load_dwordx4 v[2:5], v[34:35], off offset:3072
	s_waitcnt vmcnt(0)
	v_pk_mul_f32 v[2:3], v[2:3], v[6:7]
	v_pk_mul_f32 v[6:7], v[8:9], v[0:1] op_sel_hi:[1,0]
	v_cvt_pk_bf16_f32 v2, v2, v3
	v_pk_mul_f32 v[4:5], v[4:5], v[6:7]
	s_nop 0
	v_cvt_pk_bf16_f32 v3, v4, v5
	global_store_dwordx2 v[38:39], v[2:3], off offset:512 sc1
	v_lshl_add_u64 v[38:39], v[38:39], 0, s[78:79]
	s_cbranch_scc1 .LBB0_591
	s_branch .LBB0_579

.LBB0_622:
	v_or_b32_e32 v110, 8, v102
	v_or_b32_e32 v108, 16, v102
	s_andn2_b64 vcc, exec, s[46:47]
	v_or_b32_e32 v106, 24, v102
	s_cbranch_vccnz .LBB0_626
	s_and_b64 vcc, exec, s[36:37]
	s_cbranch_vccnz .LBB0_625
	v_and_b32_e32 v0, 7, v235
	v_lshlrev_b32_e32 v112, 4, v0
	v_add3_u32 v67, s34, v112, v71
	s_waitcnt vmcnt(7)
	v_pk_mul_f32 v[30:31], v[30:31], v[68:69] op_sel_hi:[1,0]
	ds_write2_b32 v67, v30, v31 offset1:1
	v_pk_mul_f32 v[30:31], v[32:33], v[68:69] op_sel_hi:[1,0]
	ds_write2_b32 v67, v30, v31 offset0:2 offset1:3
	v_add_u32_e32 v32, 0x420, v67
	s_waitcnt vmcnt(6)
	v_pk_mul_f32 v[30:31], v[38:39], v[66:67] op_sel_hi:[1,0]
	ds_write2_b32 v32, v30, v31 offset1:1
	v_add_u32_e32 v32, 0x428, v67
	v_pk_mul_f32 v[30:31], v[40:41], v[66:67] op_sel_hi:[1,0]
	ds_write2_b32 v32, v30, v31 offset1:1
	v_add_u32_e32 v32, 0x840, v67
	s_waitcnt vmcnt(5)
	v_pk_mul_f32 v[30:31], v[34:35], v[76:77] op_sel_hi:[1,0]
	ds_write2_b32 v32, v30, v31 offset1:1
	v_add_u32_e32 v32, 0x848, v67
	v_pk_mul_f32 v[30:31], v[36:37], v[76:77] op_sel_hi:[1,0]
	ds_write2_b32 v32, v30, v31 offset1:1
	v_add_u32_e32 v32, 0xc60, v67
	s_waitcnt vmcnt(4)
	v_pk_mul_f32 v[30:31], v[46:47], v[74:75] op_sel_hi:[1,0]
	ds_write2_b32 v32, v30, v31 offset1:1
	v_add_u32_e32 v32, 0xc68, v67
	v_pk_mul_f32 v[30:31], v[48:49], v[74:75] op_sel_hi:[1,0]
	ds_write2_b32 v32, v30, v31 offset1:1
	v_add_u32_e32 v32, 0x1080, v67
	s_waitcnt vmcnt(3)
	v_pk_mul_f32 v[30:31], v[42:43], v[84:85] op_sel_hi:[1,0]
	ds_write2_b32 v32, v30, v31 offset1:1
	v_add_u32_e32 v32, 0x1088, v67
	v_pk_mul_f32 v[30:31], v[44:45], v[84:85] op_sel_hi:[1,0]
	ds_write2_b32 v32, v30, v31 offset1:1
	v_add_u32_e32 v32, 0x14a0, v67
	s_waitcnt vmcnt(2)
	v_pk_mul_f32 v[30:31], v[54:55], v[82:83] op_sel_hi:[1,0]
	ds_write2_b32 v32, v30, v31 offset1:1
	v_add_u32_e32 v32, 0x14a8, v67
	v_pk_mul_f32 v[30:31], v[56:57], v[82:83] op_sel_hi:[1,0]
	ds_write2_b32 v32, v30, v31 offset1:1
	v_add_u32_e32 v32, 0x18c0, v67
	s_waitcnt vmcnt(1)
	v_pk_mul_f32 v[30:31], v[50:51], v[92:93] op_sel_hi:[1,0]
	ds_write2_b32 v32, v30, v31 offset1:1
	v_add_u32_e32 v32, 0x18c8, v67
	v_pk_mul_f32 v[30:31], v[52:53], v[92:93] op_sel_hi:[1,0]
	ds_write2_b32 v32, v30, v31 offset1:1
	v_add_u32_e32 v32, 0x1ce0, v67
	s_waitcnt vmcnt(0)
	v_pk_mul_f32 v[30:31], v[58:59], v[90:91] op_sel_hi:[1,0]
	ds_write2_b32 v32, v30, v31 offset1:1
	v_add_u32_e32 v32, 0x1ce8, v67
	v_pk_mul_f32 v[30:31], v[60:61], v[90:91] op_sel_hi:[1,0]
	ds_write2_b32 v32, v30, v31 offset1:1
	s_waitcnt lgkmcnt(0)
	v_mul_u32_u24_e32 v0, 0x420, v0
	v_add3_u32 v52, s34, v0, v73
	ds_read2_b32 v[34:35], v52 offset0:33 offset1:41
	ds_read2_b32 v[36:37], v52 offset1:8
	ds_read2_b32 v[38:39], v52 offset0:66 offset1:74
	ds_read2_b32 v[40:41], v52 offset0:99 offset1:107
	ds_read2_b32 v[42:43], v52 offset0:132 offset1:140
	ds_read2_b32 v[44:45], v52 offset0:165 offset1:173
	ds_read2_b32 v[46:47], v52 offset0:198 offset1:206
	ds_read2_b32 v[48:49], v52 offset0:231 offset1:239
	v_lshlrev_b32_e32 v0, 11, v102
	v_lshl_add_u64 v[50:51], s[16:17], 0, v[0:1]
	v_mov_b32_e32 v113, v1
	s_waitcnt lgkmcnt(0)
	v_cvt_pk_bf16_f32 v30, v36, v34
	v_cvt_pk_bf16_f32 v31, v38, v40
	v_cvt_pk_bf16_f32 v32, v42, v44
	v_cvt_pk_bf16_f32 v33, v46, v48
	v_lshl_add_u64 v[50:51], v[50:51], 0, v[112:113]
	global_store_dwordx4 v[50:51], v[30:33], off sc1
	v_lshlrev_b32_e32 v0, 11, v110
	s_nop 0
	v_cvt_pk_bf16_f32 v30, v37, v35
	v_cvt_pk_bf16_f32 v31, v39, v41
	v_cvt_pk_bf16_f32 v32, v43, v45
	v_cvt_pk_bf16_f32 v33, v47, v49
	ds_read2_b32 v[36:37], v52 offset0:49 offset1:57
	ds_read2_b32 v[38:39], v52 offset0:16 offset1:24
	ds_read2_b32 v[40:41], v52 offset0:82 offset1:90
	ds_read2_b32 v[42:43], v52 offset0:115 offset1:123
	ds_read2_b32 v[44:45], v52 offset0:148 offset1:156
	ds_read2_b32 v[46:47], v52 offset0:181 offset1:189
	ds_read2_b32 v[48:49], v52 offset0:214 offset1:222
	ds_read2_b32 v[50:51], v52 offset0:247 offset1:255
	v_lshl_add_u64 v[34:35], s[16:17], 0, v[0:1]
	v_lshl_add_u64 v[34:35], v[34:35], 0, v[112:113]
	v_lshlrev_b32_e32 v0, 11, v108
	global_store_dwordx4 v[34:35], v[30:33], off sc1
	v_lshl_add_u64 v[34:35], s[16:17], 0, v[0:1]
	v_lshl_add_u64 v[34:35], v[34:35], 0, v[112:113]
	s_waitcnt lgkmcnt(6)
	v_cvt_pk_bf16_f32 v30, v38, v36
	s_waitcnt lgkmcnt(4)
	v_cvt_pk_bf16_f32 v31, v40, v42
	s_waitcnt lgkmcnt(2)
	v_cvt_pk_bf16_f32 v32, v44, v46
	s_waitcnt lgkmcnt(0)
	v_cvt_pk_bf16_f32 v33, v48, v50
	v_lshlrev_b32_e32 v0, 11, v106
	global_store_dwordx4 v[34:35], v[30:33], off sc1
	v_lshl_add_u64 v[34:35], s[16:17], 0, v[0:1]
	v_lshl_add_u64 v[34:35], v[34:35], 0, v[112:113]
	v_cvt_pk_bf16_f32 v30, v39, v37
	v_cvt_pk_bf16_f32 v31, v41, v43
	v_cvt_pk_bf16_f32 v32, v45, v47
	v_cvt_pk_bf16_f32 v33, v49, v51
	global_store_dwordx4 v[34:35], v[30:33], off sc1
	s_waitcnt lgkmcnt(0)

.LBB0_641:
	s_andn2_b64 vcc, exec, s[38:39]
	s_cbranch_vccnz .LBB0_645
	s_cmp_eq_u32 s31, 0
	s_cbranch_scc1 .LBB0_644
	v_and_b32_e32 v0, 7, v235
	s_waitcnt vmcnt(7)
	v_lshlrev_b32_e32 v30, 4, v0
	v_add3_u32 v31, s34, v30, v71
	v_pk_mul_f32 v[2:3], v[2:3], v[72:73] op_sel_hi:[1,0]
	ds_write2_b32 v31, v2, v3 offset1:1
	v_pk_mul_f32 v[2:3], v[4:5], v[72:73] op_sel_hi:[1,0]
	ds_write2_b32 v31, v2, v3 offset0:2 offset1:3
	v_add_u32_e32 v4, 0x420, v31
	s_waitcnt vmcnt(6)
	v_pk_mul_f32 v[2:3], v[10:11], v[70:71] op_sel_hi:[1,0]
	ds_write2_b32 v4, v2, v3 offset1:1
	v_add_u32_e32 v4, 0x428, v31
	v_pk_mul_f32 v[2:3], v[12:13], v[70:71] op_sel_hi:[1,0]
	ds_write2_b32 v4, v2, v3 offset1:1
	v_add_u32_e32 v4, 0x840, v31
	s_waitcnt vmcnt(5)
	v_pk_mul_f32 v[2:3], v[6:7], v[80:81] op_sel_hi:[1,0]
	ds_write2_b32 v4, v2, v3 offset1:1
	v_add_u32_e32 v4, 0x848, v31
	v_pk_mul_f32 v[2:3], v[8:9], v[80:81] op_sel_hi:[1,0]
	ds_write2_b32 v4, v2, v3 offset1:1
	v_add_u32_e32 v4, 0xc60, v31
	s_waitcnt vmcnt(4)
	v_pk_mul_f32 v[2:3], v[18:19], v[78:79] op_sel_hi:[1,0]
	ds_write2_b32 v4, v2, v3 offset1:1
	v_add_u32_e32 v4, 0xc68, v31
	v_pk_mul_f32 v[2:3], v[20:21], v[78:79] op_sel_hi:[1,0]
	ds_write2_b32 v4, v2, v3 offset1:1
	v_add_u32_e32 v4, 0x1080, v31
	s_waitcnt vmcnt(3)
	v_pk_mul_f32 v[2:3], v[14:15], v[88:89] op_sel_hi:[1,0]
	ds_write2_b32 v4, v2, v3 offset1:1
	v_add_u32_e32 v4, 0x1088, v31
	v_pk_mul_f32 v[2:3], v[16:17], v[88:89] op_sel_hi:[1,0]
	ds_write2_b32 v4, v2, v3 offset1:1
	v_add_u32_e32 v4, 0x14a0, v31
	s_waitcnt vmcnt(2)
	v_pk_mul_f32 v[2:3], v[26:27], v[86:87] op_sel_hi:[1,0]
	ds_write2_b32 v4, v2, v3 offset1:1
	v_add_u32_e32 v4, 0x14a8, v31
	v_pk_mul_f32 v[2:3], v[28:29], v[86:87] op_sel_hi:[1,0]
	ds_write2_b32 v4, v2, v3 offset1:1
	v_add_u32_e32 v4, 0x18c0, v31
	s_waitcnt vmcnt(1)
	v_pk_mul_f32 v[2:3], v[22:23], v[96:97] op_sel_hi:[1,0]
	ds_write2_b32 v4, v2, v3 offset1:1
	v_add_u32_e32 v4, 0x18c8, v31
	v_pk_mul_f32 v[2:3], v[24:25], v[96:97] op_sel_hi:[1,0]
	ds_write2_b32 v4, v2, v3 offset1:1
	v_add_u32_e32 v4, 0x1ce0, v31
	s_waitcnt vmcnt(0)
	v_pk_mul_f32 v[2:3], v[62:63], v[94:95] op_sel_hi:[1,0]
	ds_write2_b32 v4, v2, v3 offset1:1
	v_add_u32_e32 v4, 0x1ce8, v31
	v_pk_mul_f32 v[2:3], v[64:65], v[94:95] op_sel_hi:[1,0]
	ds_write2_b32 v4, v2, v3 offset1:1
	s_waitcnt lgkmcnt(0)
	v_mul_u32_u24_e32 v0, 0x420, v0
	v_add3_u32 v24, s34, v0, v73
	ds_read2_b32 v[6:7], v24 offset0:33 offset1:41
	ds_read2_b32 v[8:9], v24 offset1:8
	ds_read2_b32 v[10:11], v24 offset0:66 offset1:74
	ds_read2_b32 v[12:13], v24 offset0:99 offset1:107
	ds_read2_b32 v[14:15], v24 offset0:132 offset1:140
	ds_read2_b32 v[16:17], v24 offset0:165 offset1:173
	ds_read2_b32 v[18:19], v24 offset0:198 offset1:206
	ds_read2_b32 v[20:21], v24 offset0:231 offset1:239
	v_lshlrev_b32_e32 v0, 11, v102
	v_lshl_add_u64 v[22:23], s[14:15], 0, v[0:1]
	v_mov_b32_e32 v31, v1
	s_waitcnt lgkmcnt(0)
	v_cvt_pk_bf16_f32 v2, v8, v6
	v_cvt_pk_bf16_f32 v3, v10, v12
	v_cvt_pk_bf16_f32 v4, v14, v16
	v_cvt_pk_bf16_f32 v5, v18, v20
	v_lshl_add_u64 v[22:23], v[22:23], 0, v[30:31]
	global_store_dwordx4 v[22:23], v[2:5], off sc1
	v_lshlrev_b32_e32 v0, 11, v110
	s_nop 0
	v_cvt_pk_bf16_f32 v2, v9, v7
	v_cvt_pk_bf16_f32 v3, v11, v13
	v_cvt_pk_bf16_f32 v4, v15, v17
	v_cvt_pk_bf16_f32 v5, v19, v21
	ds_read2_b32 v[8:9], v24 offset0:49 offset1:57
	ds_read2_b32 v[10:11], v24 offset0:16 offset1:24
	ds_read2_b32 v[12:13], v24 offset0:82 offset1:90
	ds_read2_b32 v[14:15], v24 offset0:115 offset1:123
	ds_read2_b32 v[16:17], v24 offset0:148 offset1:156
	ds_read2_b32 v[18:19], v24 offset0:181 offset1:189
	ds_read2_b32 v[20:21], v24 offset0:214 offset1:222
	ds_read2_b32 v[22:23], v24 offset0:247 offset1:255
	v_lshl_add_u64 v[6:7], s[14:15], 0, v[0:1]
	v_lshl_add_u64 v[6:7], v[6:7], 0, v[30:31]
	v_lshlrev_b32_e32 v0, 11, v108
	global_store_dwordx4 v[6:7], v[2:5], off sc1
	v_lshl_add_u64 v[6:7], s[14:15], 0, v[0:1]
	v_lshl_add_u64 v[6:7], v[6:7], 0, v[30:31]
	s_waitcnt lgkmcnt(6)
	v_cvt_pk_bf16_f32 v2, v10, v8
	s_waitcnt lgkmcnt(4)
	v_cvt_pk_bf16_f32 v3, v12, v14
	s_waitcnt lgkmcnt(2)
	v_cvt_pk_bf16_f32 v4, v16, v18
	s_waitcnt lgkmcnt(0)
	v_cvt_pk_bf16_f32 v5, v20, v22
	v_lshlrev_b32_e32 v0, 11, v106
	global_store_dwordx4 v[6:7], v[2:5], off sc1
	v_lshl_add_u64 v[6:7], s[14:15], 0, v[0:1]
	v_lshl_add_u64 v[6:7], v[6:7], 0, v[30:31]
	v_cvt_pk_bf16_f32 v2, v11, v9
	v_cvt_pk_bf16_f32 v3, v13, v15
	v_cvt_pk_bf16_f32 v4, v17, v19
	v_cvt_pk_bf16_f32 v5, v21, v23
	global_store_dwordx4 v[6:7], v[2:5], off sc1
	s_waitcnt lgkmcnt(0)

.LBB0_660:
	s_andn2_b64 vcc, exec, s[38:39]
	s_cbranch_vccnz .LBB0_664
	s_cmp_eq_u32 s31, 0
	s_cbranch_scc1 .LBB0_663
	v_and_b32_e32 v0, 7, v235
	s_waitcnt vmcnt(0)
	v_lshlrev_b32_e32 v62, 4, v0
	v_add3_u32 v63, s34, v62, v71
	v_pk_mul_f32 v[34:35], v[34:35], v[76:77] op_sel_hi:[1,0]
	ds_write2_b32 v63, v34, v35 offset1:1
	v_pk_mul_f32 v[34:35], v[36:37], v[76:77] op_sel_hi:[1,0]
	ds_write2_b32 v63, v34, v35 offset0:2 offset1:3
	v_add_u32_e32 v36, 0x420, v63
	v_pk_mul_f32 v[34:35], v[42:43], v[74:75] op_sel_hi:[1,0]
	ds_write2_b32 v36, v34, v35 offset1:1
	v_add_u32_e32 v36, 0x428, v63
	v_pk_mul_f32 v[34:35], v[44:45], v[74:75] op_sel_hi:[1,0]
	ds_write2_b32 v36, v34, v35 offset1:1
	v_add_u32_e32 v36, 0x840, v63
	v_pk_mul_f32 v[34:35], v[38:39], v[84:85] op_sel_hi:[1,0]
	ds_write2_b32 v36, v34, v35 offset1:1
	v_add_u32_e32 v36, 0x848, v63
	v_pk_mul_f32 v[34:35], v[40:41], v[84:85] op_sel_hi:[1,0]
	ds_write2_b32 v36, v34, v35 offset1:1
	v_add_u32_e32 v36, 0xc60, v63
	v_pk_mul_f32 v[34:35], v[50:51], v[82:83] op_sel_hi:[1,0]
	ds_write2_b32 v36, v34, v35 offset1:1
	v_add_u32_e32 v36, 0xc68, v63
	v_pk_mul_f32 v[34:35], v[52:53], v[82:83] op_sel_hi:[1,0]
	ds_write2_b32 v36, v34, v35 offset1:1
	v_add_u32_e32 v36, 0x1080, v63
	v_pk_mul_f32 v[34:35], v[46:47], v[92:93] op_sel_hi:[1,0]
	ds_write2_b32 v36, v34, v35 offset1:1
	v_add_u32_e32 v36, 0x1088, v63
	v_pk_mul_f32 v[34:35], v[48:49], v[92:93] op_sel_hi:[1,0]
	ds_write2_b32 v36, v34, v35 offset1:1
	v_add_u32_e32 v36, 0x14a0, v63
	v_pk_mul_f32 v[34:35], v[58:59], v[90:91] op_sel_hi:[1,0]
	ds_write2_b32 v36, v34, v35 offset1:1
	v_add_u32_e32 v36, 0x14a8, v63
	v_pk_mul_f32 v[34:35], v[60:61], v[90:91] op_sel_hi:[1,0]
	ds_write2_b32 v36, v34, v35 offset1:1
	v_add_u32_e32 v36, 0x18c0, v63
	v_pk_mul_f32 v[34:35], v[54:55], v[114:115] op_sel_hi:[1,0]
	ds_write2_b32 v36, v34, v35 offset1:1
	v_add_u32_e32 v36, 0x18c8, v63
	v_pk_mul_f32 v[34:35], v[56:57], v[114:115] op_sel_hi:[1,0]
	ds_write2_b32 v36, v34, v35 offset1:1
	v_add_u32_e32 v36, 0x1ce0, v63
	v_pk_mul_f32 v[34:35], v[66:67], v[112:113] op_sel_hi:[1,0]
	ds_write2_b32 v36, v34, v35 offset1:1
	v_add_u32_e32 v36, 0x1ce8, v63
	v_pk_mul_f32 v[34:35], v[68:69], v[112:113] op_sel_hi:[1,0]
	ds_write2_b32 v36, v34, v35 offset1:1
	s_waitcnt lgkmcnt(0)
	v_mul_u32_u24_e32 v0, 0x420, v0
	v_add3_u32 v56, s34, v0, v73
	ds_read2_b32 v[38:39], v56 offset0:33 offset1:41
	ds_read2_b32 v[40:41], v56 offset1:8
	ds_read2_b32 v[42:43], v56 offset0:66 offset1:74
	ds_read2_b32 v[44:45], v56 offset0:99 offset1:107
	ds_read2_b32 v[46:47], v56 offset0:132 offset1:140
	ds_read2_b32 v[48:49], v56 offset0:165 offset1:173
	ds_read2_b32 v[50:51], v56 offset0:198 offset1:206
	ds_read2_b32 v[52:53], v56 offset0:231 offset1:239
	v_lshlrev_b32_e32 v0, 11, v102
	v_lshl_add_u64 v[54:55], s[16:17], 0, v[0:1]
	v_mov_b32_e32 v63, v1
	s_waitcnt lgkmcnt(0)
	v_cvt_pk_bf16_f32 v34, v40, v38
	v_cvt_pk_bf16_f32 v35, v42, v44
	v_cvt_pk_bf16_f32 v36, v46, v48
	v_cvt_pk_bf16_f32 v37, v50, v52
	v_lshl_add_u64 v[54:55], v[54:55], 0, v[62:63]
	global_store_dwordx4 v[54:55], v[34:37], off sc1
	v_lshlrev_b32_e32 v0, 11, v110
	s_nop 0
	v_cvt_pk_bf16_f32 v34, v41, v39
	v_cvt_pk_bf16_f32 v35, v43, v45
	v_cvt_pk_bf16_f32 v36, v47, v49
	v_cvt_pk_bf16_f32 v37, v51, v53
	ds_read2_b32 v[40:41], v56 offset0:49 offset1:57
	ds_read2_b32 v[42:43], v56 offset0:16 offset1:24
	ds_read2_b32 v[44:45], v56 offset0:82 offset1:90
	ds_read2_b32 v[46:47], v56 offset0:115 offset1:123
	ds_read2_b32 v[48:49], v56 offset0:148 offset1:156
	ds_read2_b32 v[50:51], v56 offset0:181 offset1:189
	ds_read2_b32 v[52:53], v56 offset0:214 offset1:222
	ds_read2_b32 v[54:55], v56 offset0:247 offset1:255
	v_lshl_add_u64 v[38:39], s[16:17], 0, v[0:1]
	v_lshl_add_u64 v[38:39], v[38:39], 0, v[62:63]
	v_lshlrev_b32_e32 v0, 11, v108
	global_store_dwordx4 v[38:39], v[34:37], off sc1
	v_lshl_add_u64 v[38:39], s[16:17], 0, v[0:1]
	v_lshl_add_u64 v[38:39], v[38:39], 0, v[62:63]
	s_waitcnt lgkmcnt(6)
	v_cvt_pk_bf16_f32 v34, v42, v40
	s_waitcnt lgkmcnt(4)
	v_cvt_pk_bf16_f32 v35, v44, v46
	s_waitcnt lgkmcnt(2)
	v_cvt_pk_bf16_f32 v36, v48, v50
	s_waitcnt lgkmcnt(0)
	v_cvt_pk_bf16_f32 v37, v52, v54
	v_lshlrev_b32_e32 v0, 11, v106
	global_store_dwordx4 v[38:39], v[34:37], off sc1
	v_lshl_add_u64 v[38:39], s[16:17], 0, v[0:1]
	v_lshl_add_u64 v[38:39], v[38:39], 0, v[62:63]
	v_cvt_pk_bf16_f32 v34, v43, v41
	v_cvt_pk_bf16_f32 v35, v45, v47
	v_cvt_pk_bf16_f32 v36, v49, v51
	v_cvt_pk_bf16_f32 v37, v53, v55
	global_store_dwordx4 v[38:39], v[34:37], off sc1
	s_waitcnt lgkmcnt(0)

.LBB0_682:
	s_andn2_b64 vcc, exec, s[50:51]
	s_cbranch_vccnz .LBB0_686
	s_cmp_eq_u32 s31, 0
	s_cbranch_scc1 .LBB0_685
	s_waitcnt vmcnt(6)
	v_pk_mul_f32 v[2:3], v[126:127], v[2:3] op_sel_hi:[0,1]
	ds_write2_b32 v103, v2, v3 offset1:1
	v_pk_mul_f32 v[2:3], v[126:127], v[4:5] op_sel_hi:[0,1]
	ds_write2_b32 v103, v2, v3 offset0:2 offset1:3
	s_waitcnt vmcnt(5)
	v_pk_mul_f32 v[2:3], v[120:121], v[14:15] op_sel_hi:[0,1]
	v_add_u32_e32 v0, 0x420, v103
	ds_write2_b32 v0, v2, v3 offset1:1
	v_pk_mul_f32 v[2:3], v[120:121], v[16:17] op_sel_hi:[0,1]
	v_add_u32_e32 v0, 0x428, v103
	ds_write2_b32 v0, v2, v3 offset1:1
	s_waitcnt vmcnt(3)
	v_pk_mul_f32 v[2:3], v[132:133], v[6:7] op_sel_hi:[0,1]
	v_add_u32_e32 v0, 0x840, v103
	ds_write2_b32 v0, v2, v3 offset1:1
	v_pk_mul_f32 v[2:3], v[132:133], v[8:9] op_sel_hi:[0,1]
	v_add_u32_e32 v0, 0x848, v103
	ds_write2_b32 v0, v2, v3 offset1:1
	s_waitcnt vmcnt(5)
	v_pk_mul_f32 v[2:3], v[128:129], v[22:23] op_sel_hi:[0,1]
	v_add_u32_e32 v0, 0xc60, v103
	ds_write2_b32 v0, v2, v3 offset1:1
	v_pk_mul_f32 v[2:3], v[128:129], v[24:25] op_sel_hi:[0,1]
	v_add_u32_e32 v0, 0xc68, v103
	ds_write2_b32 v0, v2, v3 offset1:1
	s_waitcnt vmcnt(3)
	v_pk_mul_f32 v[2:3], v[136:137], v[10:11] op_sel_hi:[0,1]
	v_add_u32_e32 v0, 0x1080, v103
	ds_write2_b32 v0, v2, v3 offset1:1
	v_pk_mul_f32 v[2:3], v[136:137], v[12:13] op_sel_hi:[0,1]
	v_add_u32_e32 v0, 0x1088, v103
	ds_write2_b32 v0, v2, v3 offset1:1
	v_pk_mul_f32 v[2:3], v[130:131], v[26:27] op_sel_hi:[0,1]
	v_add_u32_e32 v0, 0x14a0, v103
	ds_write2_b32 v0, v2, v3 offset1:1
	v_pk_mul_f32 v[2:3], v[130:131], v[28:29] op_sel_hi:[0,1]
	v_add_u32_e32 v0, 0x14a8, v103
	ds_write2_b32 v0, v2, v3 offset1:1
	s_waitcnt vmcnt(2)
	v_pk_mul_f32 v[2:3], v[138:139], v[18:19] op_sel_hi:[0,1]
	v_add_u32_e32 v0, 0x18c0, v103
	ds_write2_b32 v0, v2, v3 offset1:1
	v_pk_mul_f32 v[2:3], v[138:139], v[20:21] op_sel_hi:[0,1]
	v_add_u32_e32 v0, 0x18c8, v103
	ds_write2_b32 v0, v2, v3 offset1:1
	s_waitcnt vmcnt(0)
	v_pk_mul_f32 v[2:3], v[134:135], v[30:31] op_sel_hi:[0,1]
	v_add_u32_e32 v0, 0x1ce0, v103
	ds_write2_b32 v0, v2, v3 offset1:1
	v_pk_mul_f32 v[2:3], v[134:135], v[32:33] op_sel_hi:[0,1]
	v_add_u32_e32 v0, 0x1ce8, v103
	ds_write2_b32 v0, v2, v3 offset1:1
	s_waitcnt lgkmcnt(0)
	ds_read2_b32 v[6:7], v99 offset0:33 offset1:41
	ds_read2_b32 v[8:9], v99 offset1:8
	ds_read2_b32 v[10:11], v99 offset0:66 offset1:74
	ds_read2_b32 v[12:13], v99 offset0:99 offset1:107
	ds_read2_b32 v[14:15], v99 offset0:132 offset1:140
	ds_read2_b32 v[16:17], v99 offset0:165 offset1:173
	ds_read2_b32 v[18:19], v99 offset0:198 offset1:206
	ds_read2_b32 v[20:21], v99 offset0:231 offset1:239
	v_lshl_add_u64 v[22:23], s[14:15], 0, v[124:125]
	v_lshlrev_b32_e32 v0, 1, v112
	s_waitcnt lgkmcnt(6)
	v_cvt_pk_bf16_f32 v2, v8, v6
	s_waitcnt lgkmcnt(4)
	v_cvt_pk_bf16_f32 v3, v10, v12
	s_waitcnt lgkmcnt(2)
	v_cvt_pk_bf16_f32 v4, v14, v16
	s_waitcnt lgkmcnt(0)
	v_cvt_pk_bf16_f32 v5, v18, v20
	v_lshl_add_u64 v[22:23], v[22:23], 0, v[0:1]
	global_store_dwordx4 v[22:23], v[2:5], off sc1
	s_nop 1
	v_cvt_pk_bf16_f32 v2, v9, v7
	v_cvt_pk_bf16_f32 v3, v11, v13
	v_cvt_pk_bf16_f32 v4, v15, v17
	v_cvt_pk_bf16_f32 v5, v19, v21
	ds_read2_b32 v[8:9], v99 offset0:49 offset1:57
	ds_read2_b32 v[10:11], v99 offset0:16 offset1:24
	ds_read2_b32 v[12:13], v99 offset0:82 offset1:90
	ds_read2_b32 v[14:15], v99 offset0:115 offset1:123
	ds_read2_b32 v[16:17], v99 offset0:148 offset1:156
	ds_read2_b32 v[18:19], v99 offset0:181 offset1:189
	ds_read2_b32 v[20:21], v99 offset0:214 offset1:222
	ds_read2_b32 v[22:23], v99 offset0:247 offset1:255
	v_lshl_add_u64 v[6:7], s[14:15], 0, v[122:123]
	v_lshl_add_u64 v[6:7], v[6:7], 0, v[0:1]
	global_store_dwordx4 v[6:7], v[2:5], off sc1
	v_lshl_add_u64 v[6:7], s[14:15], 0, v[118:119]
	v_lshl_add_u64 v[6:7], v[6:7], 0, v[0:1]
	s_waitcnt lgkmcnt(6)
	v_cvt_pk_bf16_f32 v2, v10, v8
	s_waitcnt lgkmcnt(4)
	v_cvt_pk_bf16_f32 v3, v12, v14
	s_waitcnt lgkmcnt(2)
	v_cvt_pk_bf16_f32 v4, v16, v18
	s_waitcnt lgkmcnt(0)
	v_cvt_pk_bf16_f32 v5, v20, v22
	global_store_dwordx4 v[6:7], v[2:5], off sc1
	v_lshl_add_u64 v[6:7], s[14:15], 0, v[116:117]
	v_lshl_add_u64 v[6:7], v[6:7], 0, v[0:1]
	v_cvt_pk_bf16_f32 v2, v11, v9
	v_cvt_pk_bf16_f32 v3, v13, v15
	v_cvt_pk_bf16_f32 v4, v17, v19
	v_cvt_pk_bf16_f32 v5, v21, v23
	global_store_dwordx4 v[6:7], v[2:5], off sc1
	s_waitcnt lgkmcnt(0)

.LBB0_700:
	s_andn2_b64 vcc, exec, s[50:51]
	s_cbranch_vccnz .LBB0_667
	s_cmp_eq_u32 s31, 0
	s_cbranch_scc1 .LBB0_666
	s_waitcnt vmcnt(6)
	v_pk_mul_f32 v[2:3], v[2:3], v[126:127] op_sel_hi:[1,0]
	ds_write2_b32 v103, v2, v3 offset1:1
	v_pk_mul_f32 v[2:3], v[4:5], v[126:127] op_sel_hi:[1,0]
	ds_write2_b32 v103, v2, v3 offset0:2 offset1:3
	s_waitcnt vmcnt(5)
	v_pk_mul_f32 v[2:3], v[14:15], v[120:121] op_sel_hi:[1,0]
	v_add_u32_e32 v0, 0x420, v103
	ds_write2_b32 v0, v2, v3 offset1:1
	v_pk_mul_f32 v[2:3], v[16:17], v[120:121] op_sel_hi:[1,0]
	v_add_u32_e32 v0, 0x428, v103
	ds_write2_b32 v0, v2, v3 offset1:1
	s_waitcnt vmcnt(3)
	v_pk_mul_f32 v[2:3], v[6:7], v[132:133] op_sel_hi:[1,0]
	v_add_u32_e32 v0, 0x840, v103
	ds_write2_b32 v0, v2, v3 offset1:1
	v_pk_mul_f32 v[2:3], v[8:9], v[132:133] op_sel_hi:[1,0]
	v_add_u32_e32 v0, 0x848, v103
	ds_write2_b32 v0, v2, v3 offset1:1
	v_pk_mul_f32 v[2:3], v[22:23], v[128:129] op_sel_hi:[1,0]
	v_add_u32_e32 v0, 0xc60, v103
	ds_write2_b32 v0, v2, v3 offset1:1
	v_pk_mul_f32 v[2:3], v[24:25], v[128:129] op_sel_hi:[1,0]
	v_add_u32_e32 v0, 0xc68, v103
	ds_write2_b32 v0, v2, v3 offset1:1
	v_pk_mul_f32 v[2:3], v[10:11], v[136:137] op_sel_hi:[1,0]
	v_add_u32_e32 v0, 0x1080, v103
	ds_write2_b32 v0, v2, v3 offset1:1
	v_pk_mul_f32 v[2:3], v[12:13], v[136:137] op_sel_hi:[1,0]
	v_add_u32_e32 v0, 0x1088, v103
	ds_write2_b32 v0, v2, v3 offset1:1
	v_pk_mul_f32 v[2:3], v[26:27], v[130:131] op_sel_hi:[1,0]
	v_add_u32_e32 v0, 0x14a0, v103
	ds_write2_b32 v0, v2, v3 offset1:1
	v_pk_mul_f32 v[2:3], v[28:29], v[130:131] op_sel_hi:[1,0]
	v_add_u32_e32 v0, 0x14a8, v103
	ds_write2_b32 v0, v2, v3 offset1:1
	s_waitcnt vmcnt(2)
	v_pk_mul_f32 v[2:3], v[18:19], v[138:139] op_sel_hi:[1,0]
	v_add_u32_e32 v0, 0x18c0, v103
	ds_write2_b32 v0, v2, v3 offset1:1
	v_pk_mul_f32 v[2:3], v[20:21], v[138:139] op_sel_hi:[1,0]
	v_add_u32_e32 v0, 0x18c8, v103
	ds_write2_b32 v0, v2, v3 offset1:1
	s_waitcnt vmcnt(0)
	v_pk_mul_f32 v[2:3], v[30:31], v[134:135] op_sel_hi:[1,0]
	v_add_u32_e32 v0, 0x1ce0, v103
	ds_write2_b32 v0, v2, v3 offset1:1
	v_pk_mul_f32 v[2:3], v[32:33], v[134:135] op_sel_hi:[1,0]
	v_add_u32_e32 v0, 0x1ce8, v103
	ds_write2_b32 v0, v2, v3 offset1:1
	s_waitcnt lgkmcnt(0)
	ds_read2_b32 v[6:7], v99 offset0:33 offset1:41
	ds_read2_b32 v[8:9], v99 offset1:8
	ds_read2_b32 v[10:11], v99 offset0:66 offset1:74
	ds_read2_b32 v[12:13], v99 offset0:99 offset1:107
	ds_read2_b32 v[14:15], v99 offset0:132 offset1:140
	ds_read2_b32 v[16:17], v99 offset0:165 offset1:173
	ds_read2_b32 v[18:19], v99 offset0:198 offset1:206
	ds_read2_b32 v[20:21], v99 offset0:231 offset1:239
	v_lshl_add_u64 v[22:23], s[14:15], 0, v[124:125]
	v_lshlrev_b32_e32 v0, 1, v112
	s_waitcnt lgkmcnt(6)
	v_cvt_pk_bf16_f32 v2, v8, v6
	s_waitcnt lgkmcnt(4)
	v_cvt_pk_bf16_f32 v3, v10, v12
	s_waitcnt lgkmcnt(2)
	v_cvt_pk_bf16_f32 v4, v14, v16
	s_waitcnt lgkmcnt(0)
	v_cvt_pk_bf16_f32 v5, v18, v20
	v_lshl_add_u64 v[22:23], v[22:23], 0, v[0:1]
	global_store_dwordx4 v[22:23], v[2:5], off sc1
	s_nop 1
	v_cvt_pk_bf16_f32 v2, v9, v7
	v_cvt_pk_bf16_f32 v3, v11, v13
	v_cvt_pk_bf16_f32 v4, v15, v17
	v_cvt_pk_bf16_f32 v5, v19, v21
	ds_read2_b32 v[8:9], v99 offset0:49 offset1:57
	ds_read2_b32 v[10:11], v99 offset0:16 offset1:24
	ds_read2_b32 v[12:13], v99 offset0:82 offset1:90
	ds_read2_b32 v[14:15], v99 offset0:115 offset1:123
	ds_read2_b32 v[16:17], v99 offset0:148 offset1:156
	ds_read2_b32 v[18:19], v99 offset0:181 offset1:189
	ds_read2_b32 v[20:21], v99 offset0:214 offset1:222
	ds_read2_b32 v[22:23], v99 offset0:247 offset1:255
	v_lshl_add_u64 v[6:7], s[14:15], 0, v[122:123]
	v_lshl_add_u64 v[6:7], v[6:7], 0, v[0:1]
	global_store_dwordx4 v[6:7], v[2:5], off sc1
	v_lshl_add_u64 v[6:7], s[14:15], 0, v[118:119]
	v_lshl_add_u64 v[6:7], v[6:7], 0, v[0:1]
	s_waitcnt lgkmcnt(6)
	v_cvt_pk_bf16_f32 v2, v10, v8
	s_waitcnt lgkmcnt(4)
	v_cvt_pk_bf16_f32 v3, v12, v14
	s_waitcnt lgkmcnt(2)
	v_cvt_pk_bf16_f32 v4, v16, v18
	s_waitcnt lgkmcnt(0)
	v_cvt_pk_bf16_f32 v5, v20, v22
	global_store_dwordx4 v[6:7], v[2:5], off sc1
	v_lshl_add_u64 v[6:7], s[14:15], 0, v[116:117]
	v_lshl_add_u64 v[6:7], v[6:7], 0, v[0:1]
	v_cvt_pk_bf16_f32 v2, v11, v9
	v_cvt_pk_bf16_f32 v3, v13, v15
	v_cvt_pk_bf16_f32 v4, v17, v19
	v_cvt_pk_bf16_f32 v5, v21, v23
	global_store_dwordx4 v[6:7], v[2:5], off sc1
	s_waitcnt lgkmcnt(0)
	s_branch .LBB0_666

.LBB0_725:
	s_and_b64 vcc, exec, s[46:47]
	s_cbranch_vccz .LBB0_729
	s_cmp_eq_u32 s31, 0
	s_cbranch_scc1 .LBB0_728
	s_waitcnt vmcnt(6)
	v_pk_mul_f32 v[2:3], v[2:3], v[126:127] op_sel_hi:[1,0]
	ds_write2_b32 v103, v2, v3 offset1:1
	v_pk_mul_f32 v[2:3], v[4:5], v[126:127] op_sel_hi:[1,0]
	ds_write2_b32 v103, v2, v3 offset0:2 offset1:3
	s_waitcnt vmcnt(5)
	v_pk_mul_f32 v[2:3], v[14:15], v[120:121] op_sel_hi:[1,0]
	v_add_u32_e32 v0, 0x420, v103
	ds_write2_b32 v0, v2, v3 offset1:1
	v_pk_mul_f32 v[2:3], v[16:17], v[120:121] op_sel_hi:[1,0]
	v_add_u32_e32 v0, 0x428, v103
	ds_write2_b32 v0, v2, v3 offset1:1
	s_waitcnt vmcnt(3)
	v_pk_mul_f32 v[2:3], v[6:7], v[132:133] op_sel_hi:[1,0]
	v_add_u32_e32 v0, 0x840, v103
	ds_write2_b32 v0, v2, v3 offset1:1
	v_pk_mul_f32 v[2:3], v[8:9], v[132:133] op_sel_hi:[1,0]
	v_add_u32_e32 v0, 0x848, v103
	ds_write2_b32 v0, v2, v3 offset1:1
	v_pk_mul_f32 v[2:3], v[22:23], v[128:129] op_sel_hi:[1,0]
	v_add_u32_e32 v0, 0xc60, v103
	ds_write2_b32 v0, v2, v3 offset1:1
	v_pk_mul_f32 v[2:3], v[24:25], v[128:129] op_sel_hi:[1,0]
	v_add_u32_e32 v0, 0xc68, v103
	ds_write2_b32 v0, v2, v3 offset1:1
	v_pk_mul_f32 v[2:3], v[10:11], v[136:137] op_sel_hi:[1,0]
	v_add_u32_e32 v0, 0x1080, v103
	ds_write2_b32 v0, v2, v3 offset1:1
	v_pk_mul_f32 v[2:3], v[12:13], v[136:137] op_sel_hi:[1,0]
	v_add_u32_e32 v0, 0x1088, v103
	ds_write2_b32 v0, v2, v3 offset1:1
	v_pk_mul_f32 v[2:3], v[26:27], v[130:131] op_sel_hi:[1,0]
	v_add_u32_e32 v0, 0x14a0, v103
	ds_write2_b32 v0, v2, v3 offset1:1
	v_pk_mul_f32 v[2:3], v[28:29], v[130:131] op_sel_hi:[1,0]
	v_add_u32_e32 v0, 0x14a8, v103
	ds_write2_b32 v0, v2, v3 offset1:1
	s_waitcnt vmcnt(2)
	v_pk_mul_f32 v[2:3], v[18:19], v[138:139] op_sel_hi:[1,0]
	v_add_u32_e32 v0, 0x18c0, v103
	ds_write2_b32 v0, v2, v3 offset1:1
	v_pk_mul_f32 v[2:3], v[20:21], v[138:139] op_sel_hi:[1,0]
	v_add_u32_e32 v0, 0x18c8, v103
	ds_write2_b32 v0, v2, v3 offset1:1
	s_waitcnt vmcnt(0)
	v_pk_mul_f32 v[2:3], v[30:31], v[134:135] op_sel_hi:[1,0]
	v_add_u32_e32 v0, 0x1ce0, v103
	ds_write2_b32 v0, v2, v3 offset1:1
	v_pk_mul_f32 v[2:3], v[32:33], v[134:135] op_sel_hi:[1,0]
	v_add_u32_e32 v0, 0x1ce8, v103
	ds_write2_b32 v0, v2, v3 offset1:1
	s_waitcnt lgkmcnt(0)
	ds_read2_b32 v[6:7], v99 offset0:33 offset1:41
	ds_read2_b32 v[8:9], v99 offset1:8
	ds_read2_b32 v[10:11], v99 offset0:66 offset1:74
	ds_read2_b32 v[12:13], v99 offset0:99 offset1:107
	ds_read2_b32 v[14:15], v99 offset0:132 offset1:140
	ds_read2_b32 v[16:17], v99 offset0:165 offset1:173
	ds_read2_b32 v[18:19], v99 offset0:198 offset1:206
	ds_read2_b32 v[20:21], v99 offset0:231 offset1:239
	v_lshl_add_u64 v[22:23], s[14:15], 0, v[124:125]
	v_lshlrev_b32_e32 v0, 1, v112
	s_waitcnt lgkmcnt(6)
	v_cvt_pk_bf16_f32 v2, v8, v6
	s_waitcnt lgkmcnt(4)
	v_cvt_pk_bf16_f32 v3, v10, v12
	s_waitcnt lgkmcnt(2)
	v_cvt_pk_bf16_f32 v4, v14, v16
	s_waitcnt lgkmcnt(0)
	v_cvt_pk_bf16_f32 v5, v18, v20
	v_lshl_add_u64 v[22:23], v[22:23], 0, v[0:1]
	global_store_dwordx4 v[22:23], v[2:5], off sc1
	s_nop 1
	v_cvt_pk_bf16_f32 v2, v9, v7
	v_cvt_pk_bf16_f32 v3, v11, v13
	v_cvt_pk_bf16_f32 v4, v15, v17
	v_cvt_pk_bf16_f32 v5, v19, v21
	ds_read2_b32 v[8:9], v99 offset0:49 offset1:57
	ds_read2_b32 v[10:11], v99 offset0:16 offset1:24
	ds_read2_b32 v[12:13], v99 offset0:82 offset1:90
	ds_read2_b32 v[14:15], v99 offset0:115 offset1:123
	ds_read2_b32 v[16:17], v99 offset0:148 offset1:156
	ds_read2_b32 v[18:19], v99 offset0:181 offset1:189
	ds_read2_b32 v[20:21], v99 offset0:214 offset1:222
	ds_read2_b32 v[22:23], v99 offset0:247 offset1:255
	v_lshl_add_u64 v[6:7], s[14:15], 0, v[122:123]
	v_lshl_add_u64 v[6:7], v[6:7], 0, v[0:1]
	global_store_dwordx4 v[6:7], v[2:5], off sc1
	v_lshl_add_u64 v[6:7], s[14:15], 0, v[118:119]
	v_lshl_add_u64 v[6:7], v[6:7], 0, v[0:1]
	s_waitcnt lgkmcnt(6)
	v_cvt_pk_bf16_f32 v2, v10, v8
	s_waitcnt lgkmcnt(4)
	v_cvt_pk_bf16_f32 v3, v12, v14
	s_waitcnt lgkmcnt(2)
	v_cvt_pk_bf16_f32 v4, v16, v18
	s_waitcnt lgkmcnt(0)
	v_cvt_pk_bf16_f32 v5, v20, v22
	global_store_dwordx4 v[6:7], v[2:5], off sc1
	v_lshl_add_u64 v[6:7], s[14:15], 0, v[116:117]
	v_lshl_add_u64 v[6:7], v[6:7], 0, v[0:1]
	v_cvt_pk_bf16_f32 v2, v11, v9
	v_cvt_pk_bf16_f32 v3, v13, v15
	v_cvt_pk_bf16_f32 v4, v17, v19
	v_cvt_pk_bf16_f32 v5, v21, v23
	global_store_dwordx4 v[6:7], v[2:5], off sc1
	s_waitcnt lgkmcnt(0)

.LBB0_744:
	s_andn2_b64 vcc, exec, s[46:47]
	s_cbranch_vccnz .LBB0_748
	s_cmp_eq_u32 s31, 0
	s_cbranch_scc1 .LBB0_747
	s_waitcnt vmcnt(0)
	v_pk_mul_f32 v[2:3], v[62:63], v[140:141] op_sel_hi:[1,0]
	ds_write2_b32 v103, v2, v3 offset1:1
	v_pk_mul_f32 v[2:3], v[64:65], v[140:141] op_sel_hi:[1,0]
	ds_write2_b32 v103, v2, v3 offset0:2 offset1:3
	v_pk_mul_f32 v[2:3], v[74:75], v[142:143] op_sel_hi:[1,0]
	v_add_u32_e32 v0, 0x420, v103
	ds_write2_b32 v0, v2, v3 offset1:1
	v_pk_mul_f32 v[2:3], v[76:77], v[142:143] op_sel_hi:[1,0]
	v_add_u32_e32 v0, 0x428, v103
	ds_write2_b32 v0, v2, v3 offset1:1
	v_pk_mul_f32 v[2:3], v[70:71], v[146:147] op_sel_hi:[1,0]
	v_add_u32_e32 v0, 0x840, v103
	ds_write2_b32 v0, v2, v3 offset1:1
	v_pk_mul_f32 v[2:3], v[72:73], v[146:147] op_sel_hi:[1,0]
	v_add_u32_e32 v0, 0x848, v103
	ds_write2_b32 v0, v2, v3 offset1:1
	v_pk_mul_f32 v[2:3], v[82:83], v[144:145] op_sel_hi:[1,0]
	v_add_u32_e32 v0, 0xc60, v103
	ds_write2_b32 v0, v2, v3 offset1:1
	v_pk_mul_f32 v[2:3], v[84:85], v[144:145] op_sel_hi:[1,0]
	v_add_u32_e32 v0, 0xc68, v103
	ds_write2_b32 v0, v2, v3 offset1:1
	v_pk_mul_f32 v[2:3], v[78:79], v[150:151] op_sel_hi:[1,0]
	v_add_u32_e32 v0, 0x1080, v103
	ds_write2_b32 v0, v2, v3 offset1:1
	v_pk_mul_f32 v[2:3], v[80:81], v[150:151] op_sel_hi:[1,0]
	v_add_u32_e32 v0, 0x1088, v103
	ds_write2_b32 v0, v2, v3 offset1:1
	v_pk_mul_f32 v[2:3], v[90:91], v[148:149] op_sel_hi:[1,0]
	v_add_u32_e32 v0, 0x14a0, v103
	ds_write2_b32 v0, v2, v3 offset1:1
	v_pk_mul_f32 v[2:3], v[92:93], v[148:149] op_sel_hi:[1,0]
	v_add_u32_e32 v0, 0x14a8, v103
	ds_write2_b32 v0, v2, v3 offset1:1
	v_pk_mul_f32 v[2:3], v[86:87], v[154:155] op_sel_hi:[1,0]
	v_add_u32_e32 v0, 0x18c0, v103
	ds_write2_b32 v0, v2, v3 offset1:1
	v_pk_mul_f32 v[2:3], v[88:89], v[154:155] op_sel_hi:[1,0]
	v_add_u32_e32 v0, 0x18c8, v103
	ds_write2_b32 v0, v2, v3 offset1:1
	v_pk_mul_f32 v[2:3], v[94:95], v[152:153] op_sel_hi:[1,0]
	v_add_u32_e32 v0, 0x1ce0, v103
	ds_write2_b32 v0, v2, v3 offset1:1
	v_pk_mul_f32 v[2:3], v[96:97], v[152:153] op_sel_hi:[1,0]
	v_add_u32_e32 v0, 0x1ce8, v103
	ds_write2_b32 v0, v2, v3 offset1:1
	s_waitcnt lgkmcnt(0)
	ds_read2_b32 v[6:7], v99 offset0:33 offset1:41
	ds_read2_b32 v[8:9], v99 offset1:8
	ds_read2_b32 v[10:11], v99 offset0:66 offset1:74
	ds_read2_b32 v[12:13], v99 offset0:99 offset1:107
	ds_read2_b32 v[14:15], v99 offset0:132 offset1:140
	ds_read2_b32 v[16:17], v99 offset0:165 offset1:173
	ds_read2_b32 v[18:19], v99 offset0:198 offset1:206
	ds_read2_b32 v[20:21], v99 offset0:231 offset1:239
	v_lshl_add_u64 v[22:23], s[38:39], 0, v[124:125]
	v_lshlrev_b32_e32 v0, 1, v112
	s_waitcnt lgkmcnt(6)
	v_cvt_pk_bf16_f32 v2, v8, v6
	s_waitcnt lgkmcnt(4)
	v_cvt_pk_bf16_f32 v3, v10, v12
	s_waitcnt lgkmcnt(2)
	v_cvt_pk_bf16_f32 v4, v14, v16
	s_waitcnt lgkmcnt(0)
	v_cvt_pk_bf16_f32 v5, v18, v20
	v_lshl_add_u64 v[22:23], v[22:23], 0, v[0:1]
	global_store_dwordx4 v[22:23], v[2:5], off sc1
	s_nop 1
	v_cvt_pk_bf16_f32 v2, v9, v7
	v_cvt_pk_bf16_f32 v3, v11, v13
	v_cvt_pk_bf16_f32 v4, v15, v17
	v_cvt_pk_bf16_f32 v5, v19, v21
	ds_read2_b32 v[8:9], v99 offset0:49 offset1:57
	ds_read2_b32 v[10:11], v99 offset0:16 offset1:24
	ds_read2_b32 v[12:13], v99 offset0:82 offset1:90
	ds_read2_b32 v[14:15], v99 offset0:115 offset1:123
	ds_read2_b32 v[16:17], v99 offset0:148 offset1:156
	ds_read2_b32 v[18:19], v99 offset0:181 offset1:189
	ds_read2_b32 v[20:21], v99 offset0:214 offset1:222
	ds_read2_b32 v[22:23], v99 offset0:247 offset1:255
	v_lshl_add_u64 v[6:7], s[38:39], 0, v[122:123]
	v_lshl_add_u64 v[6:7], v[6:7], 0, v[0:1]
	global_store_dwordx4 v[6:7], v[2:5], off sc1
	v_lshl_add_u64 v[6:7], s[38:39], 0, v[118:119]
	v_lshl_add_u64 v[6:7], v[6:7], 0, v[0:1]
	s_waitcnt lgkmcnt(6)
	v_cvt_pk_bf16_f32 v2, v10, v8
	s_waitcnt lgkmcnt(4)
	v_cvt_pk_bf16_f32 v3, v12, v14
	s_waitcnt lgkmcnt(2)
	v_cvt_pk_bf16_f32 v4, v16, v18
	s_waitcnt lgkmcnt(0)
	v_cvt_pk_bf16_f32 v5, v20, v22
	global_store_dwordx4 v[6:7], v[2:5], off sc1
	v_lshl_add_u64 v[6:7], s[38:39], 0, v[116:117]
	v_lshl_add_u64 v[6:7], v[6:7], 0, v[0:1]
	v_cvt_pk_bf16_f32 v2, v11, v9
	v_cvt_pk_bf16_f32 v3, v13, v15
	v_cvt_pk_bf16_f32 v4, v17, v19
	v_cvt_pk_bf16_f32 v5, v21, v23
	global_store_dwordx4 v[6:7], v[2:5], off sc1
	s_waitcnt lgkmcnt(0)

.LBB0_754:
	s_andn2_b64 vcc, exec, s[36:37]
	s_cbranch_vccnz .LBB0_751
	s_cmp_eq_u32 s31, 0
	s_cbranch_scc1 .LBB0_750
	s_waitcnt vmcnt(3)
	v_pk_mul_f32 v[34:35], v[136:137], v[34:35] op_sel_hi:[0,1]
	ds_write2_b32 v103, v34, v35 offset1:1
	v_pk_mul_f32 v[34:35], v[136:137], v[36:37] op_sel_hi:[0,1]
	ds_write2_b32 v103, v34, v35 offset0:2 offset1:3
	v_pk_mul_f32 v[34:35], v[134:135], v[42:43] op_sel_hi:[0,1]
	v_add_u32_e32 v0, 0x420, v103
	ds_write2_b32 v0, v34, v35 offset1:1
	v_pk_mul_f32 v[34:35], v[134:135], v[44:45] op_sel_hi:[0,1]
	v_add_u32_e32 v0, 0x428, v103
	ds_write2_b32 v0, v34, v35 offset1:1
	s_waitcnt vmcnt(2)
	v_pk_mul_f32 v[34:35], v[138:139], v[38:39] op_sel_hi:[0,1]
	v_add_u32_e32 v0, 0x840, v103
	ds_write2_b32 v0, v34, v35 offset1:1
	v_pk_mul_f32 v[34:35], v[138:139], v[40:41] op_sel_hi:[0,1]
	v_add_u32_e32 v0, 0x848, v103
	ds_write2_b32 v0, v34, v35 offset1:1
	v_pk_mul_f32 v[34:35], v[130:131], v[50:51] op_sel_hi:[0,1]
	v_add_u32_e32 v0, 0xc60, v103
	ds_write2_b32 v0, v34, v35 offset1:1
	v_pk_mul_f32 v[34:35], v[130:131], v[52:53] op_sel_hi:[0,1]
	v_add_u32_e32 v0, 0xc68, v103
	ds_write2_b32 v0, v34, v35 offset1:1
	v_pk_mul_f32 v[34:35], v[132:133], v[46:47] op_sel_hi:[0,1]
	v_add_u32_e32 v0, 0x1080, v103
	ds_write2_b32 v0, v34, v35 offset1:1
	v_pk_mul_f32 v[34:35], v[132:133], v[48:49] op_sel_hi:[0,1]
	v_add_u32_e32 v0, 0x1088, v103
	ds_write2_b32 v0, v34, v35 offset1:1
	s_waitcnt vmcnt(0)
	v_pk_mul_f32 v[34:35], v[126:127], v[58:59] op_sel_hi:[0,1]
	v_add_u32_e32 v0, 0x14a0, v103
	ds_write2_b32 v0, v34, v35 offset1:1
	v_pk_mul_f32 v[34:35], v[126:127], v[60:61] op_sel_hi:[0,1]
	v_add_u32_e32 v0, 0x14a8, v103
	ds_write2_b32 v0, v34, v35 offset1:1
	v_pk_mul_f32 v[34:35], v[128:129], v[54:55] op_sel_hi:[0,1]
	v_add_u32_e32 v0, 0x18c0, v103
	ds_write2_b32 v0, v34, v35 offset1:1
	v_pk_mul_f32 v[34:35], v[128:129], v[56:57] op_sel_hi:[0,1]
	v_add_u32_e32 v0, 0x18c8, v103
	ds_write2_b32 v0, v34, v35 offset1:1
	v_pk_mul_f32 v[34:35], v[120:121], v[66:67] op_sel_hi:[0,1]
	v_add_u32_e32 v0, 0x1ce0, v103
	ds_write2_b32 v0, v34, v35 offset1:1
	v_pk_mul_f32 v[34:35], v[120:121], v[68:69] op_sel_hi:[0,1]
	v_add_u32_e32 v0, 0x1ce8, v103
	ds_write2_b32 v0, v34, v35 offset1:1
	s_waitcnt lgkmcnt(0)
	ds_read2_b32 v[38:39], v99 offset0:33 offset1:41
	ds_read2_b32 v[40:41], v99 offset1:8
	ds_read2_b32 v[42:43], v99 offset0:66 offset1:74
	ds_read2_b32 v[44:45], v99 offset0:99 offset1:107
	ds_read2_b32 v[46:47], v99 offset0:132 offset1:140
	ds_read2_b32 v[48:49], v99 offset0:165 offset1:173
	ds_read2_b32 v[50:51], v99 offset0:198 offset1:206
	ds_read2_b32 v[52:53], v99 offset0:231 offset1:239
	v_mad_u64_u32 v[54:55], s[36:37], s34, v102, 0
	v_lshl_add_u64 v[54:55], v[54:55], 1, s[14:15]
	v_lshlrev_b32_e32 v0, 1, v112
	s_waitcnt lgkmcnt(6)
	v_cvt_pk_bf16_f32 v34, v40, v38
	s_waitcnt lgkmcnt(4)
	v_cvt_pk_bf16_f32 v35, v42, v44
	s_waitcnt lgkmcnt(2)
	v_cvt_pk_bf16_f32 v36, v46, v48
	s_waitcnt lgkmcnt(0)
	v_cvt_pk_bf16_f32 v37, v50, v52
	v_lshl_add_u64 v[54:55], v[54:55], 0, v[0:1]
	global_store_dwordx4 v[54:55], v[34:37], off sc1
	s_nop 1
	v_cvt_pk_bf16_f32 v34, v41, v39
	v_cvt_pk_bf16_f32 v35, v43, v45
	v_cvt_pk_bf16_f32 v36, v47, v49
	v_cvt_pk_bf16_f32 v37, v51, v53
	v_mad_u64_u32 v[38:39], s[36:37], s34, v110, 0
	ds_read2_b32 v[40:41], v99 offset0:16 offset1:24
	ds_read2_b32 v[42:43], v99 offset0:49 offset1:57
	ds_read2_b32 v[44:45], v99 offset0:82 offset1:90
	ds_read2_b32 v[46:47], v99 offset0:115 offset1:123
	ds_read2_b32 v[48:49], v99 offset0:148 offset1:156
	ds_read2_b32 v[50:51], v99 offset0:181 offset1:189
	ds_read2_b32 v[52:53], v99 offset0:214 offset1:222
	ds_read2_b32 v[54:55], v99 offset0:247 offset1:255
	v_lshl_add_u64 v[38:39], v[38:39], 1, s[14:15]
	v_lshl_add_u64 v[38:39], v[38:39], 0, v[0:1]
	global_store_dwordx4 v[38:39], v[34:37], off sc1
	v_mad_u64_u32 v[38:39], s[36:37], s34, v108, 0
	v_lshl_add_u64 v[38:39], v[38:39], 1, s[14:15]
	s_waitcnt lgkmcnt(6)
	v_cvt_pk_bf16_f32 v34, v40, v42
	s_waitcnt lgkmcnt(4)
	v_cvt_pk_bf16_f32 v35, v44, v46
	s_waitcnt lgkmcnt(2)
	v_cvt_pk_bf16_f32 v36, v48, v50
	s_waitcnt lgkmcnt(0)
	v_cvt_pk_bf16_f32 v37, v52, v54
	v_lshl_add_u64 v[38:39], v[38:39], 0, v[0:1]
	global_store_dwordx4 v[38:39], v[34:37], off sc1
	v_mad_u64_u32 v[38:39], s[36:37], s34, v106, 0
	v_lshl_add_u64 v[38:39], v[38:39], 1, s[14:15]
	v_cvt_pk_bf16_f32 v34, v41, v43
	v_cvt_pk_bf16_f32 v35, v45, v47
	v_cvt_pk_bf16_f32 v36, v49, v51
	v_cvt_pk_bf16_f32 v37, v53, v55
	v_lshl_add_u64 v[38:39], v[38:39], 0, v[0:1]
	global_store_dwordx4 v[38:39], v[34:37], off sc1
	s_waitcnt lgkmcnt(0)
	s_branch .LBB0_750

.LBB0_759:
	s_and_b64 vcc, exec, s[16:17]
	s_cbranch_vccz .LBB0_763
	s_cmp_eq_u32 s31, 0
	s_cbranch_scc1 .LBB0_762
	s_waitcnt vmcnt(3)
	v_pk_mul_f32 v[34:35], v[34:35], v[136:137] op_sel_hi:[1,0]
	ds_write2_b32 v103, v34, v35 offset1:1
	v_pk_mul_f32 v[34:35], v[36:37], v[136:137] op_sel_hi:[1,0]
	ds_write2_b32 v103, v34, v35 offset0:2 offset1:3
	v_pk_mul_f32 v[34:35], v[42:43], v[134:135] op_sel_hi:[1,0]
	v_add_u32_e32 v0, 0x420, v103
	ds_write2_b32 v0, v34, v35 offset1:1
	v_pk_mul_f32 v[34:35], v[44:45], v[134:135] op_sel_hi:[1,0]
	v_add_u32_e32 v0, 0x428, v103
	ds_write2_b32 v0, v34, v35 offset1:1
	s_waitcnt vmcnt(2)
	v_pk_mul_f32 v[34:35], v[38:39], v[138:139] op_sel_hi:[1,0]
	v_add_u32_e32 v0, 0x840, v103
	ds_write2_b32 v0, v34, v35 offset1:1
	v_pk_mul_f32 v[34:35], v[40:41], v[138:139] op_sel_hi:[1,0]
	v_add_u32_e32 v0, 0x848, v103
	ds_write2_b32 v0, v34, v35 offset1:1
	v_pk_mul_f32 v[34:35], v[50:51], v[130:131] op_sel_hi:[1,0]
	v_add_u32_e32 v0, 0xc60, v103
	ds_write2_b32 v0, v34, v35 offset1:1
	v_pk_mul_f32 v[34:35], v[52:53], v[130:131] op_sel_hi:[1,0]
	v_add_u32_e32 v0, 0xc68, v103
	ds_write2_b32 v0, v34, v35 offset1:1
	v_pk_mul_f32 v[34:35], v[46:47], v[132:133] op_sel_hi:[1,0]
	v_add_u32_e32 v0, 0x1080, v103
	ds_write2_b32 v0, v34, v35 offset1:1
	v_pk_mul_f32 v[34:35], v[48:49], v[132:133] op_sel_hi:[1,0]
	v_add_u32_e32 v0, 0x1088, v103
	ds_write2_b32 v0, v34, v35 offset1:1
	s_waitcnt vmcnt(0)
	v_pk_mul_f32 v[34:35], v[58:59], v[126:127] op_sel_hi:[1,0]
	v_add_u32_e32 v0, 0x14a0, v103
	ds_write2_b32 v0, v34, v35 offset1:1
	v_pk_mul_f32 v[34:35], v[60:61], v[126:127] op_sel_hi:[1,0]
	v_add_u32_e32 v0, 0x14a8, v103
	ds_write2_b32 v0, v34, v35 offset1:1
	v_pk_mul_f32 v[34:35], v[54:55], v[128:129] op_sel_hi:[1,0]
	v_add_u32_e32 v0, 0x18c0, v103
	ds_write2_b32 v0, v34, v35 offset1:1
	v_pk_mul_f32 v[34:35], v[56:57], v[128:129] op_sel_hi:[1,0]
	v_add_u32_e32 v0, 0x18c8, v103
	ds_write2_b32 v0, v34, v35 offset1:1
	v_pk_mul_f32 v[34:35], v[66:67], v[120:121] op_sel_hi:[1,0]
	v_add_u32_e32 v0, 0x1ce0, v103
	ds_write2_b32 v0, v34, v35 offset1:1
	v_pk_mul_f32 v[34:35], v[68:69], v[120:121] op_sel_hi:[1,0]
	v_add_u32_e32 v0, 0x1ce8, v103
	ds_write2_b32 v0, v34, v35 offset1:1
	s_waitcnt lgkmcnt(0)
	ds_read2_b32 v[38:39], v99 offset0:33 offset1:41
	ds_read2_b32 v[40:41], v99 offset1:8
	ds_read2_b32 v[42:43], v99 offset0:66 offset1:74
	ds_read2_b32 v[44:45], v99 offset0:99 offset1:107
	ds_read2_b32 v[46:47], v99 offset0:132 offset1:140
	ds_read2_b32 v[48:49], v99 offset0:165 offset1:173
	ds_read2_b32 v[50:51], v99 offset0:198 offset1:206
	ds_read2_b32 v[52:53], v99 offset0:231 offset1:239
	v_mul_u32_u24_e32 v0, s34, v102
	v_lshlrev_b32_e32 v0, 1, v0
	v_lshl_add_u64 v[54:55], s[14:15], 0, v[0:1]
	v_lshlrev_b32_e32 v0, 1, v112
	s_lshl_b32 s14, s34, 3
	s_waitcnt lgkmcnt(6)
	v_cvt_pk_bf16_f32 v34, v40, v38
	s_waitcnt lgkmcnt(4)
	v_cvt_pk_bf16_f32 v35, v42, v44
	s_waitcnt lgkmcnt(2)
	v_cvt_pk_bf16_f32 v36, v46, v48
	s_waitcnt lgkmcnt(0)
	v_cvt_pk_bf16_f32 v37, v50, v52
	v_lshl_add_u64 v[56:57], v[54:55], 0, v[0:1]
	s_ashr_i32 s15, s14, 31
	global_store_dwordx4 v[56:57], v[34:37], off sc1
	s_lshl_b64 s[14:15], s[14:15], 1
	s_nop 0
	v_cvt_pk_bf16_f32 v34, v41, v39
	v_cvt_pk_bf16_f32 v35, v43, v45
	v_cvt_pk_bf16_f32 v36, v47, v49
	v_cvt_pk_bf16_f32 v37, v51, v53
	v_lshl_add_u64 v[38:39], v[54:55], 0, s[14:15]
	ds_read2_b32 v[42:43], v99 offset0:16 offset1:24
	ds_read2_b32 v[44:45], v99 offset0:49 offset1:57
	ds_read2_b32 v[46:47], v99 offset0:82 offset1:90
	ds_read2_b32 v[48:49], v99 offset0:115 offset1:123
	ds_read2_b32 v[50:51], v99 offset0:148 offset1:156
	ds_read2_b32 v[52:53], v99 offset0:181 offset1:189
	ds_read2_b32 v[54:55], v99 offset0:214 offset1:222
	ds_read2_b32 v[56:57], v99 offset0:247 offset1:255
	v_lshl_add_u64 v[40:41], v[38:39], 0, v[0:1]
	v_lshl_add_u64 v[38:39], v[38:39], 0, s[14:15]
	global_store_dwordx4 v[40:41], v[34:37], off sc1
	v_lshl_add_u64 v[40:41], v[38:39], 0, v[0:1]
	v_lshl_add_u64 v[38:39], v[38:39], 0, s[14:15]
	s_waitcnt lgkmcnt(6)
	v_cvt_pk_bf16_f32 v34, v42, v44
	s_waitcnt lgkmcnt(4)
	v_cvt_pk_bf16_f32 v35, v46, v48
	s_waitcnt lgkmcnt(2)
	v_cvt_pk_bf16_f32 v36, v50, v52
	s_waitcnt lgkmcnt(0)
	v_cvt_pk_bf16_f32 v37, v54, v56
	global_store_dwordx4 v[40:41], v[34:37], off sc1
	v_lshl_add_u64 v[38:39], v[38:39], 0, v[0:1]
	s_nop 0
	v_cvt_pk_bf16_f32 v34, v43, v45
	v_cvt_pk_bf16_f32 v35, v47, v49
	v_cvt_pk_bf16_f32 v36, v51, v53
	v_cvt_pk_bf16_f32 v37, v55, v57
	global_store_dwordx4 v[38:39], v[34:37], off sc1
	s_waitcnt lgkmcnt(0)

.LBB0_781:
	s_andn2_b64 vcc, exec, s[46:47]
	s_cbranch_vccnz .LBB0_785
	s_cmp_eq_u32 s31, 0
	s_cbranch_scc1 .LBB0_784
	v_pk_mul_f32 v[26:27], v[134:135], v[26:27] op_sel_hi:[0,1]
	v_add_u32_e32 v0, 0x420, v103
	ds_write2_b32 v0, v26, v27 offset1:1
	v_pk_mul_f32 v[26:27], v[134:135], v[28:29] op_sel_hi:[0,1]
	v_add_u32_e32 v0, 0x428, v103
	ds_write2_b32 v0, v26, v27 offset1:1
	v_pk_mul_f32 v[22:23], v[138:139], v[22:23] op_sel_hi:[0,1]
	v_add_u32_e32 v0, 0x840, v103
	ds_write2_b32 v0, v22, v23 offset1:1
	v_pk_mul_f32 v[22:23], v[138:139], v[24:25] op_sel_hi:[0,1]
	v_add_u32_e32 v0, 0x848, v103
	ds_write2_b32 v0, v22, v23 offset1:1
	v_pk_mul_f32 v[18:19], v[130:131], v[18:19] op_sel_hi:[0,1]
	v_add_u32_e32 v0, 0xc60, v103
	ds_write2_b32 v0, v18, v19 offset1:1
	v_pk_mul_f32 v[18:19], v[130:131], v[20:21] op_sel_hi:[0,1]
	v_add_u32_e32 v0, 0xc68, v103
	ds_write2_b32 v0, v18, v19 offset1:1
	v_pk_mul_f32 v[14:15], v[132:133], v[14:15] op_sel_hi:[0,1]
	v_add_u32_e32 v0, 0x1080, v103
	ds_write2_b32 v0, v14, v15 offset1:1
	v_pk_mul_f32 v[14:15], v[132:133], v[16:17] op_sel_hi:[0,1]
	v_add_u32_e32 v0, 0x1088, v103
	ds_write2_b32 v0, v14, v15 offset1:1
	s_waitcnt vmcnt(2)
	v_pk_mul_f32 v[10:11], v[126:127], v[10:11] op_sel_hi:[0,1]
	v_add_u32_e32 v0, 0x14a0, v103
	ds_write2_b32 v0, v10, v11 offset1:1
	v_pk_mul_f32 v[10:11], v[126:127], v[12:13] op_sel_hi:[0,1]
	v_add_u32_e32 v0, 0x14a8, v103
	ds_write2_b32 v0, v10, v11 offset1:1
	s_waitcnt vmcnt(1)
	v_pk_mul_f32 v[6:7], v[128:129], v[6:7] op_sel_hi:[0,1]
	v_add_u32_e32 v0, 0x18c0, v103
	ds_write2_b32 v0, v6, v7 offset1:1
	v_pk_mul_f32 v[6:7], v[128:129], v[8:9] op_sel_hi:[0,1]
	v_add_u32_e32 v0, 0x18c8, v103
	s_waitcnt vmcnt(0)
	v_pk_mul_f32 v[30:31], v[136:137], v[30:31] op_sel_hi:[0,1]
	ds_write2_b32 v0, v6, v7 offset1:1
	v_pk_mul_f32 v[2:3], v[120:121], v[2:3] op_sel_hi:[0,1]
	v_add_u32_e32 v0, 0x1ce0, v103
	ds_write2_b32 v103, v30, v31 offset1:1
	v_pk_mul_f32 v[30:31], v[136:137], v[32:33] op_sel_hi:[0,1]
	ds_write2_b32 v0, v2, v3 offset1:1
	v_pk_mul_f32 v[2:3], v[120:121], v[4:5] op_sel_hi:[0,1]
	v_add_u32_e32 v0, 0x1ce8, v103
	ds_write2_b32 v103, v30, v31 offset0:2 offset1:3
	ds_write2_b32 v0, v2, v3 offset1:1
	s_waitcnt lgkmcnt(0)
	ds_read2_b32 v[6:7], v99 offset0:33 offset1:41
	ds_read2_b32 v[8:9], v99 offset1:8
	ds_read2_b32 v[10:11], v99 offset0:66 offset1:74
	ds_read2_b32 v[12:13], v99 offset0:99 offset1:107
	ds_read2_b32 v[14:15], v99 offset0:132 offset1:140
	ds_read2_b32 v[16:17], v99 offset0:165 offset1:173
	ds_read2_b32 v[18:19], v99 offset0:198 offset1:206
	ds_read2_b32 v[20:21], v99 offset0:231 offset1:239
	v_mad_u64_u32 v[22:23], s[36:37], s34, v102, 0
	v_lshl_add_u64 v[22:23], v[22:23], 1, s[0:1]
	v_lshlrev_b32_e32 v0, 1, v112
	s_waitcnt lgkmcnt(6)
	v_cvt_pk_bf16_f32 v2, v8, v6
	s_waitcnt lgkmcnt(4)
	v_cvt_pk_bf16_f32 v3, v10, v12
	s_waitcnt lgkmcnt(2)
	v_cvt_pk_bf16_f32 v4, v14, v16
	s_waitcnt lgkmcnt(0)
	v_cvt_pk_bf16_f32 v5, v18, v20
	v_lshl_add_u64 v[22:23], v[22:23], 0, v[0:1]
	global_store_dwordx4 v[22:23], v[2:5], off sc1
	s_nop 1
	v_cvt_pk_bf16_f32 v2, v9, v7
	v_cvt_pk_bf16_f32 v3, v11, v13
	v_cvt_pk_bf16_f32 v4, v15, v17
	v_cvt_pk_bf16_f32 v5, v19, v21
	v_mad_u64_u32 v[6:7], s[36:37], s34, v110, 0
	ds_read2_b32 v[8:9], v99 offset0:16 offset1:24
	ds_read2_b32 v[10:11], v99 offset0:49 offset1:57
	ds_read2_b32 v[12:13], v99 offset0:82 offset1:90
	ds_read2_b32 v[14:15], v99 offset0:115 offset1:123
	ds_read2_b32 v[16:17], v99 offset0:148 offset1:156
	ds_read2_b32 v[18:19], v99 offset0:181 offset1:189
	ds_read2_b32 v[20:21], v99 offset0:214 offset1:222
	ds_read2_b32 v[22:23], v99 offset0:247 offset1:255
	v_lshl_add_u64 v[6:7], v[6:7], 1, s[0:1]
	v_lshl_add_u64 v[6:7], v[6:7], 0, v[0:1]
	global_store_dwordx4 v[6:7], v[2:5], off sc1
	v_mad_u64_u32 v[6:7], s[36:37], s34, v108, 0
	v_lshl_add_u64 v[6:7], v[6:7], 1, s[0:1]
	s_waitcnt lgkmcnt(6)
	v_cvt_pk_bf16_f32 v2, v8, v10
	s_waitcnt lgkmcnt(4)
	v_cvt_pk_bf16_f32 v3, v12, v14
	s_waitcnt lgkmcnt(2)
	v_cvt_pk_bf16_f32 v4, v16, v18
	s_waitcnt lgkmcnt(0)
	v_cvt_pk_bf16_f32 v5, v20, v22
	v_lshl_add_u64 v[6:7], v[6:7], 0, v[0:1]
	global_store_dwordx4 v[6:7], v[2:5], off sc1
	v_mad_u64_u32 v[6:7], s[36:37], s34, v106, 0
	v_lshl_add_u64 v[6:7], v[6:7], 1, s[0:1]
	v_cvt_pk_bf16_f32 v2, v9, v11
	v_cvt_pk_bf16_f32 v3, v13, v15
	v_cvt_pk_bf16_f32 v4, v17, v19
	v_cvt_pk_bf16_f32 v5, v21, v23
	v_lshl_add_u64 v[6:7], v[6:7], 0, v[0:1]
	global_store_dwordx4 v[6:7], v[2:5], off sc1
	s_waitcnt lgkmcnt(0)

.LBB0_799:
	s_andn2_b64 vcc, exec, s[46:47]
	s_cbranch_vccnz .LBB0_766
	s_cmp_eq_u32 s31, 0
	s_cbranch_scc1 .LBB0_765
	v_pk_mul_f32 v[26:27], v[26:27], v[134:135] op_sel_hi:[1,0]
	v_add_u32_e32 v0, 0x420, v103
	ds_write2_b32 v0, v26, v27 offset1:1
	v_pk_mul_f32 v[26:27], v[28:29], v[134:135] op_sel_hi:[1,0]
	v_add_u32_e32 v0, 0x428, v103
	ds_write2_b32 v0, v26, v27 offset1:1
	v_pk_mul_f32 v[22:23], v[22:23], v[138:139] op_sel_hi:[1,0]
	v_add_u32_e32 v0, 0x840, v103
	ds_write2_b32 v0, v22, v23 offset1:1
	v_pk_mul_f32 v[22:23], v[24:25], v[138:139] op_sel_hi:[1,0]
	v_add_u32_e32 v0, 0x848, v103
	ds_write2_b32 v0, v22, v23 offset1:1
	v_pk_mul_f32 v[18:19], v[18:19], v[130:131] op_sel_hi:[1,0]
	v_add_u32_e32 v0, 0xc60, v103
	ds_write2_b32 v0, v18, v19 offset1:1
	v_pk_mul_f32 v[18:19], v[20:21], v[130:131] op_sel_hi:[1,0]
	v_add_u32_e32 v0, 0xc68, v103
	ds_write2_b32 v0, v18, v19 offset1:1
	v_pk_mul_f32 v[14:15], v[14:15], v[132:133] op_sel_hi:[1,0]
	v_add_u32_e32 v0, 0x1080, v103
	ds_write2_b32 v0, v14, v15 offset1:1
	v_pk_mul_f32 v[14:15], v[16:17], v[132:133] op_sel_hi:[1,0]
	v_add_u32_e32 v0, 0x1088, v103
	ds_write2_b32 v0, v14, v15 offset1:1
	s_waitcnt vmcnt(2)
	v_pk_mul_f32 v[10:11], v[10:11], v[126:127] op_sel_hi:[1,0]
	v_add_u32_e32 v0, 0x14a0, v103
	ds_write2_b32 v0, v10, v11 offset1:1
	v_pk_mul_f32 v[10:11], v[12:13], v[126:127] op_sel_hi:[1,0]
	v_add_u32_e32 v0, 0x14a8, v103
	ds_write2_b32 v0, v10, v11 offset1:1
	s_waitcnt vmcnt(1)
	v_pk_mul_f32 v[6:7], v[6:7], v[128:129] op_sel_hi:[1,0]
	v_add_u32_e32 v0, 0x18c0, v103
	ds_write2_b32 v0, v6, v7 offset1:1
	v_pk_mul_f32 v[6:7], v[8:9], v[128:129] op_sel_hi:[1,0]
	v_add_u32_e32 v0, 0x18c8, v103
	s_waitcnt vmcnt(0)
	v_pk_mul_f32 v[30:31], v[30:31], v[136:137] op_sel_hi:[1,0]
	ds_write2_b32 v0, v6, v7 offset1:1
	v_pk_mul_f32 v[2:3], v[2:3], v[120:121] op_sel_hi:[1,0]
	v_add_u32_e32 v0, 0x1ce0, v103
	ds_write2_b32 v103, v30, v31 offset1:1
	v_pk_mul_f32 v[30:31], v[32:33], v[136:137] op_sel_hi:[1,0]
	ds_write2_b32 v0, v2, v3 offset1:1
	v_pk_mul_f32 v[2:3], v[4:5], v[120:121] op_sel_hi:[1,0]
	v_add_u32_e32 v0, 0x1ce8, v103
	ds_write2_b32 v103, v30, v31 offset0:2 offset1:3
	ds_write2_b32 v0, v2, v3 offset1:1
	s_waitcnt lgkmcnt(0)
	ds_read2_b32 v[6:7], v99 offset0:33 offset1:41
	ds_read2_b32 v[8:9], v99 offset1:8
	ds_read2_b32 v[10:11], v99 offset0:66 offset1:74
	ds_read2_b32 v[12:13], v99 offset0:99 offset1:107
	ds_read2_b32 v[14:15], v99 offset0:132 offset1:140
	ds_read2_b32 v[16:17], v99 offset0:165 offset1:173
	ds_read2_b32 v[18:19], v99 offset0:198 offset1:206
	ds_read2_b32 v[20:21], v99 offset0:231 offset1:239
	v_mad_u64_u32 v[22:23], s[36:37], s34, v102, 0
	v_lshl_add_u64 v[22:23], v[22:23], 1, s[0:1]
	v_lshlrev_b32_e32 v0, 1, v112
	s_waitcnt lgkmcnt(6)
	v_cvt_pk_bf16_f32 v2, v8, v6
	s_waitcnt lgkmcnt(4)
	v_cvt_pk_bf16_f32 v3, v10, v12
	s_waitcnt lgkmcnt(2)
	v_cvt_pk_bf16_f32 v4, v14, v16
	s_waitcnt lgkmcnt(0)
	v_cvt_pk_bf16_f32 v5, v18, v20
	v_lshl_add_u64 v[22:23], v[22:23], 0, v[0:1]
	global_store_dwordx4 v[22:23], v[2:5], off sc1
	s_nop 1
	v_cvt_pk_bf16_f32 v2, v9, v7
	v_cvt_pk_bf16_f32 v3, v11, v13
	v_cvt_pk_bf16_f32 v4, v15, v17
	v_cvt_pk_bf16_f32 v5, v19, v21
	v_mad_u64_u32 v[6:7], s[36:37], s34, v110, 0
	ds_read2_b32 v[8:9], v99 offset0:16 offset1:24
	ds_read2_b32 v[10:11], v99 offset0:49 offset1:57
	ds_read2_b32 v[12:13], v99 offset0:82 offset1:90
	ds_read2_b32 v[14:15], v99 offset0:115 offset1:123
	ds_read2_b32 v[16:17], v99 offset0:148 offset1:156
	ds_read2_b32 v[18:19], v99 offset0:181 offset1:189
	ds_read2_b32 v[20:21], v99 offset0:214 offset1:222
	ds_read2_b32 v[22:23], v99 offset0:247 offset1:255
	v_lshl_add_u64 v[6:7], v[6:7], 1, s[0:1]
	v_lshl_add_u64 v[6:7], v[6:7], 0, v[0:1]
	global_store_dwordx4 v[6:7], v[2:5], off sc1
	v_mad_u64_u32 v[6:7], s[36:37], s34, v108, 0
	v_lshl_add_u64 v[6:7], v[6:7], 1, s[0:1]
	s_waitcnt lgkmcnt(6)
	v_cvt_pk_bf16_f32 v2, v8, v10
	s_waitcnt lgkmcnt(4)
	v_cvt_pk_bf16_f32 v3, v12, v14
	s_waitcnt lgkmcnt(2)
	v_cvt_pk_bf16_f32 v4, v16, v18
	s_waitcnt lgkmcnt(0)
	v_cvt_pk_bf16_f32 v5, v20, v22
	v_lshl_add_u64 v[6:7], v[6:7], 0, v[0:1]
	global_store_dwordx4 v[6:7], v[2:5], off sc1
	v_mad_u64_u32 v[6:7], s[36:37], s34, v106, 0
	v_lshl_add_u64 v[6:7], v[6:7], 1, s[0:1]
	v_cvt_pk_bf16_f32 v2, v9, v11
	v_cvt_pk_bf16_f32 v3, v13, v15
	v_cvt_pk_bf16_f32 v4, v17, v19
	v_cvt_pk_bf16_f32 v5, v21, v23
	v_lshl_add_u64 v[6:7], v[6:7], 0, v[0:1]
	global_store_dwordx4 v[6:7], v[2:5], off sc1
	s_waitcnt lgkmcnt(0)
	s_branch .LBB0_765

.LBB0_812:
	s_andn2_b64 vcc, exec, s[16:17]
	s_cbranch_vccnz .LBB0_816
	s_cmp_eq_u32 s31, 0
	s_cbranch_scc1 .LBB0_815
	v_pk_mul_f32 v[26:27], v[26:27], v[134:135] op_sel_hi:[1,0]
	v_add_u32_e32 v0, 0x420, v103
	ds_write2_b32 v0, v26, v27 offset1:1
	v_pk_mul_f32 v[26:27], v[28:29], v[134:135] op_sel_hi:[1,0]
	v_add_u32_e32 v0, 0x428, v103
	ds_write2_b32 v0, v26, v27 offset1:1
	v_pk_mul_f32 v[22:23], v[22:23], v[138:139] op_sel_hi:[1,0]
	v_add_u32_e32 v0, 0x840, v103
	ds_write2_b32 v0, v22, v23 offset1:1
	v_pk_mul_f32 v[22:23], v[24:25], v[138:139] op_sel_hi:[1,0]
	v_add_u32_e32 v0, 0x848, v103
	ds_write2_b32 v0, v22, v23 offset1:1
	v_pk_mul_f32 v[18:19], v[18:19], v[130:131] op_sel_hi:[1,0]
	v_add_u32_e32 v0, 0xc60, v103
	ds_write2_b32 v0, v18, v19 offset1:1
	v_pk_mul_f32 v[18:19], v[20:21], v[130:131] op_sel_hi:[1,0]
	v_add_u32_e32 v0, 0xc68, v103
	ds_write2_b32 v0, v18, v19 offset1:1
	v_pk_mul_f32 v[14:15], v[14:15], v[132:133] op_sel_hi:[1,0]
	v_add_u32_e32 v0, 0x1080, v103
	ds_write2_b32 v0, v14, v15 offset1:1
	v_pk_mul_f32 v[14:15], v[16:17], v[132:133] op_sel_hi:[1,0]
	v_add_u32_e32 v0, 0x1088, v103
	ds_write2_b32 v0, v14, v15 offset1:1
	s_waitcnt vmcnt(2)
	v_pk_mul_f32 v[10:11], v[10:11], v[126:127] op_sel_hi:[1,0]
	v_add_u32_e32 v0, 0x14a0, v103
	ds_write2_b32 v0, v10, v11 offset1:1
	v_pk_mul_f32 v[10:11], v[12:13], v[126:127] op_sel_hi:[1,0]
	v_add_u32_e32 v0, 0x14a8, v103
	ds_write2_b32 v0, v10, v11 offset1:1
	s_waitcnt vmcnt(1)
	v_pk_mul_f32 v[6:7], v[6:7], v[128:129] op_sel_hi:[1,0]
	v_add_u32_e32 v0, 0x18c0, v103
	ds_write2_b32 v0, v6, v7 offset1:1
	v_pk_mul_f32 v[6:7], v[8:9], v[128:129] op_sel_hi:[1,0]
	v_add_u32_e32 v0, 0x18c8, v103
	s_waitcnt vmcnt(0)
	v_pk_mul_f32 v[30:31], v[30:31], v[136:137] op_sel_hi:[1,0]
	ds_write2_b32 v0, v6, v7 offset1:1
	v_pk_mul_f32 v[2:3], v[2:3], v[120:121] op_sel_hi:[1,0]
	v_add_u32_e32 v0, 0x1ce0, v103
	ds_write2_b32 v103, v30, v31 offset1:1
	v_pk_mul_f32 v[30:31], v[32:33], v[136:137] op_sel_hi:[1,0]
	ds_write2_b32 v0, v2, v3 offset1:1
	v_pk_mul_f32 v[2:3], v[4:5], v[120:121] op_sel_hi:[1,0]
	v_add_u32_e32 v0, 0x1ce8, v103
	ds_write2_b32 v103, v30, v31 offset0:2 offset1:3
	ds_write2_b32 v0, v2, v3 offset1:1
	s_waitcnt lgkmcnt(0)
	ds_read2_b32 v[6:7], v99 offset0:33 offset1:41
	ds_read2_b32 v[8:9], v99 offset1:8
	ds_read2_b32 v[10:11], v99 offset0:66 offset1:74
	ds_read2_b32 v[12:13], v99 offset0:99 offset1:107
	ds_read2_b32 v[14:15], v99 offset0:132 offset1:140
	ds_read2_b32 v[16:17], v99 offset0:165 offset1:173
	ds_read2_b32 v[18:19], v99 offset0:198 offset1:206
	ds_read2_b32 v[20:21], v99 offset0:231 offset1:239
	v_mad_u64_u32 v[22:23], s[16:17], s34, v102, 0
	v_lshl_add_u64 v[22:23], v[22:23], 1, s[0:1]
	v_lshlrev_b32_e32 v0, 1, v112
	s_waitcnt lgkmcnt(6)
	v_cvt_pk_bf16_f32 v2, v8, v6
	s_waitcnt lgkmcnt(4)
	v_cvt_pk_bf16_f32 v3, v10, v12
	s_waitcnt lgkmcnt(2)
	v_cvt_pk_bf16_f32 v4, v14, v16
	s_waitcnt lgkmcnt(0)
	v_cvt_pk_bf16_f32 v5, v18, v20
	v_lshl_add_u64 v[22:23], v[22:23], 0, v[0:1]
	global_store_dwordx4 v[22:23], v[2:5], off sc1
	s_nop 1
	v_cvt_pk_bf16_f32 v2, v9, v7
	v_cvt_pk_bf16_f32 v3, v11, v13
	v_cvt_pk_bf16_f32 v4, v15, v17
	v_cvt_pk_bf16_f32 v5, v19, v21
	v_mad_u64_u32 v[6:7], s[16:17], s34, v110, 0
	ds_read2_b32 v[8:9], v99 offset0:16 offset1:24
	ds_read2_b32 v[10:11], v99 offset0:49 offset1:57
	ds_read2_b32 v[12:13], v99 offset0:82 offset1:90
	ds_read2_b32 v[14:15], v99 offset0:115 offset1:123
	ds_read2_b32 v[16:17], v99 offset0:148 offset1:156
	ds_read2_b32 v[18:19], v99 offset0:181 offset1:189
	ds_read2_b32 v[20:21], v99 offset0:214 offset1:222
	ds_read2_b32 v[22:23], v99 offset0:247 offset1:255
	v_lshl_add_u64 v[6:7], v[6:7], 1, s[0:1]
	v_lshl_add_u64 v[6:7], v[6:7], 0, v[0:1]
	global_store_dwordx4 v[6:7], v[2:5], off sc1
	v_mad_u64_u32 v[6:7], s[16:17], s34, v108, 0
	v_lshl_add_u64 v[6:7], v[6:7], 1, s[0:1]
	s_waitcnt lgkmcnt(6)
	v_cvt_pk_bf16_f32 v2, v8, v10
	s_waitcnt lgkmcnt(4)
	v_cvt_pk_bf16_f32 v3, v12, v14
	s_waitcnt lgkmcnt(2)
	v_cvt_pk_bf16_f32 v4, v16, v18
	s_waitcnt lgkmcnt(0)
	v_cvt_pk_bf16_f32 v5, v20, v22
	v_lshl_add_u64 v[6:7], v[6:7], 0, v[0:1]
	global_store_dwordx4 v[6:7], v[2:5], off sc1
	v_mad_u64_u32 v[6:7], s[16:17], s34, v106, 0
	v_lshl_add_u64 v[6:7], v[6:7], 1, s[0:1]
	v_cvt_pk_bf16_f32 v2, v9, v11
	v_cvt_pk_bf16_f32 v3, v13, v15
	v_cvt_pk_bf16_f32 v4, v17, v19
	v_cvt_pk_bf16_f32 v5, v21, v23
	v_lshl_add_u64 v[6:7], v[6:7], 0, v[0:1]
	global_store_dwordx4 v[6:7], v[2:5], off sc1
	s_waitcnt lgkmcnt(0)

.LBB0_817:
	s_waitcnt vmcnt(0)
	v_pk_mul_f32 v[2:3], v[62:63], v[136:137] op_sel_hi:[1,0]
	ds_write2_b32 v103, v2, v3 offset1:1
	v_pk_mul_f32 v[2:3], v[64:65], v[136:137] op_sel_hi:[1,0]
	ds_write2_b32 v103, v2, v3 offset0:2 offset1:3
	v_pk_mul_f32 v[2:3], v[50:51], v[134:135] op_sel_hi:[1,0]
	v_add_u32_e32 v0, 0x420, v103
	ds_write2_b32 v0, v2, v3 offset1:1
	v_pk_mul_f32 v[2:3], v[52:53], v[134:135] op_sel_hi:[1,0]
	v_add_u32_e32 v0, 0x428, v103
	ds_write2_b32 v0, v2, v3 offset1:1
	v_pk_mul_f32 v[2:3], v[58:59], v[138:139] op_sel_hi:[1,0]
	v_add_u32_e32 v0, 0x840, v103
	ds_write2_b32 v0, v2, v3 offset1:1
	v_pk_mul_f32 v[2:3], v[60:61], v[138:139] op_sel_hi:[1,0]
	v_add_u32_e32 v0, 0x848, v103
	ds_write2_b32 v0, v2, v3 offset1:1
	v_pk_mul_f32 v[2:3], v[42:43], v[130:131] op_sel_hi:[1,0]
	v_add_u32_e32 v0, 0xc60, v103
	ds_write2_b32 v0, v2, v3 offset1:1
	v_pk_mul_f32 v[2:3], v[44:45], v[130:131] op_sel_hi:[1,0]
	v_add_u32_e32 v0, 0xc68, v103
	ds_write2_b32 v0, v2, v3 offset1:1
	v_pk_mul_f32 v[2:3], v[54:55], v[132:133] op_sel_hi:[1,0]
	v_add_u32_e32 v0, 0x1080, v103
	ds_write2_b32 v0, v2, v3 offset1:1
	v_pk_mul_f32 v[2:3], v[56:57], v[132:133] op_sel_hi:[1,0]
	v_add_u32_e32 v0, 0x1088, v103
	ds_write2_b32 v0, v2, v3 offset1:1
	v_pk_mul_f32 v[2:3], v[38:39], v[126:127] op_sel_hi:[1,0]
	v_add_u32_e32 v0, 0x14a0, v103
	ds_write2_b32 v0, v2, v3 offset1:1
	v_pk_mul_f32 v[2:3], v[40:41], v[126:127] op_sel_hi:[1,0]
	v_add_u32_e32 v0, 0x14a8, v103
	ds_write2_b32 v0, v2, v3 offset1:1
	v_pk_mul_f32 v[2:3], v[46:47], v[128:129] op_sel_hi:[1,0]
	v_add_u32_e32 v0, 0x18c0, v103
	ds_write2_b32 v0, v2, v3 offset1:1
	v_pk_mul_f32 v[2:3], v[48:49], v[128:129] op_sel_hi:[1,0]
	v_add_u32_e32 v0, 0x18c8, v103
	ds_write2_b32 v0, v2, v3 offset1:1
	v_pk_mul_f32 v[2:3], v[34:35], v[120:121] op_sel_hi:[1,0]
	v_add_u32_e32 v0, 0x1ce0, v103
	ds_write2_b32 v0, v2, v3 offset1:1
	v_pk_mul_f32 v[2:3], v[36:37], v[120:121] op_sel_hi:[1,0]
	v_add_u32_e32 v0, 0x1ce8, v103
	ds_write2_b32 v0, v2, v3 offset1:1
	s_waitcnt lgkmcnt(0)
	ds_read2_b32 v[6:7], v99 offset0:33 offset1:41
	ds_read2_b32 v[8:9], v99 offset1:8
	ds_read2_b32 v[10:11], v99 offset0:66 offset1:74
	ds_read2_b32 v[12:13], v99 offset0:99 offset1:107
	ds_read2_b32 v[14:15], v99 offset0:132 offset1:140
	ds_read2_b32 v[16:17], v99 offset0:165 offset1:173
	ds_read2_b32 v[18:19], v99 offset0:198 offset1:206
	ds_read2_b32 v[20:21], v99 offset0:231 offset1:239
	v_mad_u64_u32 v[22:23], s[0:1], s34, v102, 0
	v_lshl_add_u64 v[22:23], v[22:23], 1, s[14:15]
	v_lshlrev_b32_e32 v0, 1, v112
	s_waitcnt lgkmcnt(6)
	v_cvt_pk_bf16_f32 v2, v8, v6
	s_waitcnt lgkmcnt(4)
	v_cvt_pk_bf16_f32 v3, v10, v12
	s_waitcnt lgkmcnt(2)
	v_cvt_pk_bf16_f32 v4, v14, v16
	s_waitcnt lgkmcnt(0)
	v_cvt_pk_bf16_f32 v5, v18, v20
	v_lshl_add_u64 v[22:23], v[22:23], 0, v[0:1]
	global_store_dwordx4 v[22:23], v[2:5], off sc1
	s_nop 1
	v_cvt_pk_bf16_f32 v2, v9, v7
	v_cvt_pk_bf16_f32 v3, v11, v13
	v_cvt_pk_bf16_f32 v4, v15, v17
	v_cvt_pk_bf16_f32 v5, v19, v21
	v_mad_u64_u32 v[6:7], s[0:1], s34, v110, 0
	ds_read2_b32 v[8:9], v99 offset0:16 offset1:24
	ds_read2_b32 v[10:11], v99 offset0:49 offset1:57
	ds_read2_b32 v[12:13], v99 offset0:82 offset1:90
	ds_read2_b32 v[14:15], v99 offset0:115 offset1:123
	ds_read2_b32 v[16:17], v99 offset0:148 offset1:156
	ds_read2_b32 v[18:19], v99 offset0:181 offset1:189
	ds_read2_b32 v[20:21], v99 offset0:214 offset1:222
	ds_read2_b32 v[22:23], v99 offset0:247 offset1:255
	v_lshl_add_u64 v[6:7], v[6:7], 1, s[14:15]
	v_lshl_add_u64 v[6:7], v[6:7], 0, v[0:1]
	global_store_dwordx4 v[6:7], v[2:5], off sc1
	v_mad_u64_u32 v[6:7], s[0:1], s34, v108, 0
	v_lshl_add_u64 v[6:7], v[6:7], 1, s[14:15]
	s_waitcnt lgkmcnt(6)
	v_cvt_pk_bf16_f32 v2, v8, v10
	s_waitcnt lgkmcnt(4)
	v_cvt_pk_bf16_f32 v3, v12, v14
	s_waitcnt lgkmcnt(2)
	v_cvt_pk_bf16_f32 v4, v16, v18
	s_waitcnt lgkmcnt(0)
	v_cvt_pk_bf16_f32 v5, v20, v22
	v_lshl_add_u64 v[6:7], v[6:7], 0, v[0:1]
	global_store_dwordx4 v[6:7], v[2:5], off sc1
	v_mad_u64_u32 v[6:7], s[0:1], s34, v106, 0
	v_lshl_add_u64 v[6:7], v[6:7], 1, s[14:15]
	v_cvt_pk_bf16_f32 v2, v9, v11
	v_cvt_pk_bf16_f32 v3, v13, v15
	v_cvt_pk_bf16_f32 v4, v17, v19
	v_cvt_pk_bf16_f32 v5, v21, v23
	v_lshl_add_u64 v[6:7], v[6:7], 0, v[0:1]
	global_store_dwordx4 v[6:7], v[2:5], off sc1
	s_waitcnt lgkmcnt(0)

.LBB0_820:
	v_add_u32_e32 v98, s92, v98
	s_mov_b32 s16, 0xbfff
	v_cmp_lt_i32_e32 vcc, s16, v98
	global_store_dwordx4 v[6:7], v[2:5], off sc1
	s_or_b64 s[14:15], vcc, s[14:15]
	v_lshl_add_u64 v[6:7], v[6:7], 0, s[34:35]
	s_andn2_b64 exec, exec, s[14:15]
	s_cbranch_execnz .LBB0_820

.LBB0_824:
	s_ashr_i32 s31, s30, 31
	s_lshl_b64 s[0:1], s[30:31], 12
	s_waitcnt lgkmcnt(0)
	v_lshl_add_u64 v[2:3], v[54:55], 0, s[0:1]
	global_load_dwordx4 v[64:67], v[2:3], off
	global_load_dwordx4 v[68:71], v[2:3], off offset:1024
	global_load_dwordx4 v[72:75], v[2:3], off offset:2048
	global_load_dwordx4 v[50:53], v[2:3], off offset:3072
	s_add_i32 s0, s30, s72
	s_ashr_i32 s1, s0, 31
	s_add_i32 s16, s37, s30
	s_lshl_b64 s[14:15], s[0:1], 12
	s_ashr_i32 s17, s16, 31
	v_lshl_add_u64 v[2:3], v[54:55], 0, s[14:15]
	s_lshl_b64 s[14:15], s[16:17], 12
	global_load_dwordx4 v[46:49], v[2:3], off
	global_load_dwordx4 v[42:45], v[2:3], off offset:1024
	global_load_dwordx4 v[38:41], v[2:3], off offset:2048
	global_load_dwordx4 v[34:37], v[2:3], off offset:3072
	v_lshl_add_u64 v[2:3], v[54:55], 0, s[14:15]
	s_mul_i32 s14, s91, 24
	s_add_i32 s14, s14, s30
	s_ashr_i32 s15, s14, 31
	s_lshl_b64 s[34:35], s[14:15], 12
	global_load_dwordx4 v[30:33], v[2:3], off
	global_load_dwordx4 v[26:29], v[2:3], off offset:1024
	global_load_dwordx4 v[22:25], v[2:3], off offset:2048
	global_load_dwordx4 v[18:21], v[2:3], off offset:3072
	v_lshl_add_u64 v[2:3], v[54:55], 0, s[34:35]
	global_load_dwordx4 v[14:17], v[2:3], off
	global_load_dwordx4 v[10:13], v[2:3], off offset:1024
	global_load_dwordx4 v[6:9], v[2:3], off offset:2048
	s_nop 0
	global_load_dwordx4 v[2:5], v[2:3], off offset:3072
	s_lshl_b64 s[34:35], s[30:31], 11
	s_waitcnt vmcnt(15)
	v_mul_f32_e32 v0, v65, v65
	v_mul_f32_e32 v76, v67, v67
	v_fmac_f32_e32 v0, v64, v64
	v_fmac_f32_e32 v76, v66, v66
	v_cvt_pk_bf16_f32 v64, v64, v65
	v_cvt_pk_bf16_f32 v65, v66, v67
	v_lshl_add_u64 v[66:67], v[56:57], 0, s[34:35]
	global_store_dwordx2 v[66:67], v[64:65], off sc1
	s_waitcnt vmcnt(15)
	v_mul_f32_e32 v64, v69, v69
	v_mul_f32_e32 v65, v71, v71
	v_fmac_f32_e32 v64, v68, v68
	v_fmac_f32_e32 v65, v70, v70
	v_add_f32_e32 v0, v0, v76
	v_add_f32_e32 v64, v64, v65
	v_add_f32_e32 v0, v0, v64
	v_cvt_pk_bf16_f32 v64, v68, v69
	v_cvt_pk_bf16_f32 v65, v70, v71
	global_store_dwordx2 v[66:67], v[64:65], off offset:512 sc1
	s_waitcnt vmcnt(15)
	v_mul_f32_e32 v64, v73, v73
	v_mul_f32_e32 v65, v75, v75
	v_fmac_f32_e32 v64, v72, v72
	v_fmac_f32_e32 v65, v74, v74
	v_add_f32_e32 v64, v64, v65
	v_add_f32_e32 v0, v0, v64
	v_cvt_pk_bf16_f32 v64, v72, v73
	v_cvt_pk_bf16_f32 v65, v74, v75
	global_store_dwordx2 v[66:67], v[64:65], off offset:1024 sc1
	s_waitcnt vmcnt(15)
	v_mul_f32_e32 v64, v51, v51
	v_mul_f32_e32 v65, v53, v53
	v_fmac_f32_e32 v64, v50, v50
	v_fmac_f32_e32 v65, v52, v52
	v_add_f32_e32 v64, v64, v65
	v_add_f32_e32 v0, v0, v64
	v_cvt_pk_bf16_f32 v50, v50, v51
	v_cvt_pk_bf16_f32 v51, v52, v53
	global_store_dwordx2 v[66:67], v[50:51], off offset:1536 sc1
	ds_bpermute_b32 v50, v58, v0
	s_waitcnt lgkmcnt(0)
	v_add_f32_e32 v0, v0, v50
	ds_bpermute_b32 v50, v59, v0
	s_waitcnt lgkmcnt(0)
	v_add_f32_e32 v0, v0, v50
	ds_bpermute_b32 v50, v60, v0
	s_waitcnt lgkmcnt(0)
	v_add_f32_e32 v0, v0, v50
	ds_bpermute_b32 v50, v61, v0
	s_waitcnt lgkmcnt(0)
	v_add_f32_e32 v0, v0, v50
	ds_bpermute_b32 v50, v62, v0
	s_waitcnt lgkmcnt(0)
	v_add_f32_e32 v0, v0, v50
	ds_bpermute_b32 v50, v63, v0
	s_and_saveexec_b64 s[34:35], vcc
	s_cbranch_execz .LBB0_826
	s_waitcnt lgkmcnt(0)
	v_add_f32_e32 v0, v0, v50
	v_fma_f32 v0, v0, s40, 0.5
	v_trunc_f32_e32 v0, v0
	v_mul_f32_e32 v50, 0x2f800000, v0
	v_floor_f32_e32 v51, v50
	v_fmac_f32_e32 v0, 0xcf800000, v51
	v_cvt_u32_f32_e32 v50, v0
	v_cvt_u32_f32_e32 v51, v51
	s_lshl_b64 s[30:31], s[30:31], 3
	s_add_u32 s30, s29, s30
	s_addc_u32 s31, s36, s31
	global_store_dwordx2 v1, v[50:51], s[30:31] sc1
.LBB0_826:
	s_or_b64 exec, exec, s[34:35]
	s_lshl_b64 s[30:31], s[0:1], 11
	s_waitcnt vmcnt(15)
	v_mul_f32_e32 v0, v47, v47
	s_waitcnt lgkmcnt(0)
	v_mul_f32_e32 v50, v49, v49
	v_fmac_f32_e32 v0, v46, v46
	v_fmac_f32_e32 v50, v48, v48
	v_cvt_pk_bf16_f32 v46, v46, v47
	v_cvt_pk_bf16_f32 v47, v48, v49
	v_lshl_add_u64 v[48:49], v[56:57], 0, s[30:31]
	global_store_dwordx2 v[48:49], v[46:47], off sc1
	s_waitcnt vmcnt(15)
	v_mul_f32_e32 v46, v43, v43
	v_fmac_f32_e32 v46, v42, v42
	v_cvt_pk_bf16_f32 v42, v42, v43
	v_cvt_pk_bf16_f32 v43, v44, v45
	v_mul_f32_e32 v47, v45, v45
	global_store_dwordx2 v[48:49], v[42:43], off offset:512 sc1
	s_waitcnt vmcnt(15)
	v_mul_f32_e32 v42, v39, v39
	v_fmac_f32_e32 v47, v44, v44
	v_fmac_f32_e32 v42, v38, v38
	v_mul_f32_e32 v43, v41, v41
	v_cvt_pk_bf16_f32 v38, v38, v39
	v_cvt_pk_bf16_f32 v39, v40, v41
	v_add_f32_e32 v0, v0, v50
	v_add_f32_e32 v46, v46, v47
	v_fmac_f32_e32 v43, v40, v40
	global_store_dwordx2 v[48:49], v[38:39], off offset:1024 sc1
	s_waitcnt vmcnt(15)
	v_mul_f32_e32 v38, v35, v35
	v_mul_f32_e32 v39, v37, v37
	v_add_f32_e32 v0, v0, v46
	v_add_f32_e32 v42, v42, v43
	v_fmac_f32_e32 v38, v34, v34
	v_fmac_f32_e32 v39, v36, v36
	v_add_f32_e32 v0, v0, v42
	v_add_f32_e32 v38, v38, v39
	v_add_f32_e32 v0, v0, v38
	v_cvt_pk_bf16_f32 v34, v34, v35
	v_cvt_pk_bf16_f32 v35, v36, v37
	global_store_dwordx2 v[48:49], v[34:35], off offset:1536 sc1
	ds_bpermute_b32 v34, v58, v0
	s_waitcnt lgkmcnt(0)
	v_add_f32_e32 v0, v0, v34
	ds_bpermute_b32 v34, v59, v0
	s_waitcnt lgkmcnt(0)
	v_add_f32_e32 v0, v0, v34
	ds_bpermute_b32 v34, v60, v0
	s_waitcnt lgkmcnt(0)
	v_add_f32_e32 v0, v0, v34
	ds_bpermute_b32 v34, v61, v0
	s_waitcnt lgkmcnt(0)
	v_add_f32_e32 v0, v0, v34
	ds_bpermute_b32 v34, v62, v0
	s_waitcnt lgkmcnt(0)
	v_add_f32_e32 v0, v0, v34
	ds_bpermute_b32 v34, v63, v0
	s_and_saveexec_b64 s[30:31], vcc
	s_cbranch_execz .LBB0_828
	s_waitcnt lgkmcnt(0)
	v_add_f32_e32 v0, v0, v34
	v_fma_f32 v0, v0, s40, 0.5
	v_trunc_f32_e32 v0, v0
	v_mul_f32_e32 v34, 0x2f800000, v0
	v_floor_f32_e32 v35, v34
	v_fmac_f32_e32 v0, 0xcf800000, v35
	v_cvt_u32_f32_e32 v34, v0
	v_cvt_u32_f32_e32 v35, v35
	s_lshl_b64 s[34:35], s[0:1], 3
	s_add_u32 s34, s29, s34
	s_addc_u32 s35, s36, s35
	global_store_dwordx2 v1, v[34:35], s[34:35] sc1
.LBB0_828:
	s_or_b64 exec, exec, s[30:31]
	s_lshl_b64 s[30:31], s[16:17], 11
	s_waitcnt vmcnt(15)
	v_mul_f32_e32 v0, v31, v31
	s_waitcnt lgkmcnt(0)
	v_mul_f32_e32 v34, v33, v33
	v_fmac_f32_e32 v0, v30, v30
	v_fmac_f32_e32 v34, v32, v32
	v_cvt_pk_bf16_f32 v30, v30, v31
	v_cvt_pk_bf16_f32 v31, v32, v33
	v_lshl_add_u64 v[32:33], v[56:57], 0, s[30:31]
	global_store_dwordx2 v[32:33], v[30:31], off sc1
	s_waitcnt vmcnt(15)
	v_mul_f32_e32 v30, v27, v27
	v_fmac_f32_e32 v30, v26, v26
	v_cvt_pk_bf16_f32 v26, v26, v27
	v_cvt_pk_bf16_f32 v27, v28, v29
	v_mul_f32_e32 v31, v29, v29
	global_store_dwordx2 v[32:33], v[26:27], off offset:512 sc1
	s_waitcnt vmcnt(15)
	v_mul_f32_e32 v26, v23, v23
	v_fmac_f32_e32 v31, v28, v28
	v_fmac_f32_e32 v26, v22, v22
	v_mul_f32_e32 v27, v25, v25
	v_cvt_pk_bf16_f32 v22, v22, v23
	v_cvt_pk_bf16_f32 v23, v24, v25
	v_add_f32_e32 v0, v0, v34
	v_add_f32_e32 v30, v30, v31
	v_fmac_f32_e32 v27, v24, v24
	global_store_dwordx2 v[32:33], v[22:23], off offset:1024 sc1
	s_waitcnt vmcnt(15)
	v_mul_f32_e32 v22, v19, v19
	v_mul_f32_e32 v23, v21, v21
	v_add_f32_e32 v0, v0, v30
	v_add_f32_e32 v26, v26, v27
	v_fmac_f32_e32 v22, v18, v18
	v_fmac_f32_e32 v23, v20, v20
	v_add_f32_e32 v0, v0, v26
	v_add_f32_e32 v22, v22, v23
	v_add_f32_e32 v0, v0, v22
	v_cvt_pk_bf16_f32 v18, v18, v19
	v_cvt_pk_bf16_f32 v19, v20, v21
	global_store_dwordx2 v[32:33], v[18:19], off offset:1536 sc1
	ds_bpermute_b32 v18, v58, v0
	s_waitcnt lgkmcnt(0)
	v_add_f32_e32 v0, v0, v18
	ds_bpermute_b32 v18, v59, v0
	s_waitcnt lgkmcnt(0)
	v_add_f32_e32 v0, v0, v18
	ds_bpermute_b32 v18, v60, v0
	s_waitcnt lgkmcnt(0)
	v_add_f32_e32 v0, v0, v18
	ds_bpermute_b32 v18, v61, v0
	s_waitcnt lgkmcnt(0)
	v_add_f32_e32 v0, v0, v18
	ds_bpermute_b32 v18, v62, v0
	s_waitcnt lgkmcnt(0)
	v_add_f32_e32 v0, v0, v18
	ds_bpermute_b32 v18, v63, v0
	s_and_saveexec_b64 s[30:31], vcc
	s_cbranch_execz .LBB0_830
	s_waitcnt lgkmcnt(0)
	v_add_f32_e32 v0, v0, v18
	v_fma_f32 v0, v0, s40, 0.5
	v_trunc_f32_e32 v0, v0
	v_mul_f32_e32 v18, 0x2f800000, v0
	v_floor_f32_e32 v19, v18
	v_fmac_f32_e32 v0, 0xcf800000, v19
	v_cvt_u32_f32_e32 v18, v0
	v_cvt_u32_f32_e32 v19, v19
	s_lshl_b64 s[16:17], s[16:17], 3
	s_add_u32 s16, s29, s16
	s_addc_u32 s17, s36, s17
	global_store_dwordx2 v1, v[18:19], s[16:17] sc1
.LBB0_830:
	s_or_b64 exec, exec, s[30:31]
	s_lshl_b64 s[16:17], s[14:15], 11
	s_waitcnt vmcnt(15)
	v_mul_f32_e32 v0, v15, v15
	s_waitcnt lgkmcnt(0)
	v_mul_f32_e32 v18, v17, v17
	v_fmac_f32_e32 v0, v14, v14
	v_fmac_f32_e32 v18, v16, v16
	v_cvt_pk_bf16_f32 v14, v14, v15
	v_cvt_pk_bf16_f32 v15, v16, v17
	v_lshl_add_u64 v[16:17], v[56:57], 0, s[16:17]
	global_store_dwordx2 v[16:17], v[14:15], off sc1
	s_waitcnt vmcnt(15)
	v_mul_f32_e32 v14, v11, v11
	v_fmac_f32_e32 v14, v10, v10
	v_cvt_pk_bf16_f32 v10, v10, v11
	v_cvt_pk_bf16_f32 v11, v12, v13
	v_mul_f32_e32 v15, v13, v13
	global_store_dwordx2 v[16:17], v[10:11], off offset:512 sc1
	s_waitcnt vmcnt(15)
	v_mul_f32_e32 v10, v7, v7
	v_fmac_f32_e32 v15, v12, v12
	v_fmac_f32_e32 v10, v6, v6
	v_mul_f32_e32 v11, v9, v9
	v_cvt_pk_bf16_f32 v6, v6, v7
	v_cvt_pk_bf16_f32 v7, v8, v9
	v_add_f32_e32 v0, v0, v18
	v_add_f32_e32 v14, v14, v15
	v_fmac_f32_e32 v11, v8, v8
	global_store_dwordx2 v[16:17], v[6:7], off offset:1024 sc1
	s_waitcnt vmcnt(15)
	v_mul_f32_e32 v6, v3, v3
	v_mul_f32_e32 v7, v5, v5
	v_add_f32_e32 v0, v0, v14
	v_add_f32_e32 v10, v10, v11
	v_fmac_f32_e32 v6, v2, v2
	v_fmac_f32_e32 v7, v4, v4
	v_add_f32_e32 v0, v0, v10
	v_add_f32_e32 v6, v6, v7
	v_add_f32_e32 v0, v0, v6
	v_cvt_pk_bf16_f32 v2, v2, v3
	v_cvt_pk_bf16_f32 v3, v4, v5
	global_store_dwordx2 v[16:17], v[2:3], off offset:1536 sc1
	ds_bpermute_b32 v2, v58, v0
	s_waitcnt lgkmcnt(0)
	v_add_f32_e32 v0, v0, v2
	ds_bpermute_b32 v2, v59, v0
	s_waitcnt lgkmcnt(0)
	v_add_f32_e32 v0, v0, v2
	ds_bpermute_b32 v2, v60, v0
	s_waitcnt lgkmcnt(0)
	v_add_f32_e32 v0, v0, v2
	ds_bpermute_b32 v2, v61, v0
	s_waitcnt lgkmcnt(0)
	v_add_f32_e32 v0, v0, v2
	ds_bpermute_b32 v2, v62, v0
	s_waitcnt lgkmcnt(0)
	v_add_f32_e32 v0, v0, v2
	ds_bpermute_b32 v2, v63, v0
	s_and_saveexec_b64 s[16:17], vcc
	s_cbranch_execz .LBB0_823
	s_waitcnt lgkmcnt(0)
	v_add_f32_e32 v0, v0, v2
	v_fma_f32 v0, v0, s40, 0.5
	v_trunc_f32_e32 v0, v0
	v_mul_f32_e32 v2, 0x2f800000, v0
	v_floor_f32_e32 v3, v2
	v_fmac_f32_e32 v0, 0xcf800000, v3
	v_cvt_u32_f32_e32 v2, v0
	v_cvt_u32_f32_e32 v3, v3
	s_lshl_b64 s[14:15], s[14:15], 3
	s_add_u32 s14, s29, s14
	s_addc_u32 s15, s36, s15
	global_store_dwordx2 v1, v[2:3], s[14:15] sc1
	s_branch .LBB0_823

.LBB0_872:
	v_lshlrev_b64 v[226:227], 11, v[212:213]
	v_pk_mul_f32 v[122:123], v[122:123], v[190:191]
	v_cndmask_b32_e64 v0, 0, 1, s[56:57]
	v_lshl_add_u64 v[190:191], s[14:15], 0, v[226:227]
	v_pk_mul_f32 v[128:129], v[128:129], v[222:223]
	v_pk_mul_f32 v[126:127], v[126:127], v[220:221]
	v_pk_mul_f32 v[124:125], v[124:125], v[192:193]
	v_cmp_ne_u32_e64 s[40:41], 1, v0
	s_andn2_b64 vcc, exec, s[56:57]
	v_lshl_add_u64 v[190:191], v[210:211], 1, v[190:191]
	s_cbranch_vccnz .LBB0_874
	v_cvt_pk_bf16_f32 v220, v126, v127
	v_cvt_pk_bf16_f32 v221, v128, v129
	v_cvt_pk_bf16_f32 v222, v122, v123
	v_cvt_pk_bf16_f32 v223, v124, v125
	global_store_dwordx4 v[190:191], v[220:223], off sc1

.LBB0_876:
	v_pk_mul_f32 v[96:97], v[96:97], v[220:221]
	v_pk_mul_f32 v[94:95], v[94:95], v[192:193]
	v_pk_mul_f32 v[92:93], v[92:93], v[188:189]
	s_and_b64 vcc, exec, s[40:41]
	v_pk_mul_f32 v[90:91], v[90:91], v[186:187]
	s_cbranch_vccnz .LBB0_878
	v_cvt_pk_bf16_f32 v186, v94, v95
	v_cvt_pk_bf16_f32 v187, v96, v97
	v_cvt_pk_bf16_f32 v188, v90, v91
	v_cvt_pk_bf16_f32 v189, v92, v93
	global_store_dwordx4 v[190:191], v[186:189], off offset:256 sc1

.LBB0_880:
	v_lshlrev_b64 v[190:191], 11, v[218:219]
	v_pk_mul_f32 v[114:115], v[114:115], v[182:183]
	v_lshl_add_u64 v[182:183], s[14:15], 0, v[190:191]
	v_pk_mul_f32 v[120:121], v[120:121], v[188:189]
	v_pk_mul_f32 v[118:119], v[118:119], v[186:187]
	v_pk_mul_f32 v[116:117], v[116:117], v[184:185]
	s_and_b64 vcc, exec, s[40:41]
	v_lshl_add_u64 v[182:183], v[210:211], 1, v[182:183]
	s_cbranch_vccnz .LBB0_882
	v_cvt_pk_bf16_f32 v184, v118, v119
	v_cvt_pk_bf16_f32 v185, v120, v121
	v_cvt_pk_bf16_f32 v186, v114, v115
	v_cvt_pk_bf16_f32 v187, v116, v117
	global_store_dwordx4 v[182:183], v[184:187], off sc1

.LBB0_884:
	v_pk_mul_f32 v[88:89], v[88:89], v[186:187]
	v_pk_mul_f32 v[86:87], v[86:87], v[184:185]
	v_pk_mul_f32 v[84:85], v[84:85], v[180:181]
	s_and_b64 vcc, exec, s[40:41]
	v_pk_mul_f32 v[82:83], v[82:83], v[178:179]
	s_cbranch_vccnz .LBB0_886
	v_cvt_pk_bf16_f32 v178, v86, v87
	v_cvt_pk_bf16_f32 v179, v88, v89
	v_cvt_pk_bf16_f32 v180, v82, v83
	v_cvt_pk_bf16_f32 v181, v84, v85
	global_store_dwordx4 v[182:183], v[178:181], off offset:256 sc1

.LBB0_888:
	v_lshlrev_b64 v[182:183], 11, v[216:217]
	v_pk_mul_f32 v[106:107], v[106:107], v[174:175]
	v_lshl_add_u64 v[174:175], s[14:15], 0, v[182:183]
	v_pk_mul_f32 v[112:113], v[112:113], v[180:181]
	v_pk_mul_f32 v[110:111], v[110:111], v[178:179]
	v_pk_mul_f32 v[108:109], v[108:109], v[176:177]
	s_and_b64 vcc, exec, s[40:41]
	v_lshl_add_u64 v[174:175], v[210:211], 1, v[174:175]
	s_cbranch_vccnz .LBB0_890
	v_cvt_pk_bf16_f32 v176, v110, v111
	v_cvt_pk_bf16_f32 v177, v112, v113
	v_cvt_pk_bf16_f32 v178, v106, v107
	v_cvt_pk_bf16_f32 v179, v108, v109
	global_store_dwordx4 v[174:175], v[176:179], off sc1

.LBB0_892:
	v_pk_mul_f32 v[80:81], v[80:81], v[178:179]
	v_pk_mul_f32 v[78:79], v[78:79], v[176:177]
	v_pk_mul_f32 v[76:77], v[76:77], v[172:173]
	s_and_b64 vcc, exec, s[40:41]
	v_pk_mul_f32 v[74:75], v[74:75], v[170:171]
	s_cbranch_vccnz .LBB0_894
	v_cvt_pk_bf16_f32 v170, v78, v79
	v_cvt_pk_bf16_f32 v171, v80, v81
	v_cvt_pk_bf16_f32 v172, v74, v75
	v_cvt_pk_bf16_f32 v173, v76, v77
	global_store_dwordx4 v[174:175], v[170:173], off offset:256 sc1

.LBB0_896:
	v_lshlrev_b64 v[174:175], 11, v[214:215]
	v_pk_mul_f32 v[98:99], v[98:99], v[166:167]
	v_lshl_add_u64 v[166:167], s[14:15], 0, v[174:175]
	v_pk_mul_f32 v[104:105], v[104:105], v[172:173]
	v_pk_mul_f32 v[102:103], v[102:103], v[170:171]
	v_pk_mul_f32 v[100:101], v[100:101], v[168:169]
	s_and_b64 vcc, exec, s[40:41]
	v_lshl_add_u64 v[166:167], v[210:211], 1, v[166:167]
	s_cbranch_vccnz .LBB0_898
	v_cvt_pk_bf16_f32 v168, v102, v103
	v_cvt_pk_bf16_f32 v169, v104, v105
	v_cvt_pk_bf16_f32 v170, v98, v99
	v_cvt_pk_bf16_f32 v171, v100, v101
	global_store_dwordx4 v[166:167], v[168:171], off sc1

.LBB0_900:
	v_pk_mul_f32 v[72:73], v[72:73], v[170:171]
	v_pk_mul_f32 v[70:71], v[70:71], v[168:169]
	v_pk_mul_f32 v[68:69], v[68:69], v[164:165]
	s_and_b64 vcc, exec, s[40:41]
	v_pk_mul_f32 v[66:67], v[66:67], v[162:163]
	s_cbranch_vccnz .LBB0_902
	v_cvt_pk_bf16_f32 v162, v70, v71
	v_cvt_pk_bf16_f32 v163, v72, v73
	v_cvt_pk_bf16_f32 v164, v66, v67
	v_cvt_pk_bf16_f32 v165, v68, v69
	global_store_dwordx4 v[166:167], v[162:165], off offset:256 sc1

.LBB0_920:
	v_lshlrev_b64 v[158:159], 11, v[218:219]
	v_lshl_add_u64 v[158:159], s[14:15], 0, v[158:159]
	v_pk_mul_f32 v[64:65], v[64:65], v[222:223]
	v_pk_mul_f32 v[62:63], v[62:63], v[220:221]
	v_pk_mul_f32 v[60:61], v[60:61], v[192:193]
	v_pk_mul_f32 v[58:59], v[58:59], v[190:191]
	s_and_b64 vcc, exec, s[40:41]
	v_lshl_add_u64 v[158:159], v[210:211], 1, v[158:159]
	s_cbranch_vccnz .LBB0_922
	v_cvt_pk_bf16_f32 v190, v62, v63
	v_cvt_pk_bf16_f32 v191, v64, v65
	v_cvt_pk_bf16_f32 v192, v58, v59
	v_cvt_pk_bf16_f32 v193, v60, v61
	global_store_dwordx4 v[158:159], v[190:193], off sc1

.LBB0_924:
	v_pk_mul_f32 v[32:33], v[32:33], v[190:191]
	v_pk_mul_f32 v[30:31], v[30:31], v[160:161]
	v_pk_mul_f32 v[28:29], v[28:29], v[188:189]
	s_and_b64 vcc, exec, s[40:41]
	v_pk_mul_f32 v[26:27], v[26:27], v[186:187]
	s_cbranch_vccnz .LBB0_926
	v_cvt_pk_bf16_f32 v154, v30, v31
	v_cvt_pk_bf16_f32 v155, v32, v33
	v_cvt_pk_bf16_f32 v156, v26, v27
	v_cvt_pk_bf16_f32 v157, v28, v29
	global_store_dwordx4 v[158:159], v[154:157], off offset:256 sc1

.LBB0_928:
	v_lshlrev_b64 v[150:151], 11, v[216:217]
	v_lshl_add_u64 v[150:151], s[14:15], 0, v[150:151]
	v_pk_mul_f32 v[56:57], v[56:57], v[158:159]
	v_pk_mul_f32 v[54:55], v[54:55], v[154:155]
	v_pk_mul_f32 v[52:53], v[52:53], v[160:161]
	v_pk_mul_f32 v[50:51], v[50:51], v[156:157]
	s_and_b64 vcc, exec, s[40:41]
	v_lshl_add_u64 v[150:151], v[210:211], 1, v[150:151]
	s_cbranch_vccnz .LBB0_930
	v_cvt_pk_bf16_f32 v152, v54, v55
	v_cvt_pk_bf16_f32 v153, v56, v57
	v_cvt_pk_bf16_f32 v154, v50, v51
	v_cvt_pk_bf16_f32 v155, v52, v53
	global_store_dwordx4 v[150:151], v[152:155], off sc1

.LBB0_932:
	v_pk_mul_f32 v[24:25], v[24:25], v[156:157]
	v_pk_mul_f32 v[22:23], v[22:23], v[152:153]
	v_pk_mul_f32 v[20:21], v[20:21], v[158:159]
	s_and_b64 vcc, exec, s[40:41]
	v_pk_mul_f32 v[18:19], v[18:19], v[154:155]
	s_cbranch_vccnz .LBB0_934
	v_cvt_pk_bf16_f32 v146, v22, v23
	v_cvt_pk_bf16_f32 v147, v24, v25
	v_cvt_pk_bf16_f32 v148, v18, v19
	v_cvt_pk_bf16_f32 v149, v20, v21
	global_store_dwordx4 v[150:151], v[146:149], off offset:256 sc1

.LBB0_936:
	v_lshlrev_b64 v[142:143], 11, v[214:215]
	v_lshl_add_u64 v[142:143], s[14:15], 0, v[142:143]
	v_pk_mul_f32 v[48:49], v[48:49], v[150:151]
	v_pk_mul_f32 v[46:47], v[46:47], v[146:147]
	v_pk_mul_f32 v[44:45], v[44:45], v[152:153]
	v_pk_mul_f32 v[42:43], v[42:43], v[148:149]
	s_and_b64 vcc, exec, s[40:41]
	v_lshl_add_u64 v[142:143], v[210:211], 1, v[142:143]
	s_cbranch_vccnz .LBB0_938
	v_cvt_pk_bf16_f32 v144, v46, v47
	v_cvt_pk_bf16_f32 v145, v48, v49
	v_cvt_pk_bf16_f32 v146, v42, v43
	v_cvt_pk_bf16_f32 v147, v44, v45
	global_store_dwordx4 v[142:143], v[144:147], off sc1

.LBB0_940:
	v_pk_mul_f32 v[16:17], v[16:17], v[148:149]
	v_pk_mul_f32 v[14:15], v[14:15], v[144:145]
	v_pk_mul_f32 v[12:13], v[12:13], v[150:151]
	s_and_b64 vcc, exec, s[40:41]
	v_pk_mul_f32 v[10:11], v[10:11], v[146:147]
	s_cbranch_vccnz .LBB0_942
	v_cvt_pk_bf16_f32 v138, v14, v15
	v_cvt_pk_bf16_f32 v139, v16, v17
	v_cvt_pk_bf16_f32 v140, v10, v11
	v_cvt_pk_bf16_f32 v141, v12, v13
	global_store_dwordx4 v[142:143], v[138:141], off offset:256 sc1

.LBB0_944:
	v_lshlrev_b64 v[134:135], 11, v[212:213]
	v_lshl_add_u64 v[134:135], s[14:15], 0, v[134:135]
	v_pk_mul_f32 v[40:41], v[40:41], v[142:143]
	v_pk_mul_f32 v[38:39], v[38:39], v[138:139]
	v_pk_mul_f32 v[36:37], v[36:37], v[144:145]
	v_pk_mul_f32 v[34:35], v[34:35], v[140:141]
	s_and_b64 vcc, exec, s[40:41]
	v_lshl_add_u64 v[134:135], v[210:211], 1, v[134:135]
	s_cbranch_vccnz .LBB0_946
	v_cvt_pk_bf16_f32 v136, v38, v39
	v_cvt_pk_bf16_f32 v137, v40, v41
	v_cvt_pk_bf16_f32 v138, v34, v35
	v_cvt_pk_bf16_f32 v139, v36, v37
	global_store_dwordx4 v[134:135], v[136:139], off sc1

.LBB0_948:
	v_pk_mul_f32 v[8:9], v[8:9], v[140:141]
	v_pk_mul_f32 v[6:7], v[6:7], v[136:137]
	v_pk_mul_f32 v[4:5], v[4:5], v[142:143]
	s_and_b64 vcc, exec, s[40:41]
	v_pk_mul_f32 v[2:3], v[2:3], v[138:139]
	s_cbranch_vccnz .LBB0_950
	v_cvt_pk_bf16_f32 v130, v6, v7
	v_cvt_pk_bf16_f32 v131, v8, v9
	v_cvt_pk_bf16_f32 v132, v2, v3
	v_cvt_pk_bf16_f32 v133, v4, v5
	global_store_dwordx4 v[134:135], v[130:133], off offset:256 sc1

.LBB0_1061:
	s_waitcnt vmcnt(0)
	v_ffbh_u32_e32 v159, v157
	v_min_u32_e32 v159, 32, v159
	v_lshlrev_b64 v[156:157], v159, v[156:157]
	v_min_u32_e32 v156, 1, v156
	v_or_b32_e32 v156, v157, v156
	v_cvt_f32_u32_e32 v156, v156
	v_sub_u32_e32 v157, 32, v159
	s_mov_b32 s36, 0x358637bd
	v_mov_b64_e32 v[164:165], s[36:37]
	v_ldexp_f32 v157, v156, v157
	v_ffbh_u32_e32 v156, v155
	v_min_u32_e32 v156, 32, v156
	v_lshlrev_b64 v[154:155], v156, v[154:155]
	v_min_u32_e32 v154, 1, v154
	v_or_b32_e32 v154, v155, v154
	v_cvt_f32_u32_e32 v154, v154
	v_sub_u32_e32 v155, 32, v156
	s_mov_b32 s48, 0x32800000
	s_mov_b32 s29, -1
	v_ldexp_f32 v156, v154, v155
	v_pk_fma_f32 v[154:155], v[156:157], s[48:49], v[164:165] op_sel_hi:[1,0,0]
	v_readlane_b32 s92, v253, 28
	v_mul_f32_e32 v156, 0x4b800000, v155
	v_cmp_gt_f32_e64 s[36:37], s96, v155
	v_cmp_gt_f32_e32 vcc, s96, v154
	v_mbcnt_lo_u32_b32 v0, s29, 0
	v_cndmask_b32_e64 v155, v155, v156, s[36:37]
	v_rsq_f32_e32 v155, v155
	v_mbcnt_hi_u32_b32 v0, s29, v0
	s_lshl_b32 s29, s84, 8
	s_add_i32 s29, s29, s52
	v_mul_f32_e32 v156, 0x45800000, v155
	v_cndmask_b32_e64 v155, v155, v156, s[36:37]
	v_mul_f32_e32 v156, 0x4b800000, v154
	v_cndmask_b32_e32 v154, v154, v156, vcc
	v_rsq_f32_e32 v154, v154
	v_and_or_b32 v158, v0, 15, s29
	v_and_b32_e32 v0, 0x70, v0
	v_ashrrev_i32_e32 v159, 31, v158
	v_mul_f32_e32 v156, 0x45800000, v154
	v_cndmask_b32_e32 v154, v154, v156, vcc
	v_ffbh_u32_e32 v156, v153
	v_min_u32_e32 v156, 32, v156
	v_lshlrev_b64 v[152:153], v156, v[152:153]
	v_min_u32_e32 v152, 1, v152
	v_or_b32_e32 v152, v153, v152
	v_cvt_f32_u32_e32 v152, v152
	v_sub_u32_e32 v153, 32, v156
	s_mov_b32 s89, 0x2e8ba2e9
	s_movk_i32 s90, 0xfea0
	v_ldexp_f32 v153, v152, v153
	v_ffbh_u32_e32 v152, v151
	v_min_u32_e32 v152, 32, v152
	v_lshlrev_b64 v[150:151], v152, v[150:151]
	v_min_u32_e32 v150, 1, v150
	v_or_b32_e32 v150, v151, v150
	v_cvt_f32_u32_e32 v150, v150
	v_sub_u32_e32 v151, 32, v152
	v_readlane_b32 s93, v253, 29
	v_ldexp_f32 v152, v150, v151
	v_pk_fma_f32 v[150:151], v[152:153], s[48:49], v[164:165] op_sel_hi:[1,0,0]
	s_nop 0
	v_mul_f32_e32 v152, 0x4b800000, v151
	v_cmp_gt_f32_e64 s[36:37], s96, v151
	v_cmp_gt_f32_e32 vcc, s96, v150
	s_nop 0
	v_cndmask_b32_e64 v151, v151, v152, s[36:37]
	v_rsq_f32_e32 v151, v151
	s_nop 0
	v_mul_f32_e32 v152, 0x45800000, v151
	v_cndmask_b32_e64 v151, v151, v152, s[36:37]
	v_mul_f32_e32 v152, 0x4b800000, v150
	v_cndmask_b32_e32 v150, v150, v152, vcc
	v_rsq_f32_e32 v150, v150
	s_nop 0
	v_mul_f32_e32 v152, 0x45800000, v150
	v_cndmask_b32_e32 v150, v150, v152, vcc
	v_ffbh_u32_e32 v152, v149
	v_min_u32_e32 v152, 32, v152
	v_lshlrev_b64 v[148:149], v152, v[148:149]
	v_min_u32_e32 v148, 1, v148
	v_or_b32_e32 v148, v149, v148
	v_cvt_f32_u32_e32 v148, v148
	v_sub_u32_e32 v149, 32, v152
	v_ldexp_f32 v149, v148, v149
	v_ffbh_u32_e32 v148, v147
	v_min_u32_e32 v148, 32, v148
	v_lshlrev_b64 v[146:147], v148, v[146:147]
	v_min_u32_e32 v146, 1, v146
	v_or_b32_e32 v146, v147, v146
	v_cvt_f32_u32_e32 v146, v146
	v_sub_u32_e32 v147, 32, v148
	v_ldexp_f32 v148, v146, v147
	v_pk_fma_f32 v[146:147], v[148:149], s[48:49], v[164:165] op_sel_hi:[1,0,0]
	s_nop 0
	v_mul_f32_e32 v148, 0x4b800000, v147
	v_cmp_gt_f32_e64 s[36:37], s96, v147
	v_cmp_gt_f32_e32 vcc, s96, v146
	s_nop 0
	v_cndmask_b32_e64 v147, v147, v148, s[36:37]
	v_rsq_f32_e32 v147, v147
	s_nop 0
	v_mul_f32_e32 v148, 0x45800000, v147
	v_cndmask_b32_e64 v149, v147, v148, s[36:37]
	v_mul_f32_e32 v147, 0x4b800000, v146
	v_cndmask_b32_e32 v146, v146, v147, vcc
	v_rsq_f32_e32 v146, v146
	s_nop 0
	v_mul_f32_e32 v147, 0x45800000, v146
	v_cndmask_b32_e32 v148, v146, v147, vcc
	v_ffbh_u32_e32 v146, v145
	v_min_u32_e32 v146, 32, v146
	v_lshlrev_b64 v[144:145], v146, v[144:145]
	v_min_u32_e32 v144, 1, v144
	v_or_b32_e32 v144, v145, v144
	v_cvt_f32_u32_e32 v144, v144
	v_sub_u32_e32 v145, 32, v146
	v_ldexp_f32 v145, v144, v145
	v_ffbh_u32_e32 v144, v143
	v_min_u32_e32 v144, 32, v144
	v_lshlrev_b64 v[142:143], v144, v[142:143]
	v_min_u32_e32 v142, 1, v142
	v_or_b32_e32 v142, v143, v142
	v_cvt_f32_u32_e32 v142, v142
	v_sub_u32_e32 v143, 32, v144
	v_ldexp_f32 v144, v142, v143
	v_pk_fma_f32 v[142:143], v[144:145], s[48:49], v[164:165] op_sel_hi:[1,0,0]
	s_nop 0
	v_mul_f32_e32 v144, 0x4b800000, v143
	v_cmp_gt_f32_e64 s[36:37], s96, v143
	v_cmp_gt_f32_e32 vcc, s96, v142
	s_nop 0
	v_cndmask_b32_e64 v143, v143, v144, s[36:37]
	v_rsq_f32_e32 v143, v143
	s_nop 0
	v_mul_f32_e32 v144, 0x45800000, v143
	v_cndmask_b32_e64 v147, v143, v144, s[36:37]
	s_ashr_i32 s36, s83, 2
	s_ashr_i32 s37, s36, 31
	s_lshl_b64 s[36:37], s[36:37], 25
	s_add_u32 s29, s60, s36
	s_addc_u32 s36, s61, s37
	s_lshl_b32 s37, s83, 9
	s_and_b32 s37, s37, 0x600
	s_add_u32 s29, s29, s37
	s_addc_u32 s37, s36, 0
	s_add_u32 s36, s29, s82
	s_addc_u32 s37, s37, 0
	v_lshl_add_u64 v[144:145], s[36:37], 0, v[0:1]
	v_mul_f32_e32 v0, 0xbfb8aa3b, v155
	v_pk_mul_f32 v[122:123], v[0:1], v[122:123] op_sel_hi:[0,1]
	v_exp_f32_e32 v122, v122
	v_pk_mul_f32 v[124:125], v[0:1], v[124:125] op_sel_hi:[0,1]
	v_pk_mul_f32 v[128:129], v[0:1], v[128:129] op_sel_hi:[0,1]
	v_pk_mul_f32 v[126:127], v[0:1], v[126:127] op_sel_hi:[0,1]
	v_add_f32_e32 v122, 1.0, v122
	v_rcp_f32_e32 v152, v122
	v_exp_f32_e32 v122, v123
	v_exp_f32_e32 v126, v126
	v_exp_f32_e32 v127, v127
	v_exp_f32_e32 v128, v128
	v_add_f32_e32 v122, 1.0, v122
	v_rcp_f32_e32 v153, v122
	v_exp_f32_e32 v122, v124
	v_exp_f32_e32 v129, v129
	v_mul_f32_e32 v143, 0x4b800000, v142
	v_cndmask_b32_e32 v142, v142, v143, vcc
	v_add_f32_e32 v122, 1.0, v122
	v_rcp_f32_e32 v155, v122
	v_exp_f32_e32 v122, v125
	v_rsq_f32_e32 v142, v142
	v_add_f32_e32 v126, 1.0, v126
	v_add_f32_e32 v127, 1.0, v127
	v_add_f32_e32 v128, 1.0, v128
	v_add_f32_e32 v129, 1.0, v129
	v_add_f32_e32 v122, 1.0, v122
	v_pk_mul_f32 v[114:115], v[0:1], v[114:115] op_sel_hi:[0,1]
	v_rcp_f32_e32 v126, v126
	v_rcp_f32_e32 v127, v127
	v_rcp_f32_e32 v128, v128
	v_rcp_f32_e32 v129, v129
	v_rcp_f32_e32 v125, v122
	v_pk_mul_f32 v[120:121], v[0:1], v[120:121] op_sel_hi:[0,1]
	v_pk_mul_f32 v[118:119], v[0:1], v[118:119] op_sel_hi:[0,1]
	v_pk_mul_f32 v[116:117], v[0:1], v[116:117] op_sel_hi:[0,1]
	v_exp_f32_e32 v0, v114
	v_exp_f32_e32 v114, v115
	v_mul_f32_e32 v143, 0x45800000, v142
	v_cndmask_b32_e32 v146, v142, v143, vcc
	v_lshlrev_b64 v[142:143], 11, v[158:159]
	v_lshl_add_u64 v[142:143], v[144:145], 0, v[142:143]
	v_cvt_pk_bf16_f32 v122, v126, v127
	v_cvt_pk_bf16_f32 v123, v128, v129
	v_cvt_pk_bf16_f32 v124, v152, v153
	v_cvt_pk_bf16_f32 v125, v155, v125
	v_add_f32_e32 v114, 1.0, v114
	global_store_dwordx4 v[142:143], v[122:125], off sc1
	v_add_f32_e32 v0, 1.0, v0
	v_rcp_f32_e32 v0, v0
	v_rcp_f32_e32 v122, v114
	v_exp_f32_e32 v114, v116
	v_exp_f32_e32 v118, v118
	v_exp_f32_e32 v119, v119
	v_exp_f32_e32 v120, v120
	v_add_f32_e32 v114, 1.0, v114
	v_exp_f32_e32 v121, v121
	v_rcp_f32_e32 v123, v114
	v_exp_f32_e32 v114, v117
	v_cvt_pk_bf16_f32 v116, v0, v122
	v_mul_f32_e32 v0, 0xbfb8aa3b, v154
	v_add_f32_e32 v118, 1.0, v118
	v_add_f32_e32 v119, 1.0, v119
	v_add_f32_e32 v120, 1.0, v120
	v_add_f32_e32 v121, 1.0, v121
	v_add_f32_e32 v114, 1.0, v114
	v_pk_mul_f32 v[106:107], v[0:1], v[106:107] op_sel_hi:[0,1]
	v_rcp_f32_e32 v118, v118
	v_rcp_f32_e32 v119, v119
	v_rcp_f32_e32 v120, v120
	v_rcp_f32_e32 v121, v121
	v_rcp_f32_e32 v117, v114
	v_exp_f32_e32 v106, v106
	v_cvt_pk_bf16_f32 v114, v118, v119
	v_cvt_pk_bf16_f32 v115, v120, v121
	v_cvt_pk_bf16_f32 v117, v123, v117
	v_add_f32_e32 v106, 1.0, v106
	global_store_dwordx4 v[142:143], v[114:117], off offset:256 sc1
	v_pk_mul_f32 v[108:109], v[0:1], v[108:109] op_sel_hi:[0,1]
	v_pk_mul_f32 v[112:113], v[0:1], v[112:113] op_sel_hi:[0,1]
	v_rcp_f32_e32 v116, v106
	v_exp_f32_e32 v106, v107
	v_pk_mul_f32 v[110:111], v[0:1], v[110:111] op_sel_hi:[0,1]
	v_exp_f32_e32 v110, v110
	v_exp_f32_e32 v111, v111
	v_add_f32_e32 v106, 1.0, v106
	v_rcp_f32_e32 v117, v106
	v_exp_f32_e32 v106, v108
	v_exp_f32_e32 v112, v112
	v_exp_f32_e32 v113, v113
	v_add_f32_e32 v110, 1.0, v110
	v_add_f32_e32 v106, 1.0, v106
	v_rcp_f32_e32 v118, v106
	v_exp_f32_e32 v106, v109
	v_add_f32_e32 v111, 1.0, v111
	v_add_f32_e32 v112, 1.0, v112
	v_add_f32_e32 v113, 1.0, v113
	v_add_f32_e32 v106, 1.0, v106
	v_pk_mul_f32 v[98:99], v[0:1], v[98:99] op_sel_hi:[0,1]
	v_rcp_f32_e32 v110, v110
	v_rcp_f32_e32 v111, v111
	v_rcp_f32_e32 v112, v112
	v_rcp_f32_e32 v113, v113
	v_rcp_f32_e32 v109, v106
	v_pk_mul_f32 v[104:105], v[0:1], v[104:105] op_sel_hi:[0,1]
	v_pk_mul_f32 v[102:103], v[0:1], v[102:103] op_sel_hi:[0,1]
	v_pk_mul_f32 v[100:101], v[0:1], v[100:101] op_sel_hi:[0,1]
	v_exp_f32_e32 v0, v98
	v_exp_f32_e32 v98, v99
	v_or_b32_e32 v114, 16, v158
	v_ashrrev_i32_e32 v115, 31, v114
	v_lshlrev_b64 v[114:115], 11, v[114:115]
	v_lshl_add_u64 v[114:115], v[144:145], 0, v[114:115]
	v_cvt_pk_bf16_f32 v106, v110, v111
	v_cvt_pk_bf16_f32 v107, v112, v113
	v_cvt_pk_bf16_f32 v108, v116, v117
	v_cvt_pk_bf16_f32 v109, v118, v109
	v_add_f32_e32 v98, 1.0, v98
	global_store_dwordx4 v[114:115], v[106:109], off sc1
	v_add_f32_e32 v0, 1.0, v0
	v_rcp_f32_e32 v0, v0
	v_rcp_f32_e32 v106, v98
	v_exp_f32_e32 v98, v100
	v_exp_f32_e32 v102, v102
	v_exp_f32_e32 v103, v103
	v_exp_f32_e32 v104, v104
	v_add_f32_e32 v98, 1.0, v98
	v_exp_f32_e32 v105, v105
	v_rcp_f32_e32 v107, v98
	v_exp_f32_e32 v98, v101
	v_cvt_pk_bf16_f32 v100, v0, v106
	v_mul_f32_e32 v0, 0xbfb8aa3b, v151
	v_add_f32_e32 v102, 1.0, v102
	v_add_f32_e32 v103, 1.0, v103
	v_add_f32_e32 v104, 1.0, v104
	v_add_f32_e32 v105, 1.0, v105
	v_add_f32_e32 v98, 1.0, v98
	v_pk_mul_f32 v[90:91], v[0:1], v[90:91] op_sel_hi:[0,1]
	v_rcp_f32_e32 v102, v102
	v_rcp_f32_e32 v103, v103
	v_rcp_f32_e32 v104, v104
	v_rcp_f32_e32 v105, v105
	v_rcp_f32_e32 v101, v98
	v_exp_f32_e32 v90, v90
	v_cvt_pk_bf16_f32 v98, v102, v103
	v_cvt_pk_bf16_f32 v99, v104, v105
	v_cvt_pk_bf16_f32 v101, v107, v101
	v_add_f32_e32 v90, 1.0, v90
	global_store_dwordx4 v[114:115], v[98:101], off offset:256 sc1
	v_pk_mul_f32 v[92:93], v[0:1], v[92:93] op_sel_hi:[0,1]
	v_pk_mul_f32 v[96:97], v[0:1], v[96:97] op_sel_hi:[0,1]
	v_rcp_f32_e32 v100, v90
	v_exp_f32_e32 v90, v91
	v_pk_mul_f32 v[94:95], v[0:1], v[94:95] op_sel_hi:[0,1]
	v_exp_f32_e32 v94, v94
	v_exp_f32_e32 v95, v95
	v_add_f32_e32 v90, 1.0, v90
	v_rcp_f32_e32 v101, v90
	v_exp_f32_e32 v90, v92
	v_exp_f32_e32 v96, v96
	v_exp_f32_e32 v97, v97
	v_add_f32_e32 v94, 1.0, v94
	v_add_f32_e32 v90, 1.0, v90
	v_rcp_f32_e32 v102, v90
	v_exp_f32_e32 v90, v93
	v_add_f32_e32 v95, 1.0, v95
	v_add_f32_e32 v96, 1.0, v96
	v_add_f32_e32 v97, 1.0, v97
	v_add_f32_e32 v90, 1.0, v90
	v_pk_mul_f32 v[82:83], v[0:1], v[82:83] op_sel_hi:[0,1]
	v_rcp_f32_e32 v94, v94
	v_rcp_f32_e32 v95, v95
	v_rcp_f32_e32 v96, v96
	v_rcp_f32_e32 v97, v97
	v_rcp_f32_e32 v93, v90
	v_pk_mul_f32 v[88:89], v[0:1], v[88:89] op_sel_hi:[0,1]
	v_pk_mul_f32 v[86:87], v[0:1], v[86:87] op_sel_hi:[0,1]
	v_pk_mul_f32 v[84:85], v[0:1], v[84:85] op_sel_hi:[0,1]
	v_exp_f32_e32 v0, v82
	v_exp_f32_e32 v82, v83
	v_or_b32_e32 v98, 32, v158
	v_ashrrev_i32_e32 v99, 31, v98
	v_lshlrev_b64 v[98:99], 11, v[98:99]
	v_lshl_add_u64 v[98:99], v[144:145], 0, v[98:99]
	v_cvt_pk_bf16_f32 v90, v94, v95
	v_cvt_pk_bf16_f32 v91, v96, v97
	v_cvt_pk_bf16_f32 v92, v100, v101
	v_cvt_pk_bf16_f32 v93, v102, v93
	v_add_f32_e32 v82, 1.0, v82
	global_store_dwordx4 v[98:99], v[90:93], off sc1
	v_add_f32_e32 v0, 1.0, v0
	v_rcp_f32_e32 v0, v0
	v_rcp_f32_e32 v90, v82
	v_exp_f32_e32 v82, v84
	v_exp_f32_e32 v86, v86
	v_exp_f32_e32 v87, v87
	v_exp_f32_e32 v88, v88
	v_add_f32_e32 v82, 1.0, v82
	v_exp_f32_e32 v89, v89
	v_rcp_f32_e32 v91, v82
	v_exp_f32_e32 v82, v85
	v_cvt_pk_bf16_f32 v84, v0, v90
	v_mul_f32_e32 v0, 0xbfb8aa3b, v150
	v_add_f32_e32 v86, 1.0, v86
	v_add_f32_e32 v87, 1.0, v87
	v_add_f32_e32 v88, 1.0, v88
	v_add_f32_e32 v89, 1.0, v89
	v_add_f32_e32 v82, 1.0, v82
	v_pk_mul_f32 v[74:75], v[0:1], v[74:75] op_sel_hi:[0,1]
	v_rcp_f32_e32 v86, v86
	v_rcp_f32_e32 v87, v87
	v_rcp_f32_e32 v88, v88
	v_rcp_f32_e32 v89, v89
	v_rcp_f32_e32 v85, v82
	v_exp_f32_e32 v74, v74
	v_cvt_pk_bf16_f32 v82, v86, v87
	v_cvt_pk_bf16_f32 v83, v88, v89
	v_cvt_pk_bf16_f32 v85, v91, v85
	v_add_f32_e32 v74, 1.0, v74
	global_store_dwordx4 v[98:99], v[82:85], off offset:256 sc1
	v_pk_mul_f32 v[76:77], v[0:1], v[76:77] op_sel_hi:[0,1]
	v_pk_mul_f32 v[80:81], v[0:1], v[80:81] op_sel_hi:[0,1]
	v_rcp_f32_e32 v84, v74
	v_exp_f32_e32 v74, v75
	v_pk_mul_f32 v[78:79], v[0:1], v[78:79] op_sel_hi:[0,1]
	v_exp_f32_e32 v78, v78
	v_exp_f32_e32 v79, v79
	v_add_f32_e32 v74, 1.0, v74
	v_rcp_f32_e32 v85, v74
	v_exp_f32_e32 v74, v76
	v_exp_f32_e32 v80, v80
	v_exp_f32_e32 v81, v81
	v_add_f32_e32 v78, 1.0, v78
	v_add_f32_e32 v74, 1.0, v74
	v_rcp_f32_e32 v86, v74
	v_exp_f32_e32 v74, v77
	v_add_f32_e32 v79, 1.0, v79
	v_add_f32_e32 v80, 1.0, v80
	v_add_f32_e32 v81, 1.0, v81
	v_add_f32_e32 v74, 1.0, v74
	v_pk_mul_f32 v[66:67], v[0:1], v[66:67] op_sel_hi:[0,1]
	v_rcp_f32_e32 v78, v78
	v_rcp_f32_e32 v79, v79
	v_rcp_f32_e32 v80, v80
	v_rcp_f32_e32 v81, v81
	v_rcp_f32_e32 v77, v74
	v_pk_mul_f32 v[72:73], v[0:1], v[72:73] op_sel_hi:[0,1]
	v_pk_mul_f32 v[70:71], v[0:1], v[70:71] op_sel_hi:[0,1]
	v_pk_mul_f32 v[68:69], v[0:1], v[68:69] op_sel_hi:[0,1]
	v_exp_f32_e32 v0, v66
	v_exp_f32_e32 v66, v67
	v_or_b32_e32 v82, 48, v158
	v_ashrrev_i32_e32 v83, 31, v82
	v_lshlrev_b64 v[82:83], 11, v[82:83]
	v_lshl_add_u64 v[82:83], v[144:145], 0, v[82:83]
	v_cvt_pk_bf16_f32 v74, v78, v79
	v_cvt_pk_bf16_f32 v75, v80, v81
	v_cvt_pk_bf16_f32 v76, v84, v85
	v_cvt_pk_bf16_f32 v77, v86, v77
	v_add_f32_e32 v66, 1.0, v66
	global_store_dwordx4 v[82:83], v[74:77], off sc1
	v_add_f32_e32 v0, 1.0, v0
	v_rcp_f32_e32 v0, v0
	v_rcp_f32_e32 v74, v66
	v_exp_f32_e32 v66, v68
	v_exp_f32_e32 v70, v70
	v_exp_f32_e32 v71, v71
	v_exp_f32_e32 v72, v72
	v_add_f32_e32 v66, 1.0, v66
	v_exp_f32_e32 v73, v73
	v_rcp_f32_e32 v75, v66
	v_exp_f32_e32 v66, v69
	v_cvt_pk_bf16_f32 v68, v0, v74
	v_mul_f32_e32 v0, 0xbfb8aa3b, v149
	v_add_f32_e32 v70, 1.0, v70
	v_add_f32_e32 v71, 1.0, v71
	v_add_f32_e32 v72, 1.0, v72
	v_add_f32_e32 v73, 1.0, v73
	v_add_f32_e32 v66, 1.0, v66
	v_pk_mul_f32 v[58:59], v[0:1], v[58:59] op_sel_hi:[0,1]
	v_rcp_f32_e32 v70, v70
	v_rcp_f32_e32 v71, v71
	v_rcp_f32_e32 v72, v72
	v_rcp_f32_e32 v73, v73
	v_rcp_f32_e32 v69, v66
	v_exp_f32_e32 v58, v58
	v_cvt_pk_bf16_f32 v66, v70, v71
	v_cvt_pk_bf16_f32 v67, v72, v73
	v_cvt_pk_bf16_f32 v69, v75, v69
	v_add_f32_e32 v58, 1.0, v58
	global_store_dwordx4 v[82:83], v[66:69], off offset:256 sc1
	v_pk_mul_f32 v[60:61], v[0:1], v[60:61] op_sel_hi:[0,1]
	v_pk_mul_f32 v[62:63], v[0:1], v[62:63] op_sel_hi:[0,1]
	v_rcp_f32_e32 v68, v58
	v_exp_f32_e32 v58, v59
	v_pk_mul_f32 v[64:65], v[0:1], v[64:65] op_sel_hi:[0,1]
	v_exp_f32_e32 v62, v62
	v_exp_f32_e32 v63, v63
	v_add_f32_e32 v58, 1.0, v58
	v_rcp_f32_e32 v69, v58
	v_exp_f32_e32 v58, v60
	v_exp_f32_e32 v64, v64
	v_exp_f32_e32 v65, v65
	v_add_f32_e32 v62, 1.0, v62
	v_add_f32_e32 v58, 1.0, v58
	v_rcp_f32_e32 v70, v58
	v_exp_f32_e32 v58, v61
	v_add_f32_e32 v63, 1.0, v63
	v_rcp_f32_e32 v62, v62
	v_rcp_f32_e32 v63, v63
	v_add_f32_e32 v64, 1.0, v64
	v_add_f32_e32 v65, 1.0, v65
	v_add_f32_e32 v58, 1.0, v58
	v_pk_mul_f32 v[50:51], v[0:1], v[50:51] op_sel_hi:[0,1]
	v_rcp_f32_e32 v64, v64
	v_rcp_f32_e32 v65, v65
	v_rcp_f32_e32 v61, v58
	v_pk_mul_f32 v[56:57], v[0:1], v[56:57] op_sel_hi:[0,1]
	v_pk_mul_f32 v[54:55], v[0:1], v[54:55] op_sel_hi:[0,1]
	v_pk_mul_f32 v[52:53], v[0:1], v[52:53] op_sel_hi:[0,1]
	v_exp_f32_e32 v0, v50
	v_exp_f32_e32 v50, v51
	s_mov_b32 s29, 0x40000
	v_cvt_pk_bf16_f32 v58, v62, v63
	v_add_co_u32_e32 v62, vcc, s29, v142
	v_cvt_pk_bf16_f32 v59, v64, v65
	v_cvt_pk_bf16_f32 v60, v68, v69
	v_cvt_pk_bf16_f32 v61, v70, v61
	v_addc_co_u32_e32 v63, vcc, 0, v143, vcc
	v_add_f32_e32 v50, 1.0, v50
	global_store_dwordx4 v[62:63], v[58:61], off sc1
	v_add_f32_e32 v0, 1.0, v0
	v_rcp_f32_e32 v0, v0
	v_rcp_f32_e32 v58, v50
	v_exp_f32_e32 v50, v52
	v_exp_f32_e32 v54, v54
	v_exp_f32_e32 v55, v55
	v_exp_f32_e32 v56, v56
	v_add_f32_e32 v50, 1.0, v50
	v_exp_f32_e32 v57, v57
	v_rcp_f32_e32 v59, v50
	v_exp_f32_e32 v50, v53
	v_cvt_pk_bf16_f32 v52, v0, v58
	v_mul_f32_e32 v0, 0xbfb8aa3b, v148
	v_add_f32_e32 v54, 1.0, v54
	v_add_f32_e32 v55, 1.0, v55
	v_add_f32_e32 v56, 1.0, v56
	v_add_f32_e32 v57, 1.0, v57
	v_add_f32_e32 v50, 1.0, v50
	v_pk_mul_f32 v[42:43], v[0:1], v[42:43] op_sel_hi:[0,1]
	v_rcp_f32_e32 v54, v54
	v_rcp_f32_e32 v55, v55
	v_rcp_f32_e32 v56, v56
	v_rcp_f32_e32 v57, v57
	v_rcp_f32_e32 v53, v50
	v_exp_f32_e32 v42, v42
	v_lshl_add_u64 v[66:67], v[142:143], 0, s[20:21]
	v_cvt_pk_bf16_f32 v50, v54, v55
	v_cvt_pk_bf16_f32 v51, v56, v57
	v_cvt_pk_bf16_f32 v53, v59, v53
	v_add_f32_e32 v42, 1.0, v42
	global_store_dwordx4 v[66:67], v[50:53], off offset:256 sc1
	v_pk_mul_f32 v[44:45], v[0:1], v[44:45] op_sel_hi:[0,1]
	v_pk_mul_f32 v[46:47], v[0:1], v[46:47] op_sel_hi:[0,1]
	v_rcp_f32_e32 v52, v42
	v_exp_f32_e32 v42, v43
	v_pk_mul_f32 v[48:49], v[0:1], v[48:49] op_sel_hi:[0,1]
	v_exp_f32_e32 v46, v46
	v_exp_f32_e32 v47, v47
	v_add_f32_e32 v42, 1.0, v42
	v_rcp_f32_e32 v53, v42
	v_exp_f32_e32 v42, v44
	v_exp_f32_e32 v48, v48
	v_exp_f32_e32 v49, v49
	v_add_f32_e32 v46, 1.0, v46
	v_add_f32_e32 v42, 1.0, v42
	v_rcp_f32_e32 v54, v42
	v_exp_f32_e32 v42, v45
	v_add_f32_e32 v47, 1.0, v47
	v_rcp_f32_e32 v46, v46
	v_rcp_f32_e32 v47, v47
	v_add_f32_e32 v48, 1.0, v48
	v_add_f32_e32 v49, 1.0, v49
	v_add_f32_e32 v42, 1.0, v42
	v_pk_mul_f32 v[34:35], v[0:1], v[34:35] op_sel_hi:[0,1]
	v_rcp_f32_e32 v48, v48
	v_rcp_f32_e32 v49, v49
	v_rcp_f32_e32 v45, v42
	v_pk_mul_f32 v[40:41], v[0:1], v[40:41] op_sel_hi:[0,1]
	v_pk_mul_f32 v[38:39], v[0:1], v[38:39] op_sel_hi:[0,1]
	v_pk_mul_f32 v[36:37], v[0:1], v[36:37] op_sel_hi:[0,1]
	v_exp_f32_e32 v0, v34
	v_exp_f32_e32 v34, v35
	s_mov_b32 s29, 0x48000
	v_cvt_pk_bf16_f32 v42, v46, v47
	v_add_co_u32_e32 v46, vcc, s29, v142
	v_cvt_pk_bf16_f32 v43, v48, v49
	v_cvt_pk_bf16_f32 v44, v52, v53
	v_cvt_pk_bf16_f32 v45, v54, v45
	v_addc_co_u32_e32 v47, vcc, 0, v143, vcc
	v_add_f32_e32 v34, 1.0, v34
	global_store_dwordx4 v[46:47], v[42:45], off sc1
	v_add_f32_e32 v0, 1.0, v0
	v_rcp_f32_e32 v0, v0
	v_rcp_f32_e32 v42, v34
	v_exp_f32_e32 v34, v36
	v_exp_f32_e32 v38, v38
	v_exp_f32_e32 v39, v39
	v_exp_f32_e32 v40, v40
	v_add_f32_e32 v34, 1.0, v34
	v_exp_f32_e32 v41, v41
	v_rcp_f32_e32 v43, v34
	v_exp_f32_e32 v34, v37
	v_cvt_pk_bf16_f32 v36, v0, v42
	v_mul_f32_e32 v0, 0xbfb8aa3b, v147
	v_add_f32_e32 v38, 1.0, v38
	v_add_f32_e32 v39, 1.0, v39
	v_add_f32_e32 v40, 1.0, v40
	v_add_f32_e32 v41, 1.0, v41
	v_add_f32_e32 v34, 1.0, v34
	v_pk_mul_f32 v[26:27], v[0:1], v[26:27] op_sel_hi:[0,1]
	v_rcp_f32_e32 v38, v38
	v_rcp_f32_e32 v39, v39
	v_rcp_f32_e32 v40, v40
	v_rcp_f32_e32 v41, v41
	v_rcp_f32_e32 v37, v34
	v_exp_f32_e32 v26, v26
	s_mov_b64 s[36:37], 0x48000
	v_lshl_add_u64 v[50:51], v[142:143], 0, s[36:37]
	v_cvt_pk_bf16_f32 v34, v38, v39
	v_cvt_pk_bf16_f32 v35, v40, v41
	v_cvt_pk_bf16_f32 v37, v43, v37
	v_add_f32_e32 v26, 1.0, v26
	global_store_dwordx4 v[50:51], v[34:37], off offset:256 sc1
	v_pk_mul_f32 v[28:29], v[0:1], v[28:29] op_sel_hi:[0,1]
	v_pk_mul_f32 v[30:31], v[0:1], v[30:31] op_sel_hi:[0,1]
	v_rcp_f32_e32 v36, v26
	v_exp_f32_e32 v26, v27
	v_pk_mul_f32 v[32:33], v[0:1], v[32:33] op_sel_hi:[0,1]
	v_exp_f32_e32 v30, v30
	v_exp_f32_e32 v31, v31
	v_add_f32_e32 v26, 1.0, v26
	v_rcp_f32_e32 v37, v26
	v_exp_f32_e32 v26, v28
	v_exp_f32_e32 v32, v32
	v_exp_f32_e32 v33, v33
	v_add_f32_e32 v30, 1.0, v30
	v_add_f32_e32 v26, 1.0, v26
	v_rcp_f32_e32 v38, v26
	v_exp_f32_e32 v26, v29
	v_add_f32_e32 v31, 1.0, v31
	v_rcp_f32_e32 v30, v30
	v_rcp_f32_e32 v31, v31
	v_add_f32_e32 v32, 1.0, v32
	v_add_f32_e32 v33, 1.0, v33
	v_add_f32_e32 v26, 1.0, v26
	v_pk_mul_f32 v[18:19], v[0:1], v[18:19] op_sel_hi:[0,1]
	v_rcp_f32_e32 v32, v32
	v_rcp_f32_e32 v33, v33
	v_rcp_f32_e32 v29, v26
	v_pk_mul_f32 v[24:25], v[0:1], v[24:25] op_sel_hi:[0,1]
	v_pk_mul_f32 v[22:23], v[0:1], v[22:23] op_sel_hi:[0,1]
	v_pk_mul_f32 v[20:21], v[0:1], v[20:21] op_sel_hi:[0,1]
	v_exp_f32_e32 v0, v18
	v_exp_f32_e32 v18, v19
	s_mov_b32 s29, 0x50000
	v_cvt_pk_bf16_f32 v26, v30, v31
	v_add_co_u32_e32 v30, vcc, s29, v142
	v_cvt_pk_bf16_f32 v27, v32, v33
	v_cvt_pk_bf16_f32 v28, v36, v37
	v_cvt_pk_bf16_f32 v29, v38, v29
	v_addc_co_u32_e32 v31, vcc, 0, v143, vcc
	v_add_f32_e32 v18, 1.0, v18
	global_store_dwordx4 v[30:31], v[26:29], off sc1
	v_add_f32_e32 v0, 1.0, v0
	v_rcp_f32_e32 v0, v0
	v_rcp_f32_e32 v26, v18
	v_exp_f32_e32 v18, v20
	v_exp_f32_e32 v22, v22
	v_exp_f32_e32 v23, v23
	v_exp_f32_e32 v24, v24
	v_add_f32_e32 v18, 1.0, v18
	v_exp_f32_e32 v25, v25
	v_rcp_f32_e32 v27, v18
	v_exp_f32_e32 v18, v21
	v_cvt_pk_bf16_f32 v20, v0, v26
	v_mul_f32_e32 v0, 0xbfb8aa3b, v146
	v_add_f32_e32 v22, 1.0, v22
	v_add_f32_e32 v23, 1.0, v23
	v_add_f32_e32 v24, 1.0, v24
	v_add_f32_e32 v25, 1.0, v25
	v_add_f32_e32 v18, 1.0, v18
	v_pk_mul_f32 v[10:11], v[0:1], v[10:11] op_sel_hi:[0,1]
	v_rcp_f32_e32 v22, v22
	v_rcp_f32_e32 v23, v23
	v_rcp_f32_e32 v24, v24
	v_rcp_f32_e32 v25, v25
	v_rcp_f32_e32 v21, v18
	v_exp_f32_e32 v10, v10
	v_lshl_add_u64 v[34:35], v[142:143], 0, s[22:23]
	v_cvt_pk_bf16_f32 v18, v22, v23
	v_cvt_pk_bf16_f32 v19, v24, v25
	v_cvt_pk_bf16_f32 v21, v27, v21
	v_add_f32_e32 v10, 1.0, v10
	global_store_dwordx4 v[34:35], v[18:21], off offset:256 sc1
	v_pk_mul_f32 v[12:13], v[0:1], v[12:13] op_sel_hi:[0,1]
	v_pk_mul_f32 v[14:15], v[0:1], v[14:15] op_sel_hi:[0,1]
	v_rcp_f32_e32 v20, v10
	v_exp_f32_e32 v10, v11
	v_pk_mul_f32 v[16:17], v[0:1], v[16:17] op_sel_hi:[0,1]
	v_exp_f32_e32 v14, v14
	v_exp_f32_e32 v15, v15
	v_add_f32_e32 v10, 1.0, v10
	v_rcp_f32_e32 v21, v10
	v_exp_f32_e32 v10, v12
	v_exp_f32_e32 v16, v16
	v_exp_f32_e32 v17, v17
	v_add_f32_e32 v14, 1.0, v14
	v_add_f32_e32 v10, 1.0, v10
	v_rcp_f32_e32 v22, v10
	v_exp_f32_e32 v10, v13
	v_add_f32_e32 v15, 1.0, v15
	v_rcp_f32_e32 v14, v14
	v_rcp_f32_e32 v15, v15
	v_add_f32_e32 v16, 1.0, v16
	v_add_f32_e32 v17, 1.0, v17
	v_add_f32_e32 v10, 1.0, v10
	v_pk_mul_f32 v[2:3], v[0:1], v[2:3] op_sel_hi:[0,1]
	v_rcp_f32_e32 v16, v16
	v_rcp_f32_e32 v17, v17
	v_rcp_f32_e32 v13, v10
	v_pk_mul_f32 v[8:9], v[0:1], v[8:9] op_sel_hi:[0,1]
	v_pk_mul_f32 v[6:7], v[0:1], v[6:7] op_sel_hi:[0,1]
	v_pk_mul_f32 v[4:5], v[0:1], v[4:5] op_sel_hi:[0,1]
	v_exp_f32_e32 v0, v2
	v_exp_f32_e32 v2, v3
	s_mov_b32 s29, 0x58000
	v_cvt_pk_bf16_f32 v10, v14, v15
	v_add_co_u32_e32 v14, vcc, s29, v142
	v_cvt_pk_bf16_f32 v11, v16, v17
	v_cvt_pk_bf16_f32 v12, v20, v21
	v_cvt_pk_bf16_f32 v13, v22, v13
	v_addc_co_u32_e32 v15, vcc, 0, v143, vcc
	v_add_f32_e32 v2, 1.0, v2
	global_store_dwordx4 v[14:15], v[10:13], off sc1
	v_exp_f32_e32 v6, v6
	v_exp_f32_e32 v7, v7
	v_rcp_f32_e32 v10, v2
	v_exp_f32_e32 v2, v4
	v_exp_f32_e32 v8, v8
	v_exp_f32_e32 v9, v9
	v_add_f32_e32 v6, 1.0, v6
	v_add_f32_e32 v2, 1.0, v2
	v_rcp_f32_e32 v11, v2
	v_exp_f32_e32 v2, v5
	v_add_f32_e32 v7, 1.0, v7
	v_add_f32_e32 v8, 1.0, v8
	v_add_f32_e32 v9, 1.0, v9
	v_add_f32_e32 v0, 1.0, v0
	v_add_f32_e32 v2, 1.0, v2
	v_rcp_f32_e32 v6, v6
	v_rcp_f32_e32 v7, v7
	v_rcp_f32_e32 v8, v8
	v_rcp_f32_e32 v9, v9
	v_rcp_f32_e32 v0, v0
	v_rcp_f32_e32 v5, v2
	s_mov_b64 s[36:37], 0x58000
	v_lshl_add_u64 v[18:19], v[142:143], 0, s[36:37]
	v_cvt_pk_bf16_f32 v2, v6, v7
	v_cvt_pk_bf16_f32 v3, v8, v9
	v_cvt_pk_bf16_f32 v4, v0, v10
	v_cvt_pk_bf16_f32 v5, v11, v5
	s_mov_b64 s[36:37], -1
	s_andn2_b64 vcc, exec, s[46:47]
	global_store_dwordx4 v[18:19], v[2:5], off offset:256 sc1
	s_cbranch_vccnz .LBB0_1054
	s_nop 0
	v_lshl_add_u32 v2, s38, 8, v160
	v_ashrrev_i32_e32 v3, 31, v2
	v_lshl_add_u64 v[2:3], v[2:3], 3, s[0:1]
	global_load_dwordx2 v[156:157], v[2:3], off nt
	global_load_dwordx2 v[154:155], v[2:3], off offset:128 nt
	global_load_dwordx2 v[152:153], v[2:3], off offset:256 nt
	global_load_dwordx2 v[150:151], v[2:3], off offset:384 nt
	global_load_dwordx2 v[148:149], v[2:3], off offset:1024 nt
	global_load_dwordx2 v[146:147], v[2:3], off offset:1152 nt
	global_load_dwordx2 v[144:145], v[2:3], off offset:1280 nt
	global_load_dwordx2 v[142:143], v[2:3], off offset:1408 nt
	s_andn2_b64 vcc, exec, s[14:15]
	s_cbranch_vccnz .LBB0_1053
	s_barrier
	s_branch .LBB0_1053

.LBB0_1071:
	s_or_b64 exec, exec, s[38:39]
	s_waitcnt lgkmcnt(0)
	ds_read_b128 v[2:5], v203 offset:49280
	ds_read_b128 v[6:9], v203 offset:49312
	s_lshl_b32 s29, s31, 12
	v_lshl_or_b32 v49, v236, 1, s29
	v_add_u32_e32 v49, v49, v242
	s_waitcnt lgkmcnt(1)
	v_rcp_f32_e32 v0, v2
	v_rcp_f32_e32 v10, v3
	v_rcp_f32_e32 v11, v4
	v_rcp_f32_e32 v12, v5
	v_mul_f32_e32 v32, v32, v0
	v_mul_f32_e32 v0, v16, v0
	v_cvt_pk_bf16_f32 v0, v0, s0
	s_waitcnt lgkmcnt(0)
	v_rcp_f32_e32 v13, v6
	ds_read_b128 v[2:5], v203 offset:49344
	v_rcp_f32_e32 v14, v7
	v_rcp_f32_e32 v15, v8
	v_rcp_f32_e32 v48, v9
	ds_read_b128 v[6:9], v203 offset:49376
	ds_write_b16 v49, v0 offset:51264
	v_mul_f32_e32 v0, v33, v10
	v_cvt_pk_bf16_f32 v0, v0, s0
	ds_write_b16 v49, v0 offset:51328
	v_mul_f32_e32 v0, v17, v10
	v_cvt_pk_bf16_f32 v0, v0, s0
	ds_write_b16 v49, v0 offset:51392
	v_mul_f32_e32 v0, v34, v11
	v_cvt_pk_bf16_f32 v0, v0, s0
	ds_write_b16 v49, v0 offset:51456
	v_mul_f32_e32 v0, v18, v11
	v_cvt_pk_bf16_f32 v0, v0, s0
	ds_write_b16 v49, v0 offset:51520
	v_mul_f32_e32 v0, v35, v12
	v_cvt_pk_bf16_f32 v0, v0, s0
	ds_write_b16 v49, v0 offset:51584
	v_mul_f32_e32 v0, v19, v12
	v_cvt_pk_bf16_f32 v0, v0, s0
	ds_write_b16 v49, v0 offset:51648
	v_mul_f32_e32 v0, v36, v13
	v_cvt_pk_bf16_f32 v0, v0, s0
	ds_write_b16 v49, v0 offset:52224
	v_mul_f32_e32 v0, v20, v13
	v_cvt_pk_bf16_f32 v0, v0, s0
	ds_write_b16 v49, v0 offset:52288
	v_mul_f32_e32 v0, v37, v14
	v_cvt_pk_bf16_f32 v0, v0, s0
	ds_write_b16 v49, v0 offset:52352
	v_mul_f32_e32 v0, v21, v14
	v_cvt_pk_bf16_f32 v0, v0, s0
	ds_write_b16 v49, v0 offset:52416
	v_mul_f32_e32 v0, v38, v15
	v_cvt_pk_bf16_f32 v0, v0, s0
	ds_write_b16 v49, v0 offset:52480
	v_mul_f32_e32 v0, v22, v15
	v_cvt_pk_bf16_f32 v0, v0, s0
	s_waitcnt lgkmcnt(13)
	v_rcp_f32_e32 v2, v2
	ds_write_b16 v49, v0 offset:52544
	v_mul_f32_e32 v0, v39, v48
	v_cvt_pk_bf16_f32 v0, v0, s0
	ds_write_b16 v49, v0 offset:52608
	v_mul_f32_e32 v0, v23, v48
	v_cvt_pk_bf16_f32 v0, v0, s0
	v_rcp_f32_e32 v3, v3
	ds_write_b16 v49, v0 offset:52672
	v_mul_f32_e32 v0, v40, v2
	v_cvt_pk_bf16_f32 v0, v0, s0
	ds_write_b16 v49, v0 offset:53248
	v_mul_f32_e32 v0, v24, v2
	v_cvt_pk_bf16_f32 v0, v0, s0
	v_rcp_f32_e32 v4, v4
	ds_write_b16 v49, v0 offset:53312
	v_mul_f32_e32 v0, v41, v3
	v_cvt_pk_bf16_f32 v0, v0, s0
	ds_write_b16 v49, v0 offset:53376
	v_mul_f32_e32 v0, v25, v3
	v_cvt_pk_bf16_f32 v0, v0, s0
	v_rcp_f32_e32 v5, v5
	ds_write_b16 v49, v0 offset:53440
	v_mul_f32_e32 v0, v42, v4
	v_cvt_pk_bf16_f32 v0, v0, s0
	ds_write_b16 v49, v0 offset:53504
	v_mul_f32_e32 v0, v26, v4
	v_cvt_pk_bf16_f32 v0, v0, s0
	s_waitcnt lgkmcnt(14)
	v_rcp_f32_e32 v6, v6
	ds_write_b16 v49, v0 offset:53568
	v_mul_f32_e32 v0, v43, v5
	v_cvt_pk_bf16_f32 v0, v0, s0
	ds_write_b16 v49, v0 offset:53632
	v_mul_f32_e32 v0, v27, v5
	v_cvt_pk_bf16_f32 v0, v0, s0
	v_rcp_f32_e32 v7, v7
	ds_write_b16 v49, v0 offset:53696
	v_mul_f32_e32 v0, v44, v6
	v_cvt_pk_bf16_f32 v0, v0, s0
	ds_write_b16 v49, v0 offset:54272
	v_mul_f32_e32 v0, v28, v6
	v_cvt_pk_bf16_f32 v0, v0, s0
	v_rcp_f32_e32 v8, v8
	ds_write_b16 v49, v0 offset:54336
	v_mul_f32_e32 v0, v45, v7
	v_cvt_pk_bf16_f32 v0, v0, s0
	ds_write_b16 v49, v0 offset:54400
	v_mul_f32_e32 v0, v29, v7
	v_cvt_pk_bf16_f32 v0, v0, s0
	v_rcp_f32_e32 v9, v9
	ds_write_b16 v49, v0 offset:54464
	v_mul_f32_e32 v0, v46, v8
	v_cvt_pk_bf16_f32 v0, v0, s0
	ds_write_b16 v49, v0 offset:54528
	v_mul_f32_e32 v0, v30, v8
	v_cvt_pk_bf16_f32 v0, v0, s0
	ds_write_b16 v49, v0 offset:54592
	v_mul_f32_e32 v0, v47, v9
	v_cvt_pk_bf16_f32 v0, v0, s0
	ds_write_b16 v49, v0 offset:54656
	v_mul_f32_e32 v0, v31, v9
	v_cvt_pk_bf16_f32 v32, v32, s0
	v_cvt_pk_bf16_f32 v0, v0, s0
	ds_write_b16 v49, v32 offset:51200
	ds_write_b16 v49, v0 offset:54720
	v_or_b32_e32 v0, s29, v204
	s_waitcnt lgkmcnt(0)
	v_add_u32_e32 v2, v0, v243
	ds_read_b128 v[2:5], v2 offset:51200
	v_add_u32_e32 v6, v0, v244
	ds_read_b128 v[6:9], v6 offset:51200
	v_mov_b32_e32 v205, v1
	v_lshl_add_u64 v[10:11], s[50:51], 0, v[204:205]
	v_mov_b32_e32 v207, v1
	v_lshl_add_u64 v[12:13], v[10:11], 0, v[206:207]
	v_mov_b32_e32 v209, v1
	s_waitcnt lgkmcnt(1)
	global_store_dwordx4 v[12:13], v[2:5], off sc1
	v_mov_b32_e32 v211, v1
	v_lshl_add_u64 v[12:13], v[10:11], 0, v[210:211]
	v_lshl_add_u64 v[2:3], v[10:11], 0, v[208:209]
	s_waitcnt lgkmcnt(0)
	global_store_dwordx4 v[2:3], v[6:9], off sc1
	v_add_u32_e32 v2, v0, v245
	ds_read_b128 v[2:5], v2 offset:51200
	v_add_u32_e32 v0, v0, v246
	ds_read_b128 v[6:9], v0 offset:51200
	v_mov_b32_e32 v213, v1
	s_mov_b64 s[52:53], 0
	s_waitcnt lgkmcnt(1)
	global_store_dwordx4 v[12:13], v[2:5], off sc1
	s_and_b64 vcc, exec, s[54:55]
	s_nop 0
	v_lshl_add_u64 v[2:3], v[10:11], 0, v[212:213]
	s_waitcnt lgkmcnt(0)
	global_store_dwordx4 v[2:3], v[6:9], off sc1
	s_waitcnt lgkmcnt(0)
	s_barrier
	s_cbranch_vccnz .LBB0_1069

.LBB0_1171:
	s_add_i32 s35, s31, s34
	s_add_u32 s29, s14, s35
	s_addc_u32 s38, s15, 0
	v_mov_b32_e32 v35, s38
	v_or_b32_e32 v34, s29, v116
	v_lshlrev_b64 v[34:35], 10, v[34:35]
	v_lshl_add_u64 v[42:43], v[140:141], 0, v[34:35]
	global_load_dwordx4 v[34:37], v[42:43], off
	v_add_co_u32_e32 v44, vcc, s10, v42
	v_add_u32_e32 v167, s34, v119
	s_nop 0
	v_addc_co_u32_e32 v45, vcc, 0, v43, vcc
	global_load_dwordx4 v[38:41], v[44:45], off
	global_load_dwordx4 v[168:171], v[42:43], off offset:32
	global_load_dwordx4 v[172:175], v[44:45], off offset:32
	global_load_dwordx4 v[176:179], v[42:43], off offset:64
	global_load_dwordx4 v[180:183], v[44:45], off offset:64
	global_load_dwordx4 v[184:187], v[42:43], off offset:96
	global_load_dwordx4 v[188:191], v[44:45], off offset:96
	v_mov_b32_e32 v43, s38
	v_or_b32_e32 v42, s29, v118
	v_lshlrev_b64 v[42:43], 10, v[42:43]
	v_lshl_add_u64 v[42:43], v[142:143], 0, v[42:43]
	global_load_dwordx4 v[82:85], v[42:43], off
	v_mov_b32_e32 v43, s38
	v_or_b32_e32 v42, s29, v124
	v_lshlrev_b64 v[42:43], 10, v[42:43]
	v_lshl_add_u64 v[42:43], v[142:143], 0, v[42:43]
	global_load_dwordx4 v[86:89], v[42:43], off
	v_mov_b32_e32 v43, s38
	v_or_b32_e32 v42, s29, v126
	v_lshlrev_b64 v[42:43], 10, v[42:43]
	v_lshl_add_u64 v[42:43], v[142:143], 0, v[42:43]
	global_load_dwordx4 v[90:93], v[42:43], off
	v_mov_b32_e32 v43, s38
	v_or_b32_e32 v42, s29, v128
	v_lshlrev_b64 v[42:43], 10, v[42:43]
	v_lshl_add_u64 v[42:43], v[142:143], 0, v[42:43]
	global_load_dwordx4 v[94:97], v[42:43], off
	v_mov_b32_e32 v43, s38
	v_or_b32_e32 v42, s29, v130
	v_lshlrev_b64 v[42:43], 10, v[42:43]
	v_lshl_add_u64 v[42:43], v[142:143], 0, v[42:43]
	global_load_dwordx4 v[98:101], v[42:43], off
	v_mov_b32_e32 v43, s38
	v_or_b32_e32 v42, s29, v132
	v_lshlrev_b64 v[42:43], 10, v[42:43]
	v_lshl_add_u64 v[42:43], v[142:143], 0, v[42:43]
	global_load_dwordx4 v[102:105], v[42:43], off
	v_mov_b32_e32 v43, s38
	v_or_b32_e32 v42, s29, v134
	v_lshlrev_b64 v[42:43], 10, v[42:43]
	v_lshl_add_u64 v[42:43], v[142:143], 0, v[42:43]
	global_load_dwordx4 v[106:109], v[42:43], off
	v_mov_b32_e32 v43, s38
	s_cmp_eq_u32 s34, 0
	v_cmp_lt_u32_e64 s[38:39], v167, v125
	s_cselect_b64 vcc, -1, 0
	v_or_b32_e32 v42, s29, v136
	v_lshlrev_b64 v[42:43], 10, v[42:43]
	v_lshl_add_u64 v[42:43], v[142:143], 0, v[42:43]
	global_load_dwordx4 v[110:113], v[42:43], off
	s_mov_b32 s29, 0xd7d1fdd
	s_waitcnt vmcnt(15)
	v_mfma_f32_32x32x16_bf16 v[50:65], v[34:37], v[66:69], 0
	s_waitcnt vmcnt(7)
	ds_write_b128 v115, v[82:85]
	s_waitcnt vmcnt(6)
	ds_write_b128 v115, v[86:89] offset:1536
	s_waitcnt vmcnt(5)
	ds_write_b128 v115, v[90:93] offset:3072
	s_waitcnt vmcnt(4)
	ds_write_b128 v115, v[94:97] offset:4608
	s_waitcnt vmcnt(3)
	ds_write_b128 v115, v[98:101] offset:6144
	s_waitcnt vmcnt(2)
	ds_write_b128 v115, v[102:105] offset:7680
	s_waitcnt vmcnt(1)
	ds_write_b128 v115, v[106:109] offset:9216
	s_waitcnt vmcnt(0)
	ds_write_b128 v115, v[110:113] offset:10752
	v_mfma_f32_32x32x16_bf16 v[50:65], v[168:171], v[70:73], v[50:65]
	v_mfma_f32_32x32x16_bf16 v[50:65], v[176:179], v[74:77], v[50:65]
	v_mfma_f32_32x32x16_bf16 v[50:65], v[184:187], v[78:81], v[50:65]
	v_mfma_f32_32x32x16_bf16 v[34:49], v[38:41], v[66:69], 0
	s_nop 10
	v_max_f32_e32 v50, v50, v50
	v_min_f32_e32 v50, 0x42fc0000, v50
	v_exp_f32_e32 v50, v50
	s_nop 0
	v_add_f32_e32 v50, 1.0, v50
	v_rcp_f32_e32 v50, v50
	v_mfma_f32_32x32x16_bf16 v[34:49], v[172:175], v[70:73], v[34:49]
	v_cndmask_b32_e64 v168, 1.0, v50, s[38:39]
	v_cndmask_b32_e32 v168, v50, v168, vcc
	v_max_f32_e32 v50, v51, v51
	v_min_f32_e32 v50, 0x42fc0000, v50
	v_exp_f32_e32 v50, v50
	v_add_u32_e32 v51, 1, v167
	v_cmp_lt_u32_e64 s[38:39], v51, v125
	v_mfma_f32_32x32x16_bf16 v[34:49], v[180:183], v[74:77], v[34:49]
	v_add_f32_e32 v50, 1.0, v50
	v_rcp_f32_e32 v50, v50
	s_nop 0
	v_cndmask_b32_e64 v51, 1.0, v50, s[38:39]
	v_cndmask_b32_e32 v169, v50, v51, vcc
	v_max_f32_e32 v50, v52, v52
	v_min_f32_e32 v50, 0x42fc0000, v50
	v_exp_f32_e32 v50, v50
	v_add_u32_e32 v51, 2, v167
	v_cmp_lt_u32_e64 s[38:39], v51, v125
	v_mfma_f32_32x32x16_bf16 v[34:49], v[188:191], v[78:81], v[34:49]
	v_add_f32_e32 v50, 1.0, v50
	v_rcp_f32_e32 v50, v50
	s_nop 0
	v_cndmask_b32_e64 v51, 1.0, v50, s[38:39]
	v_cndmask_b32_e32 v52, v50, v51, vcc
	v_max_f32_e32 v50, v53, v53
	v_min_f32_e32 v50, 0x42fc0000, v50
	v_exp_f32_e32 v50, v50
	v_add_u32_e32 v51, 3, v167
	v_cmp_lt_u32_e64 s[38:39], v51, v125
	s_nop 1
	v_max_f32_e32 v34, v34, v34
	v_add_f32_e32 v50, 1.0, v50
	v_rcp_f32_e32 v50, v50
	v_min_f32_e32 v34, 0x42fc0000, v34
	v_max_f32_e32 v35, v35, v35
	v_exp_f32_e32 v34, v34
	v_cndmask_b32_e64 v51, 1.0, v50, s[38:39]
	v_cndmask_b32_e32 v53, v50, v51, vcc
	v_max_f32_e32 v50, v54, v54
	v_min_f32_e32 v50, 0x42fc0000, v50
	v_exp_f32_e32 v50, v50
	v_cmp_lt_i32_e64 s[38:39], v167, v127
	v_min_f32_e32 v35, 0x42fc0000, v35
	v_max_f32_e32 v36, v36, v36
	v_add_f32_e32 v50, 1.0, v50
	v_rcp_f32_e32 v50, v50
	v_exp_f32_e32 v35, v35
	v_min_f32_e32 v36, 0x42fc0000, v36
	v_max_f32_e32 v37, v37, v37
	v_cndmask_b32_e64 v51, 1.0, v50, s[38:39]
	v_cndmask_b32_e32 v54, v50, v51, vcc
	v_max_f32_e32 v50, v55, v55
	v_min_f32_e32 v50, 0x42fc0000, v50
	v_exp_f32_e32 v50, v50
	v_cmp_lt_i32_e64 s[38:39], v167, v129
	v_exp_f32_e32 v36, v36
	v_min_f32_e32 v37, 0x42fc0000, v37
	v_add_f32_e32 v50, 1.0, v50
	v_rcp_f32_e32 v50, v50
	v_max_f32_e32 v38, v38, v38
	v_exp_f32_e32 v37, v37
	v_min_f32_e32 v38, 0x42fc0000, v38
	v_cndmask_b32_e64 v51, 1.0, v50, s[38:39]
	v_cndmask_b32_e32 v55, v50, v51, vcc
	v_max_f32_e32 v50, v56, v56
	v_min_f32_e32 v50, 0x42fc0000, v50
	v_exp_f32_e32 v50, v50
	v_cmp_lt_i32_e64 s[38:39], v167, v131
	v_add_f32_e32 v34, 1.0, v34
	v_exp_f32_e32 v38, v38
	v_add_f32_e32 v50, 1.0, v50
	v_rcp_f32_e32 v50, v50
	v_rcp_f32_e32 v34, v34
	v_add_f32_e32 v35, 1.0, v35
	v_rcp_f32_e32 v35, v35
	v_cndmask_b32_e64 v51, 1.0, v50, s[38:39]
	v_cndmask_b32_e32 v56, v50, v51, vcc
	v_max_f32_e32 v50, v57, v57
	v_min_f32_e32 v50, 0x42fc0000, v50
	v_exp_f32_e32 v50, v50
	v_cmp_lt_i32_e64 s[38:39], v167, v133
	v_add_f32_e32 v36, 1.0, v36
	v_rcp_f32_e32 v36, v36
	v_add_f32_e32 v50, 1.0, v50
	v_rcp_f32_e32 v50, v50
	v_add_f32_e32 v37, 1.0, v37
	v_rcp_f32_e32 v37, v37
	v_add_f32_e32 v38, 1.0, v38
	v_cndmask_b32_e64 v51, 1.0, v50, s[38:39]
	v_cndmask_b32_e32 v57, v50, v51, vcc
	v_max_f32_e32 v50, v58, v58
	v_min_f32_e32 v50, 0x42fc0000, v50
	v_exp_f32_e32 v50, v50
	v_cmp_lt_i32_e64 s[38:39], v167, v135
	v_rcp_f32_e32 v38, v38
	v_add_f32_e32 v50, 1.0, v50
	v_rcp_f32_e32 v50, v50
	s_nop 0
	v_cndmask_b32_e64 v51, 1.0, v50, s[38:39]
	v_cndmask_b32_e32 v58, v50, v51, vcc
	v_max_f32_e32 v50, v59, v59
	v_min_f32_e32 v50, 0x42fc0000, v50
	v_exp_f32_e32 v50, v50
	v_cmp_lt_i32_e64 s[38:39], v167, v137
	v_add_f32_e32 v50, 1.0, v50
	v_rcp_f32_e32 v50, v50
	s_nop 0
	v_cndmask_b32_e64 v51, 1.0, v50, s[38:39]
	v_cndmask_b32_e32 v59, v50, v51, vcc
	v_max_f32_e32 v50, v60, v60
	v_min_f32_e32 v50, 0x42fc0000, v50
	v_exp_f32_e32 v50, v50
	v_cmp_lt_i32_e64 s[38:39], v167, v144
	v_add_f32_e32 v50, 1.0, v50
	v_rcp_f32_e32 v50, v50
	s_nop 0
	v_cndmask_b32_e64 v51, 1.0, v50, s[38:39]
	v_cndmask_b32_e32 v60, v50, v51, vcc
	v_max_f32_e32 v50, v61, v61
	v_min_f32_e32 v50, 0x42fc0000, v50
	v_exp_f32_e32 v50, v50
	v_cmp_lt_i32_e64 s[38:39], v167, v145
	v_add_f32_e32 v50, 1.0, v50
	v_rcp_f32_e32 v50, v50
	s_nop 0
	v_cndmask_b32_e64 v51, 1.0, v50, s[38:39]
	v_cndmask_b32_e32 v61, v50, v51, vcc
	v_max_f32_e32 v50, v62, v62
	v_min_f32_e32 v50, 0x42fc0000, v50
	v_exp_f32_e32 v50, v50
	v_cmp_lt_i32_e64 s[38:39], v167, v146
	v_add_f32_e32 v50, 1.0, v50
	v_rcp_f32_e32 v50, v50
	s_nop 0
	v_cndmask_b32_e64 v51, 1.0, v50, s[38:39]
	v_cndmask_b32_e32 v62, v50, v51, vcc
	v_max_f32_e32 v50, v63, v63
	v_min_f32_e32 v50, 0x42fc0000, v50
	v_exp_f32_e32 v50, v50
	v_cmp_lt_i32_e64 s[38:39], v167, v147
	v_add_f32_e32 v50, 1.0, v50
	v_rcp_f32_e32 v50, v50
	s_nop 0
	v_cndmask_b32_e64 v51, 1.0, v50, s[38:39]
	v_cndmask_b32_e32 v63, v50, v51, vcc
	v_max_f32_e32 v50, v64, v64
	v_min_f32_e32 v50, 0x42fc0000, v50
	v_exp_f32_e32 v50, v50
	v_cmp_lt_i32_e64 s[38:39], v167, v148
	v_add_f32_e32 v50, 1.0, v50
	v_rcp_f32_e32 v50, v50
	s_nop 0
	v_cndmask_b32_e64 v51, 1.0, v50, s[38:39]
	v_cndmask_b32_e32 v64, v50, v51, vcc
	v_max_f32_e32 v50, v65, v65
	v_min_f32_e32 v50, 0x42fc0000, v50
	v_exp_f32_e32 v50, v50
	v_cmp_lt_i32_e64 s[38:39], v167, v149
	v_add_f32_e32 v50, 1.0, v50
	v_rcp_f32_e32 v50, v50
	s_nop 0
	v_cndmask_b32_e64 v51, 1.0, v50, s[38:39]
	v_cmp_lt_i32_e64 s[38:39], v167, v150
	v_cndmask_b32_e32 v65, v50, v51, vcc
	s_nop 0
	v_cndmask_b32_e64 v50, 1.0, v34, s[38:39]
	v_cmp_lt_i32_e64 s[38:39], v167, v151
	v_cndmask_b32_e32 v34, v34, v50, vcc
	s_nop 0
	v_cndmask_b32_e64 v50, 1.0, v35, s[38:39]
	v_cmp_lt_i32_e64 s[38:39], v167, v152
	v_cndmask_b32_e32 v35, v35, v50, vcc
	s_nop 0
	v_cndmask_b32_e64 v50, 1.0, v36, s[38:39]
	v_cmp_lt_i32_e64 s[38:39], v167, v153
	v_cndmask_b32_e32 v36, v36, v50, vcc
	s_nop 0
	v_cndmask_b32_e64 v50, 1.0, v37, s[38:39]
	v_cmp_lt_i32_e64 s[38:39], v167, v154
	v_cndmask_b32_e32 v37, v37, v50, vcc
	v_mul_f32_e32 v51, v36, v37
	v_cndmask_b32_e64 v50, 1.0, v38, s[38:39]
	v_cndmask_b32_e32 v170, v38, v50, vcc
	v_max_f32_e32 v38, v39, v39
	v_min_f32_e32 v38, 0x42fc0000, v38
	v_exp_f32_e32 v38, v38
	v_cmp_lt_i32_e64 s[38:39], v167, v155
	v_add_f32_e32 v38, 1.0, v38
	v_rcp_f32_e32 v38, v38
	s_nop 0
	v_cndmask_b32_e64 v39, 1.0, v38, s[38:39]
	v_cndmask_b32_e32 v171, v38, v39, vcc
	v_max_f32_e32 v38, v40, v40
	v_min_f32_e32 v38, 0x42fc0000, v38
	v_exp_f32_e32 v38, v38
	v_cmp_lt_i32_e64 s[38:39], v167, v156
	v_mul_f32_e32 v177, v170, v171
	v_mul_f32_e32 v40, v56, v57
	v_add_f32_e32 v38, 1.0, v38
	v_rcp_f32_e32 v38, v38
	s_nop 0
	v_cndmask_b32_e64 v39, 1.0, v38, s[38:39]
	v_cndmask_b32_e32 v172, v38, v39, vcc
	v_max_f32_e32 v38, v41, v41
	v_min_f32_e32 v38, 0x42fc0000, v38
	v_exp_f32_e32 v38, v38
	v_cmp_lt_i32_e64 s[38:39], v167, v157
	v_mul_f32_e32 v41, v58, v59
	v_add_f32_e32 v38, 1.0, v38
	v_rcp_f32_e32 v38, v38
	s_nop 0
	v_cndmask_b32_e64 v39, 1.0, v38, s[38:39]
	v_cndmask_b32_e32 v173, v38, v39, vcc
	v_max_f32_e32 v38, v42, v42
	v_min_f32_e32 v38, 0x42fc0000, v38
	v_exp_f32_e32 v38, v38
	v_cmp_lt_i32_e64 s[38:39], v167, v158
	v_mul_f32_e32 v178, v172, v173
	v_mul_f32_e32 v177, v177, v178
	v_add_f32_e32 v38, 1.0, v38
	v_rcp_f32_e32 v38, v38
	v_mov_b32_e32 v178, v177
	s_nop 1
	v_permlane32_swap_b32_e32 v177, v178
	v_cndmask_b32_e64 v39, 1.0, v38, s[38:39]
	v_cndmask_b32_e32 v42, v38, v39, vcc
	v_max_f32_e32 v38, v43, v43
	v_min_f32_e32 v38, 0x42fc0000, v38
	v_exp_f32_e32 v38, v38
	v_cmp_lt_i32_e64 s[38:39], v167, v159
	v_add_f32_e32 v38, 1.0, v38
	v_rcp_f32_e32 v38, v38
	s_nop 0
	v_cndmask_b32_e64 v39, 1.0, v38, s[38:39]
	v_cndmask_b32_e32 v43, v38, v39, vcc
	v_max_f32_e32 v38, v44, v44
	v_min_f32_e32 v38, 0x42fc0000, v38
	v_exp_f32_e32 v38, v38
	v_cmp_lt_i32_e64 s[38:39], v167, v160
	v_mul_f32_e32 v179, v42, v43
	v_sub_f32_e32 v42, 1.0, v42
	v_add_f32_e32 v38, 1.0, v38
	v_rcp_f32_e32 v38, v38
	s_nop 0
	v_cndmask_b32_e64 v39, 1.0, v38, s[38:39]
	v_cndmask_b32_e32 v44, v38, v39, vcc
	v_max_f32_e32 v38, v45, v45
	v_min_f32_e32 v38, 0x42fc0000, v38
	v_exp_f32_e32 v38, v38
	v_cmp_lt_i32_e64 s[38:39], v167, v161
	v_add_f32_e32 v38, 1.0, v38
	v_rcp_f32_e32 v38, v38
	s_nop 0
	v_cndmask_b32_e64 v39, 1.0, v38, s[38:39]
	v_cndmask_b32_e32 v45, v38, v39, vcc
	v_max_f32_e32 v38, v46, v46
	v_min_f32_e32 v38, 0x42fc0000, v38
	v_exp_f32_e32 v38, v38
	v_cmp_lt_i32_e64 s[38:39], v167, v162
	v_mul_f32_e32 v180, v44, v45
	v_mul_f32_e32 v179, v179, v180
	v_add_f32_e32 v38, 1.0, v38
	v_rcp_f32_e32 v38, v38
	v_mov_b32_e32 v180, v179
	s_nop 1
	v_permlane32_swap_b32_e32 v179, v180
	v_cndmask_b32_e64 v39, 1.0, v38, s[38:39]
	v_cndmask_b32_e32 v174, v38, v39, vcc
	v_max_f32_e32 v38, v47, v47
	v_min_f32_e32 v38, 0x42fc0000, v38
	v_exp_f32_e32 v38, v38
	v_cmp_lt_i32_e64 s[38:39], v167, v163
	v_mul_f32_e32 v47, v62, v63
	v_mul_f32_e32 v46, v60, v61
	v_add_f32_e32 v38, 1.0, v38
	v_rcp_f32_e32 v38, v38
	v_mul_f32_e32 v41, v41, v46
	v_mov_b32_e32 v46, v41
	s_nop 1
	v_permlane32_swap_b32_e32 v41, v46
	v_cndmask_b32_e64 v39, 1.0, v38, s[38:39]
	v_cndmask_b32_e32 v175, v38, v39, vcc
	v_max_f32_e32 v38, v48, v48
	v_min_f32_e32 v38, 0x42fc0000, v38
	v_exp_f32_e32 v38, v38
	v_cmp_lt_i32_e64 s[38:39], v167, v164
	v_mul_f32_e32 v181, v174, v175
	v_mul_f32_e32 v48, v64, v65
	v_add_f32_e32 v38, 1.0, v38
	v_rcp_f32_e32 v38, v38
	v_mul_f32_e32 v47, v47, v48
	v_mov_b32_e32 v48, v47
	s_nop 1
	v_permlane32_swap_b32_e32 v47, v48
	v_cndmask_b32_e64 v39, 1.0, v38, s[38:39]
	v_cndmask_b32_e32 v176, v38, v39, vcc
	v_max_f32_e32 v38, v49, v49
	v_min_f32_e32 v38, 0x42fc0000, v38
	v_exp_f32_e32 v38, v38
	v_cmp_lt_i32_e64 s[38:39], v167, v165
	v_mul_f32_e32 v49, v34, v35
	v_mul_f32_e32 v49, v49, v51
	v_add_f32_e32 v38, 1.0, v38
	v_rcp_f32_e32 v38, v38
	v_mov_b32_e32 v51, v49
	s_nop 1
	v_permlane32_swap_b32_e32 v49, v51
	v_cndmask_b32_e64 v39, 1.0, v38, s[38:39]
	v_cndmask_b32_e32 v167, v38, v39, vcc
	v_mul_f32_e32 v182, v176, v167
	v_mul_f32_e32 v181, v181, v182
	v_mov_b32_e32 v182, v181
	s_nop 1
	v_permlane32_swap_b32_e32 v181, v182
	v_mul_f32_e32 v182, v166, v182
	v_mul_f32_e32 v181, v182, v181
	v_mul_f32_e32 v180, v181, v180
	v_mul_f32_e32 v179, v180, v179
	v_mul_f32_e32 v178, v179, v178
	v_mul_f32_e32 v177, v178, v177
	v_mul_f32_e32 v51, v177, v51
	v_mul_f32_e32 v38, v168, v169
	v_mul_f32_e32 v39, v52, v53
	v_mul_f32_e32 v49, v51, v49
	v_mul_f32_e32 v50, v38, v39
	v_mul_f32_e32 v39, v54, v55
	v_mul_f32_e32 v48, v49, v48
	v_mul_f32_e32 v39, v39, v40
	v_mul_f32_e32 v47, v48, v47
	v_mov_b32_e32 v40, v39
	v_mul_f32_e32 v46, v47, v46
	s_nop 0
	v_permlane32_swap_b32_e32 v39, v40
	v_mul_f32_e32 v41, v46, v41
	v_mov_b32_e32 v38, v50
	v_mul_f32_e32 v40, v41, v40
	s_nop 0
	v_permlane32_swap_b32_e32 v50, v38
	v_mul_f32_e32 v39, v40, v39
	v_cndmask_b32_e64 v177, v177, v51, s[36:37]
	v_mul_f32_e32 v51, v39, v38
	v_cndmask_b32_e64 v38, v39, v51, s[36:37]
	v_mul_f32_e32 v39, v53, v38
	v_cndmask_b32_e64 v40, v41, v40, s[36:37]
	v_mul_f32_e32 v41, v52, v39
	v_cndmask_b32_e64 v180, v181, v180, s[36:37]
	v_cndmask_b32_e64 v181, v47, v46, s[36:37]
	v_mul_f32_e32 v46, v169, v41
	v_sub_f32_e32 v47, 1.0, v168
	v_mul_f32_e32 v46, v47, v46
	v_sub_f32_e32 v47, 1.0, v169
	v_mul_f32_e32 v41, v47, v41
	v_sub_f32_e32 v47, 1.0, v52
	v_mul_f32_e32 v39, v47, v39
	v_sub_f32_e32 v47, 1.0, v53
	v_mul_f32_e32 v38, v47, v38
	v_mul_f32_e32 v47, v57, v40
	v_cndmask_b32_e64 v178, v179, v178, s[36:37]
	v_cndmask_b32_e64 v179, v49, v48, s[36:37]
	v_mul_f32_e32 v48, v56, v47
	v_mul_f32_e32 v49, v55, v48
	v_sub_f32_e32 v52, 1.0, v54
	v_mul_f32_e32 v49, v52, v49
	v_sub_f32_e32 v52, 1.0, v55
	v_mul_f32_e32 v48, v52, v48
	v_sub_f32_e32 v52, 1.0, v56
	v_mul_f32_e32 v52, v52, v47
	v_sub_f32_e32 v47, 1.0, v57
	v_mul_f32_e32 v40, v47, v40
	v_cvt_pk_bf16_f32 v47, v39, v38
	v_mul_f32_e32 v38, v61, v181
	v_mul_f32_e32 v39, v60, v38
	v_cvt_pk_bf16_f32 v46, v46, v41
	v_cvt_pk_bf16_f32 v48, v49, v48
	v_cvt_pk_bf16_f32 v49, v52, v40
	v_mul_f32_e32 v40, v59, v39
	v_sub_f32_e32 v41, 1.0, v58
	v_mul_f32_e32 v40, v41, v40
	v_sub_f32_e32 v41, 1.0, v59
	v_mul_f32_e32 v39, v41, v39
	v_sub_f32_e32 v41, 1.0, v60
	v_mul_f32_e32 v41, v41, v38
	v_sub_f32_e32 v38, 1.0, v61
	v_mul_f32_e32 v52, v38, v181
	v_mul_f32_e32 v38, v65, v179
	v_mul_f32_e32 v53, v64, v38
	v_mul_f32_e32 v54, v63, v53
	v_sub_f32_e32 v55, 1.0, v62
	v_mul_f32_e32 v54, v55, v54
	v_sub_f32_e32 v55, 1.0, v63
	v_mul_f32_e32 v53, v55, v53
	v_sub_f32_e32 v55, 1.0, v64
	v_mul_f32_e32 v55, v55, v38
	v_sub_f32_e32 v38, 1.0, v65
	v_mul_f32_e32 v56, v38, v179
	v_cvt_pk_bf16_f32 v38, v40, v39
	v_cvt_pk_bf16_f32 v39, v41, v52
	v_mul_f32_e32 v52, v37, v177
	v_cvt_pk_bf16_f32 v40, v54, v53
	v_mul_f32_e32 v53, v36, v52
	v_sub_f32_e32 v36, 1.0, v36
	v_mul_f32_e32 v54, v35, v53
	v_sub_f32_e32 v35, 1.0, v35
	v_mul_f32_e32 v36, v36, v52
	v_mul_f32_e32 v52, v173, v178
	v_sub_f32_e32 v34, 1.0, v34
	v_mul_f32_e32 v35, v35, v53
	v_mul_f32_e32 v53, v172, v52
	v_cvt_pk_bf16_f32 v41, v55, v56
	v_mul_f32_e32 v34, v34, v54
	v_mul_f32_e32 v54, v171, v53
	v_sub_f32_e32 v55, 1.0, v170
	v_mul_f32_e32 v54, v55, v54
	v_sub_f32_e32 v55, 1.0, v171
	v_mul_f32_e32 v53, v55, v53
	v_sub_f32_e32 v55, 1.0, v172
	v_sub_f32_e32 v37, 1.0, v37
	v_mul_f32_e32 v52, v55, v52
	v_sub_f32_e32 v55, 1.0, v173
	v_mul_f32_e32 v37, v37, v177
	v_mul_f32_e32 v55, v55, v178
	v_cvt_pk_bf16_f32 v34, v34, v35
	v_cvt_pk_bf16_f32 v35, v36, v37
	v_cvt_pk_bf16_f32 v37, v52, v55
	v_mul_f32_e32 v52, v45, v180
	v_cndmask_b32_e64 v166, v166, v182, s[36:37]
	v_cvt_pk_bf16_f32 v36, v54, v53
	v_mul_f32_e32 v53, v44, v52
	v_sub_f32_e32 v44, 1.0, v44
	v_mul_f32_e32 v54, v43, v53
	v_sub_f32_e32 v43, 1.0, v43
	v_mul_f32_e32 v44, v44, v52
	v_mul_f32_e32 v52, v167, v166
	v_mul_f32_e32 v43, v43, v53
	v_mul_f32_e32 v53, v176, v52
	v_mul_f32_e32 v42, v42, v54
	v_mul_f32_e32 v54, v175, v53
	v_sub_f32_e32 v55, 1.0, v174
	v_mul_f32_e32 v54, v55, v54
	v_sub_f32_e32 v55, 1.0, v175
	v_mul_f32_e32 v53, v55, v53
	v_sub_f32_e32 v55, 1.0, v176
	v_sub_f32_e32 v45, 1.0, v45
	v_mul_f32_e32 v52, v55, v52
	v_sub_f32_e32 v55, 1.0, v167
	v_mul_f32_e32 v45, v45, v180
	v_mul_f32_e32 v55, v55, v166
	v_cvt_pk_bf16_f32 v42, v42, v43
	v_cvt_pk_bf16_f32 v43, v44, v45
	v_cvt_pk_bf16_f32 v44, v54, v53
	v_cvt_pk_bf16_f32 v45, v52, v55
	v_mul_f32_e32 v166, v51, v50
	ds_read_b64_tr_b16 v[50:51], v117
	ds_read_b64_tr_b16 v[52:53], v117 offset:1536
	ds_read_b64_tr_b16 v[54:55], v117 offset:3072
	ds_read_b64_tr_b16 v[56:57], v117 offset:4608
	ds_read_b64_tr_b16 v[58:59], v117 offset:6144
	ds_read_b64_tr_b16 v[60:61], v117 offset:7680
	ds_read_b64_tr_b16 v[62:63], v117 offset:9216
	ds_read_b64_tr_b16 v[64:65], v117 offset:10752
	s_waitcnt lgkmcnt(0)
	s_nop 0
	v_mfma_f32_32x32x16_bf16 v[18:33], v[50:53], v[46:49], v[18:33]
	v_cmp_gt_f32_e32 vcc, s29, v166
	s_cmp_lg_u64 vcc, exec
	s_cselect_b64 s[38:39], -1, 0
	s_cmp_lg_u32 s35, 0
	s_cselect_b64 s[40:41], -1, 0
	s_and_b64 s[38:39], s[40:41], s[38:39]
	s_sub_i32 s34, s34, 64
	v_mfma_f32_32x32x16_bf16 v[18:33], v[54:57], v[38:41], v[18:33]
	s_and_b64 vcc, exec, s[38:39]
	v_mfma_f32_32x32x16_bf16 v[18:33], v[58:61], v[34:37], v[18:33]
	v_mfma_f32_32x32x16_bf16 v[18:33], v[62:65], v[42:45], v[18:33]
	ds_read_b64_tr_b16 v[62:63], v117 offset:64
	ds_read_b64_tr_b16 v[64:65], v117 offset:1600
	ds_read_b64_tr_b16 v[58:59], v117 offset:3136
	ds_read_b64_tr_b16 v[60:61], v117 offset:4672
	ds_read_b64_tr_b16 v[50:51], v117 offset:6208
	ds_read_b64_tr_b16 v[52:53], v117 offset:7744
	ds_read_b64_tr_b16 v[54:55], v117 offset:9280
	ds_read_b64_tr_b16 v[56:57], v117 offset:10816
	s_waitcnt lgkmcnt(0)
	s_nop 0
	v_mfma_f32_32x32x16_bf16 v[2:17], v[62:65], v[46:49], v[2:17]
	v_mfma_f32_32x32x16_bf16 v[2:17], v[58:61], v[38:41], v[2:17]
	v_mfma_f32_32x32x16_bf16 v[2:17], v[50:53], v[34:37], v[2:17]
	v_mfma_f32_32x32x16_bf16 v[2:17], v[54:57], v[42:45], v[2:17]
	s_cbranch_vccnz .LBB0_1171
	v_lshlrev_b32_e32 v34, 1, v114
	v_mov_b32_e32 v35, v1
	v_lshl_add_u64 v[34:35], v[138:139], 0, v[34:35]
	v_cvt_pk_bf16_f32 v18, v18, v19
	v_cvt_pk_bf16_f32 v19, v20, v21
	s_nop 5
	v_cvt_pk_bf16_f32 v2, v2, v3
	v_cvt_pk_bf16_f32 v3, v4, v5
	global_store_dwordx2 v[34:35], v[18:19], off sc1
	global_store_dwordx2 v[34:35], v[2:3], off offset:64 sc1
	v_cvt_pk_bf16_f32 v2, v22, v23
	v_cvt_pk_bf16_f32 v3, v24, v25
	v_cvt_pk_bf16_f32 v4, v6, v7
	v_cvt_pk_bf16_f32 v5, v8, v9
	global_store_dwordx2 v[34:35], v[2:3], off offset:16 sc1
	global_store_dwordx2 v[34:35], v[4:5], off offset:80 sc1
	v_cvt_pk_bf16_f32 v2, v26, v27
	v_cvt_pk_bf16_f32 v3, v28, v29
	v_cvt_pk_bf16_f32 v4, v10, v11
	v_cvt_pk_bf16_f32 v5, v12, v13
	s_add_i32 s17, s17, s72
	s_add_i32 s16, s16, s72
	global_store_dwordx2 v[34:35], v[2:3], off offset:32 sc1
	global_store_dwordx2 v[34:35], v[4:5], off offset:96 sc1
	v_cvt_pk_bf16_f32 v2, v30, v31
	v_cvt_pk_bf16_f32 v3, v32, v33
	v_cvt_pk_bf16_f32 v4, v14, v15
	v_cvt_pk_bf16_f32 v5, v16, v17
	s_cmpk_lt_i32 s17, 0x1000
	global_store_dwordx2 v[34:35], v[2:3], off offset:48 sc1
	global_store_dwordx2 v[34:35], v[4:5], off offset:112 sc1
	s_cbranch_scc1 .LBB0_1170

.LBB0_1175:
	s_or_b64 exec, exec, s[16:17]
	v_lshlrev_b64 v[28:29], 9, v[98:99]
	v_lshl_add_u64 v[102:103], v[28:29], 1, v[96:97]
	global_load_dwordx4 v[82:85], v[26:27], off
	global_load_dwordx4 v[110:113], v[102:103], off
	global_load_dwordx4 v[74:77], v[26:27], off offset:1024
	global_load_dwordx4 v[78:81], v[102:103], off offset:1024
	global_load_dwordx4 v[66:69], v[26:27], off offset:2048
	global_load_dwordx4 v[70:73], v[102:103], off offset:2048
	global_load_dwordx4 v[58:61], v[26:27], off offset:3072
	global_load_dwordx4 v[62:65], v[102:103], off offset:3072
	s_movk_i32 s16, 0x1000
	v_add_co_u32_e32 v26, vcc, s16, v26
	s_waitcnt vmcnt(8)
	v_lshlrev_b32_e32 v114, 16, v90
	v_addc_co_u32_e32 v27, vcc, 0, v27, vcc
	global_load_dwordx4 v[50:53], v[26:27], off
	v_add_co_u32_e32 v100, vcc, s16, v102
	v_and_b32_e32 v115, 0xffff0000, v90
	s_nop 0
	v_addc_co_u32_e32 v101, vcc, 0, v103, vcc
	global_load_dwordx4 v[54:57], v[100:101], off
	global_load_dwordx4 v[42:45], v[26:27], off offset:1024
	global_load_dwordx4 v[46:49], v[100:101], off offset:1024
	global_load_dwordx4 v[34:37], v[26:27], off offset:2048
	global_load_dwordx4 v[38:41], v[100:101], off offset:2048
	s_nop 0
	global_load_dwordx4 v[26:29], v[26:27], off offset:3072
	s_nop 0
	global_load_dwordx4 v[30:33], v[100:101], off offset:3072
	v_lshlrev_b32_e32 v104, 16, v86
	v_and_b32_e32 v105, 0xffff0000, v86
	v_pk_mul_f32 v[116:117], v[10:11], v[114:115]
	v_lshlrev_b32_e32 v90, 16, v91
	v_pk_fma_f32 v[116:117], v[18:19], v[104:105], v[116:117]
	v_and_b32_e32 v91, 0xffff0000, v91
	v_lshlrev_b32_e32 v86, 16, v87
	v_and_b32_e32 v87, 0xffff0000, v87
	v_readlane_b32 s16, v253, 8
	v_add_u32_e32 v108, s72, v108
	s_waitcnt vmcnt(15)
	v_lshlrev_b32_e32 v104, 16, v82
	v_and_b32_e32 v105, 0xffff0000, v82
	s_waitcnt vmcnt(14)
	v_lshlrev_b32_e32 v106, 16, v110
	v_and_b32_e32 v107, 0xffff0000, v110
	v_pk_fma_f32 v[116:117], v[2:3], v[104:105], v[116:117]
	v_lshlrev_b32_e32 v82, 16, v83
	v_pk_mul_f32 v[116:117], v[116:117], v[106:107]
	v_lshlrev_b32_e32 v106, 16, v111
	v_and_b32_e32 v107, 0xffff0000, v111
	v_pk_mul_f32 v[110:111], v[12:13], v[90:91]
	v_and_b32_e32 v83, 0xffff0000, v83
	v_pk_fma_f32 v[86:87], v[20:21], v[86:87], v[110:111]
	v_lshlrev_b32_e32 v110, 16, v112
	v_pk_fma_f32 v[86:87], v[4:5], v[82:83], v[86:87]
	v_and_b32_e32 v111, 0xffff0000, v112
	v_pk_mul_f32 v[118:119], v[86:87], v[106:107]
	v_lshlrev_b32_e32 v106, 16, v92
	v_and_b32_e32 v107, 0xffff0000, v92
	v_lshlrev_b32_e32 v86, 16, v88
	v_and_b32_e32 v87, 0xffff0000, v88
	v_pk_mul_f32 v[120:121], v[14:15], v[106:107]
	v_lshlrev_b32_e32 v92, 16, v93
	v_pk_fma_f32 v[120:121], v[22:23], v[86:87], v[120:121]
	v_lshlrev_b32_e32 v86, 16, v84
	v_and_b32_e32 v87, 0xffff0000, v84
	v_pk_fma_f32 v[120:121], v[6:7], v[86:87], v[120:121]
	v_and_b32_e32 v93, 0xffff0000, v93
	v_pk_mul_f32 v[120:121], v[120:121], v[110:111]
	v_lshlrev_b32_e32 v110, 16, v113
	v_and_b32_e32 v111, 0xffff0000, v113
	v_lshlrev_b32_e32 v88, 16, v89
	v_and_b32_e32 v89, 0xffff0000, v89
	v_pk_mul_f32 v[112:113], v[16:17], v[92:93]
	v_lshlrev_b32_e32 v84, 16, v85
	v_pk_fma_f32 v[88:89], v[24:25], v[88:89], v[112:113]
	v_and_b32_e32 v85, 0xffff0000, v85
	v_pk_fma_f32 v[88:89], v[8:9], v[84:85], v[88:89]
	v_cvt_pk_bf16_f32 v112, v120, v121
	v_pk_mul_f32 v[88:89], v[88:89], v[110:111]
	v_cvt_pk_bf16_f32 v110, v116, v117
	v_cvt_pk_bf16_f32 v111, v118, v119
	v_cvt_pk_bf16_f32 v113, v88, v89
	global_store_dwordx4 v[102:103], v[110:113], off sc1
	s_waitcnt vmcnt(13)
	v_lshlrev_b32_e32 v88, 16, v78
	v_and_b32_e32 v89, 0xffff0000, v78
	v_pk_mul_f32 v[110:111], v[10:11], v[104:105]
	v_lshlrev_b32_e32 v112, 16, v74
	v_pk_fma_f32 v[110:111], v[18:19], v[114:115], v[110:111]
	v_and_b32_e32 v113, 0xffff0000, v74
	v_pk_fma_f32 v[110:111], v[2:3], v[112:113], v[110:111]
	v_lshlrev_b32_e32 v78, 16, v79
	v_pk_mul_f32 v[88:89], v[110:111], v[88:89]
	v_pk_mul_f32 v[110:111], v[12:13], v[82:83]
	v_and_b32_e32 v79, 0xffff0000, v79
	v_pk_fma_f32 v[90:91], v[20:21], v[90:91], v[110:111]
	v_lshlrev_b32_e32 v110, 16, v75
	v_and_b32_e32 v111, 0xffff0000, v75
	v_pk_fma_f32 v[74:75], v[4:5], v[110:111], v[90:91]
	v_pk_mul_f32 v[90:91], v[14:15], v[86:87]
	v_pk_mul_f32 v[78:79], v[74:75], v[78:79]
	v_pk_fma_f32 v[90:91], v[22:23], v[106:107], v[90:91]
	v_lshlrev_b32_e32 v106, 16, v76
	v_and_b32_e32 v107, 0xffff0000, v76
	v_lshlrev_b32_e32 v74, 16, v80
	v_and_b32_e32 v75, 0xffff0000, v80
	v_pk_fma_f32 v[90:91], v[6:7], v[106:107], v[90:91]
	v_add_u32_e32 v98, s16, v98
	v_pk_mul_f32 v[90:91], v[90:91], v[74:75]
	v_lshlrev_b32_e32 v74, 16, v81
	v_and_b32_e32 v75, 0xffff0000, v81
	v_pk_mul_f32 v[80:81], v[16:17], v[84:85]
	s_movk_i32 s16, 0x7ff
	v_pk_fma_f32 v[80:81], v[24:25], v[92:93], v[80:81]
	v_lshlrev_b32_e32 v92, 16, v77
	v_and_b32_e32 v93, 0xffff0000, v77
	v_pk_fma_f32 v[76:77], v[8:9], v[92:93], v[80:81]
	v_cmp_lt_i32_e32 vcc, s16, v108
	v_pk_mul_f32 v[80:81], v[76:77], v[74:75]
	v_cvt_pk_bf16_f32 v74, v88, v89
	v_cvt_pk_bf16_f32 v75, v78, v79
	v_cvt_pk_bf16_f32 v76, v90, v91
	v_cvt_pk_bf16_f32 v77, v80, v81
	global_store_dwordx4 v[102:103], v[74:77], off offset:1024 sc1
	s_waitcnt vmcnt(13)
	v_lshlrev_b32_e32 v78, 16, v66
	v_and_b32_e32 v79, 0xffff0000, v66
	v_pk_mul_f32 v[76:77], v[10:11], v[112:113]
	s_waitcnt vmcnt(12)
	v_lshlrev_b32_e32 v74, 16, v70
	v_pk_fma_f32 v[76:77], v[18:19], v[104:105], v[76:77]
	v_and_b32_e32 v75, 0xffff0000, v70
	v_pk_fma_f32 v[76:77], v[2:3], v[78:79], v[76:77]
	v_lshlrev_b32_e32 v80, 16, v67
	v_pk_mul_f32 v[74:75], v[76:77], v[74:75]
	v_pk_mul_f32 v[76:77], v[12:13], v[110:111]
	v_and_b32_e32 v81, 0xffff0000, v67
	v_pk_fma_f32 v[76:77], v[20:21], v[82:83], v[76:77]
	v_lshlrev_b32_e32 v70, 16, v71
	v_pk_fma_f32 v[66:67], v[4:5], v[80:81], v[76:77]
	v_pk_mul_f32 v[76:77], v[14:15], v[106:107]
	v_and_b32_e32 v71, 0xffff0000, v71
	v_pk_fma_f32 v[76:77], v[22:23], v[86:87], v[76:77]
	v_lshlrev_b32_e32 v82, 16, v68
	v_and_b32_e32 v83, 0xffff0000, v68
	v_pk_mul_f32 v[70:71], v[66:67], v[70:71]
	v_lshlrev_b32_e32 v66, 16, v72
	v_and_b32_e32 v67, 0xffff0000, v72
	v_pk_fma_f32 v[76:77], v[6:7], v[82:83], v[76:77]
	s_or_b64 s[14:15], vcc, s[14:15]
	v_pk_mul_f32 v[76:77], v[76:77], v[66:67]
	v_lshlrev_b32_e32 v66, 16, v73
	v_and_b32_e32 v67, 0xffff0000, v73
	v_pk_mul_f32 v[72:73], v[16:17], v[92:93]
	s_nop 0
	v_pk_fma_f32 v[72:73], v[24:25], v[84:85], v[72:73]
	v_lshlrev_b32_e32 v84, 16, v69
	v_and_b32_e32 v85, 0xffff0000, v69
	v_pk_fma_f32 v[68:69], v[8:9], v[84:85], v[72:73]
	s_nop 0
	v_pk_mul_f32 v[72:73], v[68:69], v[66:67]
	v_cvt_pk_bf16_f32 v66, v74, v75
	v_cvt_pk_bf16_f32 v67, v70, v71
	v_cvt_pk_bf16_f32 v68, v76, v77
	v_cvt_pk_bf16_f32 v69, v72, v73
	global_store_dwordx4 v[102:103], v[66:69], off offset:2048 sc1
	s_waitcnt vmcnt(12)
	v_lshlrev_b32_e32 v70, 16, v58
	v_and_b32_e32 v71, 0xffff0000, v58
	v_pk_mul_f32 v[68:69], v[10:11], v[78:79]
	s_waitcnt vmcnt(11)
	v_lshlrev_b32_e32 v66, 16, v62
	v_pk_fma_f32 v[68:69], v[18:19], v[112:113], v[68:69]
	v_and_b32_e32 v67, 0xffff0000, v62
	v_pk_fma_f32 v[68:69], v[2:3], v[70:71], v[68:69]
	v_lshlrev_b32_e32 v72, 16, v59
	v_pk_mul_f32 v[66:67], v[68:69], v[66:67]
	v_pk_mul_f32 v[68:69], v[12:13], v[80:81]
	v_and_b32_e32 v73, 0xffff0000, v59
	v_pk_fma_f32 v[68:69], v[20:21], v[110:111], v[68:69]
	v_lshlrev_b32_e32 v62, 16, v63
	v_pk_fma_f32 v[58:59], v[4:5], v[72:73], v[68:69]
	v_pk_mul_f32 v[68:69], v[14:15], v[82:83]
	v_and_b32_e32 v63, 0xffff0000, v63
	v_pk_fma_f32 v[68:69], v[22:23], v[106:107], v[68:69]
	v_lshlrev_b32_e32 v74, 16, v60
	v_and_b32_e32 v75, 0xffff0000, v60
	v_pk_mul_f32 v[62:63], v[58:59], v[62:63]
	v_lshlrev_b32_e32 v58, 16, v64
	v_and_b32_e32 v59, 0xffff0000, v64
	v_pk_fma_f32 v[68:69], v[6:7], v[74:75], v[68:69]
	v_lshlrev_b32_e32 v76, 16, v61
	v_pk_mul_f32 v[68:69], v[68:69], v[58:59]
	v_lshlrev_b32_e32 v58, 16, v65
	v_and_b32_e32 v59, 0xffff0000, v65
	v_pk_mul_f32 v[64:65], v[16:17], v[84:85]
	v_and_b32_e32 v77, 0xffff0000, v61
	v_pk_fma_f32 v[64:65], v[24:25], v[92:93], v[64:65]
	s_nop 0
	v_pk_fma_f32 v[60:61], v[8:9], v[76:77], v[64:65]
	s_nop 0
	v_pk_mul_f32 v[64:65], v[60:61], v[58:59]
	v_cvt_pk_bf16_f32 v58, v66, v67
	v_cvt_pk_bf16_f32 v59, v62, v63
	v_cvt_pk_bf16_f32 v60, v68, v69
	v_cvt_pk_bf16_f32 v61, v64, v65
	global_store_dwordx4 v[102:103], v[58:61], off offset:3072 sc1
	s_waitcnt vmcnt(11)
	v_lshlrev_b32_e32 v62, 16, v50
	v_and_b32_e32 v63, 0xffff0000, v50
	v_pk_mul_f32 v[60:61], v[10:11], v[70:71]
	s_waitcnt vmcnt(10)
	v_lshlrev_b32_e32 v58, 16, v54
	v_pk_fma_f32 v[60:61], v[18:19], v[78:79], v[60:61]
	v_and_b32_e32 v59, 0xffff0000, v54
	v_pk_fma_f32 v[60:61], v[2:3], v[62:63], v[60:61]
	v_lshlrev_b32_e32 v64, 16, v51
	v_pk_mul_f32 v[58:59], v[60:61], v[58:59]
	v_pk_mul_f32 v[60:61], v[12:13], v[72:73]
	v_and_b32_e32 v65, 0xffff0000, v51
	v_pk_fma_f32 v[60:61], v[20:21], v[80:81], v[60:61]
	v_lshlrev_b32_e32 v54, 16, v55
	v_pk_fma_f32 v[50:51], v[4:5], v[64:65], v[60:61]
	v_pk_mul_f32 v[60:61], v[14:15], v[74:75]
	v_and_b32_e32 v55, 0xffff0000, v55
	v_pk_fma_f32 v[60:61], v[22:23], v[82:83], v[60:61]
	v_lshlrev_b32_e32 v66, 16, v52
	v_and_b32_e32 v67, 0xffff0000, v52
	v_pk_mul_f32 v[54:55], v[50:51], v[54:55]
	v_lshlrev_b32_e32 v50, 16, v56
	v_and_b32_e32 v51, 0xffff0000, v56
	v_pk_fma_f32 v[60:61], v[6:7], v[66:67], v[60:61]
	v_lshlrev_b32_e32 v68, 16, v53
	v_pk_mul_f32 v[60:61], v[60:61], v[50:51]
	v_lshlrev_b32_e32 v50, 16, v57
	v_and_b32_e32 v51, 0xffff0000, v57
	v_pk_mul_f32 v[56:57], v[16:17], v[76:77]
	v_and_b32_e32 v69, 0xffff0000, v53
	v_pk_fma_f32 v[56:57], v[24:25], v[84:85], v[56:57]
	s_nop 0
	v_pk_fma_f32 v[52:53], v[8:9], v[68:69], v[56:57]
	s_nop 0
	v_pk_mul_f32 v[56:57], v[52:53], v[50:51]
	v_cvt_pk_bf16_f32 v50, v58, v59
	v_cvt_pk_bf16_f32 v51, v54, v55
	v_cvt_pk_bf16_f32 v52, v60, v61
	v_cvt_pk_bf16_f32 v53, v56, v57
	global_store_dwordx4 v[100:101], v[50:53], off sc1
	s_waitcnt vmcnt(10)
	v_lshlrev_b32_e32 v54, 16, v42
	v_and_b32_e32 v55, 0xffff0000, v42
	v_pk_mul_f32 v[52:53], v[10:11], v[62:63]
	s_waitcnt vmcnt(9)
	v_lshlrev_b32_e32 v50, 16, v46
	v_pk_fma_f32 v[52:53], v[18:19], v[70:71], v[52:53]
	v_and_b32_e32 v51, 0xffff0000, v46
	v_pk_fma_f32 v[52:53], v[2:3], v[54:55], v[52:53]
	v_lshlrev_b32_e32 v56, 16, v43
	v_pk_mul_f32 v[50:51], v[52:53], v[50:51]
	v_pk_mul_f32 v[52:53], v[12:13], v[64:65]
	v_and_b32_e32 v57, 0xffff0000, v43
	v_pk_fma_f32 v[52:53], v[20:21], v[72:73], v[52:53]
	v_lshlrev_b32_e32 v46, 16, v47
	v_pk_fma_f32 v[42:43], v[4:5], v[56:57], v[52:53]
	v_pk_mul_f32 v[52:53], v[14:15], v[66:67]
	v_and_b32_e32 v47, 0xffff0000, v47
	v_pk_fma_f32 v[52:53], v[22:23], v[74:75], v[52:53]
	v_lshlrev_b32_e32 v58, 16, v44
	v_and_b32_e32 v59, 0xffff0000, v44
	v_pk_mul_f32 v[46:47], v[42:43], v[46:47]
	v_lshlrev_b32_e32 v42, 16, v48
	v_and_b32_e32 v43, 0xffff0000, v48
	v_pk_fma_f32 v[52:53], v[6:7], v[58:59], v[52:53]
	v_lshlrev_b32_e32 v60, 16, v45
	v_pk_mul_f32 v[52:53], v[52:53], v[42:43]
	v_lshlrev_b32_e32 v42, 16, v49
	v_and_b32_e32 v43, 0xffff0000, v49
	v_pk_mul_f32 v[48:49], v[16:17], v[68:69]
	v_and_b32_e32 v61, 0xffff0000, v45
	v_pk_fma_f32 v[48:49], v[24:25], v[76:77], v[48:49]
	s_nop 0
	v_pk_fma_f32 v[44:45], v[8:9], v[60:61], v[48:49]
	s_nop 0
	v_pk_mul_f32 v[48:49], v[44:45], v[42:43]
	v_cvt_pk_bf16_f32 v42, v50, v51
	v_cvt_pk_bf16_f32 v43, v46, v47
	v_cvt_pk_bf16_f32 v44, v52, v53
	v_cvt_pk_bf16_f32 v45, v48, v49
	global_store_dwordx4 v[100:101], v[42:45], off offset:1024 sc1
	s_waitcnt vmcnt(9)
	v_lshlrev_b32_e32 v46, 16, v34
	v_and_b32_e32 v47, 0xffff0000, v34
	v_pk_mul_f32 v[44:45], v[10:11], v[54:55]
	s_waitcnt vmcnt(8)
	v_lshlrev_b32_e32 v42, 16, v38
	v_pk_fma_f32 v[44:45], v[18:19], v[62:63], v[44:45]
	v_and_b32_e32 v43, 0xffff0000, v38
	v_pk_fma_f32 v[44:45], v[2:3], v[46:47], v[44:45]
	v_lshlrev_b32_e32 v48, 16, v35
	v_pk_mul_f32 v[42:43], v[44:45], v[42:43]
	v_pk_mul_f32 v[44:45], v[12:13], v[56:57]
	v_and_b32_e32 v49, 0xffff0000, v35
	v_pk_fma_f32 v[44:45], v[20:21], v[64:65], v[44:45]
	v_lshlrev_b32_e32 v38, 16, v39
	v_pk_fma_f32 v[34:35], v[4:5], v[48:49], v[44:45]
	v_pk_mul_f32 v[44:45], v[14:15], v[58:59]
	v_and_b32_e32 v39, 0xffff0000, v39
	v_pk_fma_f32 v[44:45], v[22:23], v[66:67], v[44:45]
	v_lshlrev_b32_e32 v50, 16, v36
	v_and_b32_e32 v51, 0xffff0000, v36
	v_pk_mul_f32 v[38:39], v[34:35], v[38:39]
	v_lshlrev_b32_e32 v34, 16, v40
	v_and_b32_e32 v35, 0xffff0000, v40
	v_pk_fma_f32 v[44:45], v[6:7], v[50:51], v[44:45]
	v_lshlrev_b32_e32 v52, 16, v37
	v_pk_mul_f32 v[44:45], v[44:45], v[34:35]
	v_lshlrev_b32_e32 v34, 16, v41
	v_and_b32_e32 v35, 0xffff0000, v41
	v_pk_mul_f32 v[40:41], v[16:17], v[60:61]
	v_and_b32_e32 v53, 0xffff0000, v37
	v_pk_fma_f32 v[40:41], v[24:25], v[68:69], v[40:41]
	s_nop 0
	v_pk_fma_f32 v[36:37], v[8:9], v[52:53], v[40:41]
	s_nop 0
	v_pk_mul_f32 v[40:41], v[36:37], v[34:35]
	v_cvt_pk_bf16_f32 v34, v42, v43
	v_cvt_pk_bf16_f32 v35, v38, v39
	v_cvt_pk_bf16_f32 v36, v44, v45
	v_cvt_pk_bf16_f32 v37, v40, v41
	global_store_dwordx4 v[100:101], v[34:37], off offset:2048 sc1
	s_waitcnt vmcnt(8)
	v_lshlrev_b32_e32 v38, 16, v26
	v_and_b32_e32 v39, 0xffff0000, v26
	v_pk_mul_f32 v[36:37], v[10:11], v[46:47]
	s_waitcnt vmcnt(7)
	v_lshlrev_b32_e32 v34, 16, v30
	v_pk_fma_f32 v[36:37], v[18:19], v[54:55], v[36:37]
	v_and_b32_e32 v35, 0xffff0000, v30
	v_pk_fma_f32 v[36:37], v[2:3], v[38:39], v[36:37]
	v_lshlrev_b32_e32 v26, 16, v27
	v_pk_mul_f32 v[34:35], v[36:37], v[34:35]
	v_pk_mul_f32 v[36:37], v[12:13], v[48:49]
	v_and_b32_e32 v27, 0xffff0000, v27
	v_pk_fma_f32 v[36:37], v[20:21], v[56:57], v[36:37]
	v_lshlrev_b32_e32 v30, 16, v31
	v_pk_fma_f32 v[26:27], v[4:5], v[26:27], v[36:37]
	v_pk_mul_f32 v[36:37], v[14:15], v[50:51]
	v_and_b32_e32 v31, 0xffff0000, v31
	v_pk_fma_f32 v[36:37], v[22:23], v[58:59], v[36:37]
	v_lshlrev_b32_e32 v38, 16, v28
	v_and_b32_e32 v39, 0xffff0000, v28
	v_pk_mul_f32 v[30:31], v[26:27], v[30:31]
	v_lshlrev_b32_e32 v26, 16, v32
	v_and_b32_e32 v27, 0xffff0000, v32
	v_pk_fma_f32 v[36:37], v[6:7], v[38:39], v[36:37]
	v_lshlrev_b32_e32 v28, 16, v29
	v_pk_mul_f32 v[36:37], v[36:37], v[26:27]
	v_lshlrev_b32_e32 v26, 16, v33
	v_and_b32_e32 v27, 0xffff0000, v33
	v_pk_mul_f32 v[32:33], v[16:17], v[52:53]
	v_and_b32_e32 v29, 0xffff0000, v29
	v_pk_fma_f32 v[32:33], v[24:25], v[60:61], v[32:33]
	s_nop 0
	v_pk_fma_f32 v[28:29], v[8:9], v[28:29], v[32:33]
	s_nop 0
	v_pk_mul_f32 v[32:33], v[28:29], v[26:27]
	v_cvt_pk_bf16_f32 v26, v34, v35
	v_cvt_pk_bf16_f32 v27, v30, v31
	v_cvt_pk_bf16_f32 v28, v36, v37
	v_cvt_pk_bf16_f32 v29, v32, v33
	global_store_dwordx4 v[100:101], v[26:29], off offset:3072 sc1
	s_andn2_b64 exec, exec, s[14:15]
	s_cbranch_execz .LBB0_1178

.LBB0_1198:
	s_ashr_i32 s42, s47, 2
	s_mov_b32 s17, -1
	s_ashr_i32 s43, s42, 31
	s_lshl_b64 s[42:43], s[42:43], 21
	v_mbcnt_lo_u32_b32 v0, s17, 0
	v_mbcnt_hi_u32_b32 v138, s17, v0
	s_add_u32 s17, s93, s42
	s_addc_u32 s29, s94, s43
	s_lshl_b32 s42, s47, 19
	s_and_b32 s42, s42, 0x180000
	s_add_u32 s17, s17, s42
	s_addc_u32 s29, s29, 0
	s_ashr_i32 s47, s46, 31
	s_lshl_b64 s[42:43], s[46:47], 9
	s_add_u32 s17, s17, s42
	s_addc_u32 s29, s29, s43
	s_add_u32 s42, s17, s35
	s_addc_u32 s43, s29, 0
	v_and_b32_e32 v0, 0x70, v138
	v_lshl_add_u64 v[142:143], s[42:43], 0, v[0:1]
	v_and_or_b32 v0, v138, 15, s84
	v_lshl_add_u32 v144, s1, 8, v0
	v_ashrrev_i32_e32 v145, 31, v144
	v_lshlrev_b64 v[138:139], 11, v[144:145]
	v_pk_mul_f32 v[128:129], v[128:129], s[26:27] op_sel_hi:[1,0]
	v_pk_mul_f32 v[126:127], v[126:127], s[26:27] op_sel_hi:[1,0]
	v_pk_mul_f32 v[146:147], v[124:125], s[26:27] op_sel_hi:[1,0]
	v_pk_mul_f32 v[124:125], v[122:123], s[26:27] op_sel_hi:[1,0]
	v_lshl_add_u64 v[138:139], v[142:143], 0, v[138:139]
	v_cvt_pk_bf16_f32 v122, v126, v127
	v_cvt_pk_bf16_f32 v123, v128, v129
	v_cvt_pk_bf16_f32 v124, v124, v125
	v_cvt_pk_bf16_f32 v125, v146, v147
	global_store_dwordx4 v[138:139], v[122:125], off sc1
	v_pk_mul_f32 v[116:117], v[116:117], s[26:27] op_sel_hi:[1,0]
	v_pk_mul_f32 v[114:115], v[114:115], s[26:27] op_sel_hi:[1,0]
	v_pk_mul_f32 v[122:123], v[108:109], s[26:27] op_sel_hi:[1,0]
	v_pk_mul_f32 v[108:109], v[106:107], s[26:27] op_sel_hi:[1,0]
	v_cvt_pk_bf16_f32 v106, v114, v115
	v_cvt_pk_bf16_f32 v107, v116, v117
	v_cvt_pk_bf16_f32 v108, v108, v109
	v_cvt_pk_bf16_f32 v109, v122, v123
	global_store_dwordx4 v[138:139], v[106:109], off offset:256 sc1
	v_pk_mul_f32 v[112:113], v[112:113], s[26:27] op_sel_hi:[1,0]
	v_pk_mul_f32 v[110:111], v[110:111], s[26:27] op_sel_hi:[1,0]
	v_or_b32_e32 v106, 16, v144
	v_ashrrev_i32_e32 v107, 31, v106
	v_lshlrev_b64 v[106:107], 11, v[106:107]
	v_lshl_add_u64 v[114:115], v[142:143], 0, v[106:107]
	v_pk_mul_f32 v[108:109], v[120:121], s[26:27] op_sel_hi:[1,0]
	v_pk_mul_f32 v[106:107], v[118:119], s[26:27] op_sel_hi:[1,0]
	v_pk_mul_f32 v[100:101], v[100:101], s[26:27] op_sel_hi:[1,0]
	v_cvt_pk_bf16_f32 v106, v106, v107
	v_cvt_pk_bf16_f32 v107, v108, v109
	v_cvt_pk_bf16_f32 v108, v110, v111
	v_cvt_pk_bf16_f32 v109, v112, v113
	global_store_dwordx4 v[114:115], v[106:109], off sc1
	v_pk_mul_f32 v[98:99], v[98:99], s[26:27] op_sel_hi:[1,0]
	v_pk_mul_f32 v[96:97], v[96:97], s[26:27] op_sel_hi:[1,0]
	v_pk_mul_f32 v[106:107], v[92:93], s[26:27] op_sel_hi:[1,0]
	v_pk_mul_f32 v[92:93], v[90:91], s[26:27] op_sel_hi:[1,0]
	v_cvt_pk_bf16_f32 v90, v98, v99
	v_cvt_pk_bf16_f32 v91, v100, v101
	v_cvt_pk_bf16_f32 v92, v92, v93
	v_cvt_pk_bf16_f32 v93, v106, v107
	global_store_dwordx4 v[114:115], v[90:93], off offset:256 sc1
	v_pk_mul_f32 v[94:95], v[94:95], s[26:27] op_sel_hi:[1,0]
	v_pk_mul_f32 v[84:85], v[84:85], s[26:27] op_sel_hi:[1,0]
	v_or_b32_e32 v90, 32, v144
	v_ashrrev_i32_e32 v91, 31, v90
	v_lshlrev_b64 v[90:91], 11, v[90:91]
	v_lshl_add_u64 v[98:99], v[142:143], 0, v[90:91]
	v_pk_mul_f32 v[92:93], v[104:105], s[26:27] op_sel_hi:[1,0]
	v_pk_mul_f32 v[90:91], v[102:103], s[26:27] op_sel_hi:[1,0]
	v_pk_mul_f32 v[82:83], v[82:83], s[26:27] op_sel_hi:[1,0]
	v_cvt_pk_bf16_f32 v90, v90, v91
	v_cvt_pk_bf16_f32 v91, v92, v93
	v_cvt_pk_bf16_f32 v92, v94, v95
	v_cvt_pk_bf16_f32 v93, v96, v97
	global_store_dwordx4 v[98:99], v[90:93], off sc1
	v_pk_mul_f32 v[80:81], v[80:81], s[26:27] op_sel_hi:[1,0]
	v_pk_mul_f32 v[78:79], v[78:79], s[26:27] op_sel_hi:[1,0]
	v_pk_mul_f32 v[90:91], v[76:77], s[26:27] op_sel_hi:[1,0]
	v_pk_mul_f32 v[76:77], v[74:75], s[26:27] op_sel_hi:[1,0]
	v_cvt_pk_bf16_f32 v74, v82, v83
	v_cvt_pk_bf16_f32 v75, v84, v85
	v_cvt_pk_bf16_f32 v76, v76, v77
	v_cvt_pk_bf16_f32 v77, v90, v91
	global_store_dwordx4 v[98:99], v[74:77], off offset:256 sc1
	v_pk_mul_f32 v[72:73], v[72:73], s[26:27] op_sel_hi:[1,0]
	v_pk_mul_f32 v[70:71], v[70:71], s[26:27] op_sel_hi:[1,0]
	v_or_b32_e32 v74, 48, v144
	v_ashrrev_i32_e32 v75, 31, v74
	v_lshlrev_b64 v[74:75], 11, v[74:75]
	v_lshl_add_u64 v[82:83], v[142:143], 0, v[74:75]
	v_pk_mul_f32 v[76:77], v[88:89], s[26:27] op_sel_hi:[1,0]
	v_pk_mul_f32 v[74:75], v[86:87], s[26:27] op_sel_hi:[1,0]
	v_pk_mul_f32 v[62:63], v[62:63], s[26:27] op_sel_hi:[1,0]
	v_cvt_pk_bf16_f32 v74, v74, v75
	v_cvt_pk_bf16_f32 v75, v76, v77
	v_cvt_pk_bf16_f32 v76, v78, v79
	v_cvt_pk_bf16_f32 v77, v80, v81
	global_store_dwordx4 v[82:83], v[74:77], off sc1
	s_mov_b32 s1, 0x40000
	v_pk_mul_f32 v[64:65], v[64:65], s[26:27] op_sel_hi:[1,0]
	v_pk_mul_f32 v[74:75], v[68:69], s[26:27] op_sel_hi:[1,0]
	v_pk_mul_f32 v[68:69], v[66:67], s[26:27] op_sel_hi:[1,0]
	v_cvt_pk_bf16_f32 v66, v70, v71
	v_cvt_pk_bf16_f32 v67, v72, v73
	v_cvt_pk_bf16_f32 v68, v68, v69
	v_cvt_pk_bf16_f32 v69, v74, v75
	global_store_dwordx4 v[82:83], v[66:69], off offset:256 sc1
	v_pk_mul_f32 v[52:53], v[52:53], s[26:27] op_sel_hi:[1,0]
	v_pk_mul_f32 v[50:51], v[50:51], s[26:27] op_sel_hi:[1,0]
	v_pk_mul_f32 v[68:69], v[60:61], s[26:27] op_sel_hi:[1,0]
	v_pk_mul_f32 v[60:61], v[58:59], s[26:27] op_sel_hi:[1,0]
	v_cvt_pk_bf16_f32 v58, v62, v63
	v_add_co_u32_e32 v62, vcc, s1, v138
	v_cvt_pk_bf16_f32 v59, v64, v65
	v_cvt_pk_bf16_f32 v60, v60, v61
	v_cvt_pk_bf16_f32 v61, v68, v69
	v_addc_co_u32_e32 v63, vcc, 0, v139, vcc
	global_store_dwordx4 v[62:63], v[58:61], off sc1
	v_lshl_add_u64 v[66:67], v[138:139], 0, s[20:21]
	v_pk_mul_f32 v[46:47], v[46:47], s[26:27] op_sel_hi:[1,0]
	v_pk_mul_f32 v[58:59], v[44:45], s[26:27] op_sel_hi:[1,0]
	v_pk_mul_f32 v[44:45], v[42:43], s[26:27] op_sel_hi:[1,0]
	v_cvt_pk_bf16_f32 v42, v50, v51
	v_cvt_pk_bf16_f32 v43, v52, v53
	v_cvt_pk_bf16_f32 v44, v44, v45
	v_cvt_pk_bf16_f32 v45, v58, v59
	global_store_dwordx4 v[66:67], v[42:45], off offset:256 sc1
	s_mov_b32 s1, 0x48000
	v_pk_mul_f32 v[48:49], v[48:49], s[26:27] op_sel_hi:[1,0]
	v_pk_mul_f32 v[44:45], v[56:57], s[26:27] op_sel_hi:[1,0]
	v_pk_mul_f32 v[42:43], v[54:55], s[26:27] op_sel_hi:[1,0]
	s_mov_b64 s[42:43], 0x48000
	v_cvt_pk_bf16_f32 v42, v42, v43
	v_cvt_pk_bf16_f32 v43, v44, v45
	v_cvt_pk_bf16_f32 v44, v46, v47
	v_add_co_u32_e32 v46, vcc, s1, v138
	v_cvt_pk_bf16_f32 v45, v48, v49
	s_nop 0
	v_addc_co_u32_e32 v47, vcc, 0, v139, vcc
	global_store_dwordx4 v[46:47], v[42:45], off sc1
	v_pk_mul_f32 v[36:37], v[36:37], s[26:27] op_sel_hi:[1,0]
	v_pk_mul_f32 v[34:35], v[34:35], s[26:27] op_sel_hi:[1,0]
	v_pk_mul_f32 v[42:43], v[28:29], s[26:27] op_sel_hi:[1,0]
	v_pk_mul_f32 v[28:29], v[26:27], s[26:27] op_sel_hi:[1,0]
	v_lshl_add_u64 v[50:51], v[138:139], 0, s[42:43]
	v_cvt_pk_bf16_f32 v26, v34, v35
	v_cvt_pk_bf16_f32 v27, v36, v37
	v_cvt_pk_bf16_f32 v28, v28, v29
	v_cvt_pk_bf16_f32 v29, v42, v43
	global_store_dwordx4 v[50:51], v[26:29], off offset:256 sc1
	v_pk_mul_f32 v[30:31], v[30:31], s[26:27] op_sel_hi:[1,0]
	s_mov_b32 s1, 0x50000
	v_pk_mul_f32 v[28:29], v[40:41], s[26:27] op_sel_hi:[1,0]
	v_pk_mul_f32 v[26:27], v[38:39], s[26:27] op_sel_hi:[1,0]
	v_pk_mul_f32 v[32:33], v[32:33], s[26:27] op_sel_hi:[1,0]
	v_cvt_pk_bf16_f32 v26, v26, v27
	v_cvt_pk_bf16_f32 v27, v28, v29
	v_cvt_pk_bf16_f32 v28, v30, v31
	v_add_co_u32_e32 v30, vcc, s1, v138
	v_cvt_pk_bf16_f32 v29, v32, v33
	s_nop 0
	v_addc_co_u32_e32 v31, vcc, 0, v139, vcc
	global_store_dwordx4 v[30:31], v[26:29], off sc1
	v_pk_mul_f32 v[20:21], v[20:21], s[26:27] op_sel_hi:[1,0]
	v_pk_mul_f32 v[18:19], v[18:19], s[26:27] op_sel_hi:[1,0]
	v_pk_mul_f32 v[26:27], v[12:13], s[26:27] op_sel_hi:[1,0]
	v_pk_mul_f32 v[12:13], v[10:11], s[26:27] op_sel_hi:[1,0]
	v_lshl_add_u64 v[34:35], v[138:139], 0, s[22:23]
	v_cvt_pk_bf16_f32 v10, v18, v19
	v_cvt_pk_bf16_f32 v11, v20, v21
	v_cvt_pk_bf16_f32 v12, v12, v13
	v_cvt_pk_bf16_f32 v13, v26, v27
	global_store_dwordx4 v[34:35], v[10:13], off offset:256 sc1
	v_pk_mul_f32 v[14:15], v[14:15], s[26:27] op_sel_hi:[1,0]
	s_mov_b32 s1, 0x58000
	v_pk_mul_f32 v[12:13], v[24:25], s[26:27] op_sel_hi:[1,0]
	v_pk_mul_f32 v[10:11], v[22:23], s[26:27] op_sel_hi:[1,0]
	v_pk_mul_f32 v[16:17], v[16:17], s[26:27] op_sel_hi:[1,0]
	v_cvt_pk_bf16_f32 v10, v10, v11
	v_cvt_pk_bf16_f32 v11, v12, v13
	v_cvt_pk_bf16_f32 v12, v14, v15
	v_add_co_u32_e32 v14, vcc, s1, v138
	v_cvt_pk_bf16_f32 v13, v16, v17
	s_nop 0
	v_addc_co_u32_e32 v15, vcc, 0, v139, vcc
	s_mov_b64 s[42:43], 0x58000
	global_store_dwordx4 v[14:15], v[10:13], off sc1
	v_pk_mul_f32 v[8:9], v[8:9], s[26:27] op_sel_hi:[1,0]
	v_pk_mul_f32 v[6:7], v[6:7], s[26:27] op_sel_hi:[1,0]
	v_pk_mul_f32 v[10:11], v[4:5], s[26:27] op_sel_hi:[1,0]
	v_pk_mul_f32 v[4:5], v[2:3], s[26:27] op_sel_hi:[1,0]
	v_lshl_add_u64 v[18:19], v[138:139], 0, s[42:43]
	v_cvt_pk_bf16_f32 v2, v6, v7
	v_cvt_pk_bf16_f32 v3, v8, v9
	v_cvt_pk_bf16_f32 v4, v4, v5
	v_cvt_pk_bf16_f32 v5, v10, v11
	s_and_b64 vcc, exec, s[36:37]
	s_mov_b64 s[36:37], -1
	global_store_dwordx4 v[18:19], v[2:5], off offset:256 sc1
	s_cbranch_vccnz .LBB0_1189
	v_readlane_b32 s36, v253, 50
	v_readlane_b32 s37, v253, 51
	s_andn2_b64 vcc, exec, s[36:37]
	s_cbranch_vccnz .LBB0_1188
	s_barrier
	s_branch .LBB0_1188

.LBB0_1216:
	s_ashr_i32 s38, s47, 2
	s_mov_b32 s29, -1
	s_ashr_i32 s39, s38, 31
	s_lshl_b64 s[38:39], s[38:39], 21
	v_mbcnt_lo_u32_b32 v0, s29, 0
	v_mbcnt_hi_u32_b32 v142, s29, v0
	s_add_u32 s29, s93, s38
	s_addc_u32 s37, s94, s39
	s_lshl_b32 s38, s47, 9
	s_and_b32 s38, s38, 0x600
	s_add_u32 s29, s29, s38
	s_addc_u32 s37, s37, 0
	s_ashr_i32 s47, s46, 31
	s_lshl_b64 s[38:39], s[46:47], 9
	s_add_u32 s29, s29, s38
	s_addc_u32 s37, s37, s39
	s_add_u32 s38, s29, s35
	s_addc_u32 s39, s37, 0
	v_and_b32_e32 v0, 0x70, v142
	v_lshl_add_u64 v[140:141], s[38:39], 0, v[0:1]
	v_and_or_b32 v0, v142, 15, s84
	v_lshl_add_u32 v142, s1, 8, v0
	v_ashrrev_i32_e32 v143, 31, v142
	v_lshlrev_b64 v[144:145], 11, v[142:143]
	v_lshl_add_u64 v[144:145], v[140:141], 0, v[144:145]
	s_mov_b32 s1, 0x40000
	v_cvt_pk_bf16_f32 v62, v62, v63
	v_cvt_pk_bf16_f32 v63, v64, v65
	v_cvt_pk_bf16_f32 v64, v58, v59
	v_add_co_u32_e32 v58, vcc, s1, v144
	v_cvt_pk_bf16_f32 v70, v70, v71
	v_cvt_pk_bf16_f32 v71, v72, v73
	v_cvt_pk_bf16_f32 v72, v66, v67
	v_lshl_add_u64 v[66:67], v[144:145], 0, s[20:21]
	v_addc_co_u32_e32 v59, vcc, 0, v145, vcc
	v_cvt_pk_bf16_f32 v46, v46, v47
	v_cvt_pk_bf16_f32 v47, v48, v49
	v_cvt_pk_bf16_f32 v48, v42, v43
	v_cvt_pk_bf16_f32 v49, v44, v45
	s_mov_b32 s1, 0x48000
	global_store_dwordx4 v[66:67], v[46:49], off offset:256 sc1
	s_mov_b64 s[38:39], 0x48000
	v_cvt_pk_bf16_f32 v110, v110, v111
	v_add_co_u32_e32 v48, vcc, s1, v144
	v_cvt_pk_bf16_f32 v111, v112, v113
	v_cvt_pk_bf16_f32 v112, v106, v107
	v_or_b32_e32 v106, 16, v142
	v_lshl_add_u64 v[46:47], v[144:145], 0, s[38:39]
	v_addc_co_u32_e32 v49, vcc, 0, v145, vcc
	v_cvt_pk_bf16_f32 v30, v30, v31
	v_cvt_pk_bf16_f32 v31, v32, v33
	v_cvt_pk_bf16_f32 v32, v26, v27
	v_cvt_pk_bf16_f32 v33, v28, v29
	s_mov_b32 s1, 0x50000
	v_ashrrev_i32_e32 v107, 31, v106
	v_cvt_pk_bf16_f32 v94, v94, v95
	v_cvt_pk_bf16_f32 v95, v96, v97
	v_cvt_pk_bf16_f32 v96, v90, v91
	v_or_b32_e32 v90, 32, v142
	global_store_dwordx4 v[46:47], v[30:33], off offset:256 sc1
	v_cvt_pk_bf16_f32 v113, v108, v109
	v_lshlrev_b64 v[106:107], 11, v[106:107]
	v_add_co_u32_e32 v32, vcc, s1, v144
	v_ashrrev_i32_e32 v91, 31, v90
	v_cvt_pk_bf16_f32 v78, v78, v79
	v_cvt_pk_bf16_f32 v79, v80, v81
	v_cvt_pk_bf16_f32 v80, v74, v75
	v_or_b32_e32 v74, 48, v142
	v_lshl_add_u64 v[30:31], v[144:145], 0, s[22:23]
	v_addc_co_u32_e32 v33, vcc, 0, v145, vcc
	v_cvt_pk_bf16_f32 v14, v14, v15
	v_cvt_pk_bf16_f32 v15, v16, v17
	v_cvt_pk_bf16_f32 v16, v10, v11
	v_cvt_pk_bf16_f32 v17, v12, v13
	s_mov_b32 s1, 0x58000
	global_store_dwordx4 v[144:145], v[110:113], off offset:256 sc1
	v_cvt_pk_bf16_f32 v97, v92, v93
	v_lshlrev_b64 v[90:91], 11, v[90:91]
	v_lshl_add_u64 v[110:111], v[140:141], 0, v[106:107]
	v_ashrrev_i32_e32 v75, 31, v74
	global_store_dwordx4 v[30:31], v[14:17], off offset:256 sc1
	global_store_dwordx4 v[110:111], v[94:97], off offset:256 sc1
	v_cvt_pk_bf16_f32 v81, v76, v77
	v_add_co_u32_e32 v16, vcc, s1, v144
	v_lshl_add_u64 v[94:95], v[140:141], 0, v[90:91]
	v_lshlrev_b64 v[74:75], 11, v[74:75]
	s_mov_b64 s[38:39], 0x58000
	v_addc_co_u32_e32 v17, vcc, 0, v145, vcc
	v_cvt_pk_bf16_f32 v126, v126, v127
	v_cvt_pk_bf16_f32 v127, v128, v129
	v_cvt_pk_bf16_f32 v128, v122, v123
	v_cvt_pk_bf16_f32 v129, v124, v125
	v_cvt_pk_bf16_f32 v106, v118, v119
	v_cvt_pk_bf16_f32 v107, v120, v121
	v_cvt_pk_bf16_f32 v108, v114, v115
	v_cvt_pk_bf16_f32 v109, v116, v117
	v_cvt_pk_bf16_f32 v90, v102, v103
	v_cvt_pk_bf16_f32 v91, v104, v105
	v_cvt_pk_bf16_f32 v92, v98, v99
	v_cvt_pk_bf16_f32 v93, v100, v101
	global_store_dwordx4 v[94:95], v[78:81], off offset:256 sc1
	v_cvt_pk_bf16_f32 v76, v82, v83
	v_cvt_pk_bf16_f32 v77, v84, v85
	v_lshl_add_u64 v[78:79], v[140:141], 0, v[74:75]
	v_cvt_pk_bf16_f32 v74, v86, v87
	v_cvt_pk_bf16_f32 v75, v88, v89
	v_cvt_pk_bf16_f32 v73, v68, v69
	v_cvt_pk_bf16_f32 v65, v60, v61
	v_cvt_pk_bf16_f32 v42, v54, v55
	v_cvt_pk_bf16_f32 v43, v56, v57
	v_cvt_pk_bf16_f32 v44, v50, v51
	v_cvt_pk_bf16_f32 v45, v52, v53
	v_cvt_pk_bf16_f32 v26, v38, v39
	v_cvt_pk_bf16_f32 v27, v40, v41
	v_cvt_pk_bf16_f32 v28, v34, v35
	v_cvt_pk_bf16_f32 v29, v36, v37
	v_lshl_add_u64 v[14:15], v[144:145], 0, s[38:39]
	v_cvt_pk_bf16_f32 v10, v22, v23
	v_cvt_pk_bf16_f32 v11, v24, v25
	v_cvt_pk_bf16_f32 v12, v18, v19
	v_cvt_pk_bf16_f32 v13, v20, v21
	v_cvt_pk_bf16_f32 v6, v6, v7
	v_cvt_pk_bf16_f32 v7, v8, v9
	v_cvt_pk_bf16_f32 v8, v2, v3
	v_cvt_pk_bf16_f32 v9, v4, v5
	s_andn2_b64 vcc, exec, s[16:17]
	s_mov_b64 s[16:17], -1
	global_store_dwordx4 v[144:145], v[126:129], off sc1
	global_store_dwordx4 v[110:111], v[106:109], off sc1
	global_store_dwordx4 v[94:95], v[90:93], off sc1
	global_store_dwordx4 v[78:79], v[74:77], off sc1
	global_store_dwordx4 v[78:79], v[70:73], off offset:256 sc1
	global_store_dwordx4 v[58:59], v[62:65], off sc1
	global_store_dwordx4 v[48:49], v[42:45], off sc1
	global_store_dwordx4 v[32:33], v[26:29], off sc1
	global_store_dwordx4 v[16:17], v[10:13], off sc1
	global_store_dwordx4 v[14:15], v[6:9], off offset:256 sc1
	s_cbranch_vccnz .LBB0_1207
	v_readlane_b32 s16, v253, 50
	v_readlane_b32 s17, v253, 51
	s_andn2_b64 vcc, exec, s[16:17]
	s_cbranch_vccnz .LBB0_1206
	s_barrier
	s_branch .LBB0_1206

.LBB0_1986:
	v_cndmask_b32_e64 v4, 0, 1, s[46:47]
	v_cmp_ne_u32_e64 s[46:47], 0, v4
	v_cndmask_b32_e64 v4, 0, 1, s[42:43]
	v_cmp_ne_u32_e32 vcc, 0, v4
	s_and_saveexec_b64 s[42:43], s[38:39]
	s_cbranch_execz .LBB0_1983
	v_mov_b32_e32 v4, s46
	v_mov_b32_e32 v5, s47
	v_mov_b32_e32 v6, vcc_lo
	v_mov_b32_e32 v7, vcc_hi
	global_store_dwordx4 v1, v[4:7], s[44:45] sc1
	s_branch .LBB0_1983

.LBB0_1989:
	s_and_b64 vcc, exec, s[0:1]
	s_cbranch_vccz .LBB0_2111
	v_readlane_b32 s0, v253, 45
	s_cmp_eq_u32 s0, 0
	s_cbranch_scc0 .LBB0_2111
	v_readlane_b32 s0, v253, 41
	v_readlane_b32 s1, v253, 42
	s_andn2_b64 vcc, exec, s[0:1]
	s_cbranch_vccnz .LBB0_1995
	s_abs_i32 s1, s30
	s_mul_hi_u32 s14, s1, s27
	s_mul_i32 s14, s14, s33
	s_sub_i32 s1, s1, s14
	s_ashr_i32 s0, s30, 31
	s_sub_i32 s14, s1, s33
	s_cmp_ge_u32 s1, s33
	s_cselect_b32 s1, s14, s1
	s_sub_i32 s14, s1, s33
	s_cmp_ge_u32 s1, s33
	s_cselect_b32 s1, s14, s1
	s_xor_b32 s1, s1, s0
	s_sub_i32 s0, s1, s0
	s_ashr_i32 s1, s0, 31
	s_and_b32 s1, s1, s72
	s_add_i32 s0, s1, s0
	s_cmpk_gt_i32 s0, 0x57f
	s_cbranch_scc1 .LBB0_1994
	v_readlane_b32 s14, v253, 32
	s_lshl_b32 s14, s14, 14
	s_lshl_b64 s[16:17], s[86:87], 3
	v_readlane_b32 s34, v250, 3
	v_readlane_b32 s35, v250, 4
	s_add_u32 s16, s34, s16
	s_addc_u32 s17, s35, s17
	s_load_dwordx2 s[16:17], s[16:17], 0x90
	v_readlane_b32 s15, v253, 33
	v_readlane_b32 s15, v253, 38
	s_mul_hi_u32 s1, s15, 0xb00000
	s_mul_i32 s15, s15, 0xb00000
	s_waitcnt lgkmcnt(0)
	s_add_u32 s15, s16, s15
	s_addc_u32 s17, s17, s1
	s_ashr_i32 s1, s0, 31
	s_lshr_b32 s1, s1, 27
	s_add_i32 s1, s0, s1
	s_ashr_i32 s1, s1, 5
	s_lshl_b32 s16, s1, 6
	s_lshl_b32 s1, s1, 10
	s_lshl_b32 s0, s0, 5
	s_sub_i32 s0, s0, s1
	s_ashr_i32 s1, s0, 31
	s_waitcnt vmcnt(0)
	v_lshrrev_b32_e32 v35, 3, v198
	s_lshl_b64 s[34:35], s[0:1], 2
	s_waitcnt vmcnt(0)
	v_or_b32_e32 v30, s16, v35
	s_add_u32 s34, s15, s34
	v_lshlrev_b32_e32 v0, 4, v198
	s_addc_u32 s35, s17, s35
	v_and_b32_e32 v0, 0x70, v0
	v_ashrrev_i32_e32 v31, 31, v30
	v_or_b32_e32 v6, 8, v30
	v_lshl_add_u64 v[32:33], s[34:35], 0, v[0:1]
	v_lshlrev_b64 v[2:3], 12, v[30:31]
	v_ashrrev_i32_e32 v7, 31, v6
	v_lshl_add_u64 v[2:3], v[32:33], 0, v[2:3]
	v_lshlrev_b64 v[6:7], 12, v[6:7]
	v_or_b32_e32 v10, 16, v30
	global_load_dwordx4 v[2:5], v[2:3], off
	v_lshl_add_u64 v[6:7], v[32:33], 0, v[6:7]
	v_ashrrev_i32_e32 v11, 31, v10
	global_load_dwordx4 v[6:9], v[6:7], off
	v_lshlrev_b64 v[10:11], 12, v[10:11]
	v_or_b32_e32 v14, 24, v30
	v_lshl_add_u64 v[10:11], v[32:33], 0, v[10:11]
	v_ashrrev_i32_e32 v15, 31, v14
	global_load_dwordx4 v[10:13], v[10:11], off
	v_lshlrev_b64 v[14:15], 12, v[14:15]
	v_or_b32_e32 v18, 32, v30
	v_lshl_add_u64 v[14:15], v[32:33], 0, v[14:15]
	v_ashrrev_i32_e32 v19, 31, v18
	global_load_dwordx4 v[14:17], v[14:15], off
	v_lshlrev_b64 v[18:19], 12, v[18:19]
	v_or_b32_e32 v22, 40, v30
	v_lshl_add_u64 v[18:19], v[32:33], 0, v[18:19]
	v_ashrrev_i32_e32 v23, 31, v22
	global_load_dwordx4 v[18:21], v[18:19], off
	v_lshlrev_b64 v[22:23], 12, v[22:23]
	v_or_b32_e32 v26, 48, v30
	v_lshl_add_u64 v[22:23], v[32:33], 0, v[22:23]
	v_ashrrev_i32_e32 v27, 31, v26
	global_load_dwordx4 v[22:25], v[22:23], off
	v_lshlrev_b64 v[26:27], 12, v[26:27]
	v_or_b32_e32 v30, 56, v30
	v_lshl_add_u64 v[26:27], v[32:33], 0, v[26:27]
	v_ashrrev_i32_e32 v31, 31, v30
	global_load_dwordx4 v[26:29], v[26:27], off
	v_lshlrev_b64 v[30:31], 12, v[30:31]
	v_lshl_add_u64 v[30:31], v[32:33], 0, v[30:31]
	global_load_dwordx4 v[30:33], v[30:31], off
	s_mul_hi_i32 s1, s0, 0x1600
	s_mulk_i32 s0, 0x1600
	s_add_u32 s15, s74, s0
	s_addc_u32 s29, s75, s1
	s_ashr_i32 s17, s16, 31
	v_and_b32_e32 v0, 7, v235
	s_lshl_b64 s[0:1], s[16:17], 1
	v_lshlrev_b32_e32 v34, 4, v0
	s_add_u32 s0, s15, s0
	v_or_b32_e32 v36, s14, v34
	s_movk_i32 s15, 0x84
	v_mad_u32_u24 v36, v35, s15, v36
	v_mul_u32_u24_e32 v0, 0x420, v0
	s_addc_u32 s1, s29, s1
	s_waitcnt vmcnt(7)
	ds_write2_b32 v36, v2, v3 offset1:1
	ds_write2_b32 v36, v4, v5 offset0:2 offset1:3
	v_add_u32_e32 v2, 0x420, v36
	s_waitcnt vmcnt(6)
	ds_write2_b32 v2, v6, v7 offset1:1
	v_add_u32_e32 v2, 0x428, v36
	ds_write2_b32 v2, v8, v9 offset1:1
	v_add_u32_e32 v2, 0x840, v36
	s_waitcnt vmcnt(5)
	ds_write2_b32 v2, v10, v11 offset1:1
	v_add_u32_e32 v2, 0x848, v36
	ds_write2_b32 v2, v12, v13 offset1:1
	v_add_u32_e32 v2, 0xc60, v36
	s_waitcnt vmcnt(4)
	ds_write2_b32 v2, v14, v15 offset1:1
	v_add_u32_e32 v2, 0xc68, v36
	ds_write2_b32 v2, v16, v17 offset1:1
	v_add_u32_e32 v2, 0x1080, v36
	s_waitcnt vmcnt(3)
	ds_write2_b32 v2, v18, v19 offset1:1
	v_add_u32_e32 v2, 0x1088, v36
	ds_write2_b32 v2, v20, v21 offset1:1
	v_add_u32_e32 v2, 0x14a0, v36
	s_waitcnt vmcnt(2)
	ds_write2_b32 v2, v22, v23 offset1:1
	v_add_u32_e32 v2, 0x14a8, v36
	ds_write2_b32 v2, v24, v25 offset1:1
	v_add_u32_e32 v2, 0x18c0, v36
	s_waitcnt vmcnt(1)
	ds_write2_b32 v2, v26, v27 offset1:1
	v_add_u32_e32 v2, 0x18c8, v36
	ds_write2_b32 v2, v28, v29 offset1:1
	v_add_u32_e32 v2, 0x1ce0, v36
	s_waitcnt vmcnt(0)
	ds_write2_b32 v2, v30, v31 offset1:1
	v_add_u32_e32 v2, 0x1ce8, v36
	ds_write2_b32 v2, v32, v33 offset1:1
	s_waitcnt lgkmcnt(0)
	v_lshlrev_b32_e32 v2, 2, v35
	v_or3_b32 v26, s14, v0, v2
	v_mul_u32_u24_e32 v0, 0xb00, v35
	ds_read2_b32 v[6:7], v26 offset0:33 offset1:41
	ds_read2_b32 v[8:9], v26 offset1:8
	ds_read2_b32 v[10:11], v26 offset0:66 offset1:74
	ds_read2_b32 v[12:13], v26 offset0:99 offset1:107
	ds_read2_b32 v[14:15], v26 offset0:132 offset1:140
	ds_read2_b32 v[16:17], v26 offset0:165 offset1:173
	ds_read2_b32 v[18:19], v26 offset0:198 offset1:206
	ds_read2_b32 v[20:21], v26 offset0:231 offset1:239
	v_lshlrev_b32_e32 v0, 1, v0
	v_lshl_add_u64 v[22:23], s[0:1], 0, v[0:1]
	v_mov_b32_e32 v35, v1
	v_lshl_add_u64 v[22:23], v[22:23], 0, v[34:35]
	s_mov_b32 s0, 0x1c00000
	v_add_co_u32_e32 v24, vcc, s0, v22
	s_mov_b32 s0, 0x1c0b000
	s_nop 0
	v_addc_co_u32_e32 v25, vcc, 0, v23, vcc
	s_waitcnt lgkmcnt(6)
	v_cvt_pk_bf16_f32 v2, v8, v6
	s_waitcnt lgkmcnt(4)
	v_cvt_pk_bf16_f32 v3, v10, v12
	s_waitcnt lgkmcnt(2)
	v_cvt_pk_bf16_f32 v4, v14, v16
	s_waitcnt lgkmcnt(0)
	v_cvt_pk_bf16_f32 v5, v18, v20
	v_add_co_u32_e32 v6, vcc, s0, v22
	global_store_dwordx4 v[24:25], v[2:5], off sc1
	s_mov_b32 s0, 0x1c16000
	s_nop 0
	v_cvt_pk_bf16_f32 v2, v9, v7
	v_cvt_pk_bf16_f32 v3, v11, v13
	v_cvt_pk_bf16_f32 v4, v15, v17
	v_cvt_pk_bf16_f32 v5, v19, v21
	v_addc_co_u32_e32 v7, vcc, 0, v23, vcc
	global_store_dwordx4 v[6:7], v[2:5], off sc1
	ds_read2_b32 v[6:7], v26 offset0:49 offset1:57
	ds_read2_b32 v[8:9], v26 offset0:16 offset1:24
	ds_read2_b32 v[10:11], v26 offset0:82 offset1:90
	ds_read2_b32 v[12:13], v26 offset0:115 offset1:123
	ds_read2_b32 v[14:15], v26 offset0:148 offset1:156
	ds_read2_b32 v[16:17], v26 offset0:181 offset1:189
	ds_read2_b32 v[18:19], v26 offset0:214 offset1:222
	ds_read2_b32 v[20:21], v26 offset0:247 offset1:255
	v_add_co_u32_e32 v24, vcc, s0, v22
	s_waitcnt lgkmcnt(6)
	v_cvt_pk_bf16_f32 v2, v8, v6
	v_addc_co_u32_e32 v25, vcc, 0, v23, vcc
	s_waitcnt lgkmcnt(4)
	v_cvt_pk_bf16_f32 v3, v10, v12
	s_waitcnt lgkmcnt(2)
	v_cvt_pk_bf16_f32 v4, v14, v16
	s_waitcnt lgkmcnt(0)
	v_cvt_pk_bf16_f32 v5, v18, v20
	v_add_co_u32_e32 v6, vcc, 0x1c21000, v22
	global_store_dwordx4 v[24:25], v[2:5], off sc1
	s_nop 1
	v_cvt_pk_bf16_f32 v2, v9, v7
	v_cvt_pk_bf16_f32 v3, v11, v13
	v_cvt_pk_bf16_f32 v4, v15, v17
	v_cvt_pk_bf16_f32 v5, v19, v21
	v_addc_co_u32_e32 v7, vcc, 0, v23, vcc
	global_store_dwordx4 v[6:7], v[2:5], off sc1
	s_waitcnt lgkmcnt(0)

.LBB0_2009:
	s_waitcnt vmcnt(0)
	v_ffbh_u32_e32 v161, v157
	v_min_u32_e32 v161, 32, v161
	v_lshlrev_b64 v[156:157], v161, v[156:157]
	v_min_u32_e32 v156, 1, v156
	v_or_b32_e32 v156, v157, v156
	v_cvt_f32_u32_e32 v156, v156
	v_sub_u32_e32 v157, 32, v161
	s_mov_b32 s36, 0x358637bd
	v_mov_b64_e32 v[166:167], s[36:37]
	v_ldexp_f32 v157, v156, v157
	v_ffbh_u32_e32 v156, v155
	v_min_u32_e32 v156, 32, v156
	v_lshlrev_b64 v[154:155], v156, v[154:155]
	v_min_u32_e32 v154, 1, v154
	v_or_b32_e32 v154, v155, v154
	v_cvt_f32_u32_e32 v154, v154
	v_sub_u32_e32 v155, 32, v156
	s_mov_b32 s40, 0x32800000
	s_mov_b32 s29, -1
	v_ldexp_f32 v156, v154, v155
	v_pk_fma_f32 v[154:155], v[156:157], s[40:41], v[166:167] op_sel_hi:[1,0,0]
	s_movk_i32 s95, 0x100
	v_mul_f32_e32 v156, 0x4b800000, v155
	v_cmp_gt_f32_e64 s[36:37], s96, v155
	v_cmp_gt_f32_e32 vcc, s96, v154
	v_mbcnt_lo_u32_b32 v0, s29, 0
	v_cndmask_b32_e64 v155, v155, v156, s[36:37]
	v_rsq_f32_e32 v155, v155
	v_mbcnt_hi_u32_b32 v159, s29, v0
	s_lshl_b32 s29, s58, 8
	v_lshrrev_b32_e32 v160, 1, v159
	v_mul_f32_e32 v156, 0x45800000, v155
	v_cndmask_b32_e64 v156, v155, v156, s[36:37]
	v_mul_f32_e32 v155, 0x4b800000, v154
	v_cndmask_b32_e32 v154, v154, v155, vcc
	v_rsq_f32_e32 v154, v154
	v_and_b32_e32 v0, 15, v159
	s_add_i32 s29, s29, s34
	v_and_b32_e32 v160, 56, v160
	v_mul_f32_e32 v155, 0x45800000, v154
	v_cndmask_b32_e32 v154, v154, v155, vcc
	v_ffbh_u32_e32 v155, v153
	v_min_u32_e32 v155, 32, v155
	v_lshlrev_b64 v[152:153], v155, v[152:153]
	v_min_u32_e32 v152, 1, v152
	v_or_b32_e32 v152, v153, v152
	v_cvt_f32_u32_e32 v152, v152
	v_sub_u32_e32 v153, 32, v155
	v_or_b32_e32 v158, s29, v0
	v_add_u32_e32 v160, s85, v160
	v_ldexp_f32 v153, v152, v153
	v_ffbh_u32_e32 v152, v151
	v_min_u32_e32 v152, 32, v152
	v_lshlrev_b64 v[150:151], v152, v[150:151]
	v_min_u32_e32 v150, 1, v150
	v_or_b32_e32 v150, v151, v150
	v_cvt_f32_u32_e32 v150, v150
	v_sub_u32_e32 v151, 32, v152
	s_cmp_gt_i32 s50, 15
	v_ldexp_f32 v152, v150, v151
	v_pk_fma_f32 v[150:151], v[152:153], s[40:41], v[166:167] op_sel_hi:[1,0,0]
	s_nop 0
	v_mul_f32_e32 v152, 0x4b800000, v151
	v_cmp_gt_f32_e64 s[36:37], s96, v151
	v_cmp_gt_f32_e32 vcc, s96, v150
	s_nop 0
	v_cndmask_b32_e64 v151, v151, v152, s[36:37]
	v_rsq_f32_e32 v151, v151
	s_nop 0
	v_mul_f32_e32 v152, 0x45800000, v151
	v_cndmask_b32_e64 v152, v151, v152, s[36:37]
	v_mul_f32_e32 v151, 0x4b800000, v150
	v_cndmask_b32_e32 v150, v150, v151, vcc
	v_rsq_f32_e32 v150, v150
	s_nop 0
	v_mul_f32_e32 v151, 0x45800000, v150
	v_cndmask_b32_e32 v150, v150, v151, vcc
	v_ffbh_u32_e32 v151, v149
	v_min_u32_e32 v151, 32, v151
	v_lshlrev_b64 v[148:149], v151, v[148:149]
	v_min_u32_e32 v148, 1, v148
	v_or_b32_e32 v148, v149, v148
	v_cvt_f32_u32_e32 v148, v148
	v_sub_u32_e32 v149, 32, v151
	v_ldexp_f32 v149, v148, v149
	v_ffbh_u32_e32 v148, v147
	v_min_u32_e32 v148, 32, v148
	v_lshlrev_b64 v[146:147], v148, v[146:147]
	v_min_u32_e32 v146, 1, v146
	v_or_b32_e32 v146, v147, v146
	v_cvt_f32_u32_e32 v146, v146
	v_sub_u32_e32 v147, 32, v148
	v_ldexp_f32 v148, v146, v147
	v_pk_fma_f32 v[146:147], v[148:149], s[40:41], v[166:167] op_sel_hi:[1,0,0]
	s_nop 0
	v_mul_f32_e32 v148, 0x4b800000, v147
	v_cmp_gt_f32_e64 s[36:37], s96, v147
	v_cmp_gt_f32_e32 vcc, s96, v146
	s_nop 0
	v_cndmask_b32_e64 v147, v147, v148, s[36:37]
	v_rsq_f32_e32 v147, v147
	s_nop 0
	v_mul_f32_e32 v148, 0x45800000, v147
	v_cndmask_b32_e64 v148, v147, v148, s[36:37]
	v_mul_f32_e32 v147, 0x4b800000, v146
	v_cndmask_b32_e32 v146, v146, v147, vcc
	v_rsq_f32_e32 v146, v146
	s_nop 0
	v_mul_f32_e32 v147, 0x45800000, v146
	v_cndmask_b32_e32 v146, v146, v147, vcc
	v_ffbh_u32_e32 v147, v145
	v_min_u32_e32 v147, 32, v147
	v_lshlrev_b64 v[144:145], v147, v[144:145]
	v_min_u32_e32 v144, 1, v144
	v_or_b32_e32 v144, v145, v144
	v_cvt_f32_u32_e32 v144, v144
	v_sub_u32_e32 v145, 32, v147
	v_ldexp_f32 v145, v144, v145
	v_ffbh_u32_e32 v144, v143
	v_min_u32_e32 v144, 32, v144
	v_lshlrev_b64 v[142:143], v144, v[142:143]
	v_min_u32_e32 v142, 1, v142
	v_or_b32_e32 v142, v143, v142
	v_cvt_f32_u32_e32 v142, v142
	v_sub_u32_e32 v143, 32, v144
	v_ldexp_f32 v144, v142, v143
	v_pk_fma_f32 v[142:143], v[144:145], s[40:41], v[166:167] op_sel_hi:[1,0,0]
	s_nop 0
	v_mul_f32_e32 v144, 0x4b800000, v143
	v_cmp_gt_f32_e64 s[36:37], s96, v143
	v_cmp_gt_f32_e32 vcc, s96, v142
	s_nop 0
	v_cndmask_b32_e64 v143, v143, v144, s[36:37]
	v_rsq_f32_e32 v143, v143
	s_nop 0
	v_mul_f32_e32 v144, 0x45800000, v143
	v_cndmask_b32_e64 v144, v143, v144, s[36:37]
	v_mul_f32_e32 v143, 0x4b800000, v142
	v_cndmask_b32_e32 v142, v142, v143, vcc
	v_rsq_f32_e32 v142, v142
	s_mov_b64 s[36:37], -1
	v_mul_f32_e32 v143, 0x45800000, v142
	v_cndmask_b32_e32 v142, v142, v143, vcc
	s_cbranch_scc0 .LBB0_2021
	s_cmp_gt_u32 s50, 19
	s_cbranch_scc0 .LBB0_2018
	s_and_b64 vcc, exec, s[38:39]
	s_cbranch_vccz .LBB0_2015
	v_readlane_b32 s36, v253, 45
	v_cmp_gt_u32_e32 vcc, 16, v159
	v_readlane_b32 s37, v253, 46
	s_and_b64 s[40:41], s[36:37], vcc
	s_and_saveexec_b64 s[36:37], s[40:41]
	s_cbranch_execz .LBB0_2014
	v_ashrrev_i32_e32 v159, 31, v158
	v_lshlrev_b64 v[166:167], 5, v[158:159]
	v_mul_f32_e32 v172, 0x3d3504f3, v156
	v_lshl_add_u64 v[170:171], s[42:43], 0, v[166:167]
	v_pk_mul_f32 v[168:169], v[172:173], v[128:129] op_sel_hi:[0,1]
	v_pk_mul_f32 v[166:167], v[172:173], v[126:127] op_sel_hi:[0,1]
	global_store_dwordx4 v[170:171], v[166:169], off sc1
	v_mul_f32_e32 v174, 0x3d3504f3, v154
	s_mov_b64 s[40:41], 0x1000
	v_pk_mul_f32 v[168:169], v[172:173], v[124:125] op_sel_hi:[0,1]
	v_pk_mul_f32 v[166:167], v[172:173], v[122:123] op_sel_hi:[0,1]
	global_store_dwordx4 v[170:171], v[166:169], off offset:16 sc1
	s_nop 1
	v_or_b32_e32 v166, 16, v158
	v_ashrrev_i32_e32 v167, 31, v166
	v_lshlrev_b64 v[166:167], 5, v[166:167]
	v_lshl_add_u64 v[172:173], s[42:43], 0, v[166:167]
	v_pk_mul_f32 v[168:169], v[174:175], v[116:117] op_sel_hi:[0,1]
	v_pk_mul_f32 v[166:167], v[174:175], v[114:115] op_sel_hi:[0,1]
	global_store_dwordx4 v[172:173], v[166:169], off sc1
	s_nop 1
	v_pk_mul_f32 v[168:169], v[174:175], v[108:109] op_sel_hi:[0,1]
	v_pk_mul_f32 v[166:167], v[174:175], v[106:107] op_sel_hi:[0,1]
	global_store_dwordx4 v[172:173], v[166:169], off offset:16 sc1
	v_mul_f32_e32 v174, 0x3d3504f3, v152
	s_nop 0
	v_or_b32_e32 v166, 32, v158
	v_ashrrev_i32_e32 v167, 31, v166
	v_lshlrev_b64 v[166:167], 5, v[166:167]
	v_lshl_add_u64 v[172:173], s[42:43], 0, v[166:167]
	v_pk_mul_f32 v[168:169], v[174:175], v[100:101] op_sel_hi:[0,1]
	v_pk_mul_f32 v[166:167], v[174:175], v[98:99] op_sel_hi:[0,1]
	global_store_dwordx4 v[172:173], v[166:169], off sc1
	s_nop 1
	v_pk_mul_f32 v[168:169], v[174:175], v[92:93] op_sel_hi:[0,1]
	v_pk_mul_f32 v[166:167], v[174:175], v[90:91] op_sel_hi:[0,1]
	global_store_dwordx4 v[172:173], v[166:169], off offset:16 sc1
	v_mul_f32_e32 v174, 0x3d3504f3, v150
	s_nop 0
	v_or_b32_e32 v166, 48, v158
	v_ashrrev_i32_e32 v167, 31, v166
	v_lshlrev_b64 v[166:167], 5, v[166:167]
	v_lshl_add_u64 v[172:173], s[42:43], 0, v[166:167]
	v_pk_mul_f32 v[168:169], v[174:175], v[84:85] op_sel_hi:[0,1]
	v_pk_mul_f32 v[166:167], v[174:175], v[82:83] op_sel_hi:[0,1]
	global_store_dwordx4 v[172:173], v[166:169], off sc1
	s_nop 1
	v_pk_mul_f32 v[168:169], v[174:175], v[76:77] op_sel_hi:[0,1]
	v_pk_mul_f32 v[166:167], v[174:175], v[74:75] op_sel_hi:[0,1]
	global_store_dwordx4 v[172:173], v[166:169], off offset:16 sc1
	v_lshl_add_u64 v[172:173], v[170:171], 0, s[40:41]
	s_movk_i32 s40, 0x1000
	v_mul_f32_e32 v174, 0x3d3504f3, v148
	v_add_co_u32_e32 v176, vcc, s40, v170
	v_pk_mul_f32 v[168:169], v[174:175], v[64:65] op_sel_hi:[0,1]
	v_pk_mul_f32 v[166:167], v[174:175], v[62:63] op_sel_hi:[0,1]
	v_addc_co_u32_e32 v177, vcc, 0, v171, vcc
	global_store_dwordx4 v[176:177], v[166:169], off sc1
	s_mov_b64 s[40:41], 0x1200
	s_nop 0
	v_pk_mul_f32 v[168:169], v[174:175], v[60:61] op_sel_hi:[0,1]
	v_pk_mul_f32 v[166:167], v[174:175], v[58:59] op_sel_hi:[0,1]
	v_mul_f32_e32 v174, 0x3d3504f3, v146
	global_store_dwordx4 v[172:173], v[166:169], off offset:16 sc1
	v_lshl_add_u64 v[172:173], v[170:171], 0, s[40:41]
	s_mov_b64 s[40:41], 0x1400
	v_pk_mul_f32 v[168:169], v[174:175], v[56:57] op_sel_hi:[0,1]
	v_pk_mul_f32 v[166:167], v[174:175], v[54:55] op_sel_hi:[0,1]
	global_store_dwordx4 v[176:177], v[166:169], off offset:512 sc1
	s_nop 1
	v_pk_mul_f32 v[168:169], v[174:175], v[48:49] op_sel_hi:[0,1]
	v_pk_mul_f32 v[166:167], v[174:175], v[46:47] op_sel_hi:[0,1]
	v_mul_f32_e32 v174, 0x3d3504f3, v144
	global_store_dwordx4 v[172:173], v[166:169], off offset:16 sc1
	v_lshl_add_u64 v[172:173], v[170:171], 0, s[40:41]
	s_mov_b64 s[40:41], 0x1600
	v_pk_mul_f32 v[168:169], v[174:175], v[40:41] op_sel_hi:[0,1]
	v_pk_mul_f32 v[166:167], v[174:175], v[38:39] op_sel_hi:[0,1]
	global_store_dwordx4 v[176:177], v[166:169], off offset:1024 sc1
	v_lshl_add_u64 v[170:171], v[170:171], 0, s[40:41]
	s_nop 0
	v_pk_mul_f32 v[168:169], v[174:175], v[32:33] op_sel_hi:[0,1]
	v_pk_mul_f32 v[166:167], v[174:175], v[30:31] op_sel_hi:[0,1]
	global_store_dwordx4 v[172:173], v[166:169], off offset:16 sc1
	v_mul_f32_e32 v172, 0x3d3504f3, v142
	s_nop 0
	v_pk_mul_f32 v[168:169], v[172:173], v[24:25] op_sel_hi:[0,1]
	v_pk_mul_f32 v[166:167], v[172:173], v[22:23] op_sel_hi:[0,1]
	global_store_dwordx4 v[176:177], v[166:169], off offset:1536 sc1
	s_nop 1
	v_pk_mul_f32 v[168:169], v[172:173], v[16:17] op_sel_hi:[0,1]
	v_pk_mul_f32 v[166:167], v[172:173], v[14:15] op_sel_hi:[0,1]
	global_store_dwordx4 v[170:171], v[166:169], off offset:16 sc1

.LBB0_2015:
	s_andn2_b64 vcc, exec, s[36:37]
	s_cbranch_vccnz .LBB0_2017
	s_ashr_i32 s36, s29, 5
	s_ashr_i32 s37, s36, 31
	s_lshl_b64 s[40:41], s[36:37], 12
	v_pk_mul_f32 v[168:169], v[156:157], v[128:129] op_sel_hi:[0,1]
	v_pk_mul_f32 v[166:167], v[156:157], v[126:127] op_sel_hi:[0,1]
	v_pk_mul_f32 v[170:171], v[156:157], v[124:125] op_sel_hi:[0,1]
	v_pk_mul_f32 v[172:173], v[156:157], v[122:123] op_sel_hi:[0,1]
	s_add_u32 s40, s44, s40
	v_lshlrev_b32_e32 v145, 6, v160
	v_cvt_pk_bf16_f32 v166, v166, v167
	v_cvt_pk_bf16_f32 v167, v168, v169
	v_cvt_pk_bf16_f32 v168, v172, v173
	v_cvt_pk_bf16_f32 v169, v170, v171
	s_addc_u32 s41, s45, s41
	v_lshl_or_b32 v145, v0, 4, v145
	s_or_b32 s36, s36, 1
	global_store_dwordx4 v145, v[166:169], s[40:41] sc1
	v_pk_mul_f32 v[170:171], v[154:155], v[108:109] op_sel_hi:[0,1]
	v_pk_mul_f32 v[172:173], v[154:155], v[106:107] op_sel_hi:[0,1]
	v_pk_mul_f32 v[168:169], v[154:155], v[116:117] op_sel_hi:[0,1]
	v_pk_mul_f32 v[166:167], v[154:155], v[114:115] op_sel_hi:[0,1]
	s_ashr_i32 s37, s36, 31
	v_cvt_pk_bf16_f32 v166, v166, v167
	v_cvt_pk_bf16_f32 v167, v168, v169
	v_cvt_pk_bf16_f32 v168, v172, v173
	v_cvt_pk_bf16_f32 v169, v170, v171
	s_lshl_b64 s[36:37], s[36:37], 12
	global_store_dwordx4 v145, v[166:169], s[40:41] offset:256 sc1
	v_pk_mul_f32 v[170:171], v[152:153], v[92:93] op_sel_hi:[0,1]
	v_pk_mul_f32 v[172:173], v[152:153], v[90:91] op_sel_hi:[0,1]
	v_pk_mul_f32 v[168:169], v[152:153], v[100:101] op_sel_hi:[0,1]
	v_pk_mul_f32 v[166:167], v[152:153], v[98:99] op_sel_hi:[0,1]
	s_add_u32 s36, s44, s36
	v_cvt_pk_bf16_f32 v166, v166, v167
	v_cvt_pk_bf16_f32 v167, v168, v169
	v_cvt_pk_bf16_f32 v168, v172, v173
	v_cvt_pk_bf16_f32 v169, v170, v171
	s_addc_u32 s37, s45, s37
	global_store_dwordx4 v145, v[166:169], s[36:37] sc1
	v_or_b32_e32 v0, 48, v158
	v_pk_mul_f32 v[170:171], v[150:151], v[76:77] op_sel_hi:[0,1]
	v_pk_mul_f32 v[168:169], v[150:151], v[84:85] op_sel_hi:[0,1]
	v_pk_mul_f32 v[166:167], v[150:151], v[82:83] op_sel_hi:[0,1]
	v_cvt_pk_bf16_f32 v166, v166, v167
	v_cvt_pk_bf16_f32 v167, v168, v169
	v_cvt_pk_bf16_f32 v169, v170, v171
	v_ashrrev_i32_e32 v170, 5, v0
	v_lshlrev_b32_e32 v143, 5, v160
	v_ashrrev_i32_e32 v171, 31, v170
	v_lshlrev_b32_e32 v0, 3, v0
	s_movk_i32 s40, 0xf8
	s_add_i32 s36, s29, 0x80
	v_lshlrev_b64 v[170:171], 12, v[170:171]
	v_and_or_b32 v0, v0, s40, v143
	s_ashr_i32 s36, s36, 5
	v_pk_mul_f32 v[172:173], v[150:151], v[74:75] op_sel_hi:[0,1]
	v_lshl_add_u64 v[170:171], s[44:45], 0, v[170:171]
	v_lshlrev_b32_e32 v0, 1, v0
	s_ashr_i32 s37, s36, 31
	v_cvt_pk_bf16_f32 v168, v172, v173
	v_lshl_add_u64 v[170:171], v[170:171], 0, v[0:1]
	s_lshl_b64 s[36:37], s[36:37], 12
	global_store_dwordx4 v[170:171], v[166:169], off sc1
	v_pk_mul_f32 v[170:171], v[148:149], v[60:61] op_sel_hi:[0,1]
	v_pk_mul_f32 v[172:173], v[148:149], v[58:59] op_sel_hi:[0,1]
	v_pk_mul_f32 v[168:169], v[148:149], v[64:65] op_sel_hi:[0,1]
	v_pk_mul_f32 v[166:167], v[148:149], v[62:63] op_sel_hi:[0,1]
	s_add_u32 s36, s44, s36
	v_cvt_pk_bf16_f32 v166, v166, v167
	v_cvt_pk_bf16_f32 v167, v168, v169
	v_cvt_pk_bf16_f32 v168, v172, v173
	v_cvt_pk_bf16_f32 v169, v170, v171
	s_addc_u32 s37, s45, s37
	global_store_dwordx4 v145, v[166:169], s[36:37] sc1
	v_add_u32_e32 v0, 0x90, v158
	v_pk_mul_f32 v[170:171], v[146:147], v[48:49] op_sel_hi:[0,1]
	v_pk_mul_f32 v[168:169], v[146:147], v[56:57] op_sel_hi:[0,1]
	v_pk_mul_f32 v[166:167], v[146:147], v[54:55] op_sel_hi:[0,1]
	v_cvt_pk_bf16_f32 v166, v166, v167
	v_cvt_pk_bf16_f32 v167, v168, v169
	v_cvt_pk_bf16_f32 v169, v170, v171
	v_ashrrev_i32_e32 v170, 5, v0
	v_ashrrev_i32_e32 v171, 31, v170
	v_lshlrev_b32_e32 v0, 3, v0
	s_addk_i32 s29, 0xa0
	v_lshlrev_b64 v[170:171], 12, v[170:171]
	v_and_or_b32 v0, v0, s40, v143
	s_ashr_i32 s36, s29, 5
	v_pk_mul_f32 v[172:173], v[146:147], v[46:47] op_sel_hi:[0,1]
	v_lshl_add_u64 v[170:171], s[44:45], 0, v[170:171]
	v_lshlrev_b32_e32 v0, 1, v0
	s_ashr_i32 s37, s36, 31
	v_cvt_pk_bf16_f32 v168, v172, v173
	v_lshl_add_u64 v[170:171], v[170:171], 0, v[0:1]
	s_lshl_b64 s[36:37], s[36:37], 12
	global_store_dwordx4 v[170:171], v[166:169], off sc1
	v_pk_mul_f32 v[170:171], v[144:145], v[32:33] op_sel_hi:[0,1]
	v_pk_mul_f32 v[172:173], v[144:145], v[30:31] op_sel_hi:[0,1]
	v_pk_mul_f32 v[168:169], v[144:145], v[40:41] op_sel_hi:[0,1]
	v_pk_mul_f32 v[166:167], v[144:145], v[38:39] op_sel_hi:[0,1]
	s_add_u32 s36, s44, s36
	v_cvt_pk_bf16_f32 v166, v166, v167
	v_cvt_pk_bf16_f32 v167, v168, v169
	v_cvt_pk_bf16_f32 v168, v172, v173
	v_cvt_pk_bf16_f32 v169, v170, v171
	s_addc_u32 s37, s45, s37
	global_store_dwordx4 v145, v[166:169], s[36:37] sc1
	v_add_u32_e32 v0, 0xb0, v158
	v_pk_mul_f32 v[170:171], v[142:143], v[16:17] op_sel_hi:[0,1]
	v_pk_mul_f32 v[168:169], v[142:143], v[24:25] op_sel_hi:[0,1]
	v_pk_mul_f32 v[166:167], v[142:143], v[22:23] op_sel_hi:[0,1]
	v_cvt_pk_bf16_f32 v166, v166, v167
	v_cvt_pk_bf16_f32 v167, v168, v169
	v_cvt_pk_bf16_f32 v169, v170, v171
	v_ashrrev_i32_e32 v170, 5, v0
	v_ashrrev_i32_e32 v171, 31, v170
	v_lshlrev_b32_e32 v0, 3, v0
	v_lshlrev_b64 v[170:171], 12, v[170:171]
	v_and_or_b32 v0, v0, s40, v143
	v_pk_mul_f32 v[172:173], v[142:143], v[14:15] op_sel_hi:[0,1]
	v_lshl_add_u64 v[170:171], s[44:45], 0, v[170:171]
	v_lshlrev_b32_e32 v0, 1, v0
	v_cvt_pk_bf16_f32 v168, v172, v173
	v_lshl_add_u64 v[170:171], v[170:171], 0, v[0:1]
	global_store_dwordx4 v[170:171], v[166:169], off sc1

.LBB0_2018:
	s_andn2_b64 vcc, exec, s[36:37]
	s_cbranch_vccnz .LBB0_2020
	s_lshl_b32 s29, s50, 8
	s_add_u32 s36, s74, s29
	s_addc_u32 s37, s75, 0
	v_lshlrev_b32_e32 v0, 1, v160
	v_lshl_add_u64 v[166:167], s[36:37], 0, v[0:1]
	s_mov_b64 s[36:37], 0xd7ff000
	v_lshl_add_u64 v[170:171], v[166:167], 0, s[36:37]
	v_mul_f32_e32 v0, v156, v156
	v_pk_mul_f32 v[166:167], v[128:129], v[120:121]
	v_pk_mul_f32 v[168:169], v[126:127], v[118:119]
	v_pk_mul_f32 v[172:173], v[0:1], v[166:167] op_sel_hi:[0,1]
	v_pk_mul_f32 v[166:167], v[0:1], v[168:169] op_sel_hi:[0,1]
	v_pk_mul_f32 v[168:169], v[124:125], v[112:113]
	v_pk_mul_f32 v[174:175], v[122:123], v[110:111]
	v_ashrrev_i32_e32 v159, 31, v158
	v_pk_mul_f32 v[176:177], v[0:1], v[168:169] op_sel_hi:[0,1]
	v_pk_mul_f32 v[168:169], v[0:1], v[174:175] op_sel_hi:[0,1]
	v_cvt_pk_bf16_f32 v166, v166, v167
	v_cvt_pk_bf16_f32 v167, v172, v173
	v_lshlrev_b64 v[172:173], 10, v[158:159]
	v_cvt_pk_bf16_f32 v168, v168, v169
	v_cvt_pk_bf16_f32 v169, v176, v177
	v_lshl_add_u64 v[172:173], v[170:171], 0, v[172:173]
	global_store_dwordx4 v[172:173], v[166:169], off sc1
	v_mul_f32_e32 v0, v154, v154
	v_pk_mul_f32 v[176:177], v[106:107], v[94:95]
	v_pk_mul_f32 v[166:167], v[116:117], v[104:105]
	v_pk_mul_f32 v[168:169], v[114:115], v[102:103]
	v_pk_mul_f32 v[174:175], v[0:1], v[166:167] op_sel_hi:[0,1]
	v_pk_mul_f32 v[166:167], v[0:1], v[168:169] op_sel_hi:[0,1]
	v_cvt_pk_bf16_f32 v166, v166, v167
	v_cvt_pk_bf16_f32 v167, v174, v175
	v_or_b32_e32 v174, 16, v158
	v_pk_mul_f32 v[168:169], v[108:109], v[96:97]
	v_ashrrev_i32_e32 v175, 31, v174
	v_pk_mul_f32 v[178:179], v[0:1], v[168:169] op_sel_hi:[0,1]
	v_pk_mul_f32 v[168:169], v[0:1], v[176:177] op_sel_hi:[0,1]
	v_lshlrev_b64 v[174:175], 10, v[174:175]
	v_cvt_pk_bf16_f32 v168, v168, v169
	v_cvt_pk_bf16_f32 v169, v178, v179
	v_lshl_add_u64 v[174:175], v[170:171], 0, v[174:175]
	global_store_dwordx4 v[174:175], v[166:169], off sc1
	v_mul_f32_e32 v0, v152, v152
	v_pk_mul_f32 v[176:177], v[90:91], v[78:79]
	v_pk_mul_f32 v[166:167], v[100:101], v[88:89]
	v_pk_mul_f32 v[168:169], v[98:99], v[86:87]
	v_pk_mul_f32 v[174:175], v[0:1], v[166:167] op_sel_hi:[0,1]
	v_pk_mul_f32 v[166:167], v[0:1], v[168:169] op_sel_hi:[0,1]
	v_cvt_pk_bf16_f32 v166, v166, v167
	v_cvt_pk_bf16_f32 v167, v174, v175
	v_or_b32_e32 v174, 32, v158
	v_pk_mul_f32 v[168:169], v[92:93], v[80:81]
	v_ashrrev_i32_e32 v175, 31, v174
	v_pk_mul_f32 v[178:179], v[0:1], v[168:169] op_sel_hi:[0,1]
	v_pk_mul_f32 v[168:169], v[0:1], v[176:177] op_sel_hi:[0,1]
	v_lshlrev_b64 v[174:175], 10, v[174:175]
	v_cvt_pk_bf16_f32 v168, v168, v169
	v_cvt_pk_bf16_f32 v169, v178, v179
	v_lshl_add_u64 v[174:175], v[170:171], 0, v[174:175]
	global_store_dwordx4 v[174:175], v[166:169], off sc1
	v_mul_f32_e32 v0, v150, v150
	v_pk_mul_f32 v[176:177], v[74:75], v[66:67]
	v_pk_mul_f32 v[166:167], v[84:85], v[72:73]
	v_pk_mul_f32 v[168:169], v[82:83], v[70:71]
	v_pk_mul_f32 v[174:175], v[0:1], v[166:167] op_sel_hi:[0,1]
	v_pk_mul_f32 v[166:167], v[0:1], v[168:169] op_sel_hi:[0,1]
	v_cvt_pk_bf16_f32 v166, v166, v167
	v_cvt_pk_bf16_f32 v167, v174, v175
	v_or_b32_e32 v174, 48, v158
	v_pk_mul_f32 v[168:169], v[76:77], v[68:69]
	v_ashrrev_i32_e32 v175, 31, v174
	v_pk_mul_f32 v[178:179], v[0:1], v[168:169] op_sel_hi:[0,1]
	v_pk_mul_f32 v[168:169], v[0:1], v[176:177] op_sel_hi:[0,1]
	v_lshlrev_b64 v[174:175], 10, v[174:175]
	v_cvt_pk_bf16_f32 v168, v168, v169
	v_cvt_pk_bf16_f32 v169, v178, v179
	v_lshl_add_u64 v[170:171], v[170:171], 0, v[174:175]
	global_store_dwordx4 v[170:171], v[166:169], off sc1
	v_mul_f32_e32 v0, v148, v148
	v_pk_mul_f32 v[174:175], v[58:59], v[42:43]
	v_pk_mul_f32 v[166:167], v[64:65], v[52:53]
	v_pk_mul_f32 v[168:169], v[62:63], v[50:51]
	v_pk_mul_f32 v[170:171], v[0:1], v[166:167] op_sel_hi:[0,1]
	v_pk_mul_f32 v[166:167], v[0:1], v[168:169] op_sel_hi:[0,1]
	v_pk_mul_f32 v[168:169], v[60:61], v[44:45]
	s_mov_b32 s29, 0x20000
	v_pk_mul_f32 v[176:177], v[0:1], v[168:169] op_sel_hi:[0,1]
	v_pk_mul_f32 v[168:169], v[0:1], v[174:175] op_sel_hi:[0,1]
	v_cvt_pk_bf16_f32 v166, v166, v167
	v_cvt_pk_bf16_f32 v167, v170, v171
	v_add_co_u32_e32 v170, vcc, s29, v172
	v_cvt_pk_bf16_f32 v168, v168, v169
	v_cvt_pk_bf16_f32 v169, v176, v177
	v_addc_co_u32_e32 v171, vcc, 0, v173, vcc
	global_store_dwordx4 v[170:171], v[166:169], off sc1
	v_mul_f32_e32 v0, v146, v146
	v_pk_mul_f32 v[174:175], v[46:47], v[26:27]
	v_pk_mul_f32 v[166:167], v[56:57], v[36:37]
	v_pk_mul_f32 v[168:169], v[54:55], v[34:35]
	v_pk_mul_f32 v[170:171], v[0:1], v[166:167] op_sel_hi:[0,1]
	v_pk_mul_f32 v[166:167], v[0:1], v[168:169] op_sel_hi:[0,1]
	v_pk_mul_f32 v[168:169], v[48:49], v[28:29]
	s_mov_b32 s29, 0x24000
	v_pk_mul_f32 v[176:177], v[0:1], v[168:169] op_sel_hi:[0,1]
	v_pk_mul_f32 v[168:169], v[0:1], v[174:175] op_sel_hi:[0,1]
	v_cvt_pk_bf16_f32 v166, v166, v167
	v_cvt_pk_bf16_f32 v167, v170, v171
	v_add_co_u32_e32 v170, vcc, s29, v172
	v_cvt_pk_bf16_f32 v168, v168, v169
	v_cvt_pk_bf16_f32 v169, v176, v177
	v_addc_co_u32_e32 v171, vcc, 0, v173, vcc
	global_store_dwordx4 v[170:171], v[166:169], off sc1
	v_mul_f32_e32 v0, v144, v144
	v_pk_mul_f32 v[174:175], v[30:31], v[10:11]
	v_pk_mul_f32 v[166:167], v[40:41], v[20:21]
	v_pk_mul_f32 v[168:169], v[38:39], v[18:19]
	v_pk_mul_f32 v[170:171], v[0:1], v[166:167] op_sel_hi:[0,1]
	v_pk_mul_f32 v[166:167], v[0:1], v[168:169] op_sel_hi:[0,1]
	v_pk_mul_f32 v[168:169], v[32:33], v[12:13]
	s_mov_b32 s29, 0x28000
	v_pk_mul_f32 v[176:177], v[0:1], v[168:169] op_sel_hi:[0,1]
	v_pk_mul_f32 v[168:169], v[0:1], v[174:175] op_sel_hi:[0,1]
	v_cvt_pk_bf16_f32 v166, v166, v167
	v_cvt_pk_bf16_f32 v167, v170, v171
	v_add_co_u32_e32 v170, vcc, s29, v172
	v_cvt_pk_bf16_f32 v168, v168, v169
	v_cvt_pk_bf16_f32 v169, v176, v177
	v_addc_co_u32_e32 v171, vcc, 0, v173, vcc
	global_store_dwordx4 v[170:171], v[166:169], off sc1
	v_mul_f32_e32 v0, v142, v142
	v_pk_mul_f32 v[174:175], v[14:15], v[2:3]
	v_pk_mul_f32 v[166:167], v[24:25], v[8:9]
	v_pk_mul_f32 v[168:169], v[22:23], v[6:7]
	v_pk_mul_f32 v[170:171], v[0:1], v[166:167] op_sel_hi:[0,1]
	v_pk_mul_f32 v[166:167], v[0:1], v[168:169] op_sel_hi:[0,1]
	v_pk_mul_f32 v[168:169], v[16:17], v[4:5]
	v_cvt_pk_bf16_f32 v166, v166, v167
	v_pk_mul_f32 v[176:177], v[0:1], v[168:169] op_sel_hi:[0,1]
	v_pk_mul_f32 v[168:169], v[0:1], v[174:175] op_sel_hi:[0,1]
	v_cvt_pk_bf16_f32 v167, v170, v171
	v_add_co_u32_e32 v170, vcc, 0x2c000, v172
	v_cvt_pk_bf16_f32 v168, v168, v169
	v_cvt_pk_bf16_f32 v169, v176, v177
	v_addc_co_u32_e32 v171, vcc, 0, v173, vcc
	global_store_dwordx4 v[170:171], v[166:169], off sc1

.LBB0_2042:
	s_cmp_eq_u32 s29, 3
	s_cselect_b64 s[40:41], -1, 0
	s_or_b64 vcc, s[36:37], s[40:41]
	s_add_u32 s29, s74, s60
	s_addc_u32 s37, s75, s61
	s_lshl_b32 s36, s50, 9
	s_and_b32 s36, s36, 0x200
	v_mov_b32_e32 v0, 0x3e38aa3b
	s_add_u32 s36, s29, s36
	v_cndmask_b32_e32 v143, 1.0, v0, vcc
	s_addc_u32 s37, s37, 0
	v_lshlrev_b32_e32 v0, 1, v160
	v_lshl_add_u64 v[166:167], s[36:37], 0, v[0:1]
	v_ashrrev_i32_e32 v159, 31, v158
	v_mul_f32_e32 v0, v143, v156
	v_lshlrev_b64 v[160:161], 10, v[158:159]
	v_pk_mul_f32 v[128:129], v[0:1], v[128:129] op_sel_hi:[0,1]
	v_pk_mul_f32 v[126:127], v[0:1], v[126:127] op_sel_hi:[0,1]
	v_pk_mul_f32 v[156:157], v[0:1], v[124:125] op_sel_hi:[0,1]
	v_pk_mul_f32 v[124:125], v[0:1], v[122:123] op_sel_hi:[0,1]
	v_lshl_add_u64 v[160:161], v[166:167], 0, v[160:161]
	v_cvt_pk_bf16_f32 v122, v126, v127
	v_cvt_pk_bf16_f32 v123, v128, v129
	v_cvt_pk_bf16_f32 v124, v124, v125
	v_cvt_pk_bf16_f32 v125, v156, v157
	global_store_dwordx4 v[160:161], v[122:125], off sc1
	v_pk_mul_f32 v[120:121], v[0:1], v[120:121] op_sel_hi:[0,1]
	v_pk_mul_f32 v[118:119], v[0:1], v[118:119] op_sel_hi:[0,1]
	v_pk_mul_f32 v[122:123], v[0:1], v[112:113] op_sel_hi:[0,1]
	v_pk_mul_f32 v[112:113], v[0:1], v[110:111] op_sel_hi:[0,1]
	v_cvt_pk_bf16_f32 v110, v118, v119
	v_cvt_pk_bf16_f32 v111, v120, v121
	v_cvt_pk_bf16_f32 v112, v112, v113
	v_cvt_pk_bf16_f32 v113, v122, v123
	global_store_dwordx4 v[160:161], v[110:113], off offset:256 sc1
	v_mul_f32_e32 v0, v143, v154
	v_pk_mul_f32 v[114:115], v[0:1], v[114:115] op_sel_hi:[0,1]
	v_or_b32_e32 v110, 16, v158
	v_ashrrev_i32_e32 v111, 31, v110
	v_lshlrev_b64 v[110:111], 10, v[110:111]
	v_pk_mul_f32 v[112:113], v[0:1], v[116:117] op_sel_hi:[0,1]
	v_pk_mul_f32 v[116:117], v[0:1], v[108:109] op_sel_hi:[0,1]
	v_pk_mul_f32 v[108:109], v[0:1], v[106:107] op_sel_hi:[0,1]
	v_lshl_add_u64 v[110:111], v[166:167], 0, v[110:111]
	v_cvt_pk_bf16_f32 v106, v114, v115
	v_cvt_pk_bf16_f32 v107, v112, v113
	v_cvt_pk_bf16_f32 v108, v108, v109
	v_cvt_pk_bf16_f32 v109, v116, v117
	global_store_dwordx4 v[110:111], v[106:109], off sc1
	v_pk_mul_f32 v[104:105], v[0:1], v[104:105] op_sel_hi:[0,1]
	v_pk_mul_f32 v[102:103], v[0:1], v[102:103] op_sel_hi:[0,1]
	v_pk_mul_f32 v[106:107], v[0:1], v[96:97] op_sel_hi:[0,1]
	v_pk_mul_f32 v[96:97], v[0:1], v[94:95] op_sel_hi:[0,1]
	v_cvt_pk_bf16_f32 v94, v102, v103
	v_cvt_pk_bf16_f32 v95, v104, v105
	v_cvt_pk_bf16_f32 v96, v96, v97
	v_cvt_pk_bf16_f32 v97, v106, v107
	global_store_dwordx4 v[110:111], v[94:97], off offset:256 sc1
	v_mul_f32_e32 v0, v143, v152
	v_pk_mul_f32 v[98:99], v[0:1], v[98:99] op_sel_hi:[0,1]
	v_or_b32_e32 v94, 32, v158
	v_ashrrev_i32_e32 v95, 31, v94
	v_lshlrev_b64 v[94:95], 10, v[94:95]
	v_pk_mul_f32 v[96:97], v[0:1], v[100:101] op_sel_hi:[0,1]
	v_pk_mul_f32 v[100:101], v[0:1], v[92:93] op_sel_hi:[0,1]
	v_pk_mul_f32 v[92:93], v[0:1], v[90:91] op_sel_hi:[0,1]
	v_lshl_add_u64 v[94:95], v[166:167], 0, v[94:95]
	v_cvt_pk_bf16_f32 v90, v98, v99
	v_cvt_pk_bf16_f32 v91, v96, v97
	v_cvt_pk_bf16_f32 v92, v92, v93
	v_cvt_pk_bf16_f32 v93, v100, v101
	global_store_dwordx4 v[94:95], v[90:93], off sc1
	v_pk_mul_f32 v[88:89], v[0:1], v[88:89] op_sel_hi:[0,1]
	v_pk_mul_f32 v[86:87], v[0:1], v[86:87] op_sel_hi:[0,1]
	v_pk_mul_f32 v[90:91], v[0:1], v[80:81] op_sel_hi:[0,1]
	v_pk_mul_f32 v[80:81], v[0:1], v[78:79] op_sel_hi:[0,1]
	v_cvt_pk_bf16_f32 v78, v86, v87
	v_cvt_pk_bf16_f32 v79, v88, v89
	v_cvt_pk_bf16_f32 v80, v80, v81
	v_cvt_pk_bf16_f32 v81, v90, v91
	global_store_dwordx4 v[94:95], v[78:81], off offset:256 sc1
	v_mul_f32_e32 v0, v143, v150
	v_pk_mul_f32 v[82:83], v[0:1], v[82:83] op_sel_hi:[0,1]
	v_or_b32_e32 v78, 48, v158
	v_ashrrev_i32_e32 v79, 31, v78
	v_lshlrev_b64 v[78:79], 10, v[78:79]
	v_pk_mul_f32 v[80:81], v[0:1], v[84:85] op_sel_hi:[0,1]
	v_pk_mul_f32 v[84:85], v[0:1], v[76:77] op_sel_hi:[0,1]
	v_pk_mul_f32 v[76:77], v[0:1], v[74:75] op_sel_hi:[0,1]
	v_lshl_add_u64 v[78:79], v[166:167], 0, v[78:79]
	v_cvt_pk_bf16_f32 v74, v82, v83
	v_cvt_pk_bf16_f32 v75, v80, v81
	v_cvt_pk_bf16_f32 v76, v76, v77
	v_cvt_pk_bf16_f32 v77, v84, v85
	global_store_dwordx4 v[78:79], v[74:77], off sc1
	v_pk_mul_f32 v[72:73], v[0:1], v[72:73] op_sel_hi:[0,1]
	v_pk_mul_f32 v[70:71], v[0:1], v[70:71] op_sel_hi:[0,1]
	v_pk_mul_f32 v[74:75], v[0:1], v[68:69] op_sel_hi:[0,1]
	v_pk_mul_f32 v[68:69], v[0:1], v[66:67] op_sel_hi:[0,1]
	v_mul_f32_e32 v0, v143, v148
	v_cvt_pk_bf16_f32 v66, v70, v71
	v_cvt_pk_bf16_f32 v67, v72, v73
	v_cvt_pk_bf16_f32 v68, v68, v69
	v_cvt_pk_bf16_f32 v69, v74, v75
	v_pk_mul_f32 v[62:63], v[0:1], v[62:63] op_sel_hi:[0,1]
	s_mov_b32 s29, 0x20000
	global_store_dwordx4 v[78:79], v[66:69], off offset:256 sc1
	v_pk_mul_f32 v[64:65], v[0:1], v[64:65] op_sel_hi:[0,1]
	v_pk_mul_f32 v[52:53], v[0:1], v[52:53] op_sel_hi:[0,1]
	v_pk_mul_f32 v[68:69], v[0:1], v[60:61] op_sel_hi:[0,1]
	v_pk_mul_f32 v[60:61], v[0:1], v[58:59] op_sel_hi:[0,1]
	v_cvt_pk_bf16_f32 v58, v62, v63
	v_add_co_u32_e32 v62, vcc, s29, v160
	v_cvt_pk_bf16_f32 v59, v64, v65
	v_cvt_pk_bf16_f32 v60, v60, v61
	v_cvt_pk_bf16_f32 v61, v68, v69
	v_addc_co_u32_e32 v63, vcc, 0, v161, vcc
	global_store_dwordx4 v[62:63], v[58:61], off sc1
	v_pk_mul_f32 v[50:51], v[0:1], v[50:51] op_sel_hi:[0,1]
	v_lshl_add_u64 v[66:67], v[160:161], 0, s[24:25]
	v_pk_mul_f32 v[58:59], v[0:1], v[44:45] op_sel_hi:[0,1]
	v_pk_mul_f32 v[44:45], v[0:1], v[42:43] op_sel_hi:[0,1]
	v_cvt_pk_bf16_f32 v42, v50, v51
	v_cvt_pk_bf16_f32 v43, v52, v53
	v_cvt_pk_bf16_f32 v44, v44, v45
	v_cvt_pk_bf16_f32 v45, v58, v59
	v_mul_f32_e32 v0, v143, v146
	global_store_dwordx4 v[66:67], v[42:45], off offset:256 sc1
	v_pk_mul_f32 v[46:47], v[0:1], v[46:47] op_sel_hi:[0,1]
	s_mov_b32 s29, 0x24000
	v_pk_mul_f32 v[44:45], v[0:1], v[56:57] op_sel_hi:[0,1]
	v_pk_mul_f32 v[42:43], v[0:1], v[54:55] op_sel_hi:[0,1]
	v_pk_mul_f32 v[48:49], v[0:1], v[48:49] op_sel_hi:[0,1]
	v_cvt_pk_bf16_f32 v42, v42, v43
	v_cvt_pk_bf16_f32 v43, v44, v45
	v_cvt_pk_bf16_f32 v44, v46, v47
	v_add_co_u32_e32 v46, vcc, s29, v160
	v_cvt_pk_bf16_f32 v45, v48, v49
	s_nop 0
	v_addc_co_u32_e32 v47, vcc, 0, v161, vcc
	s_mov_b64 s[36:37], 0x24000
	global_store_dwordx4 v[46:47], v[42:45], off sc1
	v_pk_mul_f32 v[36:37], v[0:1], v[36:37] op_sel_hi:[0,1]
	v_pk_mul_f32 v[34:35], v[0:1], v[34:35] op_sel_hi:[0,1]
	v_pk_mul_f32 v[42:43], v[0:1], v[28:29] op_sel_hi:[0,1]
	v_pk_mul_f32 v[28:29], v[0:1], v[26:27] op_sel_hi:[0,1]
	v_lshl_add_u64 v[50:51], v[160:161], 0, s[36:37]
	v_cvt_pk_bf16_f32 v26, v34, v35
	v_cvt_pk_bf16_f32 v27, v36, v37
	v_cvt_pk_bf16_f32 v28, v28, v29
	v_cvt_pk_bf16_f32 v29, v42, v43
	v_mul_f32_e32 v0, v143, v144
	global_store_dwordx4 v[50:51], v[26:29], off offset:256 sc1
	v_pk_mul_f32 v[30:31], v[0:1], v[30:31] op_sel_hi:[0,1]
	s_mov_b32 s29, 0x28000
	v_pk_mul_f32 v[28:29], v[0:1], v[40:41] op_sel_hi:[0,1]
	v_pk_mul_f32 v[26:27], v[0:1], v[38:39] op_sel_hi:[0,1]
	v_pk_mul_f32 v[32:33], v[0:1], v[32:33] op_sel_hi:[0,1]
	v_cvt_pk_bf16_f32 v26, v26, v27
	v_cvt_pk_bf16_f32 v27, v28, v29
	v_cvt_pk_bf16_f32 v28, v30, v31
	v_add_co_u32_e32 v30, vcc, s29, v160
	v_cvt_pk_bf16_f32 v29, v32, v33
	s_nop 0
	v_addc_co_u32_e32 v31, vcc, 0, v161, vcc
	s_mov_b64 s[36:37], 0x28000
	global_store_dwordx4 v[30:31], v[26:29], off sc1
	v_pk_mul_f32 v[20:21], v[0:1], v[20:21] op_sel_hi:[0,1]
	v_pk_mul_f32 v[18:19], v[0:1], v[18:19] op_sel_hi:[0,1]
	v_pk_mul_f32 v[26:27], v[0:1], v[12:13] op_sel_hi:[0,1]
	v_pk_mul_f32 v[12:13], v[0:1], v[10:11] op_sel_hi:[0,1]
	v_lshl_add_u64 v[34:35], v[160:161], 0, s[36:37]
	v_cvt_pk_bf16_f32 v10, v18, v19
	v_cvt_pk_bf16_f32 v11, v20, v21
	v_cvt_pk_bf16_f32 v12, v12, v13
	v_cvt_pk_bf16_f32 v13, v26, v27
	v_mul_f32_e32 v0, v143, v142
	global_store_dwordx4 v[34:35], v[10:13], off offset:256 sc1
	v_pk_mul_f32 v[14:15], v[0:1], v[14:15] op_sel_hi:[0,1]
	s_mov_b32 s29, 0x2c000
	v_pk_mul_f32 v[12:13], v[0:1], v[24:25] op_sel_hi:[0,1]
	v_pk_mul_f32 v[10:11], v[0:1], v[22:23] op_sel_hi:[0,1]
	v_pk_mul_f32 v[16:17], v[0:1], v[16:17] op_sel_hi:[0,1]
	v_cvt_pk_bf16_f32 v10, v10, v11
	v_cvt_pk_bf16_f32 v11, v12, v13
	v_cvt_pk_bf16_f32 v12, v14, v15
	v_add_co_u32_e32 v14, vcc, s29, v160
	v_cvt_pk_bf16_f32 v13, v16, v17
	s_nop 0
	v_addc_co_u32_e32 v15, vcc, 0, v161, vcc
	s_mov_b64 s[36:37], 0x2c000
	global_store_dwordx4 v[14:15], v[10:13], off sc1
	v_pk_mul_f32 v[8:9], v[0:1], v[8:9] op_sel_hi:[0,1]
	v_pk_mul_f32 v[6:7], v[0:1], v[6:7] op_sel_hi:[0,1]
	v_pk_mul_f32 v[10:11], v[0:1], v[4:5] op_sel_hi:[0,1]
	v_pk_mul_f32 v[4:5], v[0:1], v[2:3] op_sel_hi:[0,1]
	v_lshl_add_u64 v[18:19], v[160:161], 0, s[36:37]
	v_cvt_pk_bf16_f32 v2, v6, v7
	v_cvt_pk_bf16_f32 v3, v8, v9
	v_cvt_pk_bf16_f32 v4, v4, v5
	v_cvt_pk_bf16_f32 v5, v10, v11
	global_store_dwordx4 v[18:19], v[2:5], off offset:256 sc1

.LBB0_2070:
	s_mov_b32 s17, -1
	s_ashr_i32 s51, s50, 31
	s_lshl_b64 s[50:51], s[50:51], 21
	v_mbcnt_lo_u32_b32 v0, s17, 0
	v_mbcnt_hi_u32_b32 v146, s17, v0
	s_add_u32 s17, s89, s50
	s_addc_u32 s29, s90, s51
	s_ashr_i32 s39, s38, 31
	s_lshl_b64 s[38:39], s[38:39], 9
	s_add_u32 s17, s17, s38
	s_addc_u32 s29, s29, s39
	s_add_u32 s38, s17, s92
	s_addc_u32 s39, s29, 0
	v_and_b32_e32 v0, 0x70, v146
	v_lshl_add_u64 v[144:145], s[38:39], 0, v[0:1]
	v_and_or_b32 v0, v146, 15, s67
	v_lshl_add_u32 v146, s16, 8, v0
	v_ashrrev_i32_e32 v147, 31, v146
	v_lshlrev_b64 v[148:149], 12, v[146:147]
	v_lshl_add_u64 v[148:149], v[144:145], 0, v[148:149]
	s_mov_b64 s[16:17], 0x80000
	v_cvt_pk_bf16_f32 v70, v70, v71
	v_cvt_pk_bf16_f32 v71, v72, v73
	v_cvt_pk_bf16_f32 v72, v66, v67
	v_lshl_add_u64 v[66:67], v[148:149], 0, s[16:17]
	s_mov_b32 s16, 0x80000
	v_cvt_pk_bf16_f32 v62, v62, v63
	v_cvt_pk_bf16_f32 v63, v64, v65
	v_cvt_pk_bf16_f32 v64, v58, v59
	v_add_co_u32_e32 v58, vcc, s16, v148
	v_cvt_pk_bf16_f32 v46, v46, v47
	v_cvt_pk_bf16_f32 v47, v48, v49
	v_cvt_pk_bf16_f32 v48, v42, v43
	v_cvt_pk_bf16_f32 v49, v44, v45
	s_mov_b64 s[16:17], 0x90000
	v_addc_co_u32_e32 v59, vcc, 0, v149, vcc
	global_store_dwordx4 v[66:67], v[46:49], off offset:256 sc1
	v_cvt_pk_bf16_f32 v30, v30, v31
	v_cvt_pk_bf16_f32 v31, v32, v33
	v_lshl_add_u64 v[46:47], v[148:149], 0, s[16:17]
	s_mov_b32 s16, 0x90000
	v_add_co_u32_e32 v48, vcc, s16, v148
	v_cvt_pk_bf16_f32 v32, v26, v27
	v_cvt_pk_bf16_f32 v33, v28, v29
	s_mov_b64 s[16:17], 0xa0000
	v_cvt_pk_bf16_f32 v110, v110, v111
	v_cvt_pk_bf16_f32 v111, v112, v113
	v_cvt_pk_bf16_f32 v112, v106, v107
	v_or_b32_e32 v106, 16, v146
	v_addc_co_u32_e32 v49, vcc, 0, v149, vcc
	global_store_dwordx4 v[46:47], v[30:33], off offset:256 sc1
	v_ashrrev_i32_e32 v107, 31, v106
	v_cvt_pk_bf16_f32 v94, v94, v95
	v_lshl_add_u64 v[30:31], v[148:149], 0, s[16:17]
	s_mov_b32 s16, 0xa0000
	v_cvt_pk_bf16_f32 v95, v96, v97
	v_cvt_pk_bf16_f32 v96, v90, v91
	v_or_b32_e32 v90, 32, v146
	v_add_co_u32_e32 v32, vcc, s16, v148
	v_cvt_pk_bf16_f32 v14, v14, v15
	v_cvt_pk_bf16_f32 v15, v16, v17
	v_cvt_pk_bf16_f32 v16, v10, v11
	v_cvt_pk_bf16_f32 v17, v12, v13
	s_mov_b64 s[16:17], 0xb0000
	v_cvt_pk_bf16_f32 v113, v108, v109
	v_lshlrev_b64 v[106:107], 12, v[106:107]
	v_ashrrev_i32_e32 v91, 31, v90
	v_cvt_pk_bf16_f32 v78, v78, v79
	v_cvt_pk_bf16_f32 v79, v80, v81
	v_cvt_pk_bf16_f32 v80, v74, v75
	v_or_b32_e32 v74, 48, v146
	v_addc_co_u32_e32 v33, vcc, 0, v149, vcc
	global_store_dwordx4 v[30:31], v[14:17], off offset:256 sc1
	global_store_dwordx4 v[148:149], v[110:113], off offset:256 sc1
	v_cvt_pk_bf16_f32 v97, v92, v93
	v_lshl_add_u64 v[14:15], v[148:149], 0, s[16:17]
	s_mov_b32 s16, 0xb0000
	v_lshl_add_u64 v[110:111], v[144:145], 0, v[106:107]
	v_lshlrev_b64 v[90:91], 12, v[90:91]
	v_ashrrev_i32_e32 v75, 31, v74
	v_add_co_u32_e32 v16, vcc, s16, v148
	global_store_dwordx4 v[110:111], v[94:97], off offset:256 sc1
	v_cvt_pk_bf16_f32 v81, v76, v77
	v_lshlrev_b64 v[74:75], 12, v[74:75]
	v_lshl_add_u64 v[94:95], v[144:145], 0, v[90:91]
	v_addc_co_u32_e32 v17, vcc, 0, v149, vcc
	v_cvt_pk_bf16_f32 v126, v126, v127
	v_cvt_pk_bf16_f32 v127, v128, v129
	v_cvt_pk_bf16_f32 v128, v122, v123
	v_cvt_pk_bf16_f32 v129, v124, v125
	v_cvt_pk_bf16_f32 v106, v118, v119
	v_cvt_pk_bf16_f32 v107, v120, v121
	v_cvt_pk_bf16_f32 v108, v114, v115
	v_cvt_pk_bf16_f32 v109, v116, v117
	v_cvt_pk_bf16_f32 v90, v102, v103
	v_cvt_pk_bf16_f32 v91, v104, v105
	v_cvt_pk_bf16_f32 v92, v98, v99
	v_cvt_pk_bf16_f32 v93, v100, v101
	global_store_dwordx4 v[94:95], v[78:81], off offset:256 sc1
	v_cvt_pk_bf16_f32 v76, v82, v83
	v_cvt_pk_bf16_f32 v77, v84, v85
	v_lshl_add_u64 v[78:79], v[144:145], 0, v[74:75]
	v_cvt_pk_bf16_f32 v74, v86, v87
	v_cvt_pk_bf16_f32 v75, v88, v89
	v_cvt_pk_bf16_f32 v73, v68, v69
	v_cvt_pk_bf16_f32 v65, v60, v61
	v_cvt_pk_bf16_f32 v42, v54, v55
	v_cvt_pk_bf16_f32 v43, v56, v57
	v_cvt_pk_bf16_f32 v44, v50, v51
	v_cvt_pk_bf16_f32 v45, v52, v53
	v_cvt_pk_bf16_f32 v26, v38, v39
	v_cvt_pk_bf16_f32 v27, v40, v41
	v_cvt_pk_bf16_f32 v28, v34, v35
	v_cvt_pk_bf16_f32 v29, v36, v37
	v_cvt_pk_bf16_f32 v10, v22, v23
	v_cvt_pk_bf16_f32 v11, v24, v25
	v_cvt_pk_bf16_f32 v12, v18, v19
	v_cvt_pk_bf16_f32 v13, v20, v21
	v_cvt_pk_bf16_f32 v6, v6, v7
	v_cvt_pk_bf16_f32 v7, v8, v9
	v_cvt_pk_bf16_f32 v8, v2, v3
	v_cvt_pk_bf16_f32 v9, v4, v5
	s_and_b64 vcc, exec, s[36:37]
	s_mov_b64 s[16:17], -1
	s_movk_i32 s95, 0x100
	s_movk_i32 s94, 0x2000
	global_store_dwordx4 v[148:149], v[126:129], off sc1
	global_store_dwordx4 v[110:111], v[106:109], off sc1
	global_store_dwordx4 v[94:95], v[90:93], off sc1
	global_store_dwordx4 v[78:79], v[74:77], off sc1
	global_store_dwordx4 v[78:79], v[70:73], off offset:256 sc1
	global_store_dwordx4 v[58:59], v[62:65], off sc1
	global_store_dwordx4 v[48:49], v[42:45], off sc1
	global_store_dwordx4 v[32:33], v[26:29], off sc1
	global_store_dwordx4 v[16:17], v[10:13], off sc1
	global_store_dwordx4 v[14:15], v[6:9], off offset:256 sc1
	s_cbranch_vccnz .LBB0_2055
	s_andn2_b64 vcc, exec, s[0:1]
	s_cbranch_vccnz .LBB0_2054
	s_barrier
	s_branch .LBB0_2054
